# nt2
# speedup vs baseline: 1.0553x; 1.0553x over previous
_ZN12_GLOBAL__N_16attn_qEPKDF16_S1_PK15HIP_vector_typeIfLj2EEPKhS7_PfS8_:
	s_load_dwordx8 s[4:11], s[0:1], 0x0
	s_load_dwordx4 s[16:19], s[0:1], 0x20
	s_load_dwordx2 s[20:21], s[0:1], 0x30
	v_lshlrev_b32_e32 v169, 3, v0
	s_ashr_i32 s12, s3, 4
	v_lshrrev_b32_e32 v95, 6, v0
	v_mov_b32_e32 v91, 0
	v_and_b32_e32 v96, 63, v0
	s_ashr_i32 s13, s12, 31
	v_lshlrev_b32_e32 v2, 5, v95
	v_mov_b32_e32 v3, v91
	v_lshlrev_b32_e32 v12, 2, v95
	v_lshlrev_b32_e32 v72, 4, v96
	v_mov_b32_e32 v73, v91
	v_lshl_add_u64 v[2:3], v[2:3], 0, s[12:13]
	s_waitcnt lgkmcnt(0)
	global_load_dwordx2 v[170:171], v169, s[8:9]
	v_lshl_add_u64 v[6:7], s[4:5], 0, v[72:73]
	v_lshlrev_b64 v[2:3], 10, v[2:3]
	v_or_b32_e32 v88, 1, v12
	v_lshl_add_u64 v[8:9], v[6:7], 0, v[2:3]
	v_lshlrev_b32_e32 v2, 3, v88
	v_mov_b32_e32 v3, v91
	v_lshl_add_u64 v[2:3], v[2:3], 0, s[12:13]
	v_lshlrev_b64 v[2:3], 10, v[2:3]
	v_or_b32_e32 v89, 2, v12
	v_lshl_add_u64 v[10:11], v[6:7], 0, v[2:3]
	global_load_dwordx4 v[2:5], v[8:9], off
	global_load_dwordx4 v[68:71], v[10:11], off
	v_lshlrev_b32_e32 v8, 3, v89
	v_mov_b32_e32 v9, v91
	v_or_b32_e32 v99, 3, v12
	v_lshl_add_u64 v[8:9], v[8:9], 0, s[12:13]
	v_lshlrev_b32_e32 v10, 3, v99
	v_mov_b32_e32 v11, v91
	s_mov_b32 s14, s3
	v_lshlrev_b64 v[8:9], 10, v[8:9]
	v_lshl_add_u64 v[10:11], v[10:11], 0, s[12:13]
	s_lshl_b32 s3, s3, 13
	v_lshlrev_b32_e32 v1, 8, v95
	v_lshl_add_u64 v[8:9], v[6:7], 0, v[8:9]
	v_lshlrev_b64 v[10:11], 10, v[10:11]
	s_and_b32 s3, s3, 0x1e000
	v_lshl_add_u64 v[6:7], v[6:7], 0, v[10:11]
	global_load_dwordx4 v[76:79], v[8:9], off
	global_load_dwordx4 v[80:83], v[6:7], off
	v_or_b32_e32 v8, s3, v1
	v_lshl_add_u64 v[6:7], s[6:7], 0, v[72:73]
	v_lshlrev_b32_e32 v8, 4, v8
	v_mov_b32_e32 v9, v91
	v_lshl_add_u64 v[10:11], v[6:7], 0, v[8:9]
	s_mov_b32 s3, 0x10000
	global_load_dwordx4 v[84:87], v[10:11], off
	global_load_dwordx4 v[100:103], v[10:11], off offset:1024
	global_load_dwordx4 v[104:107], v[10:11], off offset:2048
	global_load_dwordx4 v[108:111], v[10:11], off offset:3072
	v_or_b32_e32 v12, 0x8000, v8
	v_mov_b32_e32 v13, v91
	v_add_co_u32_e32 v10, vcc, s3, v10
	v_or_b32_e32 v8, 0x18000, v8
	v_lshl_add_u64 v[12:13], v[6:7], 0, v[12:13]
	v_addc_co_u32_e32 v11, vcc, 0, v11, vcc
	v_lshl_add_u64 v[6:7], v[6:7], 0, v[8:9]
	global_load_dwordx4 v[112:115], v[12:13], off
	global_load_dwordx4 v[116:119], v[12:13], off offset:1024
	global_load_dwordx4 v[120:123], v[12:13], off offset:2048
	global_load_dwordx4 v[124:127], v[12:13], off offset:3072
	global_load_dwordx4 v[128:131], v[10:11], off
	global_load_dwordx4 v[132:135], v[10:11], off offset:1024
	global_load_dwordx4 v[136:139], v[10:11], off offset:2048
	global_load_dwordx4 v[140:143], v[10:11], off offset:3072
	global_load_dwordx4 v[144:147], v[6:7], off
	global_load_dwordx4 v[148:151], v[6:7], off offset:1024
	global_load_dwordx4 v[152:155], v[6:7], off offset:2048
	global_load_dwordx4 v[156:159], v[6:7], off offset:3072
	v_lshl_or_b32 v66, s2, 11, v1
	s_ashr_i32 s15, s14, 31
	s_lshl_b64 s[0:1], s[14:15], 12
	v_ashrrev_i32_e32 v67, 31, v66
	v_ashrrev_i32_e32 v8, 4, v66
	v_lshl_add_u64 v[6:7], s[0:1], 0, v[66:67]
	v_lshlrev_b32_e32 v94, 2, v0
	s_lshl_b64 s[0:1], s[14:15], 8
	v_ashrrev_i32_e32 v9, 31, v8
	v_bfe_u32 v98, v0, 4, 2
	v_and_b32_e32 v1, 48, v94
	v_and_b32_e32 v67, 3, v0
	v_lshl_add_u64 v[8:9], s[0:1], 0, v[8:9]
	v_or3_b32 v6, v6, v1, v67
	v_or_b32_e32 v8, v8, v98
	v_and_b32_e32 v97, 15, v0
	v_lshlrev_b64 v[6:7], 6, v[6:7]
	v_lshlrev_b64 v[8:9], 10, v[8:9]
	v_and_b32_e32 v90, 48, v0
	v_lshlrev_b32_e32 v10, 4, v97
	s_waitcnt lgkmcnt(0)
	v_lshl_add_u64 v[8:9], s[16:17], 0, v[8:9]
	v_lshlrev_b32_e32 v1, 3, v0
	v_lshl_add_u64 v[6:7], s[10:11], 0, v[6:7]
	v_mov_b32_e32 v11, v91
	v_lshl_add_u64 v[92:93], v[8:9], 0, v[10:11]
	v_lshl_add_u64 v[62:63], v[6:7], 0, v[90:91]
	s_movk_i32 s0, 0x1000
	v_add_co_u32_e32 v14, vcc, s0, v62
	s_movk_i32 s1, 0x2000
	s_nop 0
	v_addc_co_u32_e32 v15, vcc, 0, v63, vcc
	v_add_co_u32_e32 v74, vcc, s1, v62
	global_load_dwordx4 v[160:163], v[62:63], off
	global_load_dwordx4 v[164:167], v[62:63], off offset:256
	global_load_dwordx4 v[26:29], v[62:63], off offset:512
	global_load_dwordx4 v[22:25], v[62:63], off offset:768
	global_load_dwordx4 v[42:45], v[92:93], off
	global_load_dwordx4 v[38:41], v[92:93], off offset:256
	global_load_dwordx4 v[10:13], v[92:93], off offset:512
	global_load_dwordx4 v[6:9], v[92:93], off offset:768
	v_addc_co_u32_e32 v75, vcc, 0, v63, vcc
	global_load_dwordx4 v[58:61], v[74:75], off offset:-4096
	global_load_dwordx4 v[54:57], v[14:15], off offset:256
	global_load_dwordx4 v[50:53], v[14:15], off offset:512
	global_load_dwordx4 v[46:49], v[14:15], off offset:768
	v_add_co_u32_e32 v14, vcc, s0, v92
	s_nop 1
	v_addc_co_u32_e32 v15, vcc, 0, v93, vcc
	v_add_co_u32_e32 v64, vcc, s1, v92
	s_nop 1
	v_addc_co_u32_e32 v65, vcc, 0, v93, vcc
	global_load_dwordx4 v[34:37], v[64:65], off offset:-4096
	global_load_dwordx4 v[30:33], v[14:15], off offset:256
	global_load_dwordx4 v[18:21], v[14:15], off offset:512
	s_nop 0
	global_load_dwordx4 v[14:17], v[14:15], off offset:768
	s_waitcnt vmcnt(31)
	v_mfma_f32_16x16x32_f16 v[84:87], v[84:87], v[2:5], 0
	v_lshl_or_b32 v73, v95, 12, v72
	s_mov_b32 s0, 0xc3e00000
	s_waitcnt vmcnt(27)
	v_mfma_f32_16x16x32_f16 v[112:115], v[112:115], v[2:5], 0
	s_waitcnt vmcnt(23)
	v_mfma_f32_16x16x32_f16 v[128:131], v[128:131], v[2:5], 0
	s_waitcnt vmcnt(19)
	v_mfma_f32_16x16x32_f16 v[2:5], v[144:147], v[2:5], 0
	v_mfma_f32_16x16x32_f16 v[84:87], v[100:103], v[68:71], v[84:87]
	v_mfma_f32_16x16x32_f16 v[100:103], v[116:119], v[68:71], v[112:115]
	v_mfma_f32_16x16x32_f16 v[112:115], v[132:135], v[68:71], v[128:131]
	s_waitcnt vmcnt(18)
	v_mfma_f32_16x16x32_f16 v[2:5], v[148:151], v[68:71], v[2:5]
	v_mfma_f32_16x16x32_f16 v[68:71], v[104:107], v[76:79], v[84:87]
	v_mfma_f32_16x16x32_f16 v[84:87], v[120:123], v[76:79], v[100:103]
	v_mfma_f32_16x16x32_f16 v[100:103], v[136:139], v[76:79], v[112:115]
	s_waitcnt vmcnt(17)
	v_mfma_f32_16x16x32_f16 v[2:5], v[152:155], v[76:79], v[2:5]
	v_mfma_f32_16x16x32_f16 v[68:71], v[108:111], v[80:83], v[68:71]
	s_waitcnt vmcnt(16)
	v_mfma_f32_16x16x32_f16 v[2:5], v[156:159], v[80:83], v[2:5]
	s_nop 5
	ds_write_b128 v73, v[68:71]
	v_mfma_f32_16x16x32_f16 v[68:71], v[124:127], v[80:83], v[84:87]
	v_lshl_or_b32 v73, v88, 10, v72
	s_nop 6
	ds_write_b128 v73, v[68:71]
	v_mfma_f32_16x16x32_f16 v[68:71], v[140:143], v[80:83], v[100:103]
	v_lshl_or_b32 v73, v89, 10, v72
	v_lshrrev_b32_e32 v80, 5, v0
	v_or_b32_e32 v78, 0x400, v80
	v_or_b32_e32 v81, 0x500, v80
	v_or_b32_e32 v83, 0x600, v80
	s_nop 2
	ds_write_b128 v73, v[68:71]
	v_lshl_or_b32 v68, v99, 10, v72
	ds_write_b128 v68, v[2:5]
	v_and_b32_e32 v2, 0x70, v94
	v_or_b32_e32 v4, 0x80, v2
	v_or_b32_e32 v68, 0x100, v80
	v_or_b32_e32 v70, 0x200, v80
	v_or_b32_e32 v72, 0x300, v80
	v_or_b32_e32 v85, 0x700, v80
	v_lshlrev_b32_e32 v3, 2, v67
	v_or_b32_e32 v5, v2, v80
	v_or_b32_e32 v69, v2, v68
	v_or_b32_e32 v68, v4, v68
	v_or_b32_e32 v71, v2, v70
	v_or_b32_e32 v70, v4, v70
	v_or_b32_e32 v73, v2, v72
	v_or_b32_e32 v79, v2, v78
	v_or_b32_e32 v82, v2, v81
	v_or_b32_e32 v84, v2, v83
	v_or_b32_e32 v2, v2, v85
	v_lshl_or_b32 v5, v5, 4, v3
	v_or_b32_e32 v67, v4, v80
	v_lshl_or_b32 v69, v69, 4, v3
	v_lshl_or_b32 v68, v68, 4, v3
	v_lshl_or_b32 v71, v71, 4, v3
	v_lshl_or_b32 v70, v70, 4, v3
	v_or_b32_e32 v72, v4, v72
	v_or_b32_e32 v78, v4, v78
	v_or_b32_e32 v81, v4, v81
	v_or_b32_e32 v83, v4, v83
	v_lshl_or_b32 v86, v2, 4, v3
	v_or_b32_e32 v2, v4, v85
	v_lshl_or_b32 v67, v67, 4, v3
	v_lshl_or_b32 v73, v73, 4, v3
	v_lshl_or_b32 v72, v72, 4, v3
	v_lshl_or_b32 v79, v79, 4, v3
	v_lshl_or_b32 v78, v78, 4, v3
	v_lshl_or_b32 v82, v82, 4, v3
	v_lshl_or_b32 v81, v81, 4, v3
	v_lshl_or_b32 v84, v84, 4, v3
	v_lshl_or_b32 v83, v83, 4, v3
	v_lshl_or_b32 v85, v2, 4, v3
	s_waitcnt lgkmcnt(0)
	s_barrier
	ds_read_b32 v2, v5
	ds_read_b32 v3, v67
	ds_read_b32 v4, v69
	ds_read_b32 v5, v68
	ds_read_b32 v68, v71
	ds_read_b32 v69, v70
	ds_read_b32 v70, v73
	ds_read_b32 v71, v72
	s_waitcnt lgkmcnt(6)
	v_pk_add_f32 v[2:3], v[2:3], 0 op_sel_hi:[1,0]
	v_or_b32_e32 v101, 0xff0, v0
	s_waitcnt lgkmcnt(4)
	v_pk_add_f32 v[2:3], v[2:3], v[4:5]
	s_waitcnt lgkmcnt(2)
	v_pk_add_f32 v[2:3], v[2:3], v[68:69]
	ds_read_b32 v4, v79
	ds_read_b32 v5, v78
	ds_read_b32 v68, v82
	ds_read_b32 v69, v81
	ds_read_b32 v72, v84
	ds_read_b32 v73, v83
	ds_read_b32 v78, v86
	ds_read_b32 v79, v85
	s_waitcnt lgkmcnt(8)
	v_pk_add_f32 v[2:3], v[2:3], v[70:71]
	s_waitcnt lgkmcnt(6)
	v_pk_add_f32 v[2:3], v[2:3], v[4:5]
	s_waitcnt lgkmcnt(4)
	v_pk_add_f32 v[2:3], v[2:3], v[68:69]
	s_waitcnt lgkmcnt(2)
	v_pk_add_f32 v[2:3], v[2:3], v[72:73]
	s_waitcnt lgkmcnt(0)
	v_pk_add_f32 v[2:3], v[2:3], v[78:79]
	s_waitcnt vmcnt(16)
	v_pk_mul_f32 v[4:5], v[170:171], v[2:3]
	v_pk_mul_f32 v[2:3], v[170:171], v[2:3] op_sel:[0,1] op_sel_hi:[1,0]
	v_sub_f32_e32 v4, v4, v5
	v_add_f32_e32 v2, v2, v3
	v_add_f32_e32 v4, v4, v4
	v_mov_b32_e32 v5, 0x43e00000
	v_add_f32_e32 v2, v2, v2
	v_med3_f32 v4, v4, s0, v5
	v_med3_f32 v2, v2, s0, v5
	v_mov_b32_e32 v3, v91
	v_cvt_pk_fp8_f32 v3, v4, v2
	v_lshlrev_b32_e32 v2, 1, v0
	v_and_b32_e32 v2, 62, v2
	v_lshl_or_b32 v2, v80, 6, v2
	ds_write_b16 v2, v3 offset:32768
	v_lshl_or_b32 v2, v97, 6, v90
	s_waitcnt lgkmcnt(0)
	s_barrier
	ds_read_b128 v[2:5], v2 offset:32768
	s_waitcnt vmcnt(12) lgkmcnt(0)
	v_mfma_f32_16x16x32_fp8_fp8 v[68:71], v[160:161], v[2:3], 0
	v_or_b32_e32 v90, v66, v90
	v_mbcnt_lo_u32_b32 v66, -1, 0
	v_mfma_f32_16x16x32_fp8_fp8 v[76:79], v[162:163], v[4:5], v[68:71]
	v_mfma_f32_16x16x32_fp8_fp8 v[68:71], v[164:165], v[2:3], 0
	v_mfma_f32_16x16x32_fp8_fp8 v[80:83], v[166:167], v[4:5], v[68:71]
	s_nop 6
	v_mbcnt_hi_u32_b32 v70, -1, v66
	v_mfma_f32_16x16x32_fp8_fp8 v[66:69], v[26:27], v[2:3], 0
	v_and_b32_e32 v27, 64, v70
	v_xor_b32_e32 v26, 16, v70
	v_add_u32_e32 v71, 64, v27
	v_cmp_lt_i32_e32 vcc, v26, v71
	v_mfma_f32_16x16x32_fp8_fp8 v[84:87], v[28:29], v[4:5], v[66:69]
	s_nop 0
	v_cndmask_b32_e32 v26, v70, v26, vcc
	v_lshlrev_b32_e32 v99, 2, v26
	v_mfma_f32_16x16x32_fp8_fp8 v[26:29], v[22:23], v[2:3], 0
	v_xor_b32_e32 v66, 32, v70
	v_cmp_lt_i32_e32 vcc, v66, v71
	v_mfma_f32_16x16x32_fp8_fp8 v[104:107], v[24:25], v[4:5], v[26:29]
	s_nop 0
	v_cndmask_b32_e32 v22, v70, v66, vcc
	v_lshlrev_b32_e32 v100, 2, v22
	global_load_dwordx4 v[70:73], v[74:75], off
	global_load_dwordx4 v[66:69], v[74:75], off offset:256
	global_load_dwordx4 v[26:29], v[74:75], off offset:512
	global_load_dwordx4 v[22:25], v[74:75], off offset:768
	v_mul_f32_e32 v74, 0x3d800000, v76
	v_mov_b32_e32 v102, 0xff800000
	v_cmp_le_i32_e32 vcc, v90, v101
	v_mul_f32_e32 v75, 0x3d800000, v77
	v_mul_f32_e32 v77, 0x3d800000, v78
	v_cndmask_b32_e32 v74, v102, v74, vcc
	v_cmp_lt_i32_e32 vcc, v90, v101
	v_or_b32_e32 v78, 2, v90
	v_mul_f32_e32 v80, 0x3d800000, v80
	v_cndmask_b32_e32 v75, v102, v75, vcc
	v_cmp_le_i32_e32 vcc, v78, v101
	v_mul_f32_e32 v78, 0x3d800000, v79
	v_or_b32_e32 v79, 3, v90
	v_cndmask_b32_e32 v77, v102, v77, vcc
	v_cmp_le_i32_e32 vcc, v79, v101
	v_or_b32_e32 v79, 4, v90
	v_mul_f32_e32 v84, 0x3d800000, v84
	v_cndmask_b32_e32 v78, v102, v78, vcc
	v_cmp_le_i32_e32 vcc, v79, v101
	s_mov_b32 s0, 0xff800000
	v_max3_f32 v76, v74, s0, v75
	v_cndmask_b32_e32 v79, v102, v80, vcc
	v_mul_f32_e32 v80, 0x3d800000, v81
	v_or_b32_e32 v81, 5, v90
	v_cmp_le_i32_e32 vcc, v81, v101
	v_mul_f32_e32 v81, 0x3d800000, v82
	v_or_b32_e32 v82, 6, v90
	v_cndmask_b32_e32 v80, v102, v80, vcc
	v_cmp_le_i32_e32 vcc, v82, v101
	v_mul_f32_e32 v82, 0x3d800000, v83
	v_or_b32_e32 v83, 7, v90
	v_cndmask_b32_e32 v81, v102, v81, vcc
	v_cmp_le_i32_e32 vcc, v83, v101
	v_or_b32_e32 v83, 8, v90
	v_max3_f32 v76, v76, v77, v78
	v_cndmask_b32_e32 v82, v102, v82, vcc
	v_cmp_le_i32_e32 vcc, v83, v101
	v_max3_f32 v76, v76, v79, v80
	v_mul_f32_e32 v88, 0x3d800000, v104
	v_cndmask_b32_e32 v83, v102, v84, vcc
	v_mul_f32_e32 v84, 0x3d800000, v85
	v_or_b32_e32 v85, 9, v90
	v_cmp_le_i32_e32 vcc, v85, v101
	v_mul_f32_e32 v85, 0x3d800000, v86
	v_or_b32_e32 v86, 10, v90
	v_cndmask_b32_e32 v84, v102, v84, vcc
	v_cmp_le_i32_e32 vcc, v86, v101
	v_mul_f32_e32 v86, 0x3d800000, v87
	v_or_b32_e32 v87, 11, v90
	v_cndmask_b32_e32 v85, v102, v85, vcc
	v_cmp_le_i32_e32 vcc, v87, v101
	v_or_b32_e32 v87, 12, v90
	v_or_b32_e32 v89, 13, v90
	v_cndmask_b32_e32 v86, v102, v86, vcc
	v_cmp_le_i32_e32 vcc, v87, v101
	v_max3_f32 v76, v76, v81, v82
	v_or_b32_e32 v103, 14, v90
	v_cndmask_b32_e32 v87, v102, v88, vcc
	v_mul_f32_e32 v88, 0x3d800000, v105
	v_cmp_le_i32_e32 vcc, v89, v101
	v_max3_f32 v76, v76, v83, v84
	v_mul_f32_e32 v89, 0x3d800000, v106
	v_cndmask_b32_e32 v88, v102, v88, vcc
	v_cmp_le_i32_e32 vcc, v103, v101
	v_or_b32_e32 v104, 15, v90
	v_max3_f32 v76, v76, v85, v86
	v_cndmask_b32_e32 v89, v102, v89, vcc
	v_mul_f32_e32 v103, 0x3d800000, v107
	v_cmp_le_i32_e32 vcc, v104, v101
	v_max3_f32 v76, v76, v87, v88
	s_mov_b32 s1, 0xf149f2ca
	v_cndmask_b32_e32 v103, v102, v103, vcc
	v_max3_f32 v76, v76, v89, v103
	ds_bpermute_b32 v104, v99, v76
	s_waitcnt lgkmcnt(0)
	v_max_f32_e32 v104, v104, v104
	v_max_f32_e32 v76, v76, v104
	ds_bpermute_b32 v104, v100, v76
	s_waitcnt lgkmcnt(0)
	v_max3_f32 v118, v76, v104, s1
	v_sub_f32_e32 v74, v74, v118
	v_mul_f32_e32 v74, 0x3fb8aa3b, v74
	v_exp_f32_e32 v108, v74
	v_sub_f32_e32 v74, v75, v118
	v_mul_f32_e32 v74, 0x3fb8aa3b, v74
	v_exp_f32_e32 v109, v74
	v_sub_f32_e32 v74, v77, v118
	v_mul_f32_e32 v74, 0x3fb8aa3b, v74
	v_exp_f32_e32 v110, v74
	v_sub_f32_e32 v74, v78, v118
	v_mul_f32_e32 v74, 0x3fb8aa3b, v74
	v_exp_f32_e32 v111, v74
	v_sub_f32_e32 v74, v79, v118
	v_mul_f32_e32 v74, 0x3fb8aa3b, v74
	v_exp_f32_e32 v112, v74
	v_sub_f32_e32 v74, v80, v118
	v_mul_f32_e32 v74, 0x3fb8aa3b, v74
	v_exp_f32_e32 v113, v74
	v_sub_f32_e32 v74, v81, v118
	v_mul_f32_e32 v74, 0x3fb8aa3b, v74
	v_exp_f32_e32 v114, v74
	v_sub_f32_e32 v74, v82, v118
	v_mul_f32_e32 v74, 0x3fb8aa3b, v74
	v_exp_f32_e32 v115, v74
	v_sub_f32_e32 v74, v83, v118
	v_mul_f32_e32 v74, 0x3fb8aa3b, v74
	v_exp_f32_e32 v116, v74
	v_sub_f32_e32 v74, v84, v118
	v_mul_f32_e32 v74, 0x3fb8aa3b, v74
	v_exp_f32_e32 v117, v74
	v_sub_f32_e32 v74, v85, v118
	v_mul_f32_e32 v74, 0x3fb8aa3b, v74
	v_exp_f32_e32 v119, v74
	v_sub_f32_e32 v74, v86, v118
	v_mul_f32_e32 v74, 0x3fb8aa3b, v74
	v_exp_f32_e32 v120, v74
	v_sub_f32_e32 v74, v87, v118
	v_mul_f32_e32 v74, 0x3fb8aa3b, v74
	v_exp_f32_e32 v121, v74
	v_sub_f32_e32 v74, v88, v118
	v_mul_f32_e32 v74, 0x3fb8aa3b, v74
	v_mov_b32_e32 v86, v91
	v_mov_b32_e32 v87, v91
	v_sub_f32_e32 v76, 0xf149f2ca, v118
	v_exp_f32_e32 v122, v74
	v_sub_f32_e32 v74, v89, v118
	v_cvt_pk_fp8_f32 v86, v108, v109
	v_cvt_pk_fp8_f32 v87, v112, v113
	v_mul_f32_e32 v76, 0x3fb8aa3b, v76
	v_mul_f32_e32 v74, 0x3fb8aa3b, v74
	v_exp_f32_e32 v123, v74
	v_sub_f32_e32 v74, v103, v118
	v_exp_f32_e32 v124, v76
	v_mul_f32_e32 v74, 0x3fb8aa3b, v74
	v_mov_b32_e32 v88, v91
	v_mov_b32_e32 v89, v91
	v_exp_f32_e32 v103, v74
	v_cvt_pk_fp8_f32 v88, v116, v117
	v_cvt_pk_fp8_f32 v86, v110, v111 op_sel:[0,0,1]
	v_cvt_pk_fp8_f32 v87, v114, v115 op_sel:[0,0,1]
	v_cvt_pk_fp8_f32 v89, v121, v122
	v_mul_f32_e32 v74, 0, v124
	v_mov_b32_e32 v75, v74
	v_mov_b32_e32 v76, v74
	v_mov_b32_e32 v77, v74
	v_cvt_pk_fp8_f32 v88, v119, v120 op_sel:[0,0,1]
	v_cvt_pk_fp8_f32 v89, v123, v103 op_sel:[0,0,1]
	s_waitcnt vmcnt(12)
	v_mfma_f32_16x16x32_fp8_fp8 v[78:81], v[42:43], v[86:87], v[74:77]
	s_nop 0
	v_mfma_f32_16x16x32_fp8_fp8 v[104:107], v[44:45], v[88:89], v[78:81]
	v_mfma_f32_16x16x32_fp8_fp8 v[42:45], v[38:39], v[86:87], v[74:77]
	v_add_f32_e32 v38, 0, v108
	v_add_f32_e32 v38, v38, v109
	v_mfma_f32_16x16x32_fp8_fp8 v[78:81], v[40:41], v[88:89], v[42:45]
	s_nop 4
	v_add_f32_e32 v42, v38, v110
	v_mfma_f32_16x16x32_fp8_fp8 v[38:41], v[10:11], v[86:87], v[74:77]
	v_add_f32_e32 v10, v42, v111
	v_add_f32_e32 v10, v10, v112
	v_add_f32_e32 v10, v10, v113
	v_add_f32_e32 v10, v10, v114
	v_add_f32_e32 v10, v10, v115
	v_mfma_f32_16x16x32_fp8_fp8 v[82:85], v[12:13], v[88:89], v[38:41]
	s_nop 2
	v_add_f32_e32 v38, v10, v116
	v_mfma_f32_16x16x32_fp8_fp8 v[10:13], v[6:7], v[86:87], v[74:77]
	v_add_f32_e32 v6, v38, v117
	v_add_f32_e32 v6, v6, v119
	v_add_f32_e32 v6, v6, v120
	v_add_f32_e32 v6, v6, v121
	v_add_f32_e32 v6, v6, v122
	v_add_f32_e32 v6, v6, v123
	v_add_f32_e32 v119, v6, v103
	v_mfma_f32_16x16x32_fp8_fp8 v[86:89], v[8:9], v[88:89], v[10:13]
	v_fmac_f32_e32 v119, 0, v124
	global_load_dwordx4 v[42:45], v[64:65], off
	global_load_dwordx4 v[38:41], v[64:65], off offset:256
	global_load_dwordx4 v[10:13], v[64:65], off offset:512
	global_load_dwordx4 v[6:9], v[64:65], off offset:768
	s_waitcnt vmcnt(12)
	v_mfma_f32_16x16x32_fp8_fp8 v[74:77], v[58:59], v[2:3], 0
	v_mfma_f32_16x16x32_fp8_fp8 v[74:77], v[60:61], v[4:5], v[74:77]
	v_mfma_f32_16x16x32_fp8_fp8 v[58:61], v[54:55], v[2:3], 0
	v_mfma_f32_16x16x32_fp8_fp8 v[54:57], v[56:57], v[4:5], v[58:61]
	v_mfma_f32_16x16x32_fp8_fp8 v[58:61], v[50:51], v[2:3], 0
	v_mfma_f32_16x16x32_fp8_fp8 v[108:111], v[52:53], v[4:5], v[58:61]
	v_mfma_f32_16x16x32_fp8_fp8 v[50:53], v[46:47], v[2:3], 0
	v_mfma_f32_16x16x32_fp8_fp8 v[112:115], v[48:49], v[4:5], v[50:53]
	s_movk_i32 s1, 0x3000
	v_add_co_u32_e32 v116, vcc, s1, v62
	s_nop 1
	v_addc_co_u32_e32 v117, vcc, 0, v63, vcc
	global_load_dwordx4 v[62:65], v[116:117], off
	global_load_dwordx4 v[58:61], v[116:117], off offset:256
	global_load_dwordx4 v[50:53], v[116:117], off offset:512
	global_load_dwordx4 v[46:49], v[116:117], off offset:768
	v_or_b32_e32 v103, 64, v90
	v_mul_f32_e32 v74, 0x3d800000, v74
	v_cmp_le_i32_e32 vcc, v103, v101
	v_or_b32_e32 v103, 0x41, v90
	v_mul_f32_e32 v75, 0x3d800000, v75
	v_cndmask_b32_e32 v74, v102, v74, vcc
	v_cmp_le_i32_e32 vcc, v103, v101
	v_or_b32_e32 v116, 0x42, v90
	v_mul_f32_e32 v76, 0x3d800000, v76
	v_cndmask_b32_e32 v75, v102, v75, vcc
	v_cmp_le_i32_e32 vcc, v116, v101
	v_or_b32_e32 v116, 0x43, v90
	v_mul_f32_e32 v77, 0x3d800000, v77
	v_cndmask_b32_e32 v76, v102, v76, vcc
	v_cmp_le_i32_e32 vcc, v116, v101
	v_or_b32_e32 v116, 0x44, v90
	v_mul_f32_e32 v54, 0x3d800000, v54
	v_cndmask_b32_e32 v77, v102, v77, vcc
	v_cmp_le_i32_e32 vcc, v116, v101
	v_or_b32_e32 v116, 0x45, v90
	v_mul_f32_e32 v55, 0x3d800000, v55
	v_cndmask_b32_e32 v54, v102, v54, vcc
	v_cmp_le_i32_e32 vcc, v116, v101
	v_or_b32_e32 v116, 0x46, v90
	v_mul_f32_e32 v56, 0x3d800000, v56
	v_cndmask_b32_e32 v55, v102, v55, vcc
	v_cmp_le_i32_e32 vcc, v116, v101
	v_or_b32_e32 v116, 0x47, v90
	v_mul_f32_e32 v57, 0x3d800000, v57
	v_cndmask_b32_e32 v56, v102, v56, vcc
	v_cmp_le_i32_e32 vcc, v116, v101
	v_or_b32_e32 v116, 0x48, v90
	v_mul_f32_e32 v108, 0x3d800000, v108
	v_cndmask_b32_e32 v57, v102, v57, vcc
	v_cmp_le_i32_e32 vcc, v116, v101
	v_or_b32_e32 v116, 0x49, v90
	v_mul_f32_e32 v109, 0x3d800000, v109
	v_cndmask_b32_e32 v108, v102, v108, vcc
	v_cmp_le_i32_e32 vcc, v116, v101
	v_or_b32_e32 v116, 0x4a, v90
	v_max3_f32 v103, v74, s0, v75
	v_cndmask_b32_e32 v109, v102, v109, vcc
	v_mul_f32_e32 v110, 0x3d800000, v110
	v_cmp_le_i32_e32 vcc, v116, v101
	v_or_b32_e32 v116, 0x4b, v90
	v_max3_f32 v103, v103, v76, v77
	v_cndmask_b32_e32 v110, v102, v110, vcc
	v_mul_f32_e32 v111, 0x3d800000, v111
	v_cmp_le_i32_e32 vcc, v116, v101
	v_or_b32_e32 v116, 0x4c, v90
	v_max3_f32 v103, v103, v54, v55
	v_cndmask_b32_e32 v111, v102, v111, vcc
	v_mul_f32_e32 v112, 0x3d800000, v112
	v_cmp_le_i32_e32 vcc, v116, v101
	v_or_b32_e32 v116, 0x4d, v90
	v_max3_f32 v103, v103, v56, v57
	v_cndmask_b32_e32 v112, v102, v112, vcc
	v_mul_f32_e32 v113, 0x3d800000, v113
	v_cmp_le_i32_e32 vcc, v116, v101
	v_or_b32_e32 v116, 0x4e, v90
	v_max3_f32 v103, v103, v108, v109
	v_cndmask_b32_e32 v113, v102, v113, vcc
	v_mul_f32_e32 v114, 0x3d800000, v114
	v_cmp_le_i32_e32 vcc, v116, v101
	v_or_b32_e32 v116, 0x4f, v90
	v_max3_f32 v103, v103, v110, v111
	v_cndmask_b32_e32 v114, v102, v114, vcc
	v_mul_f32_e32 v115, 0x3d800000, v115
	v_cmp_le_i32_e32 vcc, v116, v101
	v_max3_f32 v103, v103, v112, v113
	s_nop 0
	v_cndmask_b32_e32 v115, v102, v115, vcc
	v_max3_f32 v103, v103, v114, v115
	ds_bpermute_b32 v116, v99, v103
	s_waitcnt lgkmcnt(0)
	v_max_f32_e32 v116, v116, v116
	v_max_f32_e32 v103, v103, v116
	ds_bpermute_b32 v116, v100, v103
	s_waitcnt lgkmcnt(0)
	v_max3_f32 v103, v118, v103, v116
	v_sub_f32_e32 v54, v54, v103
	v_mul_f32_e32 v54, 0x3fb8aa3b, v54
	v_exp_f32_e32 v122, v54
	v_sub_f32_e32 v54, v55, v103
	v_mul_f32_e32 v54, 0x3fb8aa3b, v54
	v_exp_f32_e32 v123, v54
	v_sub_f32_e32 v54, v56, v103
	v_mul_f32_e32 v54, 0x3fb8aa3b, v54
	v_exp_f32_e32 v124, v54
	v_sub_f32_e32 v54, v57, v103
	v_mul_f32_e32 v54, 0x3fb8aa3b, v54
	v_exp_f32_e32 v125, v54
	v_sub_f32_e32 v54, v108, v103
	v_mul_f32_e32 v54, 0x3fb8aa3b, v54
	v_exp_f32_e32 v126, v54
	v_sub_f32_e32 v54, v109, v103
	v_mul_f32_e32 v54, 0x3fb8aa3b, v54
	v_sub_f32_e32 v74, v74, v103
	v_exp_f32_e32 v127, v54
	v_sub_f32_e32 v54, v110, v103
	v_mul_f32_e32 v74, 0x3fb8aa3b, v74
	v_mul_f32_e32 v54, 0x3fb8aa3b, v54
	v_exp_f32_e32 v117, v74
	v_sub_f32_e32 v74, v75, v103
	v_exp_f32_e32 v128, v54
	v_sub_f32_e32 v54, v111, v103
	v_mul_f32_e32 v74, 0x3fb8aa3b, v74
	v_mul_f32_e32 v54, 0x3fb8aa3b, v54
	v_sub_f32_e32 v116, v118, v103
	v_exp_f32_e32 v118, v74
	v_sub_f32_e32 v74, v76, v103
	v_exp_f32_e32 v129, v54
	v_sub_f32_e32 v54, v112, v103
	v_mul_f32_e32 v74, 0x3fb8aa3b, v74
	v_mul_f32_e32 v54, 0x3fb8aa3b, v54
	v_exp_f32_e32 v120, v74
	v_sub_f32_e32 v74, v77, v103
	v_exp_f32_e32 v130, v54
	v_sub_f32_e32 v54, v113, v103
	v_mul_f32_e32 v74, 0x3fb8aa3b, v74
	v_mul_f32_e32 v54, 0x3fb8aa3b, v54
	v_mov_b32_e32 v108, v91
	v_mov_b32_e32 v109, v91
	v_exp_f32_e32 v121, v74
	v_exp_f32_e32 v113, v54
	v_sub_f32_e32 v54, v114, v103
	v_cvt_pk_fp8_f32 v108, v117, v118
	v_cvt_pk_fp8_f32 v109, v122, v123
	v_mul_f32_e32 v54, 0x3fb8aa3b, v54
	v_mul_f32_e32 v116, 0x3fb8aa3b, v116
	v_exp_f32_e32 v114, v54
	v_sub_f32_e32 v54, v115, v103
	v_mul_f32_e32 v54, 0x3fb8aa3b, v54
	v_mov_b32_e32 v110, v91
	v_exp_f32_e32 v112, v116
	v_mov_b32_e32 v111, v91
	v_exp_f32_e32 v115, v54
	v_cvt_pk_fp8_f32 v110, v126, v127
	v_cvt_pk_fp8_f32 v108, v120, v121 op_sel:[0,0,1]
	v_cvt_pk_fp8_f32 v109, v124, v125 op_sel:[0,0,1]
	v_cvt_pk_fp8_f32 v111, v130, v113
	v_pk_mul_f32 v[56:57], v[112:113], v[106:107] op_sel_hi:[0,1]
	v_pk_mul_f32 v[54:55], v[112:113], v[104:105] op_sel_hi:[0,1]
	v_cvt_pk_fp8_f32 v110, v128, v129 op_sel:[0,0,1]
	v_cvt_pk_fp8_f32 v111, v114, v115 op_sel:[0,0,1]
	s_waitcnt vmcnt(12)
	v_mfma_f32_16x16x32_fp8_fp8 v[54:57], v[34:35], v[108:109], v[54:57]
	v_mul_f32_e64 v34, v112, v78
	v_mul_f32_e64 v35, v112, v79
	v_mfma_f32_16x16x32_fp8_fp8 v[74:77], v[36:37], v[110:111], v[54:57]
	v_mul_f32_e64 v36, v112, v80
	v_mul_f32_e64 v37, v112, v81
	s_nop 2
	v_add_f32_e32 v54, 0, v117
	v_mfma_f32_16x16x32_fp8_fp8 v[34:37], v[30:31], v[108:109], v[34:37]
	v_add_f32_e32 v30, v54, v118
	v_add_f32_e32 v30, v30, v120
	v_add_f32_e32 v30, v30, v121
	v_mfma_f32_16x16x32_fp8_fp8 v[78:81], v[32:33], v[110:111], v[34:37]
	v_mul_f32_e64 v32, v112, v84
	v_mul_f32_e64 v33, v112, v85
	s_nop 1
	v_add_f32_e32 v34, v30, v122
	v_pk_mul_f32 v[30:31], v[112:113], v[82:83] op_sel_hi:[0,1]
	s_nop 1
	v_mfma_f32_16x16x32_fp8_fp8 v[30:33], v[18:19], v[108:109], v[30:33]
	v_add_f32_e32 v18, v34, v123
	v_add_f32_e32 v18, v18, v124
	v_add_f32_e32 v18, v18, v125
	v_mfma_f32_16x16x32_fp8_fp8 v[82:85], v[20:21], v[110:111], v[30:33]
	v_mul_f32_e64 v20, v112, v88
	v_mul_f32_e64 v21, v112, v89
	s_nop 1
	v_add_f32_e32 v30, v18, v126
	v_pk_mul_f32 v[18:19], v[112:113], v[86:87] op_sel_hi:[0,1]
	s_nop 1
	v_mfma_f32_16x16x32_fp8_fp8 v[18:21], v[14:15], v[108:109], v[18:21]
	v_add_f32_e32 v14, v30, v127
	v_add_f32_e32 v14, v14, v128
	v_add_f32_e32 v14, v14, v129
	v_add_f32_e32 v14, v14, v130
	v_add_f32_e32 v14, v14, v113
	v_add_f32_e32 v14, v14, v114
	v_add_f32_e32 v86, v14, v115
	v_mfma_f32_16x16x32_fp8_fp8 v[54:57], v[16:17], v[110:111], v[18:21]
	v_fmac_f32_e32 v86, v119, v112
	v_add_co_u32_e32 v88, vcc, s1, v92
	s_nop 1
	v_addc_co_u32_e32 v89, vcc, 0, v93, vcc
	global_load_dwordx4 v[34:37], v[88:89], off
	global_load_dwordx4 v[30:33], v[88:89], off offset:256
	global_load_dwordx4 v[18:21], v[88:89], off offset:512
	global_load_dwordx4 v[14:17], v[88:89], off offset:768
	s_waitcnt vmcnt(15)
	v_mfma_f32_16x16x32_fp8_fp8 v[104:107], v[70:71], v[2:3], 0
	v_or_b32_e32 v93, 0x81, v90
	v_or_b32_e32 v108, 0x86, v90
	v_or_b32_e32 v109, 0x87, v90
	v_mfma_f32_16x16x32_fp8_fp8 v[70:73], v[72:73], v[4:5], v[104:107]
	v_or_b32_e32 v110, 0x88, v90
	v_or_b32_e32 v111, 0x89, v90
	v_or_b32_e32 v112, 0x8a, v90
	s_waitcnt vmcnt(14)
	v_mfma_f32_16x16x32_fp8_fp8 v[104:107], v[66:67], v[2:3], 0
	v_or_b32_e32 v113, 0x8b, v90
	s_nop 1
	v_mul_f32_e32 v70, 0x3d800000, v70
	v_mul_f32_e32 v71, 0x3d800000, v71
	v_mfma_f32_16x16x32_fp8_fp8 v[66:69], v[68:69], v[4:5], v[104:107]
	v_mul_f32_e32 v72, 0x3d800000, v72
	v_mul_f32_e32 v73, 0x3d800000, v73
	v_or_b32_e32 v114, 0x8c, v90
	s_waitcnt vmcnt(13)
	v_mfma_f32_16x16x32_fp8_fp8 v[104:107], v[26:27], v[2:3], 0
	v_or_b32_e32 v115, 0x8d, v90
	s_nop 1
	v_mul_f32_e32 v87, 0x3d800000, v66
	v_mul_f32_e32 v88, 0x3d800000, v67
	v_mul_f32_e32 v89, 0x3d800000, v68
	v_mul_f32_e32 v92, 0x3d800000, v69
	s_waitcnt vmcnt(12)
	v_mfma_f32_16x16x32_fp8_fp8 v[66:69], v[22:23], v[2:3], 0
	v_or_b32_e32 v116, 0x8e, v90
	v_or_b32_e32 v117, 0x8f, v90
	v_mfma_f32_16x16x32_fp8_fp8 v[22:25], v[24:25], v[4:5], v[66:69]
	v_mfma_f32_16x16x32_fp8_fp8 v[26:29], v[28:29], v[4:5], v[104:107]
	s_nop 2
	v_or_b32_e32 v104, 0x82, v90
	s_nop 2
	v_mul_f32_e32 v66, 0x3d800000, v22
	v_mul_f32_e32 v67, 0x3d800000, v23
	v_mul_f32_e32 v68, 0x3d800000, v24
	v_mul_f32_e32 v69, 0x3d800000, v25
	s_waitcnt vmcnt(7)
	v_mfma_f32_16x16x32_fp8_fp8 v[22:25], v[62:63], v[2:3], 0
	v_or_b32_e32 v105, 0x83, v90
	v_or_b32_e32 v106, 0x84, v90
	v_or_b32_e32 v107, 0x85, v90
	v_mfma_f32_16x16x32_fp8_fp8 v[62:65], v[64:65], v[4:5], v[22:25]
	v_mul_f32_e32 v26, 0x3d800000, v26
	v_mul_f32_e32 v27, 0x3d800000, v27
	v_mul_f32_e32 v28, 0x3d800000, v28
	s_waitcnt vmcnt(6)
	v_mfma_f32_16x16x32_fp8_fp8 v[22:25], v[58:59], v[2:3], 0
	v_or_b32_e32 v58, 0x80, v90
	v_cmp_le_i32_e32 vcc, v58, v101
	v_mul_f32_e32 v29, 0x3d800000, v29
	v_mfma_f32_16x16x32_fp8_fp8 v[58:61], v[60:61], v[4:5], v[22:25]
	v_cndmask_b32_e32 v70, v102, v70, vcc
	v_cmp_le_i32_e32 vcc, v93, v101
	s_waitcnt vmcnt(5)
	v_mfma_f32_16x16x32_fp8_fp8 v[22:25], v[50:51], v[2:3], 0
	v_cndmask_b32_e32 v71, v102, v71, vcc
	v_cmp_le_i32_e32 vcc, v104, v101
	v_max3_f32 v50, v70, s0, v71
	s_nop 0
	v_cndmask_b32_e32 v72, v102, v72, vcc
	v_cmp_le_i32_e32 vcc, v105, v101
	s_nop 1
	v_cndmask_b32_e32 v73, v102, v73, vcc
	v_cmp_le_i32_e32 vcc, v106, v101
	v_max3_f32 v50, v50, v72, v73
	s_nop 0
	v_cndmask_b32_e32 v87, v102, v87, vcc
	v_cmp_le_i32_e32 vcc, v107, v101
	s_nop 1
	v_cndmask_b32_e32 v88, v102, v88, vcc
	v_cmp_le_i32_e32 vcc, v108, v101
	v_max3_f32 v50, v50, v87, v88
	s_nop 0
	v_cndmask_b32_e32 v89, v102, v89, vcc
	v_cmp_le_i32_e32 vcc, v109, v101
	s_nop 1
	v_cndmask_b32_e32 v92, v102, v92, vcc
	v_cmp_le_i32_e32 vcc, v110, v101
	v_max3_f32 v50, v50, v89, v92
	s_nop 0
	v_cndmask_b32_e32 v93, v102, v26, vcc
	v_cmp_le_i32_e32 vcc, v111, v101
	s_nop 1
	v_cndmask_b32_e32 v27, v102, v27, vcc
	v_cmp_le_i32_e32 vcc, v112, v101
	v_max3_f32 v26, v50, v93, v27
	v_mfma_f32_16x16x32_fp8_fp8 v[50:53], v[52:53], v[4:5], v[22:25]
	v_cndmask_b32_e32 v28, v102, v28, vcc
	v_cmp_le_i32_e32 vcc, v113, v101
	s_nop 1
	v_cndmask_b32_e32 v29, v102, v29, vcc
	v_cmp_le_i32_e32 vcc, v114, v101
	v_max3_f32 v26, v26, v28, v29
	s_nop 0
	v_mul_f32_e32 v50, 0x3d800000, v50
	v_cndmask_b32_e32 v66, v102, v66, vcc
	v_cmp_le_i32_e32 vcc, v115, v101
	v_mul_f32_e32 v51, 0x3d800000, v51
	v_mul_f32_e32 v52, 0x3d800000, v52
	v_cndmask_b32_e32 v67, v102, v67, vcc
	v_cmp_le_i32_e32 vcc, v116, v101
	v_max3_f32 v26, v26, v66, v67
	v_mul_f32_e32 v53, 0x3d800000, v53
	v_cndmask_b32_e32 v68, v102, v68, vcc
	v_cmp_le_i32_e32 vcc, v117, v101
	s_nop 1
	v_cndmask_b32_e32 v69, v102, v69, vcc
	v_max3_f32 v26, v26, v68, v69
	ds_bpermute_b32 v104, v99, v26
	s_waitcnt lgkmcnt(0)
	v_max_f32_e32 v22, v104, v104
	v_max_f32_e32 v26, v26, v22
	ds_bpermute_b32 v104, v100, v26
	s_waitcnt vmcnt(4)
	v_mfma_f32_16x16x32_fp8_fp8 v[22:25], v[46:47], v[2:3], 0
	s_waitcnt lgkmcnt(0)
	v_max3_f32 v104, v103, v26, v104
	v_sub_f32_e32 v2, v103, v104
	v_mul_f32_e32 v2, 0x3fb8aa3b, v2
	v_exp_f32_e32 v26, v2
	v_sub_f32_e32 v2, v70, v104
	v_mul_f32_e32 v2, 0x3fb8aa3b, v2
	v_exp_f32_e32 v70, v2
	v_sub_f32_e32 v2, v71, v104
	v_mul_f32_e32 v2, 0x3fb8aa3b, v2
	v_exp_f32_e32 v71, v2
	v_sub_f32_e32 v2, v72, v104
	v_mul_f32_e32 v2, 0x3fb8aa3b, v2
	v_exp_f32_e32 v72, v2
	v_sub_f32_e32 v2, v73, v104
	v_mul_f32_e32 v2, 0x3fb8aa3b, v2
	v_exp_f32_e32 v73, v2
	v_sub_f32_e32 v2, v87, v104
	v_mul_f32_e32 v2, 0x3fb8aa3b, v2
	v_mfma_f32_16x16x32_fp8_fp8 v[46:49], v[48:49], v[4:5], v[22:25]
	v_mul_f32_e64 v4, v26, v76
	v_mul_f32_e64 v5, v26, v77
	v_exp_f32_e32 v76, v2
	v_sub_f32_e32 v2, v88, v104
	v_mul_f32_e32 v2, 0x3fb8aa3b, v2
	v_exp_f32_e32 v77, v2
	v_sub_f32_e32 v2, v89, v104
	v_mul_f32_e32 v2, 0x3fb8aa3b, v2
	v_exp_f32_e32 v87, v2
	v_sub_f32_e32 v2, v92, v104
	v_mul_f32_e32 v2, 0x3fb8aa3b, v2
	v_exp_f32_e32 v88, v2
	v_sub_f32_e32 v2, v93, v104
	v_mul_f32_e32 v2, 0x3fb8aa3b, v2
	v_exp_f32_e32 v89, v2
	v_sub_f32_e32 v2, v27, v104
	v_mul_f32_e32 v2, 0x3fb8aa3b, v2
	v_exp_f32_e32 v27, v2
	v_sub_f32_e32 v2, v28, v104
	v_mul_f32_e32 v2, 0x3fb8aa3b, v2
	v_exp_f32_e32 v92, v2
	v_sub_f32_e32 v2, v29, v104
	v_mul_f32_e32 v2, 0x3fb8aa3b, v2
	v_exp_f32_e32 v93, v2
	v_sub_f32_e32 v2, v66, v104
	v_mul_f32_e32 v2, 0x3fb8aa3b, v2
	v_exp_f32_e32 v103, v2
	v_sub_f32_e32 v2, v67, v104
	v_mul_f32_e32 v2, 0x3fb8aa3b, v2
	v_mov_b32_e32 v28, v91
	v_mov_b32_e32 v29, v91
	v_exp_f32_e32 v105, v2
	v_sub_f32_e32 v2, v68, v104
	v_cvt_pk_fp8_f32 v28, v70, v71
	v_cvt_pk_fp8_f32 v29, v76, v77
	v_mul_f32_e32 v2, 0x3fb8aa3b, v2
	v_exp_f32_e32 v68, v2
	v_sub_f32_e32 v2, v69, v104
	v_mul_f32_e32 v2, 0x3fb8aa3b, v2
	v_mov_b32_e32 v66, v91
	v_mov_b32_e32 v67, v91
	v_exp_f32_e32 v69, v2
	v_cvt_pk_fp8_f32 v28, v72, v73 op_sel:[0,0,1]
	v_cvt_pk_fp8_f32 v29, v87, v88 op_sel:[0,0,1]
	v_cvt_pk_fp8_f32 v66, v89, v27
	v_cvt_pk_fp8_f32 v67, v103, v105
	v_pk_mul_f32 v[2:3], v[26:27], v[74:75] op_sel_hi:[0,1]
	v_or_b32_e32 v74, 0xc7, v90
	v_cvt_pk_fp8_f32 v66, v92, v93 op_sel:[0,0,1]
	v_mfma_f32_16x16x32_fp8_fp8 v[2:5], v[42:43], v[28:29], v[2:5]
	v_cvt_pk_fp8_f32 v67, v68, v69 op_sel:[0,0,1]
	v_mul_f32_e32 v42, 0x3d800000, v64
	v_mul_f32_e32 v43, 0x3d800000, v65
	v_mfma_f32_16x16x32_fp8_fp8 v[22:25], v[44:45], v[66:67], v[2:5]
	v_mul_f32_e32 v44, 0x3d800000, v58
	v_mul_f32_e32 v58, 0x3d800000, v60
	s_nop 1
	v_pk_mul_f32 v[4:5], v[26:27], v[80:81] op_sel_hi:[0,1]
	v_pk_mul_f32 v[2:3], v[26:27], v[78:79] op_sel_hi:[0,1]
	v_or_b32_e32 v60, 0xc1, v90
	v_mul_f32_e32 v45, 0x3d800000, v59
	v_mfma_f32_16x16x32_fp8_fp8 v[2:5], v[38:39], v[28:29], v[2:5]
	v_mul_f32_e64 v38, v26, v82
	v_mul_f32_e64 v39, v26, v83
	v_mul_f32_e32 v59, 0x3d800000, v61
	v_or_b32_e32 v61, 0xc2, v90
	v_mfma_f32_16x16x32_fp8_fp8 v[2:5], v[40:41], v[66:67], v[2:5]
	v_mul_f32_e64 v40, v26, v84
	v_mul_f32_e64 v41, v26, v85
	v_or_b32_e32 v85, 0xc0, v90
	v_cmp_le_i32_e32 vcc, v85, v101
	v_mfma_f32_16x16x32_fp8_fp8 v[38:41], v[10:11], v[28:29], v[38:41]
	v_mul_f32_e32 v10, 0x3d800000, v62
	v_mul_f32_e32 v11, 0x3d800000, v63
	v_cndmask_b32_e32 v85, v102, v10, vcc
	v_cmp_le_i32_e32 vcc, v60, v101
	v_or_b32_e32 v62, 0xc3, v90
	v_or_b32_e32 v63, 0xc4, v90
	v_cndmask_b32_e32 v60, v102, v11, vcc
	v_cmp_le_i32_e32 vcc, v61, v101
	v_or_b32_e32 v64, 0xc5, v90
	v_or_b32_e32 v65, 0xc6, v90
	v_cndmask_b32_e32 v61, v102, v42, vcc
	v_cmp_le_i32_e32 vcc, v62, v101
	v_or_b32_e32 v75, 0xc8, v90
	v_or_b32_e32 v78, 0xc9, v90
	v_cndmask_b32_e32 v43, v102, v43, vcc
	v_cmp_le_i32_e32 vcc, v63, v101
	v_or_b32_e32 v79, 0xca, v90
	v_or_b32_e32 v80, 0xcb, v90
	v_cndmask_b32_e32 v44, v102, v44, vcc
	v_cmp_le_i32_e32 vcc, v64, v101
	v_max3_f32 v10, v85, s0, v60
	v_or_b32_e32 v81, 0xcc, v90
	v_cndmask_b32_e32 v45, v102, v45, vcc
	v_cmp_le_i32_e32 vcc, v65, v101
	v_max3_f32 v10, v10, v61, v43
	v_mul_f32_e32 v46, 0x3d800000, v46
	v_cndmask_b32_e32 v58, v102, v58, vcc
	v_cmp_le_i32_e32 vcc, v74, v101
	v_or_b32_e32 v82, 0xcd, v90
	v_max3_f32 v10, v10, v44, v45
	v_cndmask_b32_e32 v59, v102, v59, vcc
	v_cmp_le_i32_e32 vcc, v75, v101
	v_mul_f32_e32 v47, 0x3d800000, v47
	v_or_b32_e32 v83, 0xce, v90
	v_cndmask_b32_e32 v50, v102, v50, vcc
	v_cmp_le_i32_e32 vcc, v78, v101
	v_max3_f32 v10, v10, v58, v59
	v_mul_f32_e32 v48, 0x3d800000, v48
	v_cndmask_b32_e32 v51, v102, v51, vcc
	v_cmp_le_i32_e32 vcc, v79, v101
	v_or_b32_e32 v84, 0xcf, v90
	v_max3_f32 v10, v10, v50, v51
	v_cndmask_b32_e32 v52, v102, v52, vcc
	v_cmp_le_i32_e32 vcc, v80, v101
	v_mul_f32_e32 v49, 0x3d800000, v49
	v_mov_b32_e32 v90, v91
	v_cndmask_b32_e32 v53, v102, v53, vcc
	v_cmp_le_i32_e32 vcc, v81, v101
	v_max3_f32 v10, v10, v52, v53
	s_nop 0
	v_cndmask_b32_e32 v46, v102, v46, vcc
	v_cmp_le_i32_e32 vcc, v82, v101
	s_nop 1
	v_cndmask_b32_e32 v47, v102, v47, vcc
	v_cmp_le_i32_e32 vcc, v83, v101
	v_max3_f32 v10, v10, v46, v47
	s_nop 0
	v_cndmask_b32_e32 v48, v102, v48, vcc
	v_cmp_le_i32_e32 vcc, v84, v101
	s_nop 1
	v_cndmask_b32_e32 v49, v102, v49, vcc
	v_max3_f32 v42, v10, v48, v49
	ds_bpermute_b32 v62, v99, v42
	v_mfma_f32_16x16x32_fp8_fp8 v[10:13], v[12:13], v[66:67], v[38:41]
	v_cmp_gt_u32_e32 vcc, 16, v96
	s_waitcnt lgkmcnt(0)
	s_nop 0
	v_max_f32_e32 v38, v62, v62
	v_max_f32_e32 v42, v42, v38
	ds_bpermute_b32 v62, v100, v42
	v_pk_mul_f32 v[40:41], v[26:27], v[56:57] op_sel_hi:[0,1]
	v_pk_mul_f32 v[38:39], v[26:27], v[54:55] op_sel_hi:[0,1]
	s_nop 1
	v_mfma_f32_16x16x32_fp8_fp8 v[38:41], v[6:7], v[28:29], v[38:41]
	s_waitcnt lgkmcnt(0)
	v_max3_f32 v6, v104, v42, v62
	v_sub_f32_e32 v7, v104, v6
	v_mul_f32_e32 v7, 0x3fb8aa3b, v7
	v_mfma_f32_16x16x32_fp8_fp8 v[38:41], v[8:9], v[66:67], v[38:41]
	v_sub_f32_e32 v8, v60, v6
	v_mul_f32_e32 v8, 0x3fb8aa3b, v8
	v_exp_f32_e32 v42, v7
	v_exp_f32_e32 v54, v8
	v_sub_f32_e32 v8, v61, v6
	v_mul_f32_e32 v8, 0x3fb8aa3b, v8
	v_exp_f32_e32 v55, v8
	v_sub_f32_e32 v8, v43, v6
	v_mul_f32_e32 v8, 0x3fb8aa3b, v8
	v_pk_mul_f32 v[24:25], v[42:43], v[24:25] op_sel_hi:[0,1]
	v_exp_f32_e32 v43, v8
	v_sub_f32_e32 v8, v44, v6
	v_mul_f32_e32 v8, 0x3fb8aa3b, v8
	v_exp_f32_e32 v56, v8
	v_sub_f32_e32 v8, v45, v6
	v_mul_f32_e32 v8, 0x3fb8aa3b, v8
	v_exp_f32_e32 v57, v8
	v_sub_f32_e32 v8, v58, v6
	v_mul_f32_e32 v8, 0x3fb8aa3b, v8
	v_exp_f32_e32 v58, v8
	v_sub_f32_e32 v8, v59, v6
	v_mul_f32_e32 v8, 0x3fb8aa3b, v8
	v_exp_f32_e32 v59, v8
	v_sub_f32_e32 v8, v50, v6
	v_mul_f32_e32 v8, 0x3fb8aa3b, v8
	v_exp_f32_e32 v50, v8
	v_sub_f32_e32 v8, v51, v6
	v_mul_f32_e32 v8, 0x3fb8aa3b, v8
	v_exp_f32_e32 v51, v8
	v_sub_f32_e32 v8, v52, v6
	v_mul_f32_e32 v8, 0x3fb8aa3b, v8
	v_exp_f32_e32 v52, v8
	v_sub_f32_e32 v8, v53, v6
	v_mul_f32_e32 v8, 0x3fb8aa3b, v8
	v_exp_f32_e32 v53, v8
	v_sub_f32_e32 v8, v46, v6
	v_mul_f32_e32 v8, 0x3fb8aa3b, v8
	v_exp_f32_e32 v46, v8
	v_sub_f32_e32 v8, v47, v6
	v_sub_f32_e32 v7, v85, v6
	v_mul_f32_e32 v8, 0x3fb8aa3b, v8
	v_mul_f32_e32 v7, 0x3fb8aa3b, v7
	v_exp_f32_e32 v47, v8
	v_sub_f32_e32 v8, v48, v6
	v_exp_f32_e32 v7, v7
	v_mul_f32_e32 v8, 0x3fb8aa3b, v8
	v_exp_f32_e32 v48, v8
	v_sub_f32_e32 v8, v49, v6
	v_mul_f32_e32 v8, 0x3fb8aa3b, v8
	v_mov_b32_e32 v44, v91
	v_exp_f32_e32 v49, v8
	v_mov_b32_e32 v45, v91
	v_add_f32_e32 v8, 0, v70
	v_cvt_pk_fp8_f32 v44, v7, v54
	v_cvt_pk_fp8_f32 v45, v56, v57
	v_add_f32_e32 v8, v8, v71
	v_add_f32_e32 v7, 0, v7
	v_add_f32_e32 v8, v8, v72
	v_add_f32_e32 v7, v7, v54
	v_add_f32_e32 v8, v8, v73
	v_add_f32_e32 v7, v7, v55
	v_add_f32_e32 v8, v8, v76
	v_add_f32_e32 v7, v7, v43
	v_cvt_pk_fp8_f32 v44, v55, v43 op_sel:[0,0,1]
	v_cvt_pk_fp8_f32 v90, v50, v51
	v_cvt_pk_fp8_f32 v45, v58, v59 op_sel:[0,0,1]
	v_cvt_pk_fp8_f32 v91, v46, v47
	v_add_f32_e32 v8, v8, v77
	v_add_f32_e32 v7, v7, v56
	v_add_f32_e32 v8, v8, v87
	v_add_f32_e32 v7, v7, v57
	v_add_f32_e32 v8, v8, v88
	v_add_f32_e32 v7, v7, v58
	v_pk_mul_f32 v[4:5], v[42:43], v[4:5] op_sel_hi:[0,1]
	v_pk_mul_f32 v[2:3], v[42:43], v[2:3] op_sel_hi:[0,1]
	v_add_f32_e32 v8, v8, v89
	v_add_f32_e32 v7, v7, v59
	v_cvt_pk_fp8_f32 v90, v52, v53 op_sel:[0,0,1]
	v_cvt_pk_fp8_f32 v91, v48, v49 op_sel:[0,0,1]
	s_waitcnt vmcnt(2)
	v_mfma_f32_16x16x32_fp8_fp8 v[2:5], v[30:31], v[44:45], v[2:5]
	v_add_f32_e32 v8, v8, v27
	v_add_f32_e32 v7, v7, v50
	v_add_f32_e32 v8, v8, v92
	v_add_f32_e32 v7, v7, v51
	v_add_f32_e32 v8, v8, v93
	v_add_f32_e32 v7, v7, v52
	v_add_f32_e32 v8, v8, v103
	v_add_f32_e32 v7, v7, v53
	v_mfma_f32_16x16x32_fp8_fp8 v[28:31], v[32:33], v[90:91], v[2:5]
	v_add_f32_e32 v8, v8, v105
	v_add_f32_e32 v7, v7, v46
	v_add_f32_e32 v8, v8, v68
	v_pk_mul_f32 v[4:5], v[42:43], v[12:13] op_sel_hi:[0,1]
	v_pk_mul_f32 v[2:3], v[42:43], v[10:11] op_sel_hi:[0,1]
	v_add_f32_e32 v7, v7, v47
	v_add_f32_e32 v12, v8, v69
	s_waitcnt vmcnt(1)
	v_mfma_f32_16x16x32_fp8_fp8 v[2:5], v[18:19], v[44:45], v[2:5]
	v_add_f32_e32 v7, v7, v48
	v_fmac_f32_e32 v12, v86, v26
	v_add_f32_e32 v7, v7, v49
	v_fmac_f32_e32 v7, v12, v42
	v_mfma_f32_16x16x32_fp8_fp8 v[8:11], v[20:21], v[90:91], v[2:5]
	ds_bpermute_b32 v12, v99, v7
	v_pk_mul_f32 v[22:23], v[42:43], v[22:23] op_sel_hi:[0,1]
	s_nop 0
	v_pk_mul_f32 v[4:5], v[42:43], v[40:41] op_sel_hi:[0,1]
	v_pk_mul_f32 v[2:3], v[42:43], v[38:39] op_sel_hi:[0,1]
	v_mfma_f32_16x16x32_fp8_fp8 v[22:25], v[34:35], v[44:45], v[22:25]
	s_waitcnt vmcnt(0)
	v_mfma_f32_16x16x32_fp8_fp8 v[2:5], v[14:15], v[44:45], v[2:5]
	v_mfma_f32_16x16x32_fp8_fp8 v[14:17], v[16:17], v[90:91], v[2:5]
	v_mfma_f32_16x16x32_fp8_fp8 v[22:25], v[36:37], v[90:91], v[22:25]
	s_waitcnt lgkmcnt(0)
	s_nop 4
	v_add_f32_e32 v2, v7, v12
	ds_bpermute_b32 v3, v100, v2
	v_and_b32_e32 v4, 0x1c0, v0
	v_lshlrev_b32_e32 v12, 2, v97
	v_lshlrev_b32_e32 v4, 6, v4
	v_lshlrev_b32_e32 v5, 8, v98
	v_or3_b32 v4, v5, v4, v12
	v_add_u32_e32 v5, 0x400, v4
	ds_write2_b32 v4, v22, v23 offset1:16
	ds_write2_b32 v4, v24, v25 offset0:32 offset1:48
	ds_write2_b32 v5, v28, v29 offset1:16
	ds_write2_b32 v5, v30, v31 offset0:32 offset1:48
	v_add_u32_e32 v5, 0x800, v4
	v_add_u32_e32 v4, 0xc00, v4
	ds_write2_b32 v5, v8, v9 offset1:16
	ds_write2_b32 v5, v10, v11 offset0:32 offset1:48
	ds_write2_b32 v4, v14, v15 offset1:16
	ds_write2_b32 v4, v16, v17 offset0:32 offset1:48
	s_and_saveexec_b64 s[0:1], vcc
	s_cbranch_execz .LBB0_2
	s_waitcnt lgkmcnt(8)
	v_add_f32_e32 v2, v2, v3
	v_lshl_or_b32 v3, v95, 6, v12
	ds_write2st64_b32 v3, v2, v6 offset0:132 offset1:134
.LBB0_2:
	s_or_b64 exec, exec, s[0:1]
	v_add_u32_e32 v8, 0x8400, v12
	s_waitcnt lgkmcnt(0)
	s_barrier
	ds_read2_b32 v[2:3], v8 offset0:128 offset1:144
	ds_read2_b32 v[4:5], v8 offset0:160 offset1:176
	ds_read2_b32 v[6:7], v8 offset0:192 offset1:208
	ds_read2_b32 v[8:9], v8 offset0:224 offset1:240
	s_lshl_b32 s0, s14, 1
	s_add_i32 s0, s0, s2
	s_ashr_i32 s1, s0, 31
	s_waitcnt lgkmcnt(3)
	v_max_f32_e32 v10, v3, v3
	v_max_f32_e32 v11, v2, v2
	v_max_f32_e32 v10, v11, v10
	s_waitcnt lgkmcnt(2)
	v_max3_f32 v10, v10, v4, v5
	s_waitcnt lgkmcnt(1)
	v_max3_f32 v10, v10, v6, v7
	s_waitcnt lgkmcnt(0)
	v_max3_f32 v10, v10, v8, v9
	v_sub_f32_e32 v2, v2, v10
	v_sub_f32_e32 v3, v3, v10
	v_sub_f32_e32 v4, v4, v10
	v_sub_f32_e32 v5, v5, v10
	v_sub_f32_e32 v6, v6, v10
	v_sub_f32_e32 v7, v7, v10
	v_sub_f32_e32 v8, v8, v10
	v_sub_f32_e32 v9, v9, v10
	v_mul_f32_e32 v2, 0x3fb8aa3b, v2
	v_mul_f32_e32 v3, 0x3fb8aa3b, v3
	v_mul_f32_e32 v4, 0x3fb8aa3b, v4
	v_mul_f32_e32 v5, 0x3fb8aa3b, v5
	v_mul_f32_e32 v6, 0x3fb8aa3b, v6
	v_mul_f32_e32 v7, 0x3fb8aa3b, v7
	v_mul_f32_e32 v8, 0x3fb8aa3b, v8
	v_mul_f32_e32 v9, 0x3fb8aa3b, v9
	v_exp_f32_e32 v2, v2
	v_exp_f32_e32 v3, v3
	v_exp_f32_e32 v4, v4
	v_exp_f32_e32 v5, v5
	v_exp_f32_e32 v6, v6
	v_exp_f32_e32 v7, v7
	v_exp_f32_e32 v8, v8
	v_exp_f32_e32 v9, v9
	v_lshrrev_b32_e32 v11, 2, v0
	s_lshl_b64 s[2:3], s[0:1], 12
	v_lshlrev_b32_e32 v10, 8, v97
	v_and_b32_e32 v11, 0x7c, v11
	v_or3_b32 v10, s2, v10, v11
	v_mov_b32_e32 v11, s3
	v_lshl_add_u64 v[10:11], s[18:19], 0, v[10:11]
	s_mov_b64 s[2:3], 0
	s_mov_b64 s[4:5], 0x80
	s_movk_i32 s6, 0x1ff
	v_mov_b32_e32 v13, v0
.LBB0_3:
	v_and_b32_e32 v14, 0x3f0, v13
	v_add_u32_e32 v15, 0x200, v13
	v_lshl_or_b32 v20, v14, 2, v12
	v_cmp_lt_u32_e32 vcc, s6, v13
	v_mov_b32_e32 v13, v15
	ds_read2st64_b32 v[14:15], v20 offset1:16
	ds_read2st64_b32 v[16:17], v20 offset0:32 offset1:48
	ds_read2st64_b32 v[18:19], v20 offset0:64 offset1:80
	ds_read2st64_b32 v[20:21], v20 offset0:96 offset1:112
	s_or_b64 s[2:3], vcc, s[2:3]
	s_waitcnt lgkmcnt(3)
	v_pk_mul_f32 v[14:15], v[14:15], v[2:3]
	s_waitcnt lgkmcnt(2)
	v_pk_mul_f32 v[16:17], v[16:17], v[4:5]
	v_add_f32_e32 v14, 0, v14
	v_add_f32_e32 v14, v14, v15
	v_add_f32_e32 v14, v14, v16
	s_waitcnt lgkmcnt(1)
	v_pk_mul_f32 v[18:19], v[18:19], v[6:7]
	v_add_f32_e32 v14, v14, v17
	v_add_f32_e32 v14, v14, v18
	s_waitcnt lgkmcnt(0)
	v_pk_mul_f32 v[20:21], v[20:21], v[8:9]
	v_add_f32_e32 v14, v14, v19
	v_add_f32_e32 v14, v14, v20
	v_add_f32_e32 v14, v14, v21
	global_store_dword v[10:11], v14, off
	v_lshl_add_u64 v[10:11], v[10:11], 0, s[4:5]
	s_andn2_b64 exec, exec, s[2:3]
	s_cbranch_execnz .LBB0_3
	s_or_b64 exec, exec, s[2:3]
	v_cmp_gt_u32_e32 vcc, 16, v0
	s_and_saveexec_b64 s[2:3], vcc
	s_cbranch_execz .LBB0_6
	v_add_u32_e32 v0, 0x8400, v94
	ds_read2_b32 v[2:3], v0 offset0:128 offset1:144
	ds_read2_b32 v[4:5], v0 offset0:160 offset1:176
	ds_read2_b32 v[6:7], v0 offset0:192 offset1:208
	ds_read2_b32 v[8:9], v0 offset0:224 offset1:240
	ds_read2_b32 v[12:13], v0 offset1:16
	s_waitcnt lgkmcnt(4)
	v_max_f32_e32 v10, v3, v3
	v_max_f32_e32 v11, v2, v2
	v_max_f32_e32 v10, v11, v10
	s_waitcnt lgkmcnt(3)
	v_max3_f32 v10, v10, v4, v5
	s_waitcnt lgkmcnt(2)
	v_max3_f32 v10, v10, v6, v7
	s_waitcnt lgkmcnt(1)
	v_max3_f32 v10, v10, v8, v9
	v_sub_f32_e32 v2, v2, v10
	v_mul_f32_e32 v2, 0x3fb8aa3b, v2
	v_exp_f32_e32 v11, v2
	v_sub_f32_e32 v2, v3, v10
	v_mul_f32_e32 v2, 0x3fb8aa3b, v2
	v_sub_f32_e32 v4, v4, v10
	v_exp_f32_e32 v14, v2
	ds_read2_b32 v[2:3], v0 offset0:32 offset1:48
	v_mul_f32_e32 v4, 0x3fb8aa3b, v4
	v_exp_f32_e32 v4, v4
	v_sub_f32_e32 v5, v5, v10
	v_mul_f32_e32 v5, 0x3fb8aa3b, v5
	s_waitcnt lgkmcnt(1)
	v_fma_f32 v11, v12, v11, 0
	v_exp_f32_e32 v5, v5
	v_fmac_f32_e32 v11, v13, v14
	s_waitcnt lgkmcnt(0)
	v_fmac_f32_e32 v11, v2, v4
	v_sub_f32_e32 v4, v6, v10
	v_mul_f32_e32 v4, 0x3fb8aa3b, v4
	v_exp_f32_e32 v6, v4
	v_sub_f32_e32 v4, v7, v10
	v_fmac_f32_e32 v11, v3, v5
	ds_read2_b32 v[2:3], v0 offset0:64 offset1:80
	v_mul_f32_e32 v4, 0x3fb8aa3b, v4
	v_exp_f32_e32 v7, v4
	ds_read2_b32 v[4:5], v0 offset0:96 offset1:112
	v_sub_f32_e32 v0, v8, v10
	v_mul_f32_e32 v0, 0x3fb8aa3b, v0
	v_sub_f32_e32 v8, v9, v10
	v_exp_f32_e32 v0, v0
	v_mul_f32_e32 v8, 0x3fb8aa3b, v8
	v_exp_f32_e32 v8, v8
	s_waitcnt lgkmcnt(1)
	v_fmac_f32_e32 v11, v2, v6
	v_fmac_f32_e32 v11, v3, v7
	s_lshl_b64 s[0:1], s[0:1], 7
	s_waitcnt lgkmcnt(0)
	v_fmac_f32_e32 v11, v4, v0
	s_add_u32 s0, s20, s0
	v_fmac_f32_e32 v11, v5, v8
	s_addc_u32 s1, s21, s1
	global_store_dwordx2 v1, v[10:11], s[0:1]
.LBB0_6:
	s_endpgm
	s_nop 0
	s_nop 0
	s_nop 0
	s_nop 0
	s_nop 0
	s_nop 0
	s_nop 0
	s_nop 0
	s_nop 0
	s_nop 0
	s_nop 0
	s_nop 0
	s_nop 0
	s_nop 0
	s_nop 0
	s_nop 0
	s_nop 0
	s_nop 0
	s_nop 0
	s_nop 0
	s_nop 0
	s_nop 0
	s_nop 0
	s_nop 0
	s_nop 0
	s_nop 0
	s_nop 0
	s_nop 0
	s_nop 0
	s_nop 0
	s_nop 0
	s_nop 0
	s_nop 0
	s_nop 0
	s_nop 0
	s_nop 0
	s_nop 0
	s_nop 0
	s_nop 0
	s_nop 0
	s_nop 0
	s_nop 0
	s_nop 0
	s_nop 0
	s_nop 0
	s_nop 0
	s_nop 0
	s_nop 0
	s_nop 0
	s_nop 0
	s_nop 0
	s_nop 0
	s_nop 0
	s_nop 0
	s_endpgm

	.amdhsa_kernel _ZN12_GLOBAL__N_16attn_qEPKDF16_S1_PK15HIP_vector_typeIfLj2EEPKhS7_PfS8_
		.amdhsa_group_segment_fixed_size 34816
		.amdhsa_private_segment_fixed_size 0
		.amdhsa_kernarg_size 56
		.amdhsa_user_sgpr_count 2
		.amdhsa_user_sgpr_dispatch_ptr 0
		.amdhsa_user_sgpr_queue_ptr 0
		.amdhsa_user_sgpr_kernarg_segment_ptr 1
		.amdhsa_user_sgpr_dispatch_id 0
		.amdhsa_user_sgpr_kernarg_preload_length 0
		.amdhsa_user_sgpr_kernarg_preload_offset 0
		.amdhsa_user_sgpr_private_segment_size 0
		.amdhsa_uses_dynamic_stack 0
		.amdhsa_enable_private_segment 0
		.amdhsa_system_sgpr_workgroup_id_x 1
		.amdhsa_system_sgpr_workgroup_id_y 1
		.amdhsa_system_sgpr_workgroup_id_z 0
		.amdhsa_system_sgpr_workgroup_info 0
		.amdhsa_system_vgpr_workitem_id 0
		.amdhsa_next_free_vgpr 172
		.amdhsa_next_free_sgpr 24
		.amdhsa_accum_offset 172
		.amdhsa_reserve_vcc 1
		.amdhsa_float_round_mode_32 0
		.amdhsa_float_round_mode_16_64 0
		.amdhsa_float_denorm_mode_32 3
		.amdhsa_float_denorm_mode_16_64 3
		.amdhsa_dx10_clamp 1
		.amdhsa_ieee_mode 1
		.amdhsa_fp16_overflow 0
		.amdhsa_tg_split 0
		.amdhsa_exception_fp_ieee_invalid_op 0
		.amdhsa_exception_fp_denorm_src 0
		.amdhsa_exception_fp_ieee_div_zero 0
		.amdhsa_exception_fp_ieee_overflow 0
		.amdhsa_exception_fp_ieee_underflow 0
		.amdhsa_exception_fp_ieee_inexact 0
		.amdhsa_exception_int_div_zero 0
	.end_amdhsa_kernel

.LBB1_19:
	s_andn2_b64 vcc, exec, s[4:5]
	s_cbranch_vccnz .LBB1_21
	s_load_dwordx4 s[4:7], s[0:1], 0x58
	s_add_i32 s2, s16, 0xffffaa00
	s_and_b32 s8, s16, 15
	s_lshr_b32 s9, s2, 4
	s_lshl_b32 s2, s8, 8
	v_lshrrev_b32_e32 v1, 4, v0
	s_waitcnt lgkmcnt(0)
	s_add_u32 s2, s4, s2
	v_lshlrev_b32_e32 v2, 4, v0
	s_addc_u32 s3, s5, 0
	v_and_b32_e32 v18, 0xf0, v2
	v_mov_b32_e32 v19, 0
	v_lshlrev_b32_e32 v2, 10, v1
	v_lshl_add_u64 v[14:15], s[2:3], 0, v[18:19]
	v_lshl_or_b32 v16, s9, 16, v2
	v_mov_b32_e32 v17, v19
	s_movk_i32 s2, 0x104
	v_lshl_add_u64 v[10:11], v[16:17], 2, v[14:15]
	v_mad_u32_u24 v1, v1, s2, v18
	v_or_b32_e32 v18, 0x4000, v16
	v_lshl_add_u64 v[12:13], v[18:19], 2, v[14:15]
	global_load_dwordx4 v[2:5], v[10:11], off nt
	global_load_dwordx4 v[6:9], v[12:13], off nt
	v_or_b32_e32 v18, 0x8000, v16
	v_lshl_add_u64 v[10:11], v[18:19], 2, v[14:15]
	global_load_dwordx4 v[10:13], v[10:11], off nt
	v_or_b32_e32 v18, 0xc000, v16
	v_lshl_add_u64 v[14:15], v[18:19], 2, v[14:15]
	global_load_dwordx4 v[14:17], v[14:15], off nt
	v_and_b32_e32 v18, 15, v0
	v_lshrrev_b32_e32 v20, 1, v0
	s_movk_i32 s3, 0xc0
	v_and_b32_e32 v22, 24, v20
	v_lshlrev_b32_e32 v18, 2, v18
	v_and_or_b32 v18, v0, s3, v18
	v_or_b32_e32 v23, 32, v22
	v_mad_u32_u24 v22, v22, s2, v18
	v_mad_u32_u24 v23, v23, s2, v18
	v_and_b32_e32 v20, 0x60, v20
	v_add_u32_e32 v24, 0x1040, v1
	v_add_u32_e32 v25, 0x1048, v1
	v_add_u32_e32 v26, 0x2080, v1
	v_add_u32_e32 v27, 0x2088, v1
	v_add_u32_e32 v28, 0x30c0, v1
	v_add_u32_e32 v29, 0x30c8, v1
	v_add_u32_e32 v30, 0x400, v22
	v_add_u32_e32 v31, 0x400, v23
	v_lshlrev_b32_e32 v21, 3, v0
	v_lshl_or_b32 v20, s8, 7, v20
	v_and_b32_e32 v21, 0x1f8, v21
	v_lshl_add_u32 v20, s9, 1, v20
	v_lshl_or_b32 v18, v20, 9, v21
	v_lshl_add_u64 v[20:21], v[18:19], 1, s[6:7]
	v_or_b32_e32 v18, 0x200, v18
	v_lshl_add_u64 v[18:19], v[18:19], 1, s[6:7]
	s_waitcnt vmcnt(3)
	ds_write2_b32 v1, v2, v3 offset1:1
	ds_write2_b32 v1, v4, v5 offset0:2 offset1:3
	s_waitcnt vmcnt(2)
	ds_write2_b32 v24, v6, v7 offset1:1
	ds_write2_b32 v25, v8, v9 offset1:1
	s_waitcnt vmcnt(1)
	ds_write2_b32 v26, v10, v11 offset1:1
	ds_write2_b32 v27, v12, v13 offset1:1
	s_waitcnt vmcnt(0)
	ds_write2_b32 v28, v14, v15 offset1:1
	ds_write2_b32 v29, v16, v17 offset1:1
	s_waitcnt lgkmcnt(0)
	s_barrier
	ds_read2_b32 v[6:7], v22 offset1:65
	ds_read2_b32 v[2:3], v22 offset0:130 offset1:195
	ds_read2_b32 v[8:9], v30 offset0:4 offset1:69
	ds_read2_b32 v[4:5], v30 offset0:134 offset1:199
	ds_read2_b32 v[10:11], v23 offset1:65
	ds_read2_b32 v[12:13], v23 offset0:130 offset1:195
	ds_read2_b32 v[14:15], v31 offset0:4 offset1:69
	ds_read2_b32 v[16:17], v31 offset0:134 offset1:199
	s_waitcnt lgkmcnt(4)
	v_cvt_pk_f16_f32 v5, v4, v5
	v_cvt_pk_f16_f32 v4, v8, v9
	v_cvt_pk_f16_f32 v3, v2, v3
	v_cvt_pk_f16_f32 v2, v6, v7
	s_waitcnt lgkmcnt(0)
	v_cvt_pk_f16_f32 v9, v16, v17
	v_cvt_pk_f16_f32 v8, v14, v15
	v_cvt_pk_f16_f32 v7, v12, v13
	v_cvt_pk_f16_f32 v6, v10, v11
	global_store_dwordx4 v[20:21], v[2:5], off
	global_store_dwordx4 v[18:19], v[6:9], off

.LBB1_22:
	s_andn2_b64 vcc, exec, s[4:5]
	s_cbranch_vccnz .LBB1_24
	s_load_dwordx4 s[4:7], s[0:1], 0x48
	s_add_i32 s2, s16, 0xffffab00
	s_and_b32 s8, s16, 15
	s_lshr_b32 s9, s2, 4
	s_lshl_b32 s2, s8, 8
	v_lshrrev_b32_e32 v1, 4, v0
	s_waitcnt lgkmcnt(0)
	s_add_u32 s2, s4, s2
	v_lshlrev_b32_e32 v2, 4, v0
	s_addc_u32 s3, s5, 0
	v_and_b32_e32 v18, 0xf0, v2
	v_mov_b32_e32 v19, 0
	v_lshlrev_b32_e32 v2, 10, v1
	v_lshl_add_u64 v[14:15], s[2:3], 0, v[18:19]
	v_lshl_or_b32 v16, s9, 16, v2
	v_mov_b32_e32 v17, v19
	s_movk_i32 s2, 0x104
	v_lshl_add_u64 v[10:11], v[16:17], 2, v[14:15]
	v_mad_u32_u24 v1, v1, s2, v18
	v_or_b32_e32 v18, 0x4000, v16
	v_lshl_add_u64 v[12:13], v[18:19], 2, v[14:15]
	global_load_dwordx4 v[2:5], v[10:11], off nt
	global_load_dwordx4 v[6:9], v[12:13], off nt
	v_or_b32_e32 v18, 0x8000, v16
	v_lshl_add_u64 v[10:11], v[18:19], 2, v[14:15]
	global_load_dwordx4 v[10:13], v[10:11], off nt
	v_or_b32_e32 v18, 0xc000, v16
	v_lshl_add_u64 v[14:15], v[18:19], 2, v[14:15]
	global_load_dwordx4 v[14:17], v[14:15], off nt
	v_and_b32_e32 v18, 15, v0
	v_lshrrev_b32_e32 v20, 1, v0
	s_movk_i32 s3, 0xc0
	v_and_b32_e32 v22, 24, v20
	v_lshlrev_b32_e32 v18, 2, v18
	v_and_or_b32 v18, v0, s3, v18
	v_or_b32_e32 v23, 32, v22
	v_mad_u32_u24 v22, v22, s2, v18
	v_mad_u32_u24 v23, v23, s2, v18
	v_and_b32_e32 v20, 0x60, v20
	v_add_u32_e32 v24, 0x1040, v1
	v_add_u32_e32 v25, 0x1048, v1
	v_add_u32_e32 v26, 0x2080, v1
	v_add_u32_e32 v27, 0x2088, v1
	v_add_u32_e32 v28, 0x30c0, v1
	v_add_u32_e32 v29, 0x30c8, v1
	v_add_u32_e32 v30, 0x400, v22
	v_add_u32_e32 v31, 0x400, v23
	v_lshlrev_b32_e32 v21, 3, v0
	v_lshl_or_b32 v20, s8, 7, v20
	v_and_b32_e32 v21, 0x1f8, v21
	v_lshl_add_u32 v20, s9, 1, v20
	v_lshl_or_b32 v18, v20, 9, v21
	v_lshl_add_u64 v[20:21], v[18:19], 1, s[6:7]
	v_or_b32_e32 v18, 0x200, v18
	v_lshl_add_u64 v[18:19], v[18:19], 1, s[6:7]
	s_waitcnt vmcnt(3)
	ds_write2_b32 v1, v2, v3 offset1:1
	ds_write2_b32 v1, v4, v5 offset0:2 offset1:3
	s_waitcnt vmcnt(2)
	ds_write2_b32 v24, v6, v7 offset1:1
	ds_write2_b32 v25, v8, v9 offset1:1
	s_waitcnt vmcnt(1)
	ds_write2_b32 v26, v10, v11 offset1:1
	ds_write2_b32 v27, v12, v13 offset1:1
	s_waitcnt vmcnt(0)
	ds_write2_b32 v28, v14, v15 offset1:1
	ds_write2_b32 v29, v16, v17 offset1:1
	s_waitcnt lgkmcnt(0)
	s_barrier
	ds_read2_b32 v[6:7], v22 offset1:65
	ds_read2_b32 v[2:3], v22 offset0:130 offset1:195
	ds_read2_b32 v[8:9], v30 offset0:4 offset1:69
	ds_read2_b32 v[4:5], v30 offset0:134 offset1:199
	ds_read2_b32 v[10:11], v23 offset1:65
	ds_read2_b32 v[12:13], v23 offset0:130 offset1:195
	ds_read2_b32 v[14:15], v31 offset0:4 offset1:69
	ds_read2_b32 v[16:17], v31 offset0:134 offset1:199
	s_waitcnt lgkmcnt(4)
	v_cvt_pk_f16_f32 v5, v4, v5
	v_cvt_pk_f16_f32 v4, v8, v9
	v_cvt_pk_f16_f32 v3, v2, v3
	v_cvt_pk_f16_f32 v2, v6, v7
	s_waitcnt lgkmcnt(0)
	v_cvt_pk_f16_f32 v9, v16, v17
	v_cvt_pk_f16_f32 v8, v14, v15
	v_cvt_pk_f16_f32 v7, v12, v13
	v_cvt_pk_f16_f32 v6, v10, v11
	global_store_dwordx4 v[20:21], v[2:5], off
	global_store_dwordx4 v[18:19], v[6:9], off

.LBB1_25:
	s_andn2_b64 vcc, exec, s[4:5]
	s_cbranch_vccnz .LBB1_27
	s_load_dwordx4 s[4:7], s[0:1], 0x38
	s_lshl_b32 s2, s16, 6
	s_and_b32 s8, s2, 0x3c0
	s_lshl_b32 s2, s16, 2
	s_and_b32 s2, s2, 0x1ffc0
	s_add_i32 s9, s2, 0xfffeb000
	s_lshl_b32 s2, s8, 2
	v_lshlrev_b32_e32 v1, 4, v0
	s_waitcnt lgkmcnt(0)
	s_add_u32 s2, s4, s2
	v_and_b32_e32 v18, 0xf0, v1
	v_mov_b32_e32 v19, 0
	v_lshrrev_b32_e32 v1, 4, v0
	s_addc_u32 s3, s5, 0
	v_or_b32_e32 v2, s9, v1
	v_mov_b32_e32 v3, v19
	v_or_b32_e32 v22, 0x100, v0
	v_lshl_add_u64 v[14:15], s[2:3], 0, v[18:19]
	v_lshlrev_b64 v[2:3], 12, v[2:3]
	v_lshrrev_b32_e32 v25, 4, v22
	v_lshl_add_u64 v[10:11], v[14:15], 0, v[2:3]
	v_or_b32_e32 v2, s9, v25
	v_mov_b32_e32 v3, v19
	v_lshlrev_b64 v[2:3], 12, v[2:3]
	v_lshl_add_u64 v[12:13], v[14:15], 0, v[2:3]
	global_load_dwordx4 v[2:5], v[10:11], off nt
	global_load_dwordx4 v[6:9], v[12:13], off nt
	v_or_b32_e32 v10, 0x200, v0
	v_lshrrev_b32_e32 v26, 4, v10
	v_or_b32_e32 v10, s9, v26
	v_mov_b32_e32 v11, v19
	v_or_b32_e32 v16, 0x300, v0
	v_lshlrev_b64 v[10:11], 12, v[10:11]
	v_lshrrev_b32_e32 v27, 4, v16
	v_lshl_add_u64 v[10:11], v[14:15], 0, v[10:11]
	v_or_b32_e32 v16, s9, v27
	v_mov_b32_e32 v17, v19
	global_load_dwordx4 v[10:13], v[10:11], off nt
	v_lshlrev_b64 v[16:17], 12, v[16:17]
	v_lshl_add_u64 v[14:15], v[14:15], 0, v[16:17]
	global_load_dwordx4 v[14:17], v[14:15], off nt
	s_movk_i32 s4, 0x104
	v_lshrrev_b32_e32 v29, 3, v0
	v_lshlrev_b32_e32 v28, 3, v0
	v_lshrrev_b32_e32 v31, 3, v22
	v_mad_u32_u24 v1, v1, s4, v18
	v_mad_u32_u24 v25, v25, s4, v18
	v_mad_u32_u24 v32, v26, s4, v18
	v_mad_u32_u24 v33, v27, s4, v18
	v_or_b32_e32 v18, s8, v29
	v_lshlrev_b32_e32 v30, 2, v29
	v_lshlrev_b32_e32 v26, 2, v31
	v_lshlrev_b32_e32 v22, 10, v18
	v_and_b32_e32 v18, 56, v28
	s_add_u32 s2, s6, s9
	s_addc_u32 s3, s7, 0
	v_mad_u32_u24 v28, v18, s4, v30
	v_mad_u32_u24 v29, v18, s4, v26
	v_lshl_add_u64 v[26:27], s[2:3], 0, v[18:19]
	v_add_u32_e32 v18, 0x400, v28
	v_add_u32_e32 v30, 0x400, v29
	v_mov_b32_e32 v20, v19
	v_mov_b32_e32 v24, v19
	v_mov_b32_e32 v21, v19
	v_mov_b32_e32 v23, v19
	v_lshl_add_u64 v[22:23], v[26:27], 0, v[22:23]
	s_waitcnt vmcnt(3)
	ds_write2_b32 v1, v2, v3 offset1:1
	ds_write2_b32 v1, v4, v5 offset0:2 offset1:3
	s_waitcnt vmcnt(2)
	ds_write2_b32 v25, v6, v7 offset1:1
	ds_write2_b32 v25, v8, v9 offset0:2 offset1:3
	s_waitcnt vmcnt(1)
	ds_write2_b32 v32, v10, v11 offset1:1
	ds_write2_b32 v32, v12, v13 offset0:2 offset1:3
	s_waitcnt vmcnt(0)
	ds_write2_b32 v33, v14, v15 offset1:1
	ds_write2_b32 v33, v16, v17 offset0:2 offset1:3
	s_waitcnt lgkmcnt(0)
	s_barrier
	ds_read2_b32 v[2:3], v28 offset1:65
	ds_read2_b32 v[4:5], v28 offset0:130 offset1:195
	ds_read2_b32 v[6:7], v18 offset0:4 offset1:69
	ds_read2_b32 v[8:9], v18 offset0:134 offset1:199
	ds_read2_b32 v[10:11], v29 offset1:65
	ds_read2_b32 v[12:13], v29 offset0:130 offset1:195
	ds_read2_b32 v[14:15], v30 offset0:4 offset1:69
	ds_read2_b32 v[16:17], v30 offset0:134 offset1:199
	s_waitcnt lgkmcnt(7)
	v_mul_f32_e32 v1, 0x42800000, v2
	v_mul_f32_e32 v2, 0x42800000, v3
	v_cvt_pk_fp8_f32 v20, v1, v2
	s_waitcnt lgkmcnt(6)
	v_mul_f32_e32 v3, 0x42800000, v4
	v_mul_f32_e32 v4, 0x42800000, v5
	s_waitcnt lgkmcnt(5)
	v_mul_f32_e32 v5, 0x42800000, v6
	v_mul_f32_e32 v6, 0x42800000, v7
	s_waitcnt lgkmcnt(4)
	v_mul_f32_e32 v7, 0x42800000, v8
	v_mul_f32_e32 v8, 0x42800000, v9
	s_waitcnt lgkmcnt(3)
	v_mul_f32_e32 v9, 0x42800000, v10
	v_mul_f32_e32 v10, 0x42800000, v11
	v_cvt_pk_fp8_f32 v20, v3, v4 op_sel:[0,0,1]
	s_waitcnt lgkmcnt(1)
	v_mul_f32_e32 v3, 0x42800000, v14
	v_mul_f32_e32 v4, 0x42800000, v15
	v_cvt_pk_fp8_f32 v24, v9, v10
	v_mov_b32_e32 v25, v19
	v_cvt_pk_fp8_f32 v21, v5, v6
	v_cvt_pk_fp8_f32 v25, v3, v4
	v_mul_f32_e32 v1, 0x42800000, v12
	v_mul_f32_e32 v2, 0x42800000, v13
	v_cvt_pk_fp8_f32 v24, v1, v2 op_sel:[0,0,1]
	s_waitcnt lgkmcnt(0)
	v_mul_f32_e32 v1, 0x42800000, v16
	v_mul_f32_e32 v2, 0x42800000, v17
	v_cvt_pk_fp8_f32 v21, v7, v8 op_sel:[0,0,1]
	v_cvt_pk_fp8_f32 v25, v1, v2 op_sel:[0,0,1]
	v_or_b32_e32 v1, s8, v31
	v_lshlrev_b32_e32 v18, 10, v1
	v_lshl_add_u64 v[2:3], v[26:27], 0, v[18:19]
	global_store_dwordx2 v[22:23], v[20:21], off
	global_store_dwordx2 v[2:3], v[24:25], off

.LBB1_28:
	s_andn2_b64 vcc, exec, s[4:5]
	s_cbranch_vccnz .LBB1_30
	s_load_dwordx4 s[4:7], s[0:1], 0x28
	s_add_i32 s2, s16, 0xffffb400
	s_and_b32 s8, s16, 31
	s_lshr_b32 s9, s2, 5
	s_lshl_b32 s2, s8, 8
	v_lshrrev_b32_e32 v1, 4, v0
	s_waitcnt lgkmcnt(0)
	s_add_u32 s2, s4, s2
	v_lshlrev_b32_e32 v2, 4, v0
	s_addc_u32 s3, s5, 0
	v_and_b32_e32 v18, 0xf0, v2
	v_mov_b32_e32 v19, 0
	v_lshlrev_b32_e32 v2, 11, v1
	v_lshl_add_u64 v[14:15], s[2:3], 0, v[18:19]
	v_lshl_or_b32 v16, s9, 17, v2
	v_mov_b32_e32 v17, v19
	s_movk_i32 s2, 0x104
	v_lshl_add_u64 v[10:11], v[16:17], 2, v[14:15]
	v_mad_u32_u24 v1, v1, s2, v18
	v_or_b32_e32 v18, 0x8000, v16
	v_lshl_add_u64 v[12:13], v[18:19], 2, v[14:15]
	global_load_dwordx4 v[2:5], v[10:11], off nt
	global_load_dwordx4 v[6:9], v[12:13], off nt
	v_or_b32_e32 v18, 0x10000, v16
	v_lshl_add_u64 v[10:11], v[18:19], 2, v[14:15]
	global_load_dwordx4 v[10:13], v[10:11], off nt
	v_or_b32_e32 v18, 0x18000, v16
	v_lshl_add_u64 v[14:15], v[18:19], 2, v[14:15]
	global_load_dwordx4 v[14:17], v[14:15], off nt
	v_and_b32_e32 v18, 15, v0
	v_lshrrev_b32_e32 v20, 1, v0
	s_movk_i32 s3, 0xc0
	v_and_b32_e32 v20, 24, v20
	v_lshlrev_b32_e32 v18, 2, v18
	v_and_or_b32 v18, v0, s3, v18
	v_or_b32_e32 v23, 32, v20
	v_lshlrev_b32_e32 v21, 1, v0
	v_mad_u32_u24 v30, v20, s2, v18
	v_mad_u32_u24 v23, v23, s2, v18
	v_and_b32_e32 v21, 0x180, v21
	v_add_u32_e32 v24, 0x1040, v1
	v_add_u32_e32 v25, 0x1048, v1
	v_add_u32_e32 v26, 0x2080, v1
	v_add_u32_e32 v27, 0x2088, v1
	v_add_u32_e32 v28, 0x30c0, v1
	v_add_u32_e32 v29, 0x30c8, v1
	v_add_u32_e32 v31, 0x400, v30
	v_add_u32_e32 v32, 0x400, v23
	v_lshlrev_b32_e32 v22, 3, v0
	v_lshl_or_b32 v21, s8, 9, v21
	v_and_b32_e32 v22, 0x1f8, v22
	v_lshl_add_u32 v21, s9, 1, v21
	v_lshl_or_b32 v18, v21, 9, v22
	v_lshl_add_u64 v[20:21], v[18:19], 1, s[6:7]
	v_or_b32_e32 v18, 0x200, v18
	v_lshl_add_u64 v[18:19], v[18:19], 1, s[6:7]
	s_waitcnt vmcnt(3)
	ds_write2_b32 v1, v2, v3 offset1:1
	ds_write2_b32 v1, v4, v5 offset0:2 offset1:3
	s_waitcnt vmcnt(2)
	ds_write2_b32 v24, v6, v7 offset1:1
	ds_write2_b32 v25, v8, v9 offset1:1
	s_waitcnt vmcnt(1)
	ds_write2_b32 v26, v10, v11 offset1:1
	ds_write2_b32 v27, v12, v13 offset1:1
	s_waitcnt vmcnt(0)
	ds_write2_b32 v28, v14, v15 offset1:1
	ds_write2_b32 v29, v16, v17 offset1:1
	s_waitcnt lgkmcnt(0)
	s_barrier
	ds_read2_b32 v[6:7], v30 offset1:65
	ds_read2_b32 v[2:3], v30 offset0:130 offset1:195
	ds_read2_b32 v[8:9], v31 offset0:4 offset1:69
	ds_read2_b32 v[4:5], v31 offset0:134 offset1:199
	ds_read2_b32 v[10:11], v23 offset1:65
	ds_read2_b32 v[12:13], v23 offset0:130 offset1:195
	ds_read2_b32 v[14:15], v32 offset0:4 offset1:69
	ds_read2_b32 v[16:17], v32 offset0:134 offset1:199
	s_waitcnt lgkmcnt(4)
	v_cvt_pk_f16_f32 v5, v4, v5
	v_cvt_pk_f16_f32 v4, v8, v9
	v_cvt_pk_f16_f32 v3, v2, v3
	v_cvt_pk_f16_f32 v2, v6, v7
	s_waitcnt lgkmcnt(0)
	v_cvt_pk_f16_f32 v9, v16, v17
	v_cvt_pk_f16_f32 v8, v14, v15
	v_cvt_pk_f16_f32 v7, v12, v13
	v_cvt_pk_f16_f32 v6, v10, v11
	global_store_dwordx4 v[20:21], v[2:5], off
	global_store_dwordx4 v[18:19], v[6:9], off

.LBB1_31:
	s_andn2_b64 vcc, exec, s[4:5]
	s_cbranch_vccnz .LBB1_33
	s_load_dwordx4 s[4:7], s[0:1], 0x18
	s_add_i32 s8, s16, 0xffffc000
	s_and_b32 s9, s16, 63
	s_and_b32 s10, s8, 0xfffc0
	s_lshl_b32 s2, s9, 8
	v_lshrrev_b32_e32 v1, 4, v0
	s_waitcnt lgkmcnt(0)
	s_add_u32 s2, s4, s2
	v_lshlrev_b32_e32 v2, 4, v0
	s_addc_u32 s3, s5, 0
	v_and_b32_e32 v18, 0xf0, v2
	v_mov_b32_e32 v19, 0
	v_or_b32_e32 v2, s10, v1
	v_lshl_add_u64 v[14:15], s[2:3], 0, v[18:19]
	v_lshlrev_b32_e32 v16, 12, v2
	v_mov_b32_e32 v17, v19
	s_movk_i32 s2, 0x104
	v_lshl_add_u64 v[10:11], v[16:17], 2, v[14:15]
	v_mad_u32_u24 v1, v1, s2, v18
	v_or_b32_e32 v18, 0x10000, v16
	v_lshl_add_u64 v[12:13], v[18:19], 2, v[14:15]
	global_load_dwordx4 v[2:5], v[10:11], off nt
	global_load_dwordx4 v[6:9], v[12:13], off nt
	v_or_b32_e32 v18, 0x20000, v16
	v_lshl_add_u64 v[10:11], v[18:19], 2, v[14:15]
	global_load_dwordx4 v[10:13], v[10:11], off nt
	v_or_b32_e32 v18, 0x30000, v16
	v_lshl_add_u64 v[14:15], v[18:19], 2, v[14:15]
	global_load_dwordx4 v[14:17], v[14:15], off nt
	v_and_b32_e32 v20, 15, v0
	v_lshrrev_b32_e32 v21, 1, v0
	s_movk_i32 s3, 0xc0
	v_and_b32_e32 v21, 24, v21
	v_lshlrev_b32_e32 v20, 2, v20
	v_and_or_b32 v20, v0, s3, v20
	v_or_b32_e32 v23, 32, v21
	v_mad_u32_u24 v30, v21, s2, v20
	v_mad_u32_u24 v23, v23, s2, v20
	s_lshr_b32 s2, s8, 5
	v_lshrrev_b32_e32 v18, 6, v0
	v_add_u32_e32 v24, 0x1040, v1
	v_add_u32_e32 v25, 0x1048, v1
	v_add_u32_e32 v26, 0x2080, v1
	v_add_u32_e32 v27, 0x2088, v1
	v_add_u32_e32 v28, 0x30c0, v1
	v_add_u32_e32 v29, 0x30c8, v1
	v_add_u32_e32 v31, 0x400, v30
	v_add_u32_e32 v32, 0x400, v23
	s_and_b32 s2, s2, 0x7ffffe
	s_movk_i32 s4, 0x60
	v_lshlrev_b32_e32 v22, 3, v0
	v_lshl_or_b32 v18, s9, 2, v18
	v_mov_b32_e32 v20, s2
	v_and_b32_e32 v22, 0x1f8, v22
	v_mad_u32_u24 v18, v18, s4, v20
	v_lshl_or_b32 v18, v18, 9, v22
	v_lshl_add_u64 v[20:21], v[18:19], 1, s[6:7]
	v_or_b32_e32 v18, 0x200, v18
	v_lshl_add_u64 v[18:19], v[18:19], 1, s[6:7]
	s_waitcnt vmcnt(3)
	ds_write2_b32 v1, v2, v3 offset1:1
	ds_write2_b32 v1, v4, v5 offset0:2 offset1:3
	s_waitcnt vmcnt(2)
	ds_write2_b32 v24, v6, v7 offset1:1
	ds_write2_b32 v25, v8, v9 offset1:1
	s_waitcnt vmcnt(1)
	ds_write2_b32 v26, v10, v11 offset1:1
	ds_write2_b32 v27, v12, v13 offset1:1
	s_waitcnt vmcnt(0)
	ds_write2_b32 v28, v14, v15 offset1:1
	ds_write2_b32 v29, v16, v17 offset1:1
	s_waitcnt lgkmcnt(0)
	s_barrier
	ds_read2_b32 v[6:7], v30 offset1:65
	ds_read2_b32 v[2:3], v30 offset0:130 offset1:195
	ds_read2_b32 v[8:9], v31 offset0:4 offset1:69
	ds_read2_b32 v[4:5], v31 offset0:134 offset1:199
	ds_read2_b32 v[10:11], v23 offset1:65
	ds_read2_b32 v[12:13], v23 offset0:130 offset1:195
	ds_read2_b32 v[14:15], v32 offset0:4 offset1:69
	ds_read2_b32 v[16:17], v32 offset0:134 offset1:199
	s_waitcnt lgkmcnt(4)
	v_cvt_pk_f16_f32 v5, v4, v5
	v_cvt_pk_f16_f32 v4, v8, v9
	v_cvt_pk_f16_f32 v3, v2, v3
	v_cvt_pk_f16_f32 v2, v6, v7
	s_waitcnt lgkmcnt(0)
	v_cvt_pk_f16_f32 v9, v16, v17
	v_cvt_pk_f16_f32 v8, v14, v15
	v_cvt_pk_f16_f32 v7, v12, v13
	v_cvt_pk_f16_f32 v6, v10, v11
	global_store_dwordx4 v[20:21], v[2:5], off
	global_store_dwordx4 v[18:19], v[6:9], off

.LBB1_34:
	s_load_dwordx4 s[4:7], s[0:1], 0x0
	s_load_dwordx2 s[2:3], s[0:1], 0x10
	v_lshrrev_b32_e32 v1, 7, v0
	v_mov_b32_e32 v9, 0
	v_lshl_or_b32 v8, s16, 1, v1
	s_waitcnt lgkmcnt(0)
	v_lshl_add_u64 v[2:3], v[8:9], 2, s[4:5]
	global_load_dword v2, v[2:3], off
	v_lshlrev_b32_e32 v0, 3, v0
	v_and_b32_e32 v10, 0x3f8, v0
	v_mov_b32_e32 v1, v9
	v_lshlrev_b32_e32 v0, 2, v10
	v_mov_b32_e32 v11, v9
	s_waitcnt vmcnt(0)
	v_ashrrev_i32_e32 v3, 31, v2
	v_lshlrev_b64 v[2:3], 12, v[2:3]
	v_lshl_add_u64 v[2:3], s[6:7], 0, v[2:3]
	v_lshl_add_u64 v[12:13], v[2:3], 0, v[0:1]
	global_load_dwordx4 v[0:3], v[12:13], off nt
	global_load_dwordx4 v[4:7], v[12:13], off offset:16 nt
	v_mov_b32_e32 v12, v9
	v_mov_b32_e32 v13, v9
	s_waitcnt vmcnt(1)
	v_cvt_pk_fp8_f32 v12, v0, v1
	s_waitcnt vmcnt(0)
	v_cvt_pk_fp8_f32 v13, v4, v5
	v_lshlrev_b64 v[0:1], 10, v[8:9]
	v_lshl_add_u64 v[0:1], s[2:3], 0, v[0:1]
	v_cvt_pk_fp8_f32 v12, v2, v3 op_sel:[0,0,1]
	v_cvt_pk_fp8_f32 v13, v6, v7 op_sel:[0,0,1]
	v_lshl_add_u64 v[0:1], v[0:1], 0, v[10:11]
	global_store_dwordx2 v[0:1], v[12:13], off
	s_endpgm
	s_nop 0
	s_nop 0
	s_nop 0
	s_nop 0
	s_nop 0
	s_nop 0
	s_nop 0
	s_nop 0
	s_nop 0
	s_nop 0
	s_nop 0
	s_nop 0
	s_nop 0
	s_nop 0
	s_nop 0
	s_nop 0
	s_nop 0
	s_nop 0
	s_nop 0
	s_nop 0
	s_nop 0
	s_nop 0
	s_nop 0
	s_nop 0
	s_nop 0
	s_nop 0
	s_nop 0
	s_nop 0
	s_nop 0
	s_nop 0
	s_nop 0
	s_nop 0
	s_nop 0
	s_nop 0
	s_nop 0
	s_nop 0
	s_nop 0
	s_nop 0
	s_nop 0
	s_nop 0
	s_nop 0
	s_nop 0
	s_endpgm

.LBB2_6:
	s_load_dword s3, s[0:1], 0x30
	s_load_dwordx4 s[4:7], s[0:1], 0x20
	v_lshlrev_b32_e32 v2, 4, v0
	v_and_b32_e32 v10, 0xf0, v2
	v_mov_b32_e32 v11, 0
	s_waitcnt lgkmcnt(0)
	s_add_i32 s0, s2, s3
	s_add_i32 s1, s0, 0xffffff80
	s_mul_hi_i32 s0, s1, 0x10624dd3
	s_lshr_b32 s2, s0, 31
	s_ashr_i32 s0, s0, 5
	s_add_i32 s0, s0, s2
	s_mul_i32 s2, s0, 0x1f4
	s_sub_i32 s1, s1, s2
	s_lshl_b32 s2, s1, 6
	s_ashr_i32 s3, s2, 31
	s_lshl_b32 s0, s0, 6
	s_lshl_b64 s[8:9], s[2:3], 2
	s_add_u32 s4, s4, s8
	s_addc_u32 s5, s5, s9
	v_lshl_add_u64 v[6:7], s[4:5], 0, v[10:11]
	v_or_b32_e32 v2, s0, v1
	s_mov_b32 s1, 0x1f400
	v_or_b32_e32 v8, 0x200, v0
	v_mad_i64_i32 v[2:3], s[4:5], v2, s1, v[6:7]
	v_lshrrev_b32_e32 v12, 4, v8
	global_load_dwordx4 v[2:5], v[2:3], off nt
	v_or_b32_e32 v8, s0, v12
	v_mad_i64_i32 v[6:7], s[4:5], v8, s1, v[6:7]
	global_load_dwordx4 v[6:9], v[6:7], off nt
	v_lshrrev_b32_e32 v13, 3, v0
	v_lshlrev_b32_e32 v0, 3, v0
	v_and_b32_e32 v14, 56, v0
	v_mul_u32_u24_e32 v0, 0x104, v14
	s_movk_i32 s1, 0x104
	v_lshl_add_u32 v16, v13, 2, v0
	v_or_b32_e32 v0, s2, v13
	v_mad_u32_u24 v15, v1, s1, v10
	v_ashrrev_i32_e32 v1, 31, v0
	v_lshlrev_b64 v[0:1], 11, v[0:1]
	v_mad_u32_u24 v10, v12, s1, v10
	v_add_u32_e32 v17, 0x400, v16
	v_lshl_add_u64 v[0:1], s[6:7], 0, v[0:1]
	s_ashr_i32 s1, s0, 31
	v_lshl_add_u64 v[12:13], s[0:1], 1, v[0:1]
	s_waitcnt vmcnt(1)
	ds_write2_b32 v15, v2, v3 offset1:1
	ds_write2_b32 v15, v4, v5 offset0:2 offset1:3
	s_waitcnt vmcnt(0)
	ds_write2_b32 v10, v6, v7 offset1:1
	ds_write2_b32 v10, v8, v9 offset0:2 offset1:3
	s_waitcnt lgkmcnt(0)
	s_barrier
	ds_read2_b32 v[0:1], v17 offset0:134 offset1:199
	ds_read2_b32 v[4:5], v17 offset0:4 offset1:69
	ds_read2_b32 v[6:7], v16 offset0:130 offset1:195
	ds_read2_b32 v[8:9], v16 offset1:65
	v_lshlrev_b32_e32 v10, 1, v14
	s_waitcnt lgkmcnt(3)
	v_cvt_pk_f16_f32 v3, v0, v1
	s_waitcnt lgkmcnt(2)
	v_cvt_pk_f16_f32 v2, v4, v5
	s_waitcnt lgkmcnt(1)
	v_cvt_pk_f16_f32 v1, v6, v7
	s_waitcnt lgkmcnt(0)
	v_cvt_pk_f16_f32 v0, v8, v9
	v_lshl_add_u64 v[4:5], v[12:13], 0, v[10:11]
	global_store_dwordx4 v[4:5], v[0:3], off
	s_endpgm
	s_nop 0
	s_nop 0
	s_nop 0
	s_nop 0
	s_nop 0
	s_nop 0
	s_nop 0
	s_nop 0
	s_nop 0
	s_nop 0
	s_nop 0
	s_nop 0
	s_nop 0
	s_nop 0
	s_nop 0
	s_nop 0
	s_nop 0
	s_nop 0
	s_nop 0
	s_nop 0
	s_nop 0
	s_nop 0
	s_nop 0
	s_nop 0
	s_nop 0
	s_nop 0
	s_nop 0
	s_nop 0
	s_nop 0
	s_nop 0
	s_nop 0
	s_nop 0
	s_nop 0
	s_nop 0
	s_nop 0
	s_nop 0
	s_nop 0
	s_nop 0
	s_nop 0
	s_nop 0
	s_nop 0
	s_nop 0
	s_nop 0
	s_nop 0
	s_nop 0
	s_nop 0
	s_nop 0
	s_endpgm

_ZN12_GLOBAL__N_110gemm_fullkILi0ELi0EEEvPKDF16_S2_PKfPDF16_PfS6_S4_S4_S4_S4_S4_S5_:
	s_load_dwordx8 s[4:11], s[0:1], 0x0
	s_lshr_b32 s0, s2, 5
	v_lshrrev_b32_e32 v230, 6, v0
	s_and_b32 s12, s0, 0x7fffffc
	s_and_b32 s2, s2, 0x7f
	s_mov_b32 s13, 0
	v_mul_u32_u24_e32 v4, 12, v230
	v_mov_b32_e32 v3, 0
	s_lshl_b64 s[0:1], s[12:13], 10
	s_mul_i32 s13, s2, 0xc0
	v_and_b32_e32 v1, 63, v0
	v_mul_u32_u24_e32 v2, 0x18000, v230
	v_add_lshl_u32 v4, s13, v4, 10
	v_mov_b32_e32 v5, v3
	s_waitcnt lgkmcnt(0)
	v_lshl_add_u64 v[4:5], s[6:7], 0, v[4:5]
	v_lshl_add_u64 v[6:7], s[4:5], 0, v[2:3]
	v_lshlrev_b32_e32 v2, 4, v1
	s_mov_b32 s3, 0x18000
	v_lshl_add_u64 v[208:209], v[4:5], 0, v[2:3]
	v_add_co_u32_e32 v80, vcc, s3, v208
	v_lshl_add_u64 v[6:7], v[6:7], 0, s[0:1]
	s_nop 0
	v_addc_co_u32_e32 v81, vcc, 0, v209, vcc
	s_mov_b32 s0, 0x19000
	v_add_co_u32_e32 v176, vcc, s0, v208
	v_lshl_add_u64 v[212:213], v[6:7], 0, v[2:3]
	s_nop 0
	v_addc_co_u32_e32 v177, vcc, 0, v209, vcc
	s_movk_i32 s0, 0x2000
	v_add_co_u32_e32 v52, vcc, s0, v212
	s_movk_i32 s1, 0x4000
	s_nop 0
	v_addc_co_u32_e32 v53, vcc, 0, v213, vcc
	v_add_co_u32_e32 v82, vcc, s1, v212
	s_movk_i32 s1, 0x6000
	s_nop 0
	v_addc_co_u32_e32 v83, vcc, 0, v213, vcc
	v_add_co_u32_e32 v96, vcc, s1, v212
	s_movk_i32 s1, 0x1000
	s_nop 0
	v_addc_co_u32_e32 v97, vcc, 0, v213, vcc
	v_add_co_u32_e32 v168, vcc, s1, v208
	global_load_dwordx4 v[4:7], v[212:213], off
	global_load_dwordx4 v[8:11], v[212:213], off offset:1024
	global_load_dwordx4 v[12:15], v[212:213], off offset:2048
	global_load_dwordx4 v[16:19], v[212:213], off offset:3072
	global_load_dwordx4 v[20:23], v[208:209], off
	global_load_dwordx4 v[24:27], v[208:209], off offset:1024
	v_addc_co_u32_e32 v169, vcc, 0, v209, vcc
	v_add_co_u32_e32 v210, vcc, s0, v208
	s_mov_b32 s0, 0x8000
	s_nop 0
	v_addc_co_u32_e32 v211, vcc, 0, v209, vcc
	v_add_co_u32_e32 v116, vcc, s0, v212
	s_mov_b32 s0, 0xa000
	s_nop 0
	v_addc_co_u32_e32 v117, vcc, 0, v213, vcc
	v_add_co_u32_e32 v132, vcc, s0, v212
	s_mov_b32 s0, 0xc000
	s_nop 0
	v_addc_co_u32_e32 v133, vcc, 0, v213, vcc
	v_add_co_u32_e32 v164, vcc, s0, v212
	global_load_dwordx4 v[28:31], v[52:53], off
	global_load_dwordx4 v[32:35], v[52:53], off offset:1024
	global_load_dwordx4 v[36:39], v[52:53], off offset:2048
	global_load_dwordx4 v[40:43], v[52:53], off offset:3072
	global_load_dwordx4 v[44:47], v[80:81], off offset:1024
	global_load_dwordx4 v[48:51], v[80:81], off offset:2048
	s_nop 0
	global_load_dwordx4 v[52:55], v[82:83], off
	global_load_dwordx4 v[56:59], v[82:83], off offset:1024
	global_load_dwordx4 v[60:63], v[82:83], off offset:2048
	global_load_dwordx4 v[64:67], v[82:83], off offset:3072
	global_load_dwordx4 v[68:71], v[208:209], off offset:2048
	global_load_dwordx4 v[72:75], v[208:209], off offset:3072
	global_load_dwordx4 v[76:79], v[80:81], off offset:3072
	s_nop 0
	global_load_dwordx4 v[80:83], v[96:97], off
	global_load_dwordx4 v[84:87], v[96:97], off offset:1024
	global_load_dwordx4 v[88:91], v[96:97], off offset:2048
	global_load_dwordx4 v[92:95], v[96:97], off offset:3072
	s_nop 0
	global_load_dwordx4 v[96:99], v[176:177], off offset:-4096
	global_load_dwordx4 v[100:103], v[176:177], off
	global_load_dwordx4 v[104:107], v[116:117], off
	global_load_dwordx4 v[108:111], v[116:117], off offset:1024
	global_load_dwordx4 v[112:115], v[116:117], off offset:2048
	s_nop 0
	global_load_dwordx4 v[116:119], v[116:117], off offset:3072
	s_nop 0
	global_load_dwordx4 v[120:123], v[132:133], off
	global_load_dwordx4 v[124:127], v[132:133], off offset:1024
	global_load_dwordx4 v[128:131], v[132:133], off offset:2048
	s_nop 0
	global_load_dwordx4 v[132:135], v[132:133], off offset:3072
	s_nop 0
	global_load_dwordx4 v[136:139], v[168:169], off offset:1024
	global_load_dwordx4 v[140:143], v[168:169], off offset:2048
	global_load_dwordx4 v[144:147], v[176:177], off offset:1024
	global_load_dwordx4 v[148:151], v[176:177], off offset:2048
	v_addc_co_u32_e32 v165, vcc, 0, v213, vcc
	global_load_dwordx4 v[152:155], v[164:165], off
	global_load_dwordx4 v[156:159], v[164:165], off offset:1024
	global_load_dwordx4 v[160:163], v[164:165], off offset:2048
	s_nop 0
	global_load_dwordx4 v[164:167], v[164:165], off offset:3072
	s_nop 0
	global_load_dwordx4 v[168:171], v[168:169], off offset:3072
	s_nop 0
	global_load_dwordx4 v[172:175], v[210:211], off offset:-4096
	s_nop 0
	global_load_dwordx4 v[176:179], v[176:177], off offset:3072
	s_mov_b32 s0, 0xe000
	v_add_co_u32_e32 v192, vcc, s0, v212
	s_lshl_b32 s0, s2, 7
	s_nop 0
	v_addc_co_u32_e32 v193, vcc, 0, v213, vcc
	global_load_dwordx4 v[180:183], v[192:193], off
	global_load_dwordx4 v[184:187], v[192:193], off offset:1024
	global_load_dwordx4 v[188:191], v[192:193], off offset:2048
	s_nop 0
	global_load_dwordx4 v[192:195], v[192:193], off offset:3072
	v_bfe_u32 v1, v0, 6, 1
	s_add_u32 s0, s8, s0
	s_addc_u32 s1, s9, 0
	v_lshlrev_b32_e32 v196, 6, v1
	v_mov_b32_e32 v197, v3
	v_lshl_add_u64 v[196:197], s[0:1], 0, v[196:197]
	v_and_b32_e32 v198, 48, v0
	v_mov_b32_e32 v199, v3
	v_lshl_add_u64 v[228:229], v[196:197], 0, v[198:199]
	s_waitcnt vmcnt(43)
	v_mfma_f32_16x16x32_f16 v[196:199], v[20:23], v[4:7], 0
	s_waitcnt vmcnt(24)
	v_mfma_f32_16x16x32_f16 v[4:7], v[96:99], v[4:7], 0
	v_mfma_f32_16x16x32_f16 v[200:203], v[20:23], v[8:11], 0
	v_mfma_f32_16x16x32_f16 v[8:11], v[96:99], v[8:11], 0
	v_mfma_f32_16x16x32_f16 v[204:207], v[20:23], v[12:15], 0
	v_mfma_f32_16x16x32_f16 v[12:15], v[96:99], v[12:15], 0
	v_mfma_f32_16x16x32_f16 v[20:23], v[20:23], v[16:19], 0
	v_mfma_f32_16x16x32_f16 v[16:19], v[96:99], v[16:19], 0
	v_mfma_f32_16x16x32_f16 v[96:99], v[24:27], v[28:31], v[196:199]
	v_mfma_f32_16x16x32_f16 v[4:7], v[44:47], v[28:31], v[4:7]
	v_mfma_f32_16x16x32_f16 v[28:31], v[24:27], v[32:35], v[200:203]
	v_mfma_f32_16x16x32_f16 v[8:11], v[44:47], v[32:35], v[8:11]
	v_mfma_f32_16x16x32_f16 v[32:35], v[24:27], v[36:39], v[204:207]
	v_mfma_f32_16x16x32_f16 v[12:15], v[44:47], v[36:39], v[12:15]
	v_mfma_f32_16x16x32_f16 v[20:23], v[24:27], v[40:43], v[20:23]
	v_mfma_f32_16x16x32_f16 v[16:19], v[44:47], v[40:43], v[16:19]
	v_mfma_f32_16x16x32_f16 v[24:27], v[68:71], v[52:55], v[96:99]
	v_mfma_f32_16x16x32_f16 v[4:7], v[48:51], v[52:55], v[4:7]
	v_mfma_f32_16x16x32_f16 v[28:31], v[68:71], v[56:59], v[28:31]
	v_mfma_f32_16x16x32_f16 v[8:11], v[48:51], v[56:59], v[8:11]
	v_mfma_f32_16x16x32_f16 v[32:35], v[68:71], v[60:63], v[32:35]
	v_mfma_f32_16x16x32_f16 v[12:15], v[48:51], v[60:63], v[12:15]
	v_mfma_f32_16x16x32_f16 v[20:23], v[68:71], v[64:67], v[20:23]
	v_mfma_f32_16x16x32_f16 v[16:19], v[48:51], v[64:67], v[16:19]
	v_mfma_f32_16x16x32_f16 v[24:27], v[72:75], v[80:83], v[24:27]
	v_mfma_f32_16x16x32_f16 v[4:7], v[76:79], v[80:83], v[4:7]
	v_mfma_f32_16x16x32_f16 v[28:31], v[72:75], v[84:87], v[28:31]
	v_mfma_f32_16x16x32_f16 v[8:11], v[76:79], v[84:87], v[8:11]
	v_mfma_f32_16x16x32_f16 v[32:35], v[72:75], v[88:91], v[32:35]
	v_mfma_f32_16x16x32_f16 v[12:15], v[76:79], v[88:91], v[12:15]
	v_mfma_f32_16x16x32_f16 v[20:23], v[72:75], v[92:95], v[20:23]
	v_mfma_f32_16x16x32_f16 v[16:19], v[76:79], v[92:95], v[16:19]
	s_mov_b32 s0, 0x1a000
	v_add_co_u32_e32 v208, vcc, s0, v208
	s_mov_b32 s0, 0x10000
	s_nop 0
	v_addc_co_u32_e32 v209, vcc, 0, v209, vcc
	v_add_co_u32_e32 v48, vcc, s0, v212
	s_mov_b32 s0, 0x12000
	s_nop 0
	v_addc_co_u32_e32 v49, vcc, 0, v213, vcc
	v_add_co_u32_e32 v80, vcc, s0, v212
	s_mov_b32 s0, 0x14000
	s_nop 0
	v_addc_co_u32_e32 v81, vcc, 0, v213, vcc
	v_add_co_u32_e32 v96, vcc, s0, v212
	global_load_dwordx4 v[36:39], v[48:49], off
	global_load_dwordx4 v[40:43], v[48:49], off offset:1024
	global_load_dwordx4 v[44:47], v[48:49], off offset:2048
	s_nop 0
	global_load_dwordx4 v[48:51], v[48:49], off offset:3072
	s_nop 0
	global_load_dwordx4 v[52:55], v[210:211], off
	global_load_dwordx4 v[56:59], v[210:211], off offset:1024
	global_load_dwordx4 v[60:63], v[208:209], off
	global_load_dwordx4 v[64:67], v[208:209], off offset:1024
	v_addc_co_u32_e32 v97, vcc, 0, v213, vcc
	global_load_dwordx4 v[68:71], v[80:81], off
	global_load_dwordx4 v[72:75], v[80:81], off offset:1024
	global_load_dwordx4 v[76:79], v[80:81], off offset:2048
	s_nop 0
	global_load_dwordx4 v[80:83], v[80:81], off offset:3072
	s_nop 0
	global_load_dwordx4 v[84:87], v[96:97], off
	global_load_dwordx4 v[88:91], v[96:97], off offset:1024
	global_load_dwordx4 v[92:95], v[96:97], off offset:2048
	s_nop 0
	global_load_dwordx4 v[96:99], v[96:97], off offset:3072
	s_nop 0
	global_load_dwordx4 v[196:199], v[210:211], off offset:2048
	global_load_dwordx4 v[200:203], v[210:211], off offset:3072
	global_load_dwordx4 v[204:207], v[208:209], off offset:2048
	s_nop 0
	global_load_dwordx4 v[208:211], v[208:209], off offset:3072
	s_mov_b32 s0, 0x16000
	v_add_co_u32_e32 v224, vcc, s0, v212
	s_nop 1
	v_addc_co_u32_e32 v225, vcc, 0, v213, vcc
	global_load_dwordx4 v[212:215], v[224:225], off
	global_load_dwordx4 v[216:219], v[224:225], off offset:1024
	global_load_dwordx4 v[220:223], v[224:225], off offset:2048
	s_nop 0
	global_load_dwordx4 v[224:227], v[224:225], off offset:3072
	s_waitcnt vmcnt(29)
	v_mfma_f32_16x16x32_f16 v[24:27], v[172:175], v[104:107], v[24:27]
	v_mfma_f32_16x16x32_f16 v[4:7], v[100:103], v[104:107], v[4:7]
	v_mfma_f32_16x16x32_f16 v[28:31], v[172:175], v[108:111], v[28:31]
	v_mfma_f32_16x16x32_f16 v[8:11], v[100:103], v[108:111], v[8:11]
	v_mfma_f32_16x16x32_f16 v[32:35], v[172:175], v[112:115], v[32:35]
	v_mfma_f32_16x16x32_f16 v[12:15], v[100:103], v[112:115], v[12:15]
	v_mfma_f32_16x16x32_f16 v[20:23], v[172:175], v[116:119], v[20:23]
	v_mfma_f32_16x16x32_f16 v[16:19], v[100:103], v[116:119], v[16:19]
	v_mfma_f32_16x16x32_f16 v[24:27], v[136:139], v[120:123], v[24:27]
	v_mfma_f32_16x16x32_f16 v[4:7], v[144:147], v[120:123], v[4:7]
	v_mfma_f32_16x16x32_f16 v[28:31], v[136:139], v[124:127], v[28:31]
	v_mfma_f32_16x16x32_f16 v[8:11], v[144:147], v[124:127], v[8:11]
	v_mfma_f32_16x16x32_f16 v[32:35], v[136:139], v[128:131], v[32:35]
	v_mfma_f32_16x16x32_f16 v[12:15], v[144:147], v[128:131], v[12:15]
	v_mfma_f32_16x16x32_f16 v[20:23], v[136:139], v[132:135], v[20:23]
	v_mfma_f32_16x16x32_f16 v[16:19], v[144:147], v[132:135], v[16:19]
	v_mfma_f32_16x16x32_f16 v[24:27], v[140:143], v[152:155], v[24:27]
	v_mfma_f32_16x16x32_f16 v[4:7], v[148:151], v[152:155], v[4:7]
	v_mfma_f32_16x16x32_f16 v[28:31], v[140:143], v[156:159], v[28:31]
	v_mfma_f32_16x16x32_f16 v[8:11], v[148:151], v[156:159], v[8:11]
	v_mfma_f32_16x16x32_f16 v[32:35], v[140:143], v[160:163], v[32:35]
	v_mfma_f32_16x16x32_f16 v[12:15], v[148:151], v[160:163], v[12:15]
	v_mfma_f32_16x16x32_f16 v[20:23], v[140:143], v[164:167], v[20:23]
	v_mfma_f32_16x16x32_f16 v[16:19], v[148:151], v[164:167], v[16:19]
	s_waitcnt vmcnt(27)
	v_mfma_f32_16x16x32_f16 v[24:27], v[168:171], v[180:183], v[24:27]
	v_mfma_f32_16x16x32_f16 v[4:7], v[176:179], v[180:183], v[4:7]
	s_waitcnt vmcnt(26)
	v_mfma_f32_16x16x32_f16 v[28:31], v[168:171], v[184:187], v[28:31]
	v_mfma_f32_16x16x32_f16 v[8:11], v[176:179], v[184:187], v[8:11]
	s_waitcnt vmcnt(25)
	v_mfma_f32_16x16x32_f16 v[32:35], v[168:171], v[188:191], v[32:35]
	v_mfma_f32_16x16x32_f16 v[12:15], v[176:179], v[188:191], v[12:15]
	s_waitcnt vmcnt(24)
	v_mfma_f32_16x16x32_f16 v[20:23], v[168:171], v[192:195], v[20:23]
	v_mfma_f32_16x16x32_f16 v[16:19], v[176:179], v[192:195], v[16:19]
	s_waitcnt vmcnt(19)
	v_mfma_f32_16x16x32_f16 v[24:27], v[52:55], v[36:39], v[24:27]
	s_waitcnt vmcnt(17)
	v_mfma_f32_16x16x32_f16 v[4:7], v[60:63], v[36:39], v[4:7]
	v_mfma_f32_16x16x32_f16 v[28:31], v[52:55], v[40:43], v[28:31]
	v_mfma_f32_16x16x32_f16 v[8:11], v[60:63], v[40:43], v[8:11]
	v_mfma_f32_16x16x32_f16 v[32:35], v[52:55], v[44:47], v[32:35]
	v_mfma_f32_16x16x32_f16 v[12:15], v[60:63], v[44:47], v[12:15]
	v_mfma_f32_16x16x32_f16 v[20:23], v[52:55], v[48:51], v[20:23]
	v_mfma_f32_16x16x32_f16 v[16:19], v[60:63], v[48:51], v[16:19]
	s_waitcnt vmcnt(15)
	v_mfma_f32_16x16x32_f16 v[24:27], v[56:59], v[68:71], v[24:27]
	v_mfma_f32_16x16x32_f16 v[4:7], v[64:67], v[68:71], v[4:7]
	s_waitcnt vmcnt(14)
	v_mfma_f32_16x16x32_f16 v[28:31], v[56:59], v[72:75], v[28:31]
	v_mfma_f32_16x16x32_f16 v[8:11], v[64:67], v[72:75], v[8:11]
	s_waitcnt vmcnt(13)
	v_mfma_f32_16x16x32_f16 v[32:35], v[56:59], v[76:79], v[32:35]
	v_mfma_f32_16x16x32_f16 v[12:15], v[64:67], v[76:79], v[12:15]
	s_waitcnt vmcnt(12)
	v_mfma_f32_16x16x32_f16 v[20:23], v[56:59], v[80:83], v[20:23]
	v_mfma_f32_16x16x32_f16 v[16:19], v[64:67], v[80:83], v[16:19]
	s_waitcnt vmcnt(7)
	v_mfma_f32_16x16x32_f16 v[24:27], v[196:199], v[84:87], v[24:27]
	s_waitcnt vmcnt(5)
	v_mfma_f32_16x16x32_f16 v[4:7], v[204:207], v[84:87], v[4:7]
	v_mfma_f32_16x16x32_f16 v[28:31], v[196:199], v[88:91], v[28:31]
	v_mfma_f32_16x16x32_f16 v[8:11], v[204:207], v[88:91], v[8:11]
	v_mfma_f32_16x16x32_f16 v[32:35], v[196:199], v[92:95], v[32:35]
	v_mfma_f32_16x16x32_f16 v[12:15], v[204:207], v[92:95], v[12:15]
	v_mfma_f32_16x16x32_f16 v[20:23], v[196:199], v[96:99], v[20:23]
	v_mfma_f32_16x16x32_f16 v[16:19], v[204:207], v[96:99], v[16:19]
	s_waitcnt vmcnt(3)
	v_mfma_f32_16x16x32_f16 v[24:27], v[200:203], v[212:215], v[24:27]
	v_mfma_f32_16x16x32_f16 v[4:7], v[208:211], v[212:215], v[4:7]
	s_waitcnt vmcnt(2)
	v_mfma_f32_16x16x32_f16 v[28:31], v[200:203], v[216:219], v[28:31]
	v_mfma_f32_16x16x32_f16 v[8:11], v[208:211], v[216:219], v[8:11]
	s_waitcnt vmcnt(1)
	v_mfma_f32_16x16x32_f16 v[32:35], v[200:203], v[220:223], v[32:35]
	v_mfma_f32_16x16x32_f16 v[12:15], v[208:211], v[220:223], v[12:15]
	s_waitcnt vmcnt(0)
	v_mfma_f32_16x16x32_f16 v[20:23], v[200:203], v[224:227], v[20:23]
	v_mfma_f32_16x16x32_f16 v[16:19], v[208:211], v[224:227], v[16:19]
	global_load_dwordx4 v[36:39], v[228:229], off
	v_add_u32_e32 v2, 0, v2
	v_and_b32_e32 v41, 0x1c0, v0
	v_lshl_add_u32 v43, v230, 13, v2
	v_lshl_add_u32 v2, v41, 4, v2
	v_lshl_add_u32 v40, v0, 4, 0
	ds_write_b128 v43, v[24:27]
	ds_write_b128 v43, v[4:7] offset:1024
	ds_write_b128 v43, v[28:31] offset:2048
	ds_write_b128 v43, v[8:11] offset:3072
	ds_write_b128 v43, v[32:35] offset:4096
	ds_write_b128 v43, v[12:15] offset:5120
	ds_write_b128 v43, v[20:23] offset:6144
	ds_write_b128 v43, v[16:19] offset:7168
	s_waitcnt lgkmcnt(0)
	s_barrier
	ds_read_b128 v[4:7], v2 offset:8192
	ds_read_b128 v[8:11], v2 offset:16384
	ds_read_b128 v[12:15], v2 offset:24576
	ds_read_b128 v[16:19], v40
	ds_read_b128 v[20:23], v2 offset:32768
	ds_read_b128 v[24:27], v2 offset:40960
	ds_read_b128 v[28:31], v2 offset:49152
	ds_read_b128 v[32:35], v2 offset:57344
	s_waitcnt lgkmcnt(4)
	v_pk_add_f32 v[4:5], v[16:17], v[4:5]
	v_pk_add_f32 v[6:7], v[18:19], v[6:7]
	v_pk_add_f32 v[4:5], v[4:5], v[8:9]
	v_pk_add_f32 v[6:7], v[6:7], v[10:11]
	v_pk_add_f32 v[4:5], v[4:5], v[12:13]
	v_pk_add_f32 v[6:7], v[6:7], v[14:15]
	s_waitcnt lgkmcnt(3)
	v_pk_add_f32 v[4:5], v[4:5], v[20:21]
	v_pk_add_f32 v[6:7], v[6:7], v[22:23]
	s_waitcnt lgkmcnt(2)
	v_pk_add_f32 v[4:5], v[4:5], v[24:25]
	v_pk_add_f32 v[6:7], v[6:7], v[26:27]
	s_waitcnt lgkmcnt(1)
	v_pk_add_f32 v[4:5], v[4:5], v[28:29]
	v_pk_add_f32 v[6:7], v[6:7], v[30:31]
	s_waitcnt lgkmcnt(0)
	v_pk_add_f32 v[4:5], v[4:5], v[32:33]
	v_pk_add_f32 v[6:7], v[6:7], v[34:35]
	v_lshrrev_b32_e32 v42, 7, v0
	s_waitcnt vmcnt(0)
	v_pk_add_f32 v[4:5], v[36:37], v[4:5]
	v_pk_add_f32 v[6:7], v[38:39], v[6:7]
	v_mul_f32_e32 v2, 0x3d372713, v4
	v_mul_f32_e32 v8, 0x3d372713, v5
	v_mul_f32_e32 v9, 0x3d372713, v6
	v_mul_f32_e32 v2, v4, v2
	v_mul_f32_e32 v8, v5, v8
	v_mul_f32_e32 v9, v6, v9
	v_fma_f32 v2, v4, v2, v4
	v_fma_f32 v8, v5, v8, v5
	v_fma_f32 v9, v6, v9, v6
	v_mul_f32_e32 v2, 0x3f4c422a, v2
	v_mul_f32_e32 v8, 0x3f4c422a, v8
	v_mul_f32_e32 v9, 0x3f4c422a, v9
	v_add_f32_e32 v2, v2, v2
	v_add_f32_e32 v8, v8, v8
	v_add_f32_e32 v9, v9, v9
	v_mul_f32_e32 v2, 0x3fb8aa3b, v2
	v_mul_f32_e32 v11, 0x3fb8aa3b, v8
	v_mul_f32_e32 v10, 0x3d372713, v7
	v_mul_f32_e32 v12, 0x3fb8aa3b, v9
	v_exp_f32_e32 v8, v2
	v_exp_f32_e32 v9, v11
	v_mul_f32_e32 v10, v7, v10
	v_fma_f32 v10, v7, v10, v7
	v_mul_f32_e32 v10, 0x3f4c422a, v10
	v_add_f32_e32 v10, v10, v10
	v_pk_add_f32 v[8:9], v[8:9], 1.0 op_sel_hi:[1,0]
	v_mul_f32_e32 v13, 0x3fb8aa3b, v10
	v_div_scale_f32 v2, s[0:1], v9, v9, 2.0
	v_exp_f32_e32 v10, v12
	v_exp_f32_e32 v11, v13
	v_div_scale_f32 v14, s[0:1], v8, v8, 2.0
	v_rcp_f32_e32 v16, v2
	v_rcp_f32_e32 v17, v14
	v_pk_add_f32 v[10:11], v[10:11], 1.0 op_sel_hi:[1,0]
	v_div_scale_f32 v13, vcc, 2.0, v9, 2.0
	v_fma_f32 v20, -v2, v16, 1.0
	v_div_scale_f32 v15, s[0:1], v11, v11, 2.0
	v_fma_f32 v21, -v14, v17, 1.0
	v_fmac_f32_e32 v16, v20, v16
	v_div_scale_f32 v19, s[0:1], 2.0, v8, 2.0
	v_fmac_f32_e32 v17, v21, v17
	v_mul_f32_e32 v20, v13, v16
	v_mul_f32_e32 v21, v19, v17
	v_fma_f32 v23, -v2, v20, v13
	v_fma_f32 v24, -v14, v21, v19
	v_fmac_f32_e32 v20, v23, v16
	v_fmac_f32_e32 v21, v24, v17
	v_fma_f32 v2, -v2, v20, v13
	v_rcp_f32_e32 v18, v15
	v_fma_f32 v13, -v14, v21, v19
	v_div_fmas_f32 v2, v2, v16, v20
	s_mov_b64 vcc, s[0:1]
	v_div_fixup_f32 v9, v2, v9, 2.0
	v_div_fmas_f32 v2, v13, v17, v21
	v_div_fixup_f32 v8, v2, v8, 2.0
	v_pk_add_f32 v[8:9], v[8:9], 1.0 op_sel_hi:[1,0] neg_lo:[1,0] neg_hi:[1,0]
	v_pk_mul_f32 v[4:5], v[4:5], 0.5 op_sel_hi:[1,0]
	v_fma_f32 v22, -v15, v18, 1.0
	v_pk_add_f32 v[8:9], v[8:9], 1.0 op_sel_hi:[1,0]
	v_fmac_f32_e32 v18, v22, v18
	v_pk_mul_f32 v[4:5], v[4:5], v[8:9]
	v_div_scale_f32 v2, vcc, 2.0, v11, 2.0
	v_cvt_pk_f16_f32 v4, v4, v5
	v_mul_f32_e32 v5, v2, v18
	v_fma_f32 v8, -v15, v5, v2
	v_fmac_f32_e32 v5, v8, v18
	v_div_scale_f32 v8, s[0:1], v10, v10, 2.0
	v_rcp_f32_e32 v13, v8
	v_fma_f32 v2, -v15, v5, v2
	v_div_fmas_f32 v2, v2, v18, v5
	v_div_fixup_f32 v9, v2, v11, 2.0
	v_fma_f32 v2, -v8, v13, 1.0
	v_fmac_f32_e32 v13, v2, v13
	v_div_scale_f32 v2, vcc, 2.0, v10, 2.0
	v_mul_f32_e32 v5, v2, v13
	v_fma_f32 v11, -v8, v5, v2
	v_fmac_f32_e32 v5, v11, v13
	v_fma_f32 v2, -v8, v5, v2
	v_div_fmas_f32 v2, v2, v13, v5
	v_div_fixup_f32 v8, v2, v10, 2.0
	v_pk_add_f32 v[8:9], v[8:9], 1.0 op_sel_hi:[1,0] neg_lo:[1,0] neg_hi:[1,0]
	s_lshl_b32 s0, s2, 3
	v_pk_mul_f32 v[6:7], v[6:7], 0.5 op_sel_hi:[1,0]
	v_pk_add_f32 v[8:9], v[8:9], 1.0 op_sel_hi:[1,0]
	s_add_i32 s0, s0, s12
	v_pk_mul_f32 v[6:7], v[6:7], v[8:9]
	v_or_b32_e32 v2, s0, v42
	v_cvt_pk_f16_f32 v5, v6, v7
	v_lshlrev_b64 v[6:7], 6, v[2:3]
	v_lshrrev_b32_e32 v2, 1, v0
	v_and_b32_e32 v12, 15, v0
	v_and_b32_e32 v0, 16, v2
	v_lshl_or_b32 v0, v1, 5, v0
	v_or3_b32 v6, v6, v0, v12
	v_lshl_add_u64 v[0:1], v[6:7], 4, s[10:11]
	v_and_b32_e32 v2, 8, v2
	v_lshl_add_u64 v[0:1], v[0:1], 0, v[2:3]
	global_store_dwordx2 v[0:1], v[4:5], off
	s_endpgm
	s_nop 0
	s_nop 0
	s_nop 0
	s_nop 0
	s_nop 0
	s_nop 0
	s_nop 0
	s_nop 0
	s_nop 0
	s_nop 0
	s_nop 0
	s_nop 0
	s_nop 0
	s_nop 0
	s_nop 0
	s_nop 0
	s_nop 0
	s_nop 0
	s_nop 0
	s_nop 0
	s_nop 0
	s_nop 0
	s_nop 0
	s_nop 0
	s_nop 0
	s_nop 0
	s_nop 0
	s_nop 0
	s_nop 0
	s_nop 0
	s_nop 0
	s_endpgm

	.amdhsa_kernel _ZN12_GLOBAL__N_110gemm_fullkILi0ELi0EEEvPKDF16_S2_PKfPDF16_PfS6_S4_S4_S4_S4_S4_S5_
		.amdhsa_group_segment_fixed_size 0
		.amdhsa_private_segment_fixed_size 0
		.amdhsa_kernarg_size 96
		.amdhsa_user_sgpr_count 2
		.amdhsa_user_sgpr_dispatch_ptr 0
		.amdhsa_user_sgpr_queue_ptr 0
		.amdhsa_user_sgpr_kernarg_segment_ptr 1
		.amdhsa_user_sgpr_dispatch_id 0
		.amdhsa_user_sgpr_kernarg_preload_length 0
		.amdhsa_user_sgpr_kernarg_preload_offset 0
		.amdhsa_user_sgpr_private_segment_size 0
		.amdhsa_uses_dynamic_stack 0
		.amdhsa_enable_private_segment 0
		.amdhsa_system_sgpr_workgroup_id_x 1
		.amdhsa_system_sgpr_workgroup_id_y 0
		.amdhsa_system_sgpr_workgroup_id_z 0
		.amdhsa_system_sgpr_workgroup_info 0
		.amdhsa_system_vgpr_workitem_id 0
		.amdhsa_next_free_vgpr 231
		.amdhsa_next_free_sgpr 14
		.amdhsa_accum_offset 232
		.amdhsa_reserve_vcc 1
		.amdhsa_float_round_mode_32 0
		.amdhsa_float_round_mode_16_64 0
		.amdhsa_float_denorm_mode_32 3
		.amdhsa_float_denorm_mode_16_64 3
		.amdhsa_dx10_clamp 1
		.amdhsa_ieee_mode 1
		.amdhsa_fp16_overflow 0
		.amdhsa_tg_split 0
		.amdhsa_exception_fp_ieee_invalid_op 0
		.amdhsa_exception_fp_denorm_src 0
		.amdhsa_exception_fp_ieee_div_zero 0
		.amdhsa_exception_fp_ieee_overflow 0
		.amdhsa_exception_fp_ieee_underflow 0
		.amdhsa_exception_fp_ieee_inexact 0
		.amdhsa_exception_int_div_zero 0
	.end_amdhsa_kernel

_ZN12_GLOBAL__N_110gemm_fullkILi1ELi0EEEvPKDF16_S2_PKfPDF16_PfS6_S4_S4_S4_S4_S4_S5_:
	s_load_dwordx2 s[4:5], s[0:1], 0x38
	s_and_b32 s3, s2, 63
	s_lshl_b32 s16, s3, 5
	s_lshl_b32 s6, s3, 13
	v_lshlrev_b32_e32 v1, 4, v0
	s_waitcnt lgkmcnt(0)
	s_add_u32 s4, s4, s6
	s_addc_u32 s5, s5, 0
	global_load_dwordx4 v[2:5], v1, s[4:5]
	v_lshlrev_b32_e32 v1, 2, v0
	v_cmp_lt_u32_e32 vcc, 31, v0
	s_and_saveexec_b64 s[4:5], vcc
	s_xor_b64 s[4:5], exec, s[4:5]
	s_cbranch_execz .LBB9_10
	v_cmp_lt_u32_e32 vcc, 63, v0
	s_and_saveexec_b64 s[6:7], vcc
	s_xor_b64 s[6:7], exec, s[6:7]
	s_cbranch_execz .LBB9_7
	s_movk_i32 s8, 0x47
	v_cmp_lt_u32_e32 vcc, s8, v0
	s_and_saveexec_b64 s[8:9], vcc
	s_xor_b64 s[8:9], exec, s[8:9]
	s_cbranch_execz .LBB9_4
	s_load_dwordx2 s[10:11], s[0:1], 0x10
	s_lshl_b32 s12, s16, 2
	v_lshlrev_b32_e32 v6, 2, v1
	v_mov_b32_e32 v7, 0
	s_movk_i32 s14, 0x50
	s_waitcnt lgkmcnt(0)
	s_add_u32 s10, s10, s12
	s_addc_u32 s11, s11, 0
	s_movk_i32 s12, 0xfb80
	v_lshl_add_u64 v[6:7], s[10:11], 0, v[6:7]
	s_mov_b32 s13, -1
	v_lshl_add_u64 v[6:7], v[6:7], 0, s[12:13]
	v_mov_b32_e32 v8, s11
	v_cmp_gt_u32_e32 vcc, s14, v0
	s_nop 1
	v_cndmask_b32_e32 v7, v8, v7, vcc
	v_mov_b32_e32 v8, s10
	v_cndmask_b32_e32 v6, v8, v6, vcc
.LBB9_4:
	s_andn2_saveexec_b64 s[8:9], s[8:9]
	s_cbranch_execz .LBB9_6
	s_load_dwordx2 s[10:11], s[0:1], 0x50
	s_lshl_b32 s12, s16, 2
	v_lshlrev_b32_e32 v6, 2, v1
	v_mov_b32_e32 v7, 0
	s_waitcnt lgkmcnt(0)
	s_add_u32 s10, s10, s12
	s_addc_u32 s11, s11, 0
	v_lshl_add_u64 v[6:7], s[10:11], 0, v[6:7]
	s_movk_i32 s10, 0xfc00
	s_mov_b32 s11, -1
	v_lshl_add_u64 v[6:7], v[6:7], 0, s[10:11]

.LBB9_7:
	s_andn2_saveexec_b64 s[6:7], s[6:7]
	s_cbranch_execz .LBB9_9
	s_load_dwordx2 s[8:9], s[0:1], 0x48
	s_lshl_b32 s10, s3, 9
	v_lshlrev_b32_e32 v6, 2, v1
	v_mov_b32_e32 v7, 0
	s_waitcnt lgkmcnt(0)
	s_add_u32 s8, s8, s10
	s_addc_u32 s9, s9, 0
	v_lshl_add_u64 v[6:7], s[8:9], 0, v[6:7]
	s_movk_i32 s8, 0xfe00
	s_mov_b32 s9, -1
	v_lshl_add_u64 v[6:7], v[6:7], 0, s[8:9]

.LBB9_10:
	s_or_saveexec_b64 s[14:15], s[4:5]
	s_load_dwordx2 s[12:13], s[0:1], 0x58
	s_load_dwordx4 s[4:7], s[0:1], 0x20
	s_load_dwordx4 s[8:11], s[0:1], 0x0
	s_xor_b64 exec, exec, s[14:15]
	s_cbranch_execz .LBB9_12
	s_load_dwordx2 s[0:1], s[0:1], 0x40
	s_lshl_b32 s17, s3, 9
	v_lshlrev_b32_e32 v6, 2, v1
	v_mov_b32_e32 v7, 0
	s_waitcnt lgkmcnt(0)
	s_add_u32 s0, s0, s17
	s_addc_u32 s1, s1, 0
	v_lshl_add_u64 v[6:7], s[0:1], 0, v[6:7]
.LBB9_12:
	s_or_b64 exec, exec, s[14:15]
	v_lshrrev_b32_e32 v174, 6, v0
	v_mov_b32_e32 v9, 0
	v_lshlrev_b32_e32 v10, 14, v174
	v_and_b32_e32 v14, 63, v0
	s_lshr_b32 s0, s2, 5
	v_lshlrev_b32_e32 v8, 17, v174
	v_lshl_or_b32 v10, s3, 18, v10
	v_mov_b32_e32 v11, v9
	s_and_b32 s0, s0, 0x7fffffe
	s_mov_b32 s1, 0
	s_waitcnt lgkmcnt(0)
	v_lshl_add_u64 v[10:11], s[10:11], 0, v[10:11]
	v_lshl_add_u64 v[12:13], s[8:9], 0, v[8:9]
	v_lshlrev_b32_e32 v16, 4, v14
	v_mov_b32_e32 v17, v9
	v_lshrrev_b32_e32 v8, 8, v0
	s_lshl_b64 s[14:15], s[0:1], 10
	v_lshl_add_u64 v[170:171], v[10:11], 0, v[16:17]
	v_or_b32_e32 v19, s0, v8
	s_mov_b32 s0, 0x20000
	v_add_co_u32_e32 v22, vcc, s0, v170
	v_lshrrev_b32_e32 v11, 2, v0
	s_nop 0
	v_addc_co_u32_e32 v23, vcc, 0, v171, vcc
	s_mov_b32 s0, 0x21000
	v_lshl_add_u64 v[12:13], v[12:13], 0, s[14:15]
	v_lshrrev_b32_e32 v10, 3, v0
	v_and_b32_e32 v11, 12, v11
	v_add_co_u32_e32 v140, vcc, s0, v170
	v_lshl_add_u64 v[168:169], v[12:13], 0, v[16:17]
	v_and_b32_e32 v17, 15, v0
	v_bfe_u32 v21, v0, 6, 1
	v_and_or_b32 v20, v10, 16, v11
	v_addc_co_u32_e32 v141, vcc, 0, v171, vcc
	s_movk_i32 s0, 0x2000
	v_lshl_or_b32 v8, v19, 4, v17
	v_lshl_or_b32 v18, v21, 1, v20
	v_add_co_u32_e32 v56, vcc, s0, v168
	v_or_b32_e32 v12, s16, v18
	v_lshlrev_b64 v[10:11], 13, v[8:9]
	v_addc_co_u32_e32 v57, vcc, 0, v169, vcc
	s_movk_i32 s1, 0x4000
	v_lshlrev_b64 v[14:15], 11, v[8:9]
	v_lshl_add_u64 v[10:11], s[4:5], 0, v[10:11]
	v_lshlrev_b32_e32 v8, 2, v12
	v_add_co_u32_e32 v76, vcc, s1, v168
	v_lshl_add_u64 v[10:11], v[10:11], 0, v[8:9]
	s_nop 0
	v_addc_co_u32_e32 v77, vcc, 0, v169, vcc
	s_movk_i32 s1, 0x6000
	global_load_dwordx2 v[12:13], v[10:11], off
	global_load_dwordx4 v[24:27], v[168:169], off
	global_load_dwordx4 v[28:31], v[168:169], off offset:1024
	global_load_dwordx4 v[32:35], v[170:171], off
	global_load_dwordx4 v[36:39], v[170:171], off offset:1024
	global_load_dwordx4 v[40:43], v[56:57], off
	global_load_dwordx4 v[44:47], v[56:57], off offset:1024
	global_load_dwordx4 v[48:51], v[22:23], off offset:1024
	global_load_dwordx4 v[52:55], v[22:23], off offset:2048
	s_nop 0
	global_load_dwordx4 v[56:59], v[76:77], off
	global_load_dwordx4 v[60:63], v[76:77], off offset:1024
	global_load_dwordx4 v[64:67], v[170:171], off offset:2048
	global_load_dwordx4 v[68:71], v[170:171], off offset:3072
	global_load_dwordx4 v[72:75], v[22:23], off offset:3072
	v_add_co_u32_e32 v22, vcc, s1, v168
	s_movk_i32 s1, 0x1000
	s_nop 0
	v_addc_co_u32_e32 v23, vcc, 0, v169, vcc
	global_load_dwordx4 v[76:79], v[22:23], off
	global_load_dwordx4 v[80:83], v[22:23], off offset:1024
	v_add_co_u32_e32 v22, vcc, s1, v170
	global_load_dwordx4 v[84:87], v[140:141], off offset:-4096
	global_load_dwordx4 v[88:91], v[140:141], off
	v_addc_co_u32_e32 v23, vcc, 0, v171, vcc
	v_add_co_u32_e32 v156, vcc, s0, v170
	s_mov_b32 s0, 0x8000
	s_nop 0
	v_addc_co_u32_e32 v157, vcc, 0, v171, vcc
	v_add_co_u32_e32 v100, vcc, s0, v168
	s_mov_b32 s0, 0xa000
	s_nop 0
	v_addc_co_u32_e32 v101, vcc, 0, v169, vcc
	v_add_co_u32_e32 v116, vcc, s0, v168
	s_mov_b32 s0, 0xc000
	s_nop 0
	v_addc_co_u32_e32 v117, vcc, 0, v169, vcc
	global_load_dwordx4 v[92:95], v[100:101], off
	global_load_dwordx4 v[96:99], v[100:101], off offset:1024
	s_nop 0
	global_load_dwordx4 v[100:103], v[116:117], off
	global_load_dwordx4 v[104:107], v[116:117], off offset:1024
	global_load_dwordx4 v[108:111], v[22:23], off offset:1024
	global_load_dwordx4 v[112:115], v[22:23], off offset:2048
	s_nop 0
	global_load_dwordx4 v[116:119], v[140:141], off offset:1024
	global_load_dwordx4 v[120:123], v[140:141], off offset:2048
	v_add_co_u32_e32 v128, vcc, s0, v168
	s_mov_b32 s0, 0xe000
	s_nop 0
	v_addc_co_u32_e32 v129, vcc, 0, v169, vcc
	global_load_dwordx4 v[124:127], v[128:129], off
	s_nop 0
	global_load_dwordx4 v[128:131], v[128:129], off offset:1024
	s_nop 0
	global_load_dwordx4 v[132:135], v[22:23], off offset:3072
	global_load_dwordx4 v[136:139], v[156:157], off offset:-4096
	s_nop 0
	global_load_dwordx4 v[140:143], v[140:141], off offset:3072
	v_add_co_u32_e32 v22, vcc, s0, v168
	s_nop 1
	v_addc_co_u32_e32 v23, vcc, 0, v169, vcc
	global_load_dwordx4 v[144:147], v[22:23], off
	global_load_dwordx4 v[148:151], v[22:23], off offset:1024
	v_lshrrev_b32_e32 v22, 7, v0
	s_waitcnt vmcnt(29)
	v_mfma_f32_16x16x32_f16 v[152:155], v[32:35], v[24:27], 0
	s_waitcnt vmcnt(16)
	v_mfma_f32_16x16x32_f16 v[24:27], v[84:87], v[24:27], 0
	v_mfma_f32_16x16x32_f16 v[32:35], v[32:35], v[28:31], 0
	v_mfma_f32_16x16x32_f16 v[28:31], v[84:87], v[28:31], 0
	v_mfma_f32_16x16x32_f16 v[84:87], v[36:39], v[40:43], v[152:155]
	v_mfma_f32_16x16x32_f16 v[24:27], v[48:51], v[40:43], v[24:27]
	v_mfma_f32_16x16x32_f16 v[32:35], v[36:39], v[44:47], v[32:35]
	v_mfma_f32_16x16x32_f16 v[28:31], v[48:51], v[44:47], v[28:31]
	v_mfma_f32_16x16x32_f16 v[36:39], v[64:67], v[56:59], v[84:87]
	v_mfma_f32_16x16x32_f16 v[24:27], v[52:55], v[56:59], v[24:27]
	v_mfma_f32_16x16x32_f16 v[32:35], v[64:67], v[60:63], v[32:35]
	v_mfma_f32_16x16x32_f16 v[28:31], v[52:55], v[60:63], v[28:31]
	v_mfma_f32_16x16x32_f16 v[36:39], v[68:71], v[76:79], v[36:39]
	v_mfma_f32_16x16x32_f16 v[24:27], v[72:75], v[76:79], v[24:27]
	v_mfma_f32_16x16x32_f16 v[32:35], v[68:71], v[80:83], v[32:35]
	v_mfma_f32_16x16x32_f16 v[28:31], v[72:75], v[80:83], v[28:31]
	s_mov_b32 s0, 0x22000
	v_add_co_u32_e32 v158, vcc, s0, v170
	s_mov_b32 s0, 0x23000
	s_nop 0
	v_addc_co_u32_e32 v159, vcc, 0, v171, vcc
	v_add_co_u32_e32 v172, vcc, s0, v170
	s_mov_b32 s0, 0x10000
	s_nop 0
	v_addc_co_u32_e32 v173, vcc, 0, v171, vcc
	v_add_co_u32_e32 v52, vcc, s0, v168
	s_mov_b32 s0, 0x12000
	s_nop 0
	v_addc_co_u32_e32 v53, vcc, 0, v169, vcc
	v_add_co_u32_e32 v64, vcc, s0, v168
	s_mov_b32 s0, 0x14000
	s_nop 0
	v_addc_co_u32_e32 v65, vcc, 0, v169, vcc
	v_add_co_u32_e32 v80, vcc, s0, v168
	global_load_dwordx4 v[40:43], v[172:173], off offset:-4096
	s_nop 0
	v_addc_co_u32_e32 v81, vcc, 0, v169, vcc
	global_load_dwordx4 v[44:47], v[52:53], off
	global_load_dwordx4 v[48:51], v[52:53], off offset:1024
	s_nop 0
	global_load_dwordx4 v[52:55], v[156:157], off
	global_load_dwordx4 v[56:59], v[156:157], off offset:1024
	global_load_dwordx4 v[60:63], v[64:65], off
	s_nop 0
	global_load_dwordx4 v[64:67], v[64:65], off offset:1024
	s_nop 0
	global_load_dwordx4 v[68:71], v[158:159], off offset:1024
	global_load_dwordx4 v[72:75], v[158:159], off offset:2048
	global_load_dwordx4 v[76:79], v[80:81], off
	s_nop 0
	global_load_dwordx4 v[80:83], v[80:81], off offset:1024
	s_nop 0
	global_load_dwordx4 v[84:87], v[156:157], off offset:2048
	global_load_dwordx4 v[152:155], v[156:157], off offset:3072
	s_nop 0
	global_load_dwordx4 v[156:159], v[158:159], off offset:3072
	s_mov_b32 s0, 0x16000
	v_add_co_u32_e32 v164, vcc, s0, v168
	s_nop 1
	v_addc_co_u32_e32 v165, vcc, 0, v169, vcc
	global_load_dwordx4 v[160:163], v[164:165], off
	s_nop 0
	global_load_dwordx4 v[164:167], v[164:165], off offset:1024
	s_waitcnt vmcnt(19)
	v_mfma_f32_16x16x32_f16 v[36:39], v[136:139], v[92:95], v[36:39]
	v_mfma_f32_16x16x32_f16 v[24:27], v[88:91], v[92:95], v[24:27]
	v_mfma_f32_16x16x32_f16 v[32:35], v[136:139], v[96:99], v[32:35]
	v_mfma_f32_16x16x32_f16 v[28:31], v[88:91], v[96:99], v[28:31]
	v_mfma_f32_16x16x32_f16 v[36:39], v[108:111], v[100:103], v[36:39]
	v_mfma_f32_16x16x32_f16 v[24:27], v[116:119], v[100:103], v[24:27]
	v_mfma_f32_16x16x32_f16 v[32:35], v[108:111], v[104:107], v[32:35]
	v_mfma_f32_16x16x32_f16 v[28:31], v[116:119], v[104:107], v[28:31]
	v_mfma_f32_16x16x32_f16 v[36:39], v[112:115], v[124:127], v[36:39]
	v_mfma_f32_16x16x32_f16 v[24:27], v[120:123], v[124:127], v[24:27]
	v_mfma_f32_16x16x32_f16 v[32:35], v[112:115], v[128:131], v[32:35]
	v_mfma_f32_16x16x32_f16 v[28:31], v[120:123], v[128:131], v[28:31]
	s_waitcnt vmcnt(17)
	v_mfma_f32_16x16x32_f16 v[36:39], v[132:135], v[144:147], v[36:39]
	v_mfma_f32_16x16x32_f16 v[24:27], v[140:143], v[144:147], v[24:27]
	s_waitcnt vmcnt(16)
	v_mfma_f32_16x16x32_f16 v[32:35], v[132:135], v[148:151], v[32:35]
	v_mfma_f32_16x16x32_f16 v[28:31], v[140:143], v[148:151], v[28:31]
	s_movk_i32 s0, 0x3000
	v_add_co_u32_e32 v132, vcc, s0, v170
	s_mov_b32 s0, 0x18000
	s_nop 0
	v_addc_co_u32_e32 v133, vcc, 0, v171, vcc
	v_add_co_u32_e32 v104, vcc, s0, v168
	s_mov_b32 s0, 0x1a000
	s_nop 0
	v_addc_co_u32_e32 v105, vcc, 0, v169, vcc
	v_add_co_u32_e32 v116, vcc, s0, v168
	s_mov_b32 s0, 0x1c000
	s_nop 0
	v_addc_co_u32_e32 v117, vcc, 0, v169, vcc
	v_add_co_u32_e32 v124, vcc, s0, v168
	global_load_dwordx4 v[88:91], v[104:105], off
	global_load_dwordx4 v[92:95], v[104:105], off offset:1024
	global_load_dwordx4 v[96:99], v[132:133], off
	global_load_dwordx4 v[100:103], v[132:133], off offset:1024
	s_nop 0
	global_load_dwordx4 v[104:107], v[172:173], off
	global_load_dwordx4 v[108:111], v[172:173], off offset:1024
	v_addc_co_u32_e32 v125, vcc, 0, v169, vcc
	global_load_dwordx4 v[112:115], v[116:117], off
	s_nop 0
	global_load_dwordx4 v[116:119], v[116:117], off offset:1024
	s_nop 0
	global_load_dwordx4 v[120:123], v[124:125], off
	s_nop 0
	global_load_dwordx4 v[124:127], v[124:125], off offset:1024
	s_nop 0
	global_load_dwordx4 v[128:131], v[132:133], off offset:2048
	s_nop 0
	global_load_dwordx4 v[132:135], v[132:133], off offset:3072
	s_nop 0
	global_load_dwordx4 v[136:139], v[172:173], off offset:2048
	global_load_dwordx4 v[140:143], v[172:173], off offset:3072
	s_mov_b32 s0, 0x1e000
	v_add_co_u32_e32 v148, vcc, s0, v168
	s_nop 1
	v_addc_co_u32_e32 v149, vcc, 0, v169, vcc
	global_load_dwordx4 v[144:147], v[148:149], off
	s_nop 0
	global_load_dwordx4 v[148:151], v[148:149], off offset:1024
	s_waitcnt vmcnt(28)
	v_mfma_f32_16x16x32_f16 v[36:39], v[52:55], v[44:47], v[36:39]
	v_mfma_f32_16x16x32_f16 v[24:27], v[40:43], v[44:47], v[24:27]
	v_mfma_f32_16x16x32_f16 v[32:35], v[52:55], v[48:51], v[32:35]
	v_mfma_f32_16x16x32_f16 v[28:31], v[40:43], v[48:51], v[28:31]
	s_waitcnt vmcnt(26)
	v_mfma_f32_16x16x32_f16 v[36:39], v[56:59], v[60:63], v[36:39]
	s_waitcnt vmcnt(24)
	v_mfma_f32_16x16x32_f16 v[24:27], v[68:71], v[60:63], v[24:27]
	v_mfma_f32_16x16x32_f16 v[32:35], v[56:59], v[64:67], v[32:35]
	v_mfma_f32_16x16x32_f16 v[28:31], v[68:71], v[64:67], v[28:31]
	s_waitcnt vmcnt(20)
	v_mfma_f32_16x16x32_f16 v[36:39], v[84:87], v[76:79], v[36:39]
	v_mfma_f32_16x16x32_f16 v[24:27], v[72:75], v[76:79], v[24:27]
	v_mfma_f32_16x16x32_f16 v[32:35], v[84:87], v[80:83], v[32:35]
	v_mfma_f32_16x16x32_f16 v[28:31], v[72:75], v[80:83], v[28:31]
	s_waitcnt vmcnt(17)
	v_mfma_f32_16x16x32_f16 v[36:39], v[152:155], v[160:163], v[36:39]
	v_mfma_f32_16x16x32_f16 v[24:27], v[156:159], v[160:163], v[24:27]
	s_waitcnt vmcnt(16)
	v_mfma_f32_16x16x32_f16 v[32:35], v[152:155], v[164:167], v[32:35]
	v_mfma_f32_16x16x32_f16 v[28:31], v[156:159], v[164:167], v[28:31]
	s_waitcnt vmcnt(13)
	v_mfma_f32_16x16x32_f16 v[36:39], v[96:99], v[88:91], v[36:39]
	s_waitcnt vmcnt(11)
	v_mfma_f32_16x16x32_f16 v[24:27], v[104:107], v[88:91], v[24:27]
	v_mfma_f32_16x16x32_f16 v[32:35], v[96:99], v[92:95], v[32:35]
	v_mfma_f32_16x16x32_f16 v[28:31], v[104:107], v[92:95], v[28:31]
	s_waitcnt vmcnt(9)
	v_mfma_f32_16x16x32_f16 v[36:39], v[100:103], v[112:115], v[36:39]
	v_mfma_f32_16x16x32_f16 v[24:27], v[108:111], v[112:115], v[24:27]
	s_waitcnt vmcnt(8)
	v_mfma_f32_16x16x32_f16 v[32:35], v[100:103], v[116:119], v[32:35]
	v_mfma_f32_16x16x32_f16 v[28:31], v[108:111], v[116:119], v[28:31]
	s_waitcnt vmcnt(5)
	v_mfma_f32_16x16x32_f16 v[36:39], v[128:131], v[120:123], v[36:39]
	s_waitcnt vmcnt(3)
	v_mfma_f32_16x16x32_f16 v[24:27], v[136:139], v[120:123], v[24:27]
	v_mfma_f32_16x16x32_f16 v[32:35], v[128:131], v[124:127], v[32:35]
	v_mfma_f32_16x16x32_f16 v[28:31], v[136:139], v[124:127], v[28:31]
	s_waitcnt vmcnt(1)
	v_mfma_f32_16x16x32_f16 v[36:39], v[132:135], v[144:147], v[36:39]
	v_mfma_f32_16x16x32_f16 v[24:27], v[140:143], v[144:147], v[24:27]
	s_waitcnt vmcnt(0)
	v_mfma_f32_16x16x32_f16 v[32:35], v[132:135], v[148:151], v[32:35]
	v_mfma_f32_16x16x32_f16 v[28:31], v[140:143], v[148:151], v[28:31]
	v_lshlrev_b32_e32 v23, 12, v174
	v_add3_u32 v23, 0, v16, v23
	s_nop 1
	ds_write_b128 v23, v[36:39]
	ds_write_b128 v23, v[24:27] offset:1024
	s_nop 0
	ds_write_b128 v23, v[32:35] offset:2048
	ds_write_b128 v23, v[28:31] offset:3072
	v_lshrrev_b32_e32 v23, 4, v0
	v_and_b32_e32 v24, 60, v1
	v_mul_u32_u24_e32 v23, 0x110, v23
	v_lshlrev_b32_e32 v24, 2, v24
	s_movk_i32 s0, 0x50
	v_add3_u32 v23, 0, v23, v24
	v_cmp_gt_u32_e32 vcc, s0, v0
	ds_write_b128 v23, v[2:5] offset:32768
	s_and_saveexec_b64 s[0:1], vcc
	s_cbranch_execz .LBB9_14
	global_load_dwordx4 v[2:5], v[6:7], off
	v_lshl_add_u32 v0, v1, 2, 0
	s_waitcnt vmcnt(0)
	ds_write_b128 v0, v[2:5] offset:41472
.LBB9_14:
	s_or_b64 exec, exec, s[0:1]
	v_lshlrev_b32_e32 v0, 10, v22
	v_add3_u32 v16, 0, v0, v16
	s_waitcnt lgkmcnt(0)
	s_barrier
	ds_read_b128 v[0:3], v16
	ds_read_b128 v[4:7], v16 offset:4096
	ds_read_b128 v[22:25], v16 offset:8192
	ds_read_b128 v[26:29], v16 offset:12288
	v_cmp_eq_u32_e32 vcc, 0, v21
	s_waitcnt lgkmcnt(2)
	v_pk_add_f32 v[2:3], v[2:3], v[6:7]
	v_pk_add_f32 v[4:5], v[0:1], v[4:5]
	s_waitcnt lgkmcnt(1)
	v_pk_add_f32 v[6:7], v[2:3], v[24:25]
	ds_read_b128 v[0:3], v16 offset:16384
	v_pk_add_f32 v[4:5], v[4:5], v[22:23]
	s_waitcnt lgkmcnt(1)
	v_pk_add_f32 v[22:23], v[6:7], v[28:29]
	v_pk_add_f32 v[26:27], v[4:5], v[26:27]
	ds_read_b128 v[4:7], v16 offset:20480
	s_waitcnt lgkmcnt(1)
	v_pk_add_f32 v[28:29], v[22:23], v[2:3]
	ds_read_b128 v[22:25], v16 offset:24576
	v_pk_add_f32 v[26:27], v[26:27], v[0:1]
	ds_read_b128 v[0:3], v16 offset:28672
	s_waitcnt lgkmcnt(2)
	v_pk_add_f32 v[6:7], v[28:29], v[6:7]
	v_lshl_add_u32 v16, v18, 2, 0
	s_waitcnt lgkmcnt(1)
	v_pk_add_f32 v[6:7], v[6:7], v[24:25]
	v_pk_add_f32 v[4:5], v[26:27], v[4:5]
	s_waitcnt lgkmcnt(0)
	v_pk_add_f32 v[2:3], v[6:7], v[2:3]
	ds_read_b64 v[6:7], v16 offset:42624
	v_pk_add_f32 v[4:5], v[4:5], v[22:23]
	s_nop 0
	v_pk_add_f32 v[0:1], v[4:5], v[0:1]
	v_lshl_add_u64 v[4:5], v[14:15], 2, s[6:7]
	v_cndmask_b32_e32 v1, v3, v1, vcc
	v_cndmask_b32_e32 v0, v2, v0, vcc
	v_mad_u32_u24 v2, v18, 12, v16
	ds_read_b128 v[22:25], v2 offset:41472
	s_waitcnt lgkmcnt(1)
	v_pk_add_f32 v[0:1], v[0:1], v[6:7]
	v_lshl_add_u64 v[4:5], v[4:5], 0, v[8:9]
	v_pk_add_f32 v[14:15], v[12:13], v[0:1]
	v_or_b32_e32 v1, 1, v18
	global_store_dwordx2 v[4:5], v[14:15], off
	v_lshl_add_u32 v0, v18, 8, v2
	v_lshl_add_u32 v5, v1, 4, 0
	v_mad_i32_i24 v4, v18, -12, v2
	v_lshl_add_u32 v6, v1, 8, v5
	ds_read_b128 v[26:29], v0 offset:33008
	ds_read_b128 v[0:3], v2 offset:41984
	ds_read_b128 v[30:33], v6 offset:33008
	ds_read_b64 v[12:13], v4 offset:42496
	ds_read_b128 v[34:37], v5 offset:41472
	s_waitcnt lgkmcnt(4)
	v_mov_b32_e32 v38, v26
	v_mov_b32_e32 v40, v22
	s_waitcnt lgkmcnt(2)
	v_mov_b32_e32 v39, v30
	v_mov_b32_e32 v30, v27
	s_waitcnt lgkmcnt(0)
	v_mov_b32_e32 v41, v34
	v_pk_fma_f32 v[38:39], v[14:15], v[38:39], v[40:41]
	v_mov_b32_e32 v34, v23
	v_mul_f32_e32 v8, 0x3d372713, v38
	v_mul_f32_e32 v8, v38, v8
	v_fma_f32 v8, v38, v8, v38
	v_mul_f32_e32 v8, 0x3f4c422a, v8
	v_add_f32_e32 v8, v8, v8
	v_mul_f32_e32 v8, 0x3fb8aa3b, v8
	v_pk_fma_f32 v[26:27], v[14:15], v[30:31], v[34:35]
	v_exp_f32_e32 v22, v8
	v_mul_f32_e32 v8, 0x3d372713, v26
	v_mul_f32_e32 v8, v26, v8
	v_fma_f32 v8, v26, v8, v26
	v_mul_f32_e32 v16, 0x3d372713, v39
	v_mul_f32_e32 v8, 0x3f4c422a, v8
	v_mul_f32_e32 v16, v39, v16
	v_add_f32_e32 v8, v8, v8
	v_mov_b32_e32 v34, v28
	v_mov_b32_e32 v35, v32
	v_mov_b32_e32 v40, v24
	v_mov_b32_e32 v41, v36
	v_fma_f32 v16, v39, v16, v39
	v_mul_f32_e32 v8, 0x3fb8aa3b, v8
	v_pk_fma_f32 v[34:35], v[14:15], v[34:35], v[40:41]
	v_mul_f32_e32 v16, 0x3f4c422a, v16
	v_exp_f32_e32 v30, v8
	v_mul_f32_e32 v8, 0x3d372713, v34
	v_add_f32_e32 v16, v16, v16
	v_mul_f32_e32 v8, v34, v8
	v_mul_f32_e32 v16, 0x3fb8aa3b, v16
	v_fma_f32 v8, v34, v8, v34
	v_exp_f32_e32 v23, v16
	v_mul_f32_e32 v8, 0x3f4c422a, v8
	v_add_f32_e32 v8, v8, v8
	v_mov_b32_e32 v32, v29
	v_mov_b32_e32 v36, v25
	v_mul_f32_e32 v8, 0x3fb8aa3b, v8
	v_pk_fma_f32 v[14:15], v[14:15], v[32:33], v[36:37]
	v_exp_f32_e32 v24, v8
	v_mul_f32_e32 v8, 0x3d372713, v14
	v_pk_add_f32 v[22:23], v[22:23], 1.0 op_sel_hi:[1,0]
	v_mul_f32_e32 v8, v14, v8
	v_div_scale_f32 v16, s[0:1], v23, v23, 2.0
	v_fma_f32 v8, v14, v8, v14
	v_rcp_f32_e32 v21, v16
	v_mul_f32_e32 v8, 0x3f4c422a, v8
	v_add_f32_e32 v8, v8, v8
	v_mul_f32_e32 v8, 0x3fb8aa3b, v8
	v_exp_f32_e32 v28, v8
	v_fma_f32 v8, -v16, v21, 1.0
	v_fmac_f32_e32 v21, v8, v21
	v_div_scale_f32 v8, vcc, 2.0, v23, 2.0
	v_mul_f32_e32 v25, v8, v21
	v_fma_f32 v29, -v16, v25, v8
	v_fmac_f32_e32 v25, v29, v21
	v_fma_f32 v8, -v16, v25, v8
	v_div_scale_f32 v16, s[0:1], v22, v22, 2.0
	v_rcp_f32_e32 v29, v16
	v_div_fmas_f32 v8, v8, v21, v25
	v_div_fixup_f32 v23, v8, v23, 2.0
	ds_read_b128 v[4:7], v5 offset:41984
	v_fma_f32 v8, -v16, v29, 1.0
	v_fmac_f32_e32 v29, v8, v29
	v_div_scale_f32 v8, vcc, 2.0, v22, 2.0
	v_mul_f32_e32 v21, v8, v29
	v_fma_f32 v25, -v16, v21, v8
	v_fmac_f32_e32 v21, v25, v29
	v_fma_f32 v8, -v16, v21, v8
	v_div_fmas_f32 v8, v8, v29, v21
	v_div_fixup_f32 v22, v8, v22, 2.0
	v_mul_f32_e32 v8, 0x3d372713, v27
	v_mul_f32_e32 v8, v27, v8
	v_fma_f32 v8, v27, v8, v27
	v_mul_f32_e32 v8, 0x3f4c422a, v8
	v_add_f32_e32 v8, v8, v8
	v_mul_f32_e32 v8, 0x3fb8aa3b, v8
	v_exp_f32_e32 v31, v8
	v_pk_add_f32 v[22:23], v[22:23], 1.0 op_sel_hi:[1,0] neg_lo:[1,0] neg_hi:[1,0]
	v_pk_mul_f32 v[32:33], v[38:39], 0.5 op_sel_hi:[1,0]
	v_pk_add_f32 v[22:23], v[22:23], 1.0 op_sel_hi:[1,0]
	v_pk_add_f32 v[30:31], v[30:31], 1.0 op_sel_hi:[1,0]
	v_pk_mul_f32 v[22:23], v[32:33], v[22:23]
	v_div_scale_f32 v8, s[0:1], v31, v31, 2.0
	v_rcp_f32_e32 v16, v8
	v_mov_b32_e32 v32, v0
	s_waitcnt lgkmcnt(0)
	v_mov_b32_e32 v33, v4
	v_pk_mul_f32 v[26:27], v[26:27], 0.5 op_sel_hi:[1,0]
	v_fma_f32 v0, -v8, v16, 1.0
	v_fmac_f32_e32 v16, v0, v16
	v_div_scale_f32 v0, vcc, 2.0, v31, 2.0
	v_mul_f32_e32 v4, v0, v16
	v_fma_f32 v21, -v8, v4, v0
	v_fmac_f32_e32 v4, v21, v16
	v_fma_f32 v0, -v8, v4, v0
	v_div_scale_f32 v8, s[0:1], v30, v30, 2.0
	v_rcp_f32_e32 v21, v8
	v_div_fmas_f32 v0, v0, v16, v4
	v_div_fixup_f32 v31, v0, v31, 2.0
	v_fma_f32 v0, -v8, v21, 1.0
	v_fmac_f32_e32 v21, v0, v21
	v_div_scale_f32 v0, vcc, 2.0, v30, 2.0
	v_mul_f32_e32 v4, v0, v21
	v_fma_f32 v16, -v8, v4, v0
	v_fmac_f32_e32 v4, v16, v21
	v_fma_f32 v0, -v8, v4, v0
	v_div_fmas_f32 v0, v0, v21, v4
	v_div_fixup_f32 v30, v0, v30, 2.0
	v_mul_f32_e32 v0, 0x3d372713, v35
	v_mul_f32_e32 v0, v35, v0
	v_fma_f32 v0, v35, v0, v35
	v_mul_f32_e32 v0, 0x3f4c422a, v0
	v_add_f32_e32 v0, v0, v0
	v_mul_f32_e32 v0, 0x3fb8aa3b, v0
	v_exp_f32_e32 v25, v0
	v_pk_add_f32 v[30:31], v[30:31], 1.0 op_sel_hi:[1,0] neg_lo:[1,0] neg_hi:[1,0]
	v_mov_b32_e32 v4, v1
	v_pk_add_f32 v[30:31], v[30:31], 1.0 op_sel_hi:[1,0]
	v_pk_add_f32 v[24:25], v[24:25], 1.0 op_sel_hi:[1,0]
	v_pk_mul_f32 v[26:27], v[26:27], v[30:31]
	v_div_scale_f32 v8, s[0:1], v25, v25, 2.0
	v_rcp_f32_e32 v16, v8
	v_pk_mul_f32 v[0:1], v[26:27], v[4:5]
	v_fma_f32 v4, -v8, v16, 1.0
	v_fmac_f32_e32 v16, v4, v16
	v_div_scale_f32 v4, vcc, 2.0, v25, 2.0
	v_mul_f32_e32 v5, v4, v16
	v_fma_f32 v21, -v8, v5, v4
	v_fmac_f32_e32 v5, v21, v16
	v_fma_f32 v4, -v8, v5, v4
	v_div_scale_f32 v8, s[0:1], v24, v24, 2.0
	v_rcp_f32_e32 v21, v8
	v_div_fmas_f32 v4, v4, v16, v5
	v_div_fixup_f32 v5, v4, v25, 2.0
	v_pk_fma_f32 v[0:1], v[22:23], v[32:33], v[0:1]
	v_fma_f32 v4, -v8, v21, 1.0
	v_fmac_f32_e32 v21, v4, v21
	v_div_scale_f32 v4, vcc, 2.0, v24, 2.0
	v_mul_f32_e32 v16, v4, v21
	v_fma_f32 v22, -v8, v16, v4
	v_fmac_f32_e32 v16, v22, v21
	v_fma_f32 v4, -v8, v16, v4
	v_mul_f32_e32 v8, 0x3d372713, v15
	v_mul_f32_e32 v8, v15, v8
	v_fma_f32 v8, v15, v8, v15
	v_mul_f32_e32 v8, 0x3f4c422a, v8
	v_add_f32_e32 v8, v8, v8
	v_mul_f32_e32 v8, 0x3fb8aa3b, v8
	v_div_fmas_f32 v4, v4, v21, v16
	v_exp_f32_e32 v29, v8
	v_div_fixup_f32 v4, v4, v24, 2.0
	v_pk_add_f32 v[4:5], v[4:5], 1.0 op_sel_hi:[1,0] neg_lo:[1,0] neg_hi:[1,0]
	v_pk_mul_f32 v[22:23], v[34:35], 0.5 op_sel_hi:[1,0]
	v_pk_add_f32 v[4:5], v[4:5], 1.0 op_sel_hi:[1,0]
	v_mov_b32_e32 v24, v2
	v_pk_mul_f32 v[4:5], v[22:23], v[4:5]
	v_pk_add_f32 v[22:23], v[28:29], 1.0 op_sel_hi:[1,0]
	v_mov_b32_e32 v25, v6
	v_div_scale_f32 v8, s[0:1], v23, v23, 2.0
	v_rcp_f32_e32 v16, v8
	v_pk_fma_f32 v[0:1], v[4:5], v[24:25], v[0:1]
	v_div_scale_f32 v6, s[0:1], v22, v22, 2.0
	v_fma_f32 v2, -v8, v16, 1.0
	v_fmac_f32_e32 v16, v2, v16
	v_div_scale_f32 v2, vcc, 2.0, v23, 2.0
	v_mul_f32_e32 v4, v2, v16
	v_fma_f32 v5, -v8, v4, v2
	v_fmac_f32_e32 v4, v5, v16
	v_fma_f32 v2, -v8, v4, v2
	v_rcp_f32_e32 v8, v6
	v_div_fmas_f32 v2, v2, v16, v4
	v_div_fixup_f32 v5, v2, v23, 2.0
	v_pk_mul_f32 v[14:15], v[14:15], 0.5 op_sel_hi:[1,0]
	v_fma_f32 v2, -v6, v8, 1.0
	v_fmac_f32_e32 v8, v2, v8
	v_div_scale_f32 v2, vcc, 2.0, v22, 2.0
	v_mul_f32_e32 v4, v2, v8
	v_fma_f32 v16, -v6, v4, v2
	v_fmac_f32_e32 v4, v16, v8
	v_fma_f32 v2, -v6, v4, v2
	v_div_fmas_f32 v2, v2, v8, v4
	v_div_fixup_f32 v4, v2, v22, 2.0
	v_pk_add_f32 v[4:5], v[4:5], 1.0 op_sel_hi:[1,0] neg_lo:[1,0] neg_hi:[1,0]
	v_mov_b32_e32 v6, v3
	v_pk_add_f32 v[4:5], v[4:5], 1.0 op_sel_hi:[1,0]
	s_mov_b32 s0, 0x100000
	v_pk_mul_f32 v[4:5], v[14:15], v[4:5]
	v_add_co_u32_e32 v2, vcc, s0, v10
	v_pk_fma_f32 v[0:1], v[4:5], v[6:7], v[0:1]
	s_lshl_b32 s0, s3, 3
	v_pk_add_f32 v[0:1], v[12:13], v[0:1]
	v_addc_co_u32_e32 v3, vcc, 0, v11, vcc
	s_addk_i32 s0, 0x100
	global_store_dwordx2 v[2:3], v[0:1], off
	v_add_u32_e32 v8, s0, v19
	v_lshlrev_b32_e32 v3, 1, v20
	v_cvt_pk_f16_f32 v2, v0, v1
	v_lshlrev_b64 v[0:1], 6, v[8:9]
	v_and_b32_e32 v3, 48, v3
	v_or3_b32 v0, v0, v3, v17
	v_and_b32_e32 v3, 6, v18
	v_lshl_add_u64 v[0:1], v[0:1], 4, s[12:13]
	v_lshlrev_b32_e32 v8, 1, v3
	v_lshl_add_u64 v[0:1], v[0:1], 0, v[8:9]
	global_store_dword v[0:1], v2, off
	s_endpgm
	s_nop 0
	s_nop 0
	s_nop 0
	s_endpgm

	.amdhsa_kernel _ZN12_GLOBAL__N_110gemm_fullkILi1ELi0EEEvPKDF16_S2_PKfPDF16_PfS6_S4_S4_S4_S4_S4_S5_
		.amdhsa_group_segment_fixed_size 0
		.amdhsa_private_segment_fixed_size 0
		.amdhsa_kernarg_size 96
		.amdhsa_user_sgpr_count 2
		.amdhsa_user_sgpr_dispatch_ptr 0
		.amdhsa_user_sgpr_queue_ptr 0
		.amdhsa_user_sgpr_kernarg_segment_ptr 1
		.amdhsa_user_sgpr_dispatch_id 0
		.amdhsa_user_sgpr_kernarg_preload_length 0
		.amdhsa_user_sgpr_kernarg_preload_offset 0
		.amdhsa_user_sgpr_private_segment_size 0
		.amdhsa_uses_dynamic_stack 0
		.amdhsa_enable_private_segment 0
		.amdhsa_system_sgpr_workgroup_id_x 1
		.amdhsa_system_sgpr_workgroup_id_y 0
		.amdhsa_system_sgpr_workgroup_id_z 0
		.amdhsa_system_sgpr_workgroup_info 0
		.amdhsa_system_vgpr_workitem_id 0
		.amdhsa_next_free_vgpr 175
		.amdhsa_next_free_sgpr 18
		.amdhsa_accum_offset 176
		.amdhsa_reserve_vcc 1
		.amdhsa_float_round_mode_32 0
		.amdhsa_float_round_mode_16_64 0
		.amdhsa_float_denorm_mode_32 3
		.amdhsa_float_denorm_mode_16_64 3
		.amdhsa_dx10_clamp 1
		.amdhsa_ieee_mode 1
		.amdhsa_fp16_overflow 0
		.amdhsa_tg_split 0
		.amdhsa_exception_fp_ieee_invalid_op 0
		.amdhsa_exception_fp_denorm_src 0
		.amdhsa_exception_fp_ieee_div_zero 0
		.amdhsa_exception_fp_ieee_overflow 0
		.amdhsa_exception_fp_ieee_underflow 0
		.amdhsa_exception_fp_ieee_inexact 0
		.amdhsa_exception_int_div_zero 0
	.end_amdhsa_kernel

_ZN12_GLOBAL__N_110gemm_fullkILi0ELi1EEEvPKDF16_S2_PKfPDF16_PfS6_S4_S4_S4_S4_S4_S5_:
	s_load_dwordx8 s[4:11], s[0:1], 0x0
	s_lshr_b32 s0, s2, 5
	v_lshrrev_b32_e32 v230, 6, v0
	s_and_b32 s12, s0, 0x7fffffc
	s_and_b32 s2, s2, 0x7f
	s_mov_b32 s13, 0
	v_mul_u32_u24_e32 v4, 12, v230
	v_mov_b32_e32 v3, 0
	s_lshl_b64 s[0:1], s[12:13], 10
	s_mul_i32 s13, s2, 0xc0
	v_and_b32_e32 v1, 63, v0
	v_mul_u32_u24_e32 v2, 0x18000, v230
	v_add_lshl_u32 v4, s13, v4, 10
	v_mov_b32_e32 v5, v3
	s_waitcnt lgkmcnt(0)
	v_lshl_add_u64 v[4:5], s[6:7], 0, v[4:5]
	v_lshl_add_u64 v[6:7], s[4:5], 0, v[2:3]
	v_lshlrev_b32_e32 v2, 4, v1
	s_mov_b32 s3, 0x18000
	v_lshl_add_u64 v[208:209], v[4:5], 0, v[2:3]
	v_add_co_u32_e32 v80, vcc, s3, v208
	v_lshl_add_u64 v[6:7], v[6:7], 0, s[0:1]
	s_nop 0
	v_addc_co_u32_e32 v81, vcc, 0, v209, vcc
	s_mov_b32 s0, 0x19000
	v_add_co_u32_e32 v176, vcc, s0, v208
	v_lshl_add_u64 v[212:213], v[6:7], 0, v[2:3]
	s_nop 0
	v_addc_co_u32_e32 v177, vcc, 0, v209, vcc
	s_movk_i32 s0, 0x2000
	v_add_co_u32_e32 v52, vcc, s0, v212
	s_movk_i32 s1, 0x4000
	s_nop 0
	v_addc_co_u32_e32 v53, vcc, 0, v213, vcc
	v_add_co_u32_e32 v82, vcc, s1, v212
	s_movk_i32 s1, 0x6000
	s_nop 0
	v_addc_co_u32_e32 v83, vcc, 0, v213, vcc
	v_add_co_u32_e32 v96, vcc, s1, v212
	s_movk_i32 s1, 0x1000
	s_nop 0
	v_addc_co_u32_e32 v97, vcc, 0, v213, vcc
	v_add_co_u32_e32 v168, vcc, s1, v208
	global_load_dwordx4 v[4:7], v[212:213], off
	global_load_dwordx4 v[8:11], v[212:213], off offset:1024
	global_load_dwordx4 v[12:15], v[212:213], off offset:2048
	global_load_dwordx4 v[16:19], v[212:213], off offset:3072
	global_load_dwordx4 v[20:23], v[208:209], off
	global_load_dwordx4 v[24:27], v[208:209], off offset:1024
	v_addc_co_u32_e32 v169, vcc, 0, v209, vcc
	v_add_co_u32_e32 v210, vcc, s0, v208
	s_mov_b32 s0, 0x8000
	s_nop 0
	v_addc_co_u32_e32 v211, vcc, 0, v209, vcc
	v_add_co_u32_e32 v116, vcc, s0, v212
	s_mov_b32 s0, 0xa000
	s_nop 0
	v_addc_co_u32_e32 v117, vcc, 0, v213, vcc
	v_add_co_u32_e32 v132, vcc, s0, v212
	s_mov_b32 s0, 0xc000
	s_nop 0
	v_addc_co_u32_e32 v133, vcc, 0, v213, vcc
	v_add_co_u32_e32 v164, vcc, s0, v212
	global_load_dwordx4 v[28:31], v[52:53], off
	global_load_dwordx4 v[32:35], v[52:53], off offset:1024
	global_load_dwordx4 v[36:39], v[52:53], off offset:2048
	global_load_dwordx4 v[40:43], v[52:53], off offset:3072
	global_load_dwordx4 v[44:47], v[80:81], off offset:1024
	global_load_dwordx4 v[48:51], v[80:81], off offset:2048
	s_nop 0
	global_load_dwordx4 v[52:55], v[82:83], off
	global_load_dwordx4 v[56:59], v[82:83], off offset:1024
	global_load_dwordx4 v[60:63], v[82:83], off offset:2048
	global_load_dwordx4 v[64:67], v[82:83], off offset:3072
	global_load_dwordx4 v[68:71], v[208:209], off offset:2048
	global_load_dwordx4 v[72:75], v[208:209], off offset:3072
	global_load_dwordx4 v[76:79], v[80:81], off offset:3072
	s_nop 0
	global_load_dwordx4 v[80:83], v[96:97], off
	global_load_dwordx4 v[84:87], v[96:97], off offset:1024
	global_load_dwordx4 v[88:91], v[96:97], off offset:2048
	global_load_dwordx4 v[92:95], v[96:97], off offset:3072
	s_nop 0
	global_load_dwordx4 v[96:99], v[176:177], off offset:-4096
	global_load_dwordx4 v[100:103], v[176:177], off
	global_load_dwordx4 v[104:107], v[116:117], off
	global_load_dwordx4 v[108:111], v[116:117], off offset:1024
	global_load_dwordx4 v[112:115], v[116:117], off offset:2048
	s_nop 0
	global_load_dwordx4 v[116:119], v[116:117], off offset:3072
	s_nop 0
	global_load_dwordx4 v[120:123], v[132:133], off
	global_load_dwordx4 v[124:127], v[132:133], off offset:1024
	global_load_dwordx4 v[128:131], v[132:133], off offset:2048
	s_nop 0
	global_load_dwordx4 v[132:135], v[132:133], off offset:3072
	s_nop 0
	global_load_dwordx4 v[136:139], v[168:169], off offset:1024
	global_load_dwordx4 v[140:143], v[168:169], off offset:2048
	global_load_dwordx4 v[144:147], v[176:177], off offset:1024
	global_load_dwordx4 v[148:151], v[176:177], off offset:2048
	v_addc_co_u32_e32 v165, vcc, 0, v213, vcc
	global_load_dwordx4 v[152:155], v[164:165], off
	global_load_dwordx4 v[156:159], v[164:165], off offset:1024
	global_load_dwordx4 v[160:163], v[164:165], off offset:2048
	s_nop 0
	global_load_dwordx4 v[164:167], v[164:165], off offset:3072
	s_nop 0
	global_load_dwordx4 v[168:171], v[168:169], off offset:3072
	s_nop 0
	global_load_dwordx4 v[172:175], v[210:211], off offset:-4096
	s_nop 0
	global_load_dwordx4 v[176:179], v[176:177], off offset:3072
	s_mov_b32 s0, 0xe000
	v_add_co_u32_e32 v192, vcc, s0, v212
	s_lshl_b32 s0, s2, 7
	s_nop 0
	v_addc_co_u32_e32 v193, vcc, 0, v213, vcc
	global_load_dwordx4 v[180:183], v[192:193], off
	global_load_dwordx4 v[184:187], v[192:193], off offset:1024
	global_load_dwordx4 v[188:191], v[192:193], off offset:2048
	s_nop 0
	global_load_dwordx4 v[192:195], v[192:193], off offset:3072
	v_bfe_u32 v1, v0, 6, 1
	s_add_u32 s0, s8, s0
	s_addc_u32 s1, s9, 0
	v_lshlrev_b32_e32 v196, 6, v1
	v_mov_b32_e32 v197, v3
	v_lshl_add_u64 v[196:197], s[0:1], 0, v[196:197]
	v_and_b32_e32 v198, 48, v0
	v_mov_b32_e32 v199, v3
	v_lshl_add_u64 v[228:229], v[196:197], 0, v[198:199]
	s_waitcnt vmcnt(43)
	v_mfma_f32_16x16x32_f16 v[196:199], v[20:23], v[4:7], 0
	s_waitcnt vmcnt(24)
	v_mfma_f32_16x16x32_f16 v[4:7], v[96:99], v[4:7], 0
	v_mfma_f32_16x16x32_f16 v[200:203], v[20:23], v[8:11], 0
	v_mfma_f32_16x16x32_f16 v[8:11], v[96:99], v[8:11], 0
	v_mfma_f32_16x16x32_f16 v[204:207], v[20:23], v[12:15], 0
	v_mfma_f32_16x16x32_f16 v[12:15], v[96:99], v[12:15], 0
	v_mfma_f32_16x16x32_f16 v[20:23], v[20:23], v[16:19], 0
	v_mfma_f32_16x16x32_f16 v[16:19], v[96:99], v[16:19], 0
	v_mfma_f32_16x16x32_f16 v[96:99], v[24:27], v[28:31], v[196:199]
	v_mfma_f32_16x16x32_f16 v[4:7], v[44:47], v[28:31], v[4:7]
	v_mfma_f32_16x16x32_f16 v[28:31], v[24:27], v[32:35], v[200:203]
	v_mfma_f32_16x16x32_f16 v[8:11], v[44:47], v[32:35], v[8:11]
	v_mfma_f32_16x16x32_f16 v[32:35], v[24:27], v[36:39], v[204:207]
	v_mfma_f32_16x16x32_f16 v[12:15], v[44:47], v[36:39], v[12:15]
	v_mfma_f32_16x16x32_f16 v[20:23], v[24:27], v[40:43], v[20:23]
	v_mfma_f32_16x16x32_f16 v[16:19], v[44:47], v[40:43], v[16:19]
	v_mfma_f32_16x16x32_f16 v[24:27], v[68:71], v[52:55], v[96:99]
	v_mfma_f32_16x16x32_f16 v[4:7], v[48:51], v[52:55], v[4:7]
	v_mfma_f32_16x16x32_f16 v[28:31], v[68:71], v[56:59], v[28:31]
	v_mfma_f32_16x16x32_f16 v[8:11], v[48:51], v[56:59], v[8:11]
	v_mfma_f32_16x16x32_f16 v[32:35], v[68:71], v[60:63], v[32:35]
	v_mfma_f32_16x16x32_f16 v[12:15], v[48:51], v[60:63], v[12:15]
	v_mfma_f32_16x16x32_f16 v[20:23], v[68:71], v[64:67], v[20:23]
	v_mfma_f32_16x16x32_f16 v[16:19], v[48:51], v[64:67], v[16:19]
	v_mfma_f32_16x16x32_f16 v[24:27], v[72:75], v[80:83], v[24:27]
	v_mfma_f32_16x16x32_f16 v[4:7], v[76:79], v[80:83], v[4:7]
	v_mfma_f32_16x16x32_f16 v[28:31], v[72:75], v[84:87], v[28:31]
	v_mfma_f32_16x16x32_f16 v[8:11], v[76:79], v[84:87], v[8:11]
	v_mfma_f32_16x16x32_f16 v[32:35], v[72:75], v[88:91], v[32:35]
	v_mfma_f32_16x16x32_f16 v[12:15], v[76:79], v[88:91], v[12:15]
	v_mfma_f32_16x16x32_f16 v[20:23], v[72:75], v[92:95], v[20:23]
	v_mfma_f32_16x16x32_f16 v[16:19], v[76:79], v[92:95], v[16:19]
	s_mov_b32 s0, 0x1a000
	v_add_co_u32_e32 v208, vcc, s0, v208
	s_mov_b32 s0, 0x10000
	s_nop 0
	v_addc_co_u32_e32 v209, vcc, 0, v209, vcc
	v_add_co_u32_e32 v48, vcc, s0, v212
	s_mov_b32 s0, 0x12000
	s_nop 0
	v_addc_co_u32_e32 v49, vcc, 0, v213, vcc
	v_add_co_u32_e32 v80, vcc, s0, v212
	s_mov_b32 s0, 0x14000
	s_nop 0
	v_addc_co_u32_e32 v81, vcc, 0, v213, vcc
	v_add_co_u32_e32 v96, vcc, s0, v212
	global_load_dwordx4 v[36:39], v[48:49], off
	global_load_dwordx4 v[40:43], v[48:49], off offset:1024
	global_load_dwordx4 v[44:47], v[48:49], off offset:2048
	s_nop 0
	global_load_dwordx4 v[48:51], v[48:49], off offset:3072
	s_nop 0
	global_load_dwordx4 v[52:55], v[210:211], off
	global_load_dwordx4 v[56:59], v[210:211], off offset:1024
	global_load_dwordx4 v[60:63], v[208:209], off
	global_load_dwordx4 v[64:67], v[208:209], off offset:1024
	v_addc_co_u32_e32 v97, vcc, 0, v213, vcc
	global_load_dwordx4 v[68:71], v[80:81], off
	global_load_dwordx4 v[72:75], v[80:81], off offset:1024
	global_load_dwordx4 v[76:79], v[80:81], off offset:2048
	s_nop 0
	global_load_dwordx4 v[80:83], v[80:81], off offset:3072
	s_nop 0
	global_load_dwordx4 v[84:87], v[96:97], off
	global_load_dwordx4 v[88:91], v[96:97], off offset:1024
	global_load_dwordx4 v[92:95], v[96:97], off offset:2048
	s_nop 0
	global_load_dwordx4 v[96:99], v[96:97], off offset:3072
	s_nop 0
	global_load_dwordx4 v[196:199], v[210:211], off offset:2048
	global_load_dwordx4 v[200:203], v[210:211], off offset:3072
	global_load_dwordx4 v[204:207], v[208:209], off offset:2048
	s_nop 0
	global_load_dwordx4 v[208:211], v[208:209], off offset:3072
	s_mov_b32 s0, 0x16000
	v_add_co_u32_e32 v224, vcc, s0, v212
	s_nop 1
	v_addc_co_u32_e32 v225, vcc, 0, v213, vcc
	global_load_dwordx4 v[212:215], v[224:225], off
	global_load_dwordx4 v[216:219], v[224:225], off offset:1024
	global_load_dwordx4 v[220:223], v[224:225], off offset:2048
	s_nop 0
	global_load_dwordx4 v[224:227], v[224:225], off offset:3072
	s_waitcnt vmcnt(29)
	v_mfma_f32_16x16x32_f16 v[24:27], v[172:175], v[104:107], v[24:27]
	v_mfma_f32_16x16x32_f16 v[4:7], v[100:103], v[104:107], v[4:7]
	v_mfma_f32_16x16x32_f16 v[28:31], v[172:175], v[108:111], v[28:31]
	v_mfma_f32_16x16x32_f16 v[8:11], v[100:103], v[108:111], v[8:11]
	v_mfma_f32_16x16x32_f16 v[32:35], v[172:175], v[112:115], v[32:35]
	v_mfma_f32_16x16x32_f16 v[12:15], v[100:103], v[112:115], v[12:15]
	v_mfma_f32_16x16x32_f16 v[20:23], v[172:175], v[116:119], v[20:23]
	v_mfma_f32_16x16x32_f16 v[16:19], v[100:103], v[116:119], v[16:19]
	v_mfma_f32_16x16x32_f16 v[24:27], v[136:139], v[120:123], v[24:27]
	v_mfma_f32_16x16x32_f16 v[4:7], v[144:147], v[120:123], v[4:7]
	v_mfma_f32_16x16x32_f16 v[28:31], v[136:139], v[124:127], v[28:31]
	v_mfma_f32_16x16x32_f16 v[8:11], v[144:147], v[124:127], v[8:11]
	v_mfma_f32_16x16x32_f16 v[32:35], v[136:139], v[128:131], v[32:35]
	v_mfma_f32_16x16x32_f16 v[12:15], v[144:147], v[128:131], v[12:15]
	v_mfma_f32_16x16x32_f16 v[20:23], v[136:139], v[132:135], v[20:23]
	v_mfma_f32_16x16x32_f16 v[16:19], v[144:147], v[132:135], v[16:19]
	v_mfma_f32_16x16x32_f16 v[24:27], v[140:143], v[152:155], v[24:27]
	v_mfma_f32_16x16x32_f16 v[4:7], v[148:151], v[152:155], v[4:7]
	v_mfma_f32_16x16x32_f16 v[28:31], v[140:143], v[156:159], v[28:31]
	v_mfma_f32_16x16x32_f16 v[8:11], v[148:151], v[156:159], v[8:11]
	v_mfma_f32_16x16x32_f16 v[32:35], v[140:143], v[160:163], v[32:35]
	v_mfma_f32_16x16x32_f16 v[12:15], v[148:151], v[160:163], v[12:15]
	v_mfma_f32_16x16x32_f16 v[20:23], v[140:143], v[164:167], v[20:23]
	v_mfma_f32_16x16x32_f16 v[16:19], v[148:151], v[164:167], v[16:19]
	s_waitcnt vmcnt(27)
	v_mfma_f32_16x16x32_f16 v[24:27], v[168:171], v[180:183], v[24:27]
	v_mfma_f32_16x16x32_f16 v[4:7], v[176:179], v[180:183], v[4:7]
	s_waitcnt vmcnt(26)
	v_mfma_f32_16x16x32_f16 v[28:31], v[168:171], v[184:187], v[28:31]
	v_mfma_f32_16x16x32_f16 v[8:11], v[176:179], v[184:187], v[8:11]
	s_waitcnt vmcnt(25)
	v_mfma_f32_16x16x32_f16 v[32:35], v[168:171], v[188:191], v[32:35]
	v_mfma_f32_16x16x32_f16 v[12:15], v[176:179], v[188:191], v[12:15]
	s_waitcnt vmcnt(24)
	v_mfma_f32_16x16x32_f16 v[20:23], v[168:171], v[192:195], v[20:23]
	v_mfma_f32_16x16x32_f16 v[16:19], v[176:179], v[192:195], v[16:19]
	s_waitcnt vmcnt(19)
	v_mfma_f32_16x16x32_f16 v[24:27], v[52:55], v[36:39], v[24:27]
	s_waitcnt vmcnt(17)
	v_mfma_f32_16x16x32_f16 v[4:7], v[60:63], v[36:39], v[4:7]
	v_mfma_f32_16x16x32_f16 v[28:31], v[52:55], v[40:43], v[28:31]
	v_mfma_f32_16x16x32_f16 v[8:11], v[60:63], v[40:43], v[8:11]
	v_mfma_f32_16x16x32_f16 v[32:35], v[52:55], v[44:47], v[32:35]
	v_mfma_f32_16x16x32_f16 v[12:15], v[60:63], v[44:47], v[12:15]
	v_mfma_f32_16x16x32_f16 v[20:23], v[52:55], v[48:51], v[20:23]
	v_mfma_f32_16x16x32_f16 v[16:19], v[60:63], v[48:51], v[16:19]
	s_waitcnt vmcnt(15)
	v_mfma_f32_16x16x32_f16 v[24:27], v[56:59], v[68:71], v[24:27]
	v_mfma_f32_16x16x32_f16 v[4:7], v[64:67], v[68:71], v[4:7]
	s_waitcnt vmcnt(14)
	v_mfma_f32_16x16x32_f16 v[28:31], v[56:59], v[72:75], v[28:31]
	v_mfma_f32_16x16x32_f16 v[8:11], v[64:67], v[72:75], v[8:11]
	s_waitcnt vmcnt(13)
	v_mfma_f32_16x16x32_f16 v[32:35], v[56:59], v[76:79], v[32:35]
	v_mfma_f32_16x16x32_f16 v[12:15], v[64:67], v[76:79], v[12:15]
	s_waitcnt vmcnt(12)
	v_mfma_f32_16x16x32_f16 v[20:23], v[56:59], v[80:83], v[20:23]
	v_mfma_f32_16x16x32_f16 v[16:19], v[64:67], v[80:83], v[16:19]
	s_waitcnt vmcnt(7)
	v_mfma_f32_16x16x32_f16 v[24:27], v[196:199], v[84:87], v[24:27]
	s_waitcnt vmcnt(5)
	v_mfma_f32_16x16x32_f16 v[4:7], v[204:207], v[84:87], v[4:7]
	v_mfma_f32_16x16x32_f16 v[28:31], v[196:199], v[88:91], v[28:31]
	v_mfma_f32_16x16x32_f16 v[8:11], v[204:207], v[88:91], v[8:11]
	v_mfma_f32_16x16x32_f16 v[32:35], v[196:199], v[92:95], v[32:35]
	v_mfma_f32_16x16x32_f16 v[12:15], v[204:207], v[92:95], v[12:15]
	v_mfma_f32_16x16x32_f16 v[20:23], v[196:199], v[96:99], v[20:23]
	v_mfma_f32_16x16x32_f16 v[16:19], v[204:207], v[96:99], v[16:19]
	s_waitcnt vmcnt(3)
	v_mfma_f32_16x16x32_f16 v[24:27], v[200:203], v[212:215], v[24:27]
	v_mfma_f32_16x16x32_f16 v[4:7], v[208:211], v[212:215], v[4:7]
	s_waitcnt vmcnt(2)
	v_mfma_f32_16x16x32_f16 v[28:31], v[200:203], v[216:219], v[28:31]
	v_mfma_f32_16x16x32_f16 v[8:11], v[208:211], v[216:219], v[8:11]
	s_waitcnt vmcnt(1)
	v_mfma_f32_16x16x32_f16 v[32:35], v[200:203], v[220:223], v[32:35]
	v_mfma_f32_16x16x32_f16 v[12:15], v[208:211], v[220:223], v[12:15]
	s_waitcnt vmcnt(0)
	v_mfma_f32_16x16x32_f16 v[20:23], v[200:203], v[224:227], v[20:23]
	v_mfma_f32_16x16x32_f16 v[16:19], v[208:211], v[224:227], v[16:19]
	global_load_dwordx4 v[36:39], v[228:229], off
	v_add_u32_e32 v2, 0, v2
	v_and_b32_e32 v41, 0x1c0, v0
	v_lshl_add_u32 v43, v230, 13, v2
	v_lshl_add_u32 v2, v41, 4, v2
	v_lshl_add_u32 v40, v0, 4, 0
	ds_write_b128 v43, v[24:27]
	ds_write_b128 v43, v[4:7] offset:1024
	ds_write_b128 v43, v[28:31] offset:2048
	ds_write_b128 v43, v[8:11] offset:3072
	ds_write_b128 v43, v[32:35] offset:4096
	ds_write_b128 v43, v[12:15] offset:5120
	ds_write_b128 v43, v[20:23] offset:6144
	ds_write_b128 v43, v[16:19] offset:7168
	s_waitcnt lgkmcnt(0)
	s_barrier
	ds_read_b128 v[4:7], v2 offset:8192
	ds_read_b128 v[8:11], v2 offset:16384
	ds_read_b128 v[12:15], v2 offset:24576
	ds_read_b128 v[16:19], v40
	ds_read_b128 v[20:23], v2 offset:32768
	ds_read_b128 v[24:27], v2 offset:40960
	ds_read_b128 v[28:31], v2 offset:49152
	ds_read_b128 v[32:35], v2 offset:57344
	s_waitcnt lgkmcnt(4)
	v_pk_add_f32 v[4:5], v[16:17], v[4:5]
	v_pk_add_f32 v[6:7], v[18:19], v[6:7]
	v_pk_add_f32 v[4:5], v[4:5], v[8:9]
	v_pk_add_f32 v[6:7], v[6:7], v[10:11]
	v_pk_add_f32 v[4:5], v[4:5], v[12:13]
	v_pk_add_f32 v[6:7], v[6:7], v[14:15]
	s_waitcnt lgkmcnt(3)
	v_pk_add_f32 v[4:5], v[4:5], v[20:21]
	v_pk_add_f32 v[6:7], v[6:7], v[22:23]
	s_waitcnt lgkmcnt(2)
	v_pk_add_f32 v[4:5], v[4:5], v[24:25]
	v_pk_add_f32 v[6:7], v[6:7], v[26:27]
	s_waitcnt lgkmcnt(1)
	v_pk_add_f32 v[4:5], v[4:5], v[28:29]
	v_pk_add_f32 v[6:7], v[6:7], v[30:31]
	s_waitcnt lgkmcnt(0)
	v_pk_add_f32 v[4:5], v[4:5], v[32:33]
	v_pk_add_f32 v[6:7], v[6:7], v[34:35]
	v_lshrrev_b32_e32 v42, 7, v0
	s_waitcnt vmcnt(0)
	v_pk_add_f32 v[4:5], v[36:37], v[4:5]
	v_pk_add_f32 v[6:7], v[38:39], v[6:7]
	v_mul_f32_e32 v2, 0x3d372713, v4
	v_mul_f32_e32 v8, 0x3d372713, v5
	v_mul_f32_e32 v9, 0x3d372713, v6
	v_mul_f32_e32 v2, v4, v2
	v_mul_f32_e32 v8, v5, v8
	v_mul_f32_e32 v9, v6, v9
	v_fma_f32 v2, v4, v2, v4
	v_fma_f32 v8, v5, v8, v5
	v_fma_f32 v9, v6, v9, v6
	v_mul_f32_e32 v2, 0x3f4c422a, v2
	v_mul_f32_e32 v8, 0x3f4c422a, v8
	v_mul_f32_e32 v9, 0x3f4c422a, v9
	v_add_f32_e32 v2, v2, v2
	v_add_f32_e32 v8, v8, v8
	v_add_f32_e32 v9, v9, v9
	v_mul_f32_e32 v2, 0x3fb8aa3b, v2
	v_mul_f32_e32 v11, 0x3fb8aa3b, v8
	v_mul_f32_e32 v10, 0x3d372713, v7
	v_mul_f32_e32 v12, 0x3fb8aa3b, v9
	v_exp_f32_e32 v8, v2
	v_exp_f32_e32 v9, v11
	v_mul_f32_e32 v10, v7, v10
	v_fma_f32 v10, v7, v10, v7
	v_mul_f32_e32 v10, 0x3f4c422a, v10
	v_add_f32_e32 v10, v10, v10
	v_pk_add_f32 v[8:9], v[8:9], 1.0 op_sel_hi:[1,0]
	v_mul_f32_e32 v13, 0x3fb8aa3b, v10
	v_div_scale_f32 v2, s[0:1], v9, v9, 2.0
	v_exp_f32_e32 v10, v12
	v_exp_f32_e32 v11, v13
	v_div_scale_f32 v14, s[0:1], v8, v8, 2.0
	v_rcp_f32_e32 v16, v2
	v_rcp_f32_e32 v17, v14
	v_pk_add_f32 v[10:11], v[10:11], 1.0 op_sel_hi:[1,0]
	v_div_scale_f32 v13, vcc, 2.0, v9, 2.0
	v_fma_f32 v20, -v2, v16, 1.0
	v_div_scale_f32 v15, s[0:1], v11, v11, 2.0
	v_fma_f32 v21, -v14, v17, 1.0
	v_fmac_f32_e32 v16, v20, v16
	v_div_scale_f32 v19, s[0:1], 2.0, v8, 2.0
	v_fmac_f32_e32 v17, v21, v17
	v_mul_f32_e32 v20, v13, v16
	v_mul_f32_e32 v21, v19, v17
	v_fma_f32 v23, -v2, v20, v13
	v_fma_f32 v24, -v14, v21, v19
	v_fmac_f32_e32 v20, v23, v16
	v_fmac_f32_e32 v21, v24, v17
	v_fma_f32 v2, -v2, v20, v13
	v_rcp_f32_e32 v18, v15
	v_fma_f32 v13, -v14, v21, v19
	v_div_fmas_f32 v2, v2, v16, v20
	s_mov_b64 vcc, s[0:1]
	v_div_fixup_f32 v9, v2, v9, 2.0
	v_div_fmas_f32 v2, v13, v17, v21
	v_div_fixup_f32 v8, v2, v8, 2.0
	v_pk_add_f32 v[8:9], v[8:9], 1.0 op_sel_hi:[1,0] neg_lo:[1,0] neg_hi:[1,0]
	v_pk_mul_f32 v[4:5], v[4:5], 0.5 op_sel_hi:[1,0]
	v_fma_f32 v22, -v15, v18, 1.0
	v_pk_add_f32 v[8:9], v[8:9], 1.0 op_sel_hi:[1,0]
	v_fmac_f32_e32 v18, v22, v18
	v_pk_mul_f32 v[4:5], v[4:5], v[8:9]
	v_div_scale_f32 v2, vcc, 2.0, v11, 2.0
	v_cvt_pk_f16_f32 v4, v4, v5
	v_mul_f32_e32 v5, v2, v18
	v_fma_f32 v8, -v15, v5, v2
	v_fmac_f32_e32 v5, v8, v18
	v_div_scale_f32 v8, s[0:1], v10, v10, 2.0
	v_rcp_f32_e32 v13, v8
	v_fma_f32 v2, -v15, v5, v2
	v_div_fmas_f32 v2, v2, v18, v5
	v_div_fixup_f32 v9, v2, v11, 2.0
	v_fma_f32 v2, -v8, v13, 1.0
	v_fmac_f32_e32 v13, v2, v13
	v_div_scale_f32 v2, vcc, 2.0, v10, 2.0
	v_mul_f32_e32 v5, v2, v13
	v_fma_f32 v11, -v8, v5, v2
	v_fmac_f32_e32 v5, v11, v13
	v_fma_f32 v2, -v8, v5, v2
	v_div_fmas_f32 v2, v2, v13, v5
	v_div_fixup_f32 v8, v2, v10, 2.0
	v_pk_add_f32 v[8:9], v[8:9], 1.0 op_sel_hi:[1,0] neg_lo:[1,0] neg_hi:[1,0]
	s_lshl_b32 s0, s2, 3
	v_pk_mul_f32 v[6:7], v[6:7], 0.5 op_sel_hi:[1,0]
	v_pk_add_f32 v[8:9], v[8:9], 1.0 op_sel_hi:[1,0]
	s_add_i32 s0, s0, s12
	v_pk_mul_f32 v[6:7], v[6:7], v[8:9]
	v_or_b32_e32 v2, s0, v42
	v_cvt_pk_f16_f32 v5, v6, v7
	v_lshlrev_b64 v[6:7], 6, v[2:3]
	v_lshrrev_b32_e32 v2, 1, v0
	v_and_b32_e32 v12, 15, v0
	v_and_b32_e32 v0, 16, v2
	v_lshl_or_b32 v0, v1, 5, v0
	v_or3_b32 v6, v6, v0, v12
	v_lshl_add_u64 v[0:1], v[6:7], 4, s[10:11]
	v_and_b32_e32 v2, 8, v2
	v_lshl_add_u64 v[0:1], v[0:1], 0, v[2:3]
	global_store_dwordx2 v[0:1], v[4:5], off
	s_endpgm
	s_nop 0
	s_nop 0
	s_nop 0
	s_nop 0
	s_nop 0
	s_nop 0
	s_nop 0
	s_nop 0
	s_nop 0
	s_nop 0
	s_nop 0
	s_nop 0
	s_nop 0
	s_nop 0
	s_nop 0
	s_nop 0
	s_nop 0
	s_nop 0
	s_nop 0
	s_nop 0
	s_nop 0
	s_nop 0
	s_nop 0
	s_nop 0
	s_nop 0
	s_nop 0
	s_nop 0
	s_nop 0
	s_nop 0
	s_nop 0
	s_nop 0
	s_endpgm

	.amdhsa_kernel _ZN12_GLOBAL__N_110gemm_fullkILi0ELi1EEEvPKDF16_S2_PKfPDF16_PfS6_S4_S4_S4_S4_S4_S5_
		.amdhsa_group_segment_fixed_size 0
		.amdhsa_private_segment_fixed_size 0
		.amdhsa_kernarg_size 96
		.amdhsa_user_sgpr_count 2
		.amdhsa_user_sgpr_dispatch_ptr 0
		.amdhsa_user_sgpr_queue_ptr 0
		.amdhsa_user_sgpr_kernarg_segment_ptr 1
		.amdhsa_user_sgpr_dispatch_id 0
		.amdhsa_user_sgpr_kernarg_preload_length 0
		.amdhsa_user_sgpr_kernarg_preload_offset 0
		.amdhsa_user_sgpr_private_segment_size 0
		.amdhsa_uses_dynamic_stack 0
		.amdhsa_enable_private_segment 0
		.amdhsa_system_sgpr_workgroup_id_x 1
		.amdhsa_system_sgpr_workgroup_id_y 0
		.amdhsa_system_sgpr_workgroup_id_z 0
		.amdhsa_system_sgpr_workgroup_info 0
		.amdhsa_system_vgpr_workitem_id 0
		.amdhsa_next_free_vgpr 231
		.amdhsa_next_free_sgpr 14
		.amdhsa_accum_offset 232
		.amdhsa_reserve_vcc 1
		.amdhsa_float_round_mode_32 0
		.amdhsa_float_round_mode_16_64 0
		.amdhsa_float_denorm_mode_32 3
		.amdhsa_float_denorm_mode_16_64 3
		.amdhsa_dx10_clamp 1
		.amdhsa_ieee_mode 1
		.amdhsa_fp16_overflow 0
		.amdhsa_tg_split 0
		.amdhsa_exception_fp_ieee_invalid_op 0
		.amdhsa_exception_fp_denorm_src 0
		.amdhsa_exception_fp_ieee_div_zero 0
		.amdhsa_exception_fp_ieee_overflow 0
		.amdhsa_exception_fp_ieee_underflow 0
		.amdhsa_exception_fp_ieee_inexact 0
		.amdhsa_exception_int_div_zero 0
	.end_amdhsa_kernel

_ZN12_GLOBAL__N_110gemm_fullkILi1ELi1EEEvPKDF16_S2_PKfPDF16_PfS6_S4_S4_S4_S4_S4_S5_:
	s_load_dwordx2 s[4:5], s[0:1], 0x38
	s_load_dwordx2 s[10:11], s[0:1], 0x20
	s_and_b32 s3, s2, 63
	s_lshl_b32 s16, s3, 5
	s_lshl_b32 s6, s3, 13
	s_waitcnt lgkmcnt(0)
	s_add_u32 s4, s4, s6
	s_addc_u32 s5, s5, 0
	v_lshlrev_b32_e32 v1, 4, v0
	global_load_dwordx4 v[2:5], v1, s[4:5]
	v_lshlrev_b32_e32 v1, 2, v0
	v_cmp_lt_u32_e32 vcc, 31, v0
	s_and_saveexec_b64 s[4:5], vcc
	s_xor_b64 s[4:5], exec, s[4:5]
	s_cbranch_execz .LBB11_10
	v_cmp_lt_u32_e32 vcc, 63, v0
	s_and_saveexec_b64 s[6:7], vcc
	s_xor_b64 s[6:7], exec, s[6:7]
	s_cbranch_execz .LBB11_7
	s_movk_i32 s8, 0x47
	v_cmp_lt_u32_e32 vcc, s8, v0
	s_and_saveexec_b64 s[8:9], vcc
	s_xor_b64 s[8:9], exec, s[8:9]
	s_cbranch_execz .LBB11_4
	s_load_dwordx2 s[12:13], s[0:1], 0x10
	s_lshl_b32 s14, s16, 2
	v_lshlrev_b32_e32 v6, 2, v1
	v_mov_b32_e32 v7, 0
	s_movk_i32 s17, 0x50
	s_waitcnt lgkmcnt(0)
	s_add_u32 s12, s12, s14
	s_addc_u32 s13, s13, 0
	s_movk_i32 s14, 0xfb80
	v_lshl_add_u64 v[6:7], s[12:13], 0, v[6:7]
	s_mov_b32 s15, -1
	v_lshl_add_u64 v[6:7], v[6:7], 0, s[14:15]
	v_mov_b32_e32 v8, s13
	v_cmp_gt_u32_e32 vcc, s17, v0
	s_nop 1
	v_cndmask_b32_e32 v7, v8, v7, vcc
	v_mov_b32_e32 v8, s12
	v_cndmask_b32_e32 v6, v8, v6, vcc
.LBB11_4:
	s_andn2_saveexec_b64 s[8:9], s[8:9]
	s_cbranch_execz .LBB11_6
	s_load_dwordx2 s[12:13], s[0:1], 0x50
	s_lshl_b32 s14, s16, 2
	v_lshlrev_b32_e32 v6, 2, v1
	v_mov_b32_e32 v7, 0
	s_waitcnt lgkmcnt(0)
	s_add_u32 s12, s12, s14
	s_addc_u32 s13, s13, 0
	v_lshl_add_u64 v[6:7], s[12:13], 0, v[6:7]
	s_movk_i32 s12, 0xfc00
	s_mov_b32 s13, -1
	v_lshl_add_u64 v[6:7], v[6:7], 0, s[12:13]

.LBB11_7:
	s_andn2_saveexec_b64 s[6:7], s[6:7]
	s_cbranch_execz .LBB11_9
	s_load_dwordx2 s[8:9], s[0:1], 0x48
	s_lshl_b32 s12, s3, 9
	v_lshlrev_b32_e32 v6, 2, v1
	v_mov_b32_e32 v7, 0
	s_waitcnt lgkmcnt(0)
	s_add_u32 s8, s8, s12
	s_addc_u32 s9, s9, 0
	v_lshl_add_u64 v[6:7], s[8:9], 0, v[6:7]
	s_movk_i32 s8, 0xfe00
	s_mov_b32 s9, -1
	v_lshl_add_u64 v[6:7], v[6:7], 0, s[8:9]

.LBB11_10:
	s_or_saveexec_b64 s[14:15], s[4:5]
	s_load_dwordx2 s[8:9], s[0:1], 0x58
	s_load_dwordx2 s[12:13], s[0:1], 0x28
	s_load_dwordx4 s[4:7], s[0:1], 0x0
	s_xor_b64 exec, exec, s[14:15]
	s_cbranch_execz .LBB11_12
	s_load_dwordx2 s[0:1], s[0:1], 0x40
	s_lshl_b32 s17, s3, 9
	v_lshlrev_b32_e32 v6, 2, v1
	v_mov_b32_e32 v7, 0
	s_waitcnt lgkmcnt(0)
	s_add_u32 s0, s0, s17
	s_addc_u32 s1, s1, 0
	v_lshl_add_u64 v[6:7], s[0:1], 0, v[6:7]
.LBB11_12:
	s_or_b64 exec, exec, s[14:15]
	v_lshrrev_b32_e32 v176, 6, v0
	s_lshr_b32 s0, s2, 5
	v_mov_b32_e32 v9, 0
	v_lshlrev_b32_e32 v10, 14, v176
	v_and_b32_e32 v14, 63, v0
	s_and_b32 s0, s0, 0x7fffffe
	s_mov_b32 s1, 0
	v_lshlrev_b32_e32 v8, 17, v176
	v_lshl_or_b32 v10, s3, 18, v10
	v_mov_b32_e32 v11, v9
	s_lshl_b64 s[14:15], s[0:1], 10
	s_waitcnt lgkmcnt(0)
	v_lshl_add_u64 v[10:11], s[6:7], 0, v[10:11]
	v_lshl_add_u64 v[12:13], s[4:5], 0, v[8:9]
	v_lshlrev_b32_e32 v18, 4, v14
	v_mov_b32_e32 v19, v9
	v_lshl_add_u64 v[12:13], v[12:13], 0, s[14:15]
	v_lshl_add_u64 v[172:173], v[10:11], 0, v[18:19]
	v_lshrrev_b32_e32 v8, 8, v0
	v_lshrrev_b32_e32 v11, 2, v0
	v_lshl_add_u64 v[170:171], v[12:13], 0, v[18:19]
	v_and_b32_e32 v19, 15, v0
	v_or_b32_e32 v21, s0, v8
	v_lshrrev_b32_e32 v8, 3, v0
	v_and_b32_e32 v11, 12, v11
	v_bfe_u32 v23, v0, 6, 1
	v_lshl_or_b32 v10, v21, 4, v19
	v_and_or_b32 v22, v8, 16, v11
	v_mov_b32_e32 v11, v9
	v_lshl_or_b32 v20, v23, 1, v22
	v_lshlrev_b64 v[12:13], 11, v[10:11]
	s_mov_b64 s[0:1], 0x40000
	v_or_b32_e32 v8, s16, v20
	v_lshl_add_u64 v[16:17], v[12:13], 0, s[0:1]
	v_lshl_add_u64 v[12:13], v[16:17], 2, s[10:11]
	v_lshlrev_b32_e32 v8, 2, v8
	v_lshl_add_u64 v[12:13], v[12:13], 0, v[8:9]
	global_load_dwordx2 v[14:15], v[12:13], off
	v_lshl_add_u64 v[24:25], s[12:13], 0, v[8:9]
	v_lshlrev_b64 v[12:13], 13, v[10:11]
	s_mov_b32 s0, 0x20000
	v_lshl_add_u64 v[10:11], v[24:25], 0, v[12:13]
	v_add_co_u32_e32 v24, vcc, s0, v172
	s_mov_b32 s0, 0x21000
	s_nop 0
	v_addc_co_u32_e32 v25, vcc, 0, v173, vcc
	v_add_co_u32_e32 v142, vcc, s0, v172
	s_movk_i32 s0, 0x2000
	s_nop 0
	v_addc_co_u32_e32 v143, vcc, 0, v173, vcc
	v_add_co_u32_e32 v58, vcc, s0, v170
	s_movk_i32 s1, 0x4000
	s_nop 0
	v_addc_co_u32_e32 v59, vcc, 0, v171, vcc
	v_add_co_u32_e32 v78, vcc, s1, v170
	s_movk_i32 s1, 0x6000
	s_nop 0
	v_addc_co_u32_e32 v79, vcc, 0, v171, vcc
	global_load_dwordx2 v[10:11], v[10:11], off
	s_nop 0
	global_load_dwordx4 v[26:29], v[170:171], off
	global_load_dwordx4 v[30:33], v[170:171], off offset:1024
	global_load_dwordx4 v[34:37], v[172:173], off
	global_load_dwordx4 v[38:41], v[172:173], off offset:1024
	global_load_dwordx4 v[42:45], v[58:59], off
	global_load_dwordx4 v[46:49], v[58:59], off offset:1024
	global_load_dwordx4 v[50:53], v[24:25], off offset:1024
	global_load_dwordx4 v[54:57], v[24:25], off offset:2048
	s_nop 0
	global_load_dwordx4 v[58:61], v[78:79], off
	global_load_dwordx4 v[62:65], v[78:79], off offset:1024
	global_load_dwordx4 v[66:69], v[172:173], off offset:2048
	global_load_dwordx4 v[70:73], v[172:173], off offset:3072
	global_load_dwordx4 v[74:77], v[24:25], off offset:3072
	v_add_co_u32_e32 v24, vcc, s1, v170
	s_movk_i32 s1, 0x1000
	s_nop 0
	v_addc_co_u32_e32 v25, vcc, 0, v171, vcc
	global_load_dwordx4 v[78:81], v[24:25], off
	global_load_dwordx4 v[82:85], v[24:25], off offset:1024
	v_add_co_u32_e32 v24, vcc, s1, v172
	global_load_dwordx4 v[86:89], v[142:143], off offset:-4096
	global_load_dwordx4 v[90:93], v[142:143], off
	v_addc_co_u32_e32 v25, vcc, 0, v173, vcc
	v_add_co_u32_e32 v158, vcc, s0, v172
	s_mov_b32 s0, 0x8000
	s_nop 0
	v_addc_co_u32_e32 v159, vcc, 0, v173, vcc
	v_add_co_u32_e32 v102, vcc, s0, v170
	s_mov_b32 s0, 0xa000
	s_nop 0
	v_addc_co_u32_e32 v103, vcc, 0, v171, vcc
	v_add_co_u32_e32 v114, vcc, s0, v170
	s_mov_b32 s0, 0xc000
	s_nop 0
	v_addc_co_u32_e32 v115, vcc, 0, v171, vcc
	global_load_dwordx4 v[94:97], v[102:103], off
	global_load_dwordx4 v[98:101], v[102:103], off offset:1024
	s_nop 0
	global_load_dwordx4 v[102:105], v[114:115], off
	global_load_dwordx4 v[106:109], v[114:115], off offset:1024
	global_load_dwordx4 v[110:113], v[24:25], off offset:1024
	s_nop 0
	global_load_dwordx4 v[114:117], v[24:25], off offset:2048
	global_load_dwordx4 v[118:121], v[142:143], off offset:1024
	global_load_dwordx4 v[122:125], v[142:143], off offset:2048
	v_add_co_u32_e32 v130, vcc, s0, v170
	s_mov_b32 s0, 0xe000
	s_nop 0
	v_addc_co_u32_e32 v131, vcc, 0, v171, vcc
	global_load_dwordx4 v[126:129], v[130:131], off
	s_nop 0
	global_load_dwordx4 v[130:133], v[130:131], off offset:1024
	s_nop 0
	global_load_dwordx4 v[134:137], v[24:25], off offset:3072
	global_load_dwordx4 v[138:141], v[158:159], off offset:-4096
	s_nop 0
	global_load_dwordx4 v[142:145], v[142:143], off offset:3072
	v_add_co_u32_e32 v24, vcc, s0, v170
	s_nop 1
	v_addc_co_u32_e32 v25, vcc, 0, v171, vcc
	global_load_dwordx4 v[146:149], v[24:25], off
	global_load_dwordx4 v[150:153], v[24:25], off offset:1024
	v_lshrrev_b32_e32 v24, 7, v0
	s_waitcnt vmcnt(29)
	v_mfma_f32_16x16x32_f16 v[154:157], v[34:37], v[26:29], 0
	s_waitcnt vmcnt(16)
	v_mfma_f32_16x16x32_f16 v[26:29], v[86:89], v[26:29], 0
	v_mfma_f32_16x16x32_f16 v[34:37], v[34:37], v[30:33], 0
	v_mfma_f32_16x16x32_f16 v[30:33], v[86:89], v[30:33], 0
	v_mfma_f32_16x16x32_f16 v[86:89], v[38:41], v[42:45], v[154:157]
	v_mfma_f32_16x16x32_f16 v[26:29], v[50:53], v[42:45], v[26:29]
	v_mfma_f32_16x16x32_f16 v[34:37], v[38:41], v[46:49], v[34:37]
	v_mfma_f32_16x16x32_f16 v[30:33], v[50:53], v[46:49], v[30:33]
	v_mfma_f32_16x16x32_f16 v[38:41], v[66:69], v[58:61], v[86:89]
	v_mfma_f32_16x16x32_f16 v[26:29], v[54:57], v[58:61], v[26:29]
	v_mfma_f32_16x16x32_f16 v[34:37], v[66:69], v[62:65], v[34:37]
	v_mfma_f32_16x16x32_f16 v[30:33], v[54:57], v[62:65], v[30:33]
	v_mfma_f32_16x16x32_f16 v[38:41], v[70:73], v[78:81], v[38:41]
	v_mfma_f32_16x16x32_f16 v[26:29], v[74:77], v[78:81], v[26:29]
	v_mfma_f32_16x16x32_f16 v[34:37], v[70:73], v[82:85], v[34:37]
	v_mfma_f32_16x16x32_f16 v[30:33], v[74:77], v[82:85], v[30:33]
	s_mov_b32 s0, 0x22000
	v_add_co_u32_e32 v160, vcc, s0, v172
	s_mov_b32 s0, 0x23000
	s_nop 0
	v_addc_co_u32_e32 v161, vcc, 0, v173, vcc
	v_add_co_u32_e32 v174, vcc, s0, v172
	s_mov_b32 s0, 0x10000
	s_nop 0
	v_addc_co_u32_e32 v175, vcc, 0, v173, vcc
	v_add_co_u32_e32 v50, vcc, s0, v170
	s_mov_b32 s0, 0x12000
	s_nop 0
	v_addc_co_u32_e32 v51, vcc, 0, v171, vcc
	v_add_co_u32_e32 v66, vcc, s0, v170
	s_mov_b32 s0, 0x14000
	s_nop 0
	v_addc_co_u32_e32 v67, vcc, 0, v171, vcc
	v_add_co_u32_e32 v82, vcc, s0, v170
	global_load_dwordx4 v[42:45], v[174:175], off offset:-4096
	s_nop 0
	v_addc_co_u32_e32 v83, vcc, 0, v171, vcc
	global_load_dwordx4 v[46:49], v[50:51], off
	s_nop 0
	global_load_dwordx4 v[50:53], v[50:51], off offset:1024
	s_nop 0
	global_load_dwordx4 v[54:57], v[158:159], off
	global_load_dwordx4 v[58:61], v[158:159], off offset:1024
	global_load_dwordx4 v[62:65], v[66:67], off
	s_nop 0
	global_load_dwordx4 v[66:69], v[66:67], off offset:1024
	s_nop 0
	global_load_dwordx4 v[70:73], v[160:161], off offset:1024
	global_load_dwordx4 v[74:77], v[160:161], off offset:2048
	global_load_dwordx4 v[78:81], v[82:83], off
	s_nop 0
	global_load_dwordx4 v[82:85], v[82:83], off offset:1024
	s_nop 0
	global_load_dwordx4 v[86:89], v[158:159], off offset:2048
	global_load_dwordx4 v[154:157], v[158:159], off offset:3072
	s_nop 0
	global_load_dwordx4 v[158:161], v[160:161], off offset:3072
	s_mov_b32 s0, 0x16000
	v_add_co_u32_e32 v166, vcc, s0, v170
	s_nop 1
	v_addc_co_u32_e32 v167, vcc, 0, v171, vcc
	global_load_dwordx4 v[162:165], v[166:167], off
	s_nop 0
	global_load_dwordx4 v[166:169], v[166:167], off offset:1024
	s_waitcnt vmcnt(19)
	v_mfma_f32_16x16x32_f16 v[38:41], v[138:141], v[94:97], v[38:41]
	v_mfma_f32_16x16x32_f16 v[26:29], v[90:93], v[94:97], v[26:29]
	v_mfma_f32_16x16x32_f16 v[34:37], v[138:141], v[98:101], v[34:37]
	v_mfma_f32_16x16x32_f16 v[30:33], v[90:93], v[98:101], v[30:33]
	v_mfma_f32_16x16x32_f16 v[38:41], v[110:113], v[102:105], v[38:41]
	v_mfma_f32_16x16x32_f16 v[26:29], v[118:121], v[102:105], v[26:29]
	v_mfma_f32_16x16x32_f16 v[34:37], v[110:113], v[106:109], v[34:37]
	v_mfma_f32_16x16x32_f16 v[30:33], v[118:121], v[106:109], v[30:33]
	v_mfma_f32_16x16x32_f16 v[38:41], v[114:117], v[126:129], v[38:41]
	v_mfma_f32_16x16x32_f16 v[26:29], v[122:125], v[126:129], v[26:29]
	v_mfma_f32_16x16x32_f16 v[34:37], v[114:117], v[130:133], v[34:37]
	v_mfma_f32_16x16x32_f16 v[30:33], v[122:125], v[130:133], v[30:33]
	s_waitcnt vmcnt(17)
	v_mfma_f32_16x16x32_f16 v[38:41], v[134:137], v[146:149], v[38:41]
	v_mfma_f32_16x16x32_f16 v[26:29], v[142:145], v[146:149], v[26:29]
	s_waitcnt vmcnt(16)
	v_mfma_f32_16x16x32_f16 v[34:37], v[134:137], v[150:153], v[34:37]
	v_mfma_f32_16x16x32_f16 v[30:33], v[142:145], v[150:153], v[30:33]
	s_movk_i32 s0, 0x3000
	v_add_co_u32_e32 v134, vcc, s0, v172
	s_mov_b32 s0, 0x18000
	s_nop 0
	v_addc_co_u32_e32 v135, vcc, 0, v173, vcc
	v_add_co_u32_e32 v102, vcc, s0, v170
	s_mov_b32 s0, 0x1a000
	s_nop 0
	v_addc_co_u32_e32 v103, vcc, 0, v171, vcc
	v_add_co_u32_e32 v118, vcc, s0, v170
	s_mov_b32 s0, 0x1c000
	s_nop 0
	v_addc_co_u32_e32 v119, vcc, 0, v171, vcc
	v_add_co_u32_e32 v126, vcc, s0, v170
	global_load_dwordx4 v[90:93], v[102:103], off
	global_load_dwordx4 v[94:97], v[102:103], off offset:1024
	global_load_dwordx4 v[98:101], v[134:135], off
	s_nop 0
	global_load_dwordx4 v[102:105], v[134:135], off offset:1024
	global_load_dwordx4 v[106:109], v[174:175], off
	global_load_dwordx4 v[110:113], v[174:175], off offset:1024
	v_addc_co_u32_e32 v127, vcc, 0, v171, vcc
	global_load_dwordx4 v[114:117], v[118:119], off
	s_nop 0
	global_load_dwordx4 v[118:121], v[118:119], off offset:1024
	s_nop 0
	global_load_dwordx4 v[122:125], v[126:127], off
	s_nop 0
	global_load_dwordx4 v[126:129], v[126:127], off offset:1024
	s_nop 0
	global_load_dwordx4 v[130:133], v[134:135], off offset:2048
	s_nop 0
	global_load_dwordx4 v[134:137], v[134:135], off offset:3072
	s_nop 0
	global_load_dwordx4 v[138:141], v[174:175], off offset:2048
	global_load_dwordx4 v[142:145], v[174:175], off offset:3072
	s_mov_b32 s0, 0x1e000
	v_add_co_u32_e32 v150, vcc, s0, v170
	s_nop 1
	v_addc_co_u32_e32 v151, vcc, 0, v171, vcc
	global_load_dwordx4 v[146:149], v[150:151], off
	s_nop 0
	global_load_dwordx4 v[150:153], v[150:151], off offset:1024
	s_waitcnt vmcnt(28)
	v_mfma_f32_16x16x32_f16 v[38:41], v[54:57], v[46:49], v[38:41]
	v_mfma_f32_16x16x32_f16 v[26:29], v[42:45], v[46:49], v[26:29]
	v_mfma_f32_16x16x32_f16 v[34:37], v[54:57], v[50:53], v[34:37]
	v_mfma_f32_16x16x32_f16 v[30:33], v[42:45], v[50:53], v[30:33]
	s_waitcnt vmcnt(26)
	v_mfma_f32_16x16x32_f16 v[38:41], v[58:61], v[62:65], v[38:41]
	s_waitcnt vmcnt(24)
	v_mfma_f32_16x16x32_f16 v[26:29], v[70:73], v[62:65], v[26:29]
	v_mfma_f32_16x16x32_f16 v[34:37], v[58:61], v[66:69], v[34:37]
	v_mfma_f32_16x16x32_f16 v[30:33], v[70:73], v[66:69], v[30:33]
	s_waitcnt vmcnt(20)
	v_mfma_f32_16x16x32_f16 v[38:41], v[86:89], v[78:81], v[38:41]
	v_mfma_f32_16x16x32_f16 v[26:29], v[74:77], v[78:81], v[26:29]
	v_mfma_f32_16x16x32_f16 v[34:37], v[86:89], v[82:85], v[34:37]
	v_mfma_f32_16x16x32_f16 v[30:33], v[74:77], v[82:85], v[30:33]
	s_waitcnt vmcnt(17)
	v_mfma_f32_16x16x32_f16 v[38:41], v[154:157], v[162:165], v[38:41]
	v_mfma_f32_16x16x32_f16 v[26:29], v[158:161], v[162:165], v[26:29]
	s_waitcnt vmcnt(16)
	v_mfma_f32_16x16x32_f16 v[34:37], v[154:157], v[166:169], v[34:37]
	v_mfma_f32_16x16x32_f16 v[30:33], v[158:161], v[166:169], v[30:33]
	s_waitcnt vmcnt(13)
	v_mfma_f32_16x16x32_f16 v[38:41], v[98:101], v[90:93], v[38:41]
	s_waitcnt vmcnt(11)
	v_mfma_f32_16x16x32_f16 v[26:29], v[106:109], v[90:93], v[26:29]
	v_mfma_f32_16x16x32_f16 v[34:37], v[98:101], v[94:97], v[34:37]
	v_mfma_f32_16x16x32_f16 v[30:33], v[106:109], v[94:97], v[30:33]
	s_waitcnt vmcnt(9)
	v_mfma_f32_16x16x32_f16 v[38:41], v[102:105], v[114:117], v[38:41]
	v_mfma_f32_16x16x32_f16 v[26:29], v[110:113], v[114:117], v[26:29]
	s_waitcnt vmcnt(8)
	v_mfma_f32_16x16x32_f16 v[34:37], v[102:105], v[118:121], v[34:37]
	v_mfma_f32_16x16x32_f16 v[30:33], v[110:113], v[118:121], v[30:33]
	s_waitcnt vmcnt(5)
	v_mfma_f32_16x16x32_f16 v[38:41], v[130:133], v[122:125], v[38:41]
	s_waitcnt vmcnt(3)
	v_mfma_f32_16x16x32_f16 v[26:29], v[138:141], v[122:125], v[26:29]
	v_mfma_f32_16x16x32_f16 v[34:37], v[130:133], v[126:129], v[34:37]
	v_mfma_f32_16x16x32_f16 v[30:33], v[138:141], v[126:129], v[30:33]
	s_waitcnt vmcnt(1)
	v_mfma_f32_16x16x32_f16 v[38:41], v[134:137], v[146:149], v[38:41]
	v_mfma_f32_16x16x32_f16 v[26:29], v[142:145], v[146:149], v[26:29]
	s_waitcnt vmcnt(0)
	v_mfma_f32_16x16x32_f16 v[34:37], v[134:137], v[150:153], v[34:37]
	v_mfma_f32_16x16x32_f16 v[30:33], v[142:145], v[150:153], v[30:33]
	v_lshlrev_b32_e32 v25, 12, v176
	v_add3_u32 v25, 0, v18, v25
	s_nop 1
	ds_write_b128 v25, v[38:41]
	ds_write_b128 v25, v[26:29] offset:1024
	s_nop 0
	ds_write_b128 v25, v[34:37] offset:2048
	ds_write_b128 v25, v[30:33] offset:3072
	v_lshrrev_b32_e32 v25, 4, v0
	v_and_b32_e32 v26, 60, v1
	v_mul_u32_u24_e32 v25, 0x110, v25
	v_lshlrev_b32_e32 v26, 2, v26
	s_movk_i32 s0, 0x50
	v_add3_u32 v25, 0, v25, v26
	v_cmp_gt_u32_e32 vcc, s0, v0
	ds_write_b128 v25, v[2:5] offset:32768
	s_and_saveexec_b64 s[0:1], vcc
	s_cbranch_execz .LBB11_14
	global_load_dwordx4 v[2:5], v[6:7], off
	v_lshl_add_u32 v0, v1, 2, 0
	s_waitcnt vmcnt(0)
	ds_write_b128 v0, v[2:5] offset:41472
.LBB11_14:
	s_or_b64 exec, exec, s[0:1]
	v_lshlrev_b32_e32 v0, 10, v24
	v_add3_u32 v18, 0, v0, v18
	s_waitcnt lgkmcnt(0)
	s_barrier
	ds_read_b128 v[0:3], v18
	ds_read_b128 v[4:7], v18 offset:4096
	ds_read_b128 v[24:27], v18 offset:8192
	ds_read_b128 v[28:31], v18 offset:12288
	v_cmp_eq_u32_e32 vcc, 0, v23
	s_waitcnt lgkmcnt(2)
	v_pk_add_f32 v[2:3], v[2:3], v[6:7]
	v_pk_add_f32 v[4:5], v[0:1], v[4:5]
	s_waitcnt lgkmcnt(1)
	v_pk_add_f32 v[6:7], v[2:3], v[26:27]
	ds_read_b128 v[0:3], v18 offset:16384
	v_pk_add_f32 v[4:5], v[4:5], v[24:25]
	s_waitcnt lgkmcnt(1)
	v_pk_add_f32 v[24:25], v[6:7], v[30:31]
	v_pk_add_f32 v[28:29], v[4:5], v[28:29]
	ds_read_b128 v[4:7], v18 offset:20480
	s_waitcnt lgkmcnt(1)
	v_pk_add_f32 v[30:31], v[24:25], v[2:3]
	ds_read_b128 v[24:27], v18 offset:24576
	v_pk_add_f32 v[28:29], v[28:29], v[0:1]
	ds_read_b128 v[0:3], v18 offset:28672
	s_waitcnt lgkmcnt(2)
	v_pk_add_f32 v[6:7], v[30:31], v[6:7]
	v_lshl_add_u32 v18, v20, 2, 0
	s_waitcnt lgkmcnt(1)
	v_pk_add_f32 v[6:7], v[6:7], v[26:27]
	v_pk_add_f32 v[4:5], v[28:29], v[4:5]
	s_waitcnt lgkmcnt(0)
	v_pk_add_f32 v[2:3], v[6:7], v[2:3]
	ds_read_b64 v[6:7], v18 offset:42624
	v_pk_add_f32 v[4:5], v[4:5], v[24:25]
	s_nop 0
	v_pk_add_f32 v[0:1], v[4:5], v[0:1]
	v_lshl_add_u64 v[4:5], v[16:17], 2, s[12:13]
	v_cndmask_b32_e32 v1, v3, v1, vcc
	v_cndmask_b32_e32 v0, v2, v0, vcc
	v_mad_u32_u24 v2, v20, 12, v18
	ds_read_b128 v[24:27], v2 offset:41472
	s_waitcnt lgkmcnt(1)
	v_pk_add_f32 v[0:1], v[0:1], v[6:7]
	v_lshl_add_u64 v[4:5], v[4:5], 0, v[8:9]
	v_pk_add_f32 v[16:17], v[14:15], v[0:1]
	v_or_b32_e32 v0, 1, v20
	global_store_dwordx2 v[4:5], v[16:17], off
	v_lshl_add_u32 v5, v0, 4, 0
	v_lshl_add_u32 v3, v20, 8, v2
	v_lshl_add_u32 v6, v0, 8, v5
	v_lshl_add_u64 v[0:1], s[10:11], 0, v[12:13]
	v_mad_i32_i24 v4, v20, -12, v2
	v_lshl_add_u64 v[12:13], v[0:1], 0, v[8:9]
	ds_read_b128 v[28:31], v3 offset:32992
	ds_read_b64 v[14:15], v4 offset:42496
	ds_read_b128 v[32:35], v3 offset:33008
	ds_read_b128 v[36:39], v6 offset:32992
	ds_read_b128 v[0:3], v2 offset:41984
	ds_read_b128 v[40:43], v5 offset:41472
	ds_read_b128 v[44:47], v6 offset:33008
	s_waitcnt lgkmcnt(6)
	v_mov_b32_e32 v48, v28
	s_waitcnt lgkmcnt(3)
	v_mov_b32_e32 v49, v36
	v_mov_b32_e32 v50, v24
	s_waitcnt lgkmcnt(1)
	v_mov_b32_e32 v51, v40
	v_pk_fma_f32 v[48:49], v[10:11], v[48:49], v[50:51]
	v_mov_b32_e32 v50, v32
	s_waitcnt lgkmcnt(0)
	v_mov_b32_e32 v51, v44
	v_pk_fma_f32 v[48:49], v[16:17], v[50:51], v[48:49]
	v_mov_b32_e32 v36, v29
	v_mul_f32_e32 v8, 0x3d372713, v48
	v_mul_f32_e32 v8, v48, v8
	v_fma_f32 v8, v48, v8, v48
	v_mul_f32_e32 v8, 0x3f4c422a, v8
	v_mov_b32_e32 v40, v25
	v_add_f32_e32 v8, v8, v8
	v_pk_fma_f32 v[28:29], v[10:11], v[36:37], v[40:41]
	v_mov_b32_e32 v44, v33
	v_mul_f32_e32 v8, 0x3fb8aa3b, v8
	v_pk_fma_f32 v[28:29], v[16:17], v[44:45], v[28:29]
	v_exp_f32_e32 v24, v8
	v_mul_f32_e32 v8, 0x3d372713, v28
	v_mov_b32_e32 v36, v30
	v_mov_b32_e32 v37, v38
	v_mov_b32_e32 v40, v26
	v_mov_b32_e32 v41, v42
	v_mov_b32_e32 v38, v31
	v_mov_b32_e32 v42, v27
	v_mul_f32_e32 v8, v28, v8
	v_pk_fma_f32 v[36:37], v[10:11], v[36:37], v[40:41]
	v_mov_b32_e32 v40, v34
	v_mov_b32_e32 v41, v46
	v_pk_fma_f32 v[10:11], v[10:11], v[38:39], v[42:43]
	v_mov_b32_e32 v46, v35
	v_fma_f32 v8, v28, v8, v28
	v_pk_fma_f32 v[36:37], v[16:17], v[40:41], v[36:37]
	v_pk_fma_f32 v[10:11], v[16:17], v[46:47], v[10:11]
	v_mul_f32_e32 v16, 0x3d372713, v49
	v_mul_f32_e32 v8, 0x3f4c422a, v8
	v_mul_f32_e32 v16, v49, v16
	v_add_f32_e32 v8, v8, v8
	v_fma_f32 v16, v49, v16, v49
	v_mul_f32_e32 v8, 0x3fb8aa3b, v8
	v_mul_f32_e32 v16, 0x3f4c422a, v16
	v_exp_f32_e32 v32, v8
	v_mul_f32_e32 v8, 0x3d372713, v36
	v_add_f32_e32 v16, v16, v16
	v_mul_f32_e32 v8, v36, v8
	v_mul_f32_e32 v16, 0x3fb8aa3b, v16
	v_fma_f32 v8, v36, v8, v36
	v_exp_f32_e32 v25, v16
	v_mul_f32_e32 v8, 0x3f4c422a, v8
	v_add_f32_e32 v8, v8, v8
	v_mul_f32_e32 v8, 0x3fb8aa3b, v8
	v_exp_f32_e32 v26, v8
	v_mul_f32_e32 v8, 0x3d372713, v10
	v_pk_add_f32 v[16:17], v[24:25], 1.0 op_sel_hi:[1,0]
	v_mul_f32_e32 v8, v10, v8
	v_div_scale_f32 v18, s[0:1], v17, v17, 2.0
	v_fma_f32 v8, v10, v8, v10
	v_rcp_f32_e32 v23, v18
	v_mul_f32_e32 v8, 0x3f4c422a, v8
	v_add_f32_e32 v8, v8, v8
	v_mul_f32_e32 v8, 0x3fb8aa3b, v8
	v_exp_f32_e32 v24, v8
	v_fma_f32 v8, -v18, v23, 1.0
	v_fmac_f32_e32 v23, v8, v23
	v_div_scale_f32 v8, vcc, 2.0, v17, 2.0
	v_mul_f32_e32 v25, v8, v23
	v_fma_f32 v27, -v18, v25, v8
	v_fmac_f32_e32 v25, v27, v23
	v_fma_f32 v8, -v18, v25, v8
	v_div_scale_f32 v18, s[0:1], v16, v16, 2.0
	v_rcp_f32_e32 v27, v18
	v_div_fmas_f32 v8, v8, v23, v25
	v_div_fixup_f32 v17, v8, v17, 2.0
	ds_read_b128 v[4:7], v5 offset:41984
	v_fma_f32 v8, -v18, v27, 1.0
	v_fmac_f32_e32 v27, v8, v27
	v_div_scale_f32 v8, vcc, 2.0, v16, 2.0
	v_mul_f32_e32 v23, v8, v27
	v_fma_f32 v25, -v18, v23, v8
	v_fmac_f32_e32 v23, v25, v27
	v_fma_f32 v8, -v18, v23, v8
	v_div_fmas_f32 v8, v8, v27, v23
	v_div_fixup_f32 v16, v8, v16, 2.0
	v_mul_f32_e32 v8, 0x3d372713, v29
	v_mul_f32_e32 v8, v29, v8
	v_fma_f32 v8, v29, v8, v29
	v_mul_f32_e32 v8, 0x3f4c422a, v8
	v_add_f32_e32 v8, v8, v8
	v_mul_f32_e32 v8, 0x3fb8aa3b, v8
	v_exp_f32_e32 v33, v8
	v_pk_add_f32 v[16:17], v[16:17], 1.0 op_sel_hi:[1,0] neg_lo:[1,0] neg_hi:[1,0]
	v_pk_mul_f32 v[30:31], v[48:49], 0.5 op_sel_hi:[1,0]
	v_pk_add_f32 v[16:17], v[16:17], 1.0 op_sel_hi:[1,0]
	v_pk_add_f32 v[32:33], v[32:33], 1.0 op_sel_hi:[1,0]
	v_pk_mul_f32 v[16:17], v[30:31], v[16:17]
	v_div_scale_f32 v8, s[0:1], v33, v33, 2.0
	v_rcp_f32_e32 v18, v8
	v_mov_b32_e32 v30, v0
	s_waitcnt lgkmcnt(0)
	v_mov_b32_e32 v31, v4
	v_pk_mul_f32 v[28:29], v[28:29], 0.5 op_sel_hi:[1,0]
	v_fma_f32 v0, -v8, v18, 1.0
	v_fmac_f32_e32 v18, v0, v18
	v_div_scale_f32 v0, vcc, 2.0, v33, 2.0
	v_mul_f32_e32 v4, v0, v18
	v_fma_f32 v23, -v8, v4, v0
	v_fmac_f32_e32 v4, v23, v18
	v_fma_f32 v0, -v8, v4, v0
	v_div_scale_f32 v8, s[0:1], v32, v32, 2.0
	v_rcp_f32_e32 v23, v8
	v_div_fmas_f32 v0, v0, v18, v4
	v_div_fixup_f32 v33, v0, v33, 2.0
	v_fma_f32 v0, -v8, v23, 1.0
	v_fmac_f32_e32 v23, v0, v23
	v_div_scale_f32 v0, vcc, 2.0, v32, 2.0
	v_mul_f32_e32 v4, v0, v23
	v_fma_f32 v18, -v8, v4, v0
	v_fmac_f32_e32 v4, v18, v23
	v_fma_f32 v0, -v8, v4, v0
	v_div_fmas_f32 v0, v0, v23, v4
	v_div_fixup_f32 v32, v0, v32, 2.0
	v_mul_f32_e32 v0, 0x3d372713, v37
	v_mul_f32_e32 v0, v37, v0
	v_fma_f32 v0, v37, v0, v37
	v_mul_f32_e32 v0, 0x3f4c422a, v0
	v_add_f32_e32 v0, v0, v0
	v_mul_f32_e32 v0, 0x3fb8aa3b, v0
	v_exp_f32_e32 v27, v0
	v_pk_add_f32 v[32:33], v[32:33], 1.0 op_sel_hi:[1,0] neg_lo:[1,0] neg_hi:[1,0]
	v_mov_b32_e32 v4, v1
	v_pk_add_f32 v[32:33], v[32:33], 1.0 op_sel_hi:[1,0]
	v_pk_add_f32 v[26:27], v[26:27], 1.0 op_sel_hi:[1,0]
	v_pk_mul_f32 v[28:29], v[28:29], v[32:33]
	v_div_scale_f32 v8, s[0:1], v27, v27, 2.0
	v_rcp_f32_e32 v18, v8
	v_pk_mul_f32 v[0:1], v[28:29], v[4:5]
	v_fma_f32 v4, -v8, v18, 1.0
	v_fmac_f32_e32 v18, v4, v18
	v_div_scale_f32 v4, vcc, 2.0, v27, 2.0
	v_mul_f32_e32 v5, v4, v18
	v_pk_fma_f32 v[0:1], v[16:17], v[30:31], v[0:1]
	v_fma_f32 v16, -v8, v5, v4
	v_fmac_f32_e32 v5, v16, v18
	v_fma_f32 v4, -v8, v5, v4
	v_div_scale_f32 v8, s[0:1], v26, v26, 2.0
	v_rcp_f32_e32 v16, v8
	v_div_fmas_f32 v4, v4, v18, v5
	v_div_fixup_f32 v5, v4, v27, 2.0
	v_fma_f32 v4, -v8, v16, 1.0
	v_fmac_f32_e32 v16, v4, v16
	v_div_scale_f32 v4, vcc, 2.0, v26, 2.0
	v_mul_f32_e32 v17, v4, v16
	v_fma_f32 v18, -v8, v17, v4
	v_fmac_f32_e32 v17, v18, v16
	v_fma_f32 v4, -v8, v17, v4
	v_mul_f32_e32 v8, 0x3d372713, v11
	v_mul_f32_e32 v8, v11, v8
	v_fma_f32 v8, v11, v8, v11
	v_mul_f32_e32 v8, 0x3f4c422a, v8
	v_add_f32_e32 v8, v8, v8
	v_mul_f32_e32 v8, 0x3fb8aa3b, v8
	v_div_fmas_f32 v4, v4, v16, v17
	v_exp_f32_e32 v25, v8
	v_div_fixup_f32 v4, v4, v26, 2.0
	v_pk_add_f32 v[4:5], v[4:5], 1.0 op_sel_hi:[1,0] neg_lo:[1,0] neg_hi:[1,0]
	v_pk_mul_f32 v[16:17], v[36:37], 0.5 op_sel_hi:[1,0]
	v_pk_add_f32 v[4:5], v[4:5], 1.0 op_sel_hi:[1,0]
	v_pk_mul_f32 v[10:11], v[10:11], 0.5 op_sel_hi:[1,0]
	v_pk_mul_f32 v[4:5], v[16:17], v[4:5]
	v_pk_add_f32 v[16:17], v[24:25], 1.0 op_sel_hi:[1,0]
	v_mov_b32_e32 v24, v2
	v_div_scale_f32 v8, s[0:1], v17, v17, 2.0
	v_rcp_f32_e32 v18, v8
	v_mov_b32_e32 v25, v6
	v_pk_fma_f32 v[0:1], v[4:5], v[24:25], v[0:1]
	v_div_scale_f32 v6, s[0:1], v16, v16, 2.0
	v_fma_f32 v2, -v8, v18, 1.0
	v_fmac_f32_e32 v18, v2, v18
	v_div_scale_f32 v2, vcc, 2.0, v17, 2.0
	v_mul_f32_e32 v4, v2, v18
	v_fma_f32 v5, -v8, v4, v2
	v_fmac_f32_e32 v4, v5, v18
	v_fma_f32 v2, -v8, v4, v2
	v_rcp_f32_e32 v8, v6
	v_div_fmas_f32 v2, v2, v18, v4
	v_div_fixup_f32 v5, v2, v17, 2.0
	s_mov_b32 s0, 0x200000
	v_fma_f32 v2, -v6, v8, 1.0
	v_fmac_f32_e32 v8, v2, v8
	v_div_scale_f32 v2, vcc, 2.0, v16, 2.0
	v_mul_f32_e32 v4, v2, v8
	v_fma_f32 v17, -v6, v4, v2
	v_fmac_f32_e32 v4, v17, v8
	v_fma_f32 v2, -v6, v4, v2
	v_div_fmas_f32 v2, v2, v8, v4
	v_div_fixup_f32 v4, v2, v16, 2.0
	v_pk_add_f32 v[4:5], v[4:5], 1.0 op_sel_hi:[1,0] neg_lo:[1,0] neg_hi:[1,0]
	v_mov_b32_e32 v6, v3
	v_pk_add_f32 v[4:5], v[4:5], 1.0 op_sel_hi:[1,0]
	v_add_co_u32_e32 v2, vcc, s0, v12
	v_pk_mul_f32 v[4:5], v[10:11], v[4:5]
	s_lshl_b32 s0, s3, 3
	v_pk_fma_f32 v[0:1], v[4:5], v[6:7], v[0:1]
	v_addc_co_u32_e32 v3, vcc, 0, v13, vcc
	v_pk_add_f32 v[0:1], v[14:15], v[0:1]
	s_addk_i32 s0, 0x100
	global_store_dwordx2 v[2:3], v[0:1], off
	v_add_u32_e32 v8, s0, v21
	v_lshlrev_b32_e32 v3, 1, v22
	v_cvt_pk_f16_f32 v2, v0, v1
	v_lshlrev_b64 v[0:1], 6, v[8:9]
	v_and_b32_e32 v3, 48, v3
	v_or3_b32 v0, v0, v3, v19
	v_and_b32_e32 v3, 6, v20
	v_lshl_add_u64 v[0:1], v[0:1], 4, s[8:9]
	v_lshlrev_b32_e32 v8, 1, v3
	v_lshl_add_u64 v[0:1], v[0:1], 0, v[8:9]
	global_store_dword v[0:1], v2, off
	s_endpgm
	s_nop 0
	s_nop 0
	s_nop 0
	s_nop 0
	s_nop 0
	s_nop 0
	s_nop 0
	s_nop 0
	s_nop 0
	s_nop 0
	s_nop 0
	s_nop 0
	s_nop 0
	s_nop 0
	s_nop 0
	s_nop 0
	s_nop 0
	s_nop 0
	s_nop 0
	s_nop 0
	s_nop 0
	s_nop 0
	s_nop 0
	s_nop 0
	s_nop 0
	s_nop 0
	s_nop 0
	s_endpgm

	.amdhsa_kernel _ZN12_GLOBAL__N_110gemm_fullkILi1ELi1EEEvPKDF16_S2_PKfPDF16_PfS6_S4_S4_S4_S4_S4_S5_
		.amdhsa_group_segment_fixed_size 0
		.amdhsa_private_segment_fixed_size 0
		.amdhsa_kernarg_size 96
		.amdhsa_user_sgpr_count 2
		.amdhsa_user_sgpr_dispatch_ptr 0
		.amdhsa_user_sgpr_queue_ptr 0
		.amdhsa_user_sgpr_kernarg_segment_ptr 1
		.amdhsa_user_sgpr_dispatch_id 0
		.amdhsa_user_sgpr_kernarg_preload_length 0
		.amdhsa_user_sgpr_kernarg_preload_offset 0
		.amdhsa_user_sgpr_private_segment_size 0
		.amdhsa_uses_dynamic_stack 0
		.amdhsa_enable_private_segment 0
		.amdhsa_system_sgpr_workgroup_id_x 1
		.amdhsa_system_sgpr_workgroup_id_y 0
		.amdhsa_system_sgpr_workgroup_id_z 0
		.amdhsa_system_sgpr_workgroup_info 0
		.amdhsa_system_vgpr_workitem_id 0
		.amdhsa_next_free_vgpr 177
		.amdhsa_next_free_sgpr 18
		.amdhsa_accum_offset 180
		.amdhsa_reserve_vcc 1
		.amdhsa_float_round_mode_32 0
		.amdhsa_float_round_mode_16_64 0
		.amdhsa_float_denorm_mode_32 3
		.amdhsa_float_denorm_mode_16_64 3
		.amdhsa_dx10_clamp 1
		.amdhsa_ieee_mode 1
		.amdhsa_fp16_overflow 0
		.amdhsa_tg_split 0
		.amdhsa_exception_fp_ieee_invalid_op 0
		.amdhsa_exception_fp_denorm_src 0
		.amdhsa_exception_fp_ieee_div_zero 0
		.amdhsa_exception_fp_ieee_overflow 0
		.amdhsa_exception_fp_ieee_underflow 0
		.amdhsa_exception_fp_ieee_inexact 0
		.amdhsa_exception_int_div_zero 0
	.end_amdhsa_kernel

_ZN12_GLOBAL__N_110gemm_fullkILi0ELi2EEEvPKDF16_S2_PKfPDF16_PfS6_S4_S4_S4_S4_S4_S5_:
	s_load_dwordx8 s[4:11], s[0:1], 0x0
	s_lshr_b32 s0, s2, 5
	v_lshrrev_b32_e32 v230, 6, v0
	s_and_b32 s12, s0, 0x7fffffc
	s_and_b32 s2, s2, 0x7f
	s_mov_b32 s13, 0
	v_mul_u32_u24_e32 v4, 12, v230
	v_mov_b32_e32 v3, 0
	s_lshl_b64 s[0:1], s[12:13], 10
	s_mul_i32 s13, s2, 0xc0
	v_and_b32_e32 v1, 63, v0
	v_mul_u32_u24_e32 v2, 0x18000, v230
	v_add_lshl_u32 v4, s13, v4, 10
	v_mov_b32_e32 v5, v3
	s_waitcnt lgkmcnt(0)
	v_lshl_add_u64 v[4:5], s[6:7], 0, v[4:5]
	v_lshl_add_u64 v[6:7], s[4:5], 0, v[2:3]
	v_lshlrev_b32_e32 v2, 4, v1
	s_mov_b32 s3, 0x18000
	v_lshl_add_u64 v[208:209], v[4:5], 0, v[2:3]
	v_add_co_u32_e32 v80, vcc, s3, v208
	v_lshl_add_u64 v[6:7], v[6:7], 0, s[0:1]
	s_nop 0
	v_addc_co_u32_e32 v81, vcc, 0, v209, vcc
	s_mov_b32 s0, 0x19000
	v_add_co_u32_e32 v176, vcc, s0, v208
	v_lshl_add_u64 v[212:213], v[6:7], 0, v[2:3]
	s_nop 0
	v_addc_co_u32_e32 v177, vcc, 0, v209, vcc
	s_movk_i32 s0, 0x2000
	v_add_co_u32_e32 v52, vcc, s0, v212
	s_movk_i32 s1, 0x4000
	s_nop 0
	v_addc_co_u32_e32 v53, vcc, 0, v213, vcc
	v_add_co_u32_e32 v82, vcc, s1, v212
	s_movk_i32 s1, 0x6000
	s_nop 0
	v_addc_co_u32_e32 v83, vcc, 0, v213, vcc
	v_add_co_u32_e32 v96, vcc, s1, v212
	s_movk_i32 s1, 0x1000
	s_nop 0
	v_addc_co_u32_e32 v97, vcc, 0, v213, vcc
	v_add_co_u32_e32 v168, vcc, s1, v208
	global_load_dwordx4 v[4:7], v[212:213], off
	global_load_dwordx4 v[8:11], v[212:213], off offset:1024
	global_load_dwordx4 v[12:15], v[212:213], off offset:2048
	global_load_dwordx4 v[16:19], v[212:213], off offset:3072
	global_load_dwordx4 v[20:23], v[208:209], off
	global_load_dwordx4 v[24:27], v[208:209], off offset:1024
	v_addc_co_u32_e32 v169, vcc, 0, v209, vcc
	v_add_co_u32_e32 v210, vcc, s0, v208
	s_mov_b32 s0, 0x8000
	s_nop 0
	v_addc_co_u32_e32 v211, vcc, 0, v209, vcc
	v_add_co_u32_e32 v116, vcc, s0, v212
	s_mov_b32 s0, 0xa000
	s_nop 0
	v_addc_co_u32_e32 v117, vcc, 0, v213, vcc
	v_add_co_u32_e32 v132, vcc, s0, v212
	s_mov_b32 s0, 0xc000
	s_nop 0
	v_addc_co_u32_e32 v133, vcc, 0, v213, vcc
	v_add_co_u32_e32 v164, vcc, s0, v212
	global_load_dwordx4 v[28:31], v[52:53], off
	global_load_dwordx4 v[32:35], v[52:53], off offset:1024
	global_load_dwordx4 v[36:39], v[52:53], off offset:2048
	global_load_dwordx4 v[40:43], v[52:53], off offset:3072
	global_load_dwordx4 v[44:47], v[80:81], off offset:1024
	global_load_dwordx4 v[48:51], v[80:81], off offset:2048
	s_nop 0
	global_load_dwordx4 v[52:55], v[82:83], off
	global_load_dwordx4 v[56:59], v[82:83], off offset:1024
	global_load_dwordx4 v[60:63], v[82:83], off offset:2048
	global_load_dwordx4 v[64:67], v[82:83], off offset:3072
	global_load_dwordx4 v[68:71], v[208:209], off offset:2048
	global_load_dwordx4 v[72:75], v[208:209], off offset:3072
	global_load_dwordx4 v[76:79], v[80:81], off offset:3072
	s_nop 0
	global_load_dwordx4 v[80:83], v[96:97], off
	global_load_dwordx4 v[84:87], v[96:97], off offset:1024
	global_load_dwordx4 v[88:91], v[96:97], off offset:2048
	global_load_dwordx4 v[92:95], v[96:97], off offset:3072
	s_nop 0
	global_load_dwordx4 v[96:99], v[176:177], off offset:-4096
	global_load_dwordx4 v[100:103], v[176:177], off
	global_load_dwordx4 v[104:107], v[116:117], off
	global_load_dwordx4 v[108:111], v[116:117], off offset:1024
	global_load_dwordx4 v[112:115], v[116:117], off offset:2048
	s_nop 0
	global_load_dwordx4 v[116:119], v[116:117], off offset:3072
	s_nop 0
	global_load_dwordx4 v[120:123], v[132:133], off
	global_load_dwordx4 v[124:127], v[132:133], off offset:1024
	global_load_dwordx4 v[128:131], v[132:133], off offset:2048
	s_nop 0
	global_load_dwordx4 v[132:135], v[132:133], off offset:3072
	s_nop 0
	global_load_dwordx4 v[136:139], v[168:169], off offset:1024
	global_load_dwordx4 v[140:143], v[168:169], off offset:2048
	global_load_dwordx4 v[144:147], v[176:177], off offset:1024
	global_load_dwordx4 v[148:151], v[176:177], off offset:2048
	v_addc_co_u32_e32 v165, vcc, 0, v213, vcc
	global_load_dwordx4 v[152:155], v[164:165], off
	global_load_dwordx4 v[156:159], v[164:165], off offset:1024
	global_load_dwordx4 v[160:163], v[164:165], off offset:2048
	s_nop 0
	global_load_dwordx4 v[164:167], v[164:165], off offset:3072
	s_nop 0
	global_load_dwordx4 v[168:171], v[168:169], off offset:3072
	s_nop 0
	global_load_dwordx4 v[172:175], v[210:211], off offset:-4096
	s_nop 0
	global_load_dwordx4 v[176:179], v[176:177], off offset:3072
	s_mov_b32 s0, 0xe000
	v_add_co_u32_e32 v192, vcc, s0, v212
	s_lshl_b32 s0, s2, 7
	s_nop 0
	v_addc_co_u32_e32 v193, vcc, 0, v213, vcc
	global_load_dwordx4 v[180:183], v[192:193], off
	global_load_dwordx4 v[184:187], v[192:193], off offset:1024
	global_load_dwordx4 v[188:191], v[192:193], off offset:2048
	s_nop 0
	global_load_dwordx4 v[192:195], v[192:193], off offset:3072
	v_bfe_u32 v1, v0, 6, 1
	s_add_u32 s0, s8, s0
	s_addc_u32 s1, s9, 0
	v_lshlrev_b32_e32 v196, 6, v1
	v_mov_b32_e32 v197, v3
	v_lshl_add_u64 v[196:197], s[0:1], 0, v[196:197]
	v_and_b32_e32 v198, 48, v0
	v_mov_b32_e32 v199, v3
	v_lshl_add_u64 v[228:229], v[196:197], 0, v[198:199]
	s_waitcnt vmcnt(43)
	v_mfma_f32_16x16x32_f16 v[196:199], v[20:23], v[4:7], 0
	s_waitcnt vmcnt(24)
	v_mfma_f32_16x16x32_f16 v[4:7], v[96:99], v[4:7], 0
	v_mfma_f32_16x16x32_f16 v[200:203], v[20:23], v[8:11], 0
	v_mfma_f32_16x16x32_f16 v[8:11], v[96:99], v[8:11], 0
	v_mfma_f32_16x16x32_f16 v[204:207], v[20:23], v[12:15], 0
	v_mfma_f32_16x16x32_f16 v[12:15], v[96:99], v[12:15], 0
	v_mfma_f32_16x16x32_f16 v[20:23], v[20:23], v[16:19], 0
	v_mfma_f32_16x16x32_f16 v[16:19], v[96:99], v[16:19], 0
	v_mfma_f32_16x16x32_f16 v[96:99], v[24:27], v[28:31], v[196:199]
	v_mfma_f32_16x16x32_f16 v[4:7], v[44:47], v[28:31], v[4:7]
	v_mfma_f32_16x16x32_f16 v[28:31], v[24:27], v[32:35], v[200:203]
	v_mfma_f32_16x16x32_f16 v[8:11], v[44:47], v[32:35], v[8:11]
	v_mfma_f32_16x16x32_f16 v[32:35], v[24:27], v[36:39], v[204:207]
	v_mfma_f32_16x16x32_f16 v[12:15], v[44:47], v[36:39], v[12:15]
	v_mfma_f32_16x16x32_f16 v[20:23], v[24:27], v[40:43], v[20:23]
	v_mfma_f32_16x16x32_f16 v[16:19], v[44:47], v[40:43], v[16:19]
	v_mfma_f32_16x16x32_f16 v[24:27], v[68:71], v[52:55], v[96:99]
	v_mfma_f32_16x16x32_f16 v[4:7], v[48:51], v[52:55], v[4:7]
	v_mfma_f32_16x16x32_f16 v[28:31], v[68:71], v[56:59], v[28:31]
	v_mfma_f32_16x16x32_f16 v[8:11], v[48:51], v[56:59], v[8:11]
	v_mfma_f32_16x16x32_f16 v[32:35], v[68:71], v[60:63], v[32:35]
	v_mfma_f32_16x16x32_f16 v[12:15], v[48:51], v[60:63], v[12:15]
	v_mfma_f32_16x16x32_f16 v[20:23], v[68:71], v[64:67], v[20:23]
	v_mfma_f32_16x16x32_f16 v[16:19], v[48:51], v[64:67], v[16:19]
	v_mfma_f32_16x16x32_f16 v[24:27], v[72:75], v[80:83], v[24:27]
	v_mfma_f32_16x16x32_f16 v[4:7], v[76:79], v[80:83], v[4:7]
	v_mfma_f32_16x16x32_f16 v[28:31], v[72:75], v[84:87], v[28:31]
	v_mfma_f32_16x16x32_f16 v[8:11], v[76:79], v[84:87], v[8:11]
	v_mfma_f32_16x16x32_f16 v[32:35], v[72:75], v[88:91], v[32:35]
	v_mfma_f32_16x16x32_f16 v[12:15], v[76:79], v[88:91], v[12:15]
	v_mfma_f32_16x16x32_f16 v[20:23], v[72:75], v[92:95], v[20:23]
	v_mfma_f32_16x16x32_f16 v[16:19], v[76:79], v[92:95], v[16:19]
	s_mov_b32 s0, 0x1a000
	v_add_co_u32_e32 v208, vcc, s0, v208
	s_mov_b32 s0, 0x10000
	s_nop 0
	v_addc_co_u32_e32 v209, vcc, 0, v209, vcc
	v_add_co_u32_e32 v48, vcc, s0, v212
	s_mov_b32 s0, 0x12000
	s_nop 0
	v_addc_co_u32_e32 v49, vcc, 0, v213, vcc
	v_add_co_u32_e32 v80, vcc, s0, v212
	s_mov_b32 s0, 0x14000
	s_nop 0
	v_addc_co_u32_e32 v81, vcc, 0, v213, vcc
	v_add_co_u32_e32 v96, vcc, s0, v212
	global_load_dwordx4 v[36:39], v[48:49], off
	global_load_dwordx4 v[40:43], v[48:49], off offset:1024
	global_load_dwordx4 v[44:47], v[48:49], off offset:2048
	s_nop 0
	global_load_dwordx4 v[48:51], v[48:49], off offset:3072
	s_nop 0
	global_load_dwordx4 v[52:55], v[210:211], off
	global_load_dwordx4 v[56:59], v[210:211], off offset:1024
	global_load_dwordx4 v[60:63], v[208:209], off
	global_load_dwordx4 v[64:67], v[208:209], off offset:1024
	v_addc_co_u32_e32 v97, vcc, 0, v213, vcc
	global_load_dwordx4 v[68:71], v[80:81], off
	global_load_dwordx4 v[72:75], v[80:81], off offset:1024
	global_load_dwordx4 v[76:79], v[80:81], off offset:2048
	s_nop 0
	global_load_dwordx4 v[80:83], v[80:81], off offset:3072
	s_nop 0
	global_load_dwordx4 v[84:87], v[96:97], off
	global_load_dwordx4 v[88:91], v[96:97], off offset:1024
	global_load_dwordx4 v[92:95], v[96:97], off offset:2048
	s_nop 0
	global_load_dwordx4 v[96:99], v[96:97], off offset:3072
	s_nop 0
	global_load_dwordx4 v[196:199], v[210:211], off offset:2048
	global_load_dwordx4 v[200:203], v[210:211], off offset:3072
	global_load_dwordx4 v[204:207], v[208:209], off offset:2048
	s_nop 0
	global_load_dwordx4 v[208:211], v[208:209], off offset:3072
	s_mov_b32 s0, 0x16000
	v_add_co_u32_e32 v224, vcc, s0, v212
	s_nop 1
	v_addc_co_u32_e32 v225, vcc, 0, v213, vcc
	global_load_dwordx4 v[212:215], v[224:225], off
	global_load_dwordx4 v[216:219], v[224:225], off offset:1024
	global_load_dwordx4 v[220:223], v[224:225], off offset:2048
	s_nop 0
	global_load_dwordx4 v[224:227], v[224:225], off offset:3072
	s_waitcnt vmcnt(29)
	v_mfma_f32_16x16x32_f16 v[24:27], v[172:175], v[104:107], v[24:27]
	v_mfma_f32_16x16x32_f16 v[4:7], v[100:103], v[104:107], v[4:7]
	v_mfma_f32_16x16x32_f16 v[28:31], v[172:175], v[108:111], v[28:31]
	v_mfma_f32_16x16x32_f16 v[8:11], v[100:103], v[108:111], v[8:11]
	v_mfma_f32_16x16x32_f16 v[32:35], v[172:175], v[112:115], v[32:35]
	v_mfma_f32_16x16x32_f16 v[12:15], v[100:103], v[112:115], v[12:15]
	v_mfma_f32_16x16x32_f16 v[20:23], v[172:175], v[116:119], v[20:23]
	v_mfma_f32_16x16x32_f16 v[16:19], v[100:103], v[116:119], v[16:19]
	v_mfma_f32_16x16x32_f16 v[24:27], v[136:139], v[120:123], v[24:27]
	v_mfma_f32_16x16x32_f16 v[4:7], v[144:147], v[120:123], v[4:7]
	v_mfma_f32_16x16x32_f16 v[28:31], v[136:139], v[124:127], v[28:31]
	v_mfma_f32_16x16x32_f16 v[8:11], v[144:147], v[124:127], v[8:11]
	v_mfma_f32_16x16x32_f16 v[32:35], v[136:139], v[128:131], v[32:35]
	v_mfma_f32_16x16x32_f16 v[12:15], v[144:147], v[128:131], v[12:15]
	v_mfma_f32_16x16x32_f16 v[20:23], v[136:139], v[132:135], v[20:23]
	v_mfma_f32_16x16x32_f16 v[16:19], v[144:147], v[132:135], v[16:19]
	v_mfma_f32_16x16x32_f16 v[24:27], v[140:143], v[152:155], v[24:27]
	v_mfma_f32_16x16x32_f16 v[4:7], v[148:151], v[152:155], v[4:7]
	v_mfma_f32_16x16x32_f16 v[28:31], v[140:143], v[156:159], v[28:31]
	v_mfma_f32_16x16x32_f16 v[8:11], v[148:151], v[156:159], v[8:11]
	v_mfma_f32_16x16x32_f16 v[32:35], v[140:143], v[160:163], v[32:35]
	v_mfma_f32_16x16x32_f16 v[12:15], v[148:151], v[160:163], v[12:15]
	v_mfma_f32_16x16x32_f16 v[20:23], v[140:143], v[164:167], v[20:23]
	v_mfma_f32_16x16x32_f16 v[16:19], v[148:151], v[164:167], v[16:19]
	s_waitcnt vmcnt(27)
	v_mfma_f32_16x16x32_f16 v[24:27], v[168:171], v[180:183], v[24:27]
	v_mfma_f32_16x16x32_f16 v[4:7], v[176:179], v[180:183], v[4:7]
	s_waitcnt vmcnt(26)
	v_mfma_f32_16x16x32_f16 v[28:31], v[168:171], v[184:187], v[28:31]
	v_mfma_f32_16x16x32_f16 v[8:11], v[176:179], v[184:187], v[8:11]
	s_waitcnt vmcnt(25)
	v_mfma_f32_16x16x32_f16 v[32:35], v[168:171], v[188:191], v[32:35]
	v_mfma_f32_16x16x32_f16 v[12:15], v[176:179], v[188:191], v[12:15]
	s_waitcnt vmcnt(24)
	v_mfma_f32_16x16x32_f16 v[20:23], v[168:171], v[192:195], v[20:23]
	v_mfma_f32_16x16x32_f16 v[16:19], v[176:179], v[192:195], v[16:19]
	s_waitcnt vmcnt(19)
	v_mfma_f32_16x16x32_f16 v[24:27], v[52:55], v[36:39], v[24:27]
	s_waitcnt vmcnt(17)
	v_mfma_f32_16x16x32_f16 v[4:7], v[60:63], v[36:39], v[4:7]
	v_mfma_f32_16x16x32_f16 v[28:31], v[52:55], v[40:43], v[28:31]
	v_mfma_f32_16x16x32_f16 v[8:11], v[60:63], v[40:43], v[8:11]
	v_mfma_f32_16x16x32_f16 v[32:35], v[52:55], v[44:47], v[32:35]
	v_mfma_f32_16x16x32_f16 v[12:15], v[60:63], v[44:47], v[12:15]
	v_mfma_f32_16x16x32_f16 v[20:23], v[52:55], v[48:51], v[20:23]
	v_mfma_f32_16x16x32_f16 v[16:19], v[60:63], v[48:51], v[16:19]
	s_waitcnt vmcnt(15)
	v_mfma_f32_16x16x32_f16 v[24:27], v[56:59], v[68:71], v[24:27]
	v_mfma_f32_16x16x32_f16 v[4:7], v[64:67], v[68:71], v[4:7]
	s_waitcnt vmcnt(14)
	v_mfma_f32_16x16x32_f16 v[28:31], v[56:59], v[72:75], v[28:31]
	v_mfma_f32_16x16x32_f16 v[8:11], v[64:67], v[72:75], v[8:11]
	s_waitcnt vmcnt(13)
	v_mfma_f32_16x16x32_f16 v[32:35], v[56:59], v[76:79], v[32:35]
	v_mfma_f32_16x16x32_f16 v[12:15], v[64:67], v[76:79], v[12:15]
	s_waitcnt vmcnt(12)
	v_mfma_f32_16x16x32_f16 v[20:23], v[56:59], v[80:83], v[20:23]
	v_mfma_f32_16x16x32_f16 v[16:19], v[64:67], v[80:83], v[16:19]
	s_waitcnt vmcnt(7)
	v_mfma_f32_16x16x32_f16 v[24:27], v[196:199], v[84:87], v[24:27]
	s_waitcnt vmcnt(5)
	v_mfma_f32_16x16x32_f16 v[4:7], v[204:207], v[84:87], v[4:7]
	v_mfma_f32_16x16x32_f16 v[28:31], v[196:199], v[88:91], v[28:31]
	v_mfma_f32_16x16x32_f16 v[8:11], v[204:207], v[88:91], v[8:11]
	v_mfma_f32_16x16x32_f16 v[32:35], v[196:199], v[92:95], v[32:35]
	v_mfma_f32_16x16x32_f16 v[12:15], v[204:207], v[92:95], v[12:15]
	v_mfma_f32_16x16x32_f16 v[20:23], v[196:199], v[96:99], v[20:23]
	v_mfma_f32_16x16x32_f16 v[16:19], v[204:207], v[96:99], v[16:19]
	s_waitcnt vmcnt(3)
	v_mfma_f32_16x16x32_f16 v[24:27], v[200:203], v[212:215], v[24:27]
	v_mfma_f32_16x16x32_f16 v[4:7], v[208:211], v[212:215], v[4:7]
	s_waitcnt vmcnt(2)
	v_mfma_f32_16x16x32_f16 v[28:31], v[200:203], v[216:219], v[28:31]
	v_mfma_f32_16x16x32_f16 v[8:11], v[208:211], v[216:219], v[8:11]
	s_waitcnt vmcnt(1)
	v_mfma_f32_16x16x32_f16 v[32:35], v[200:203], v[220:223], v[32:35]
	v_mfma_f32_16x16x32_f16 v[12:15], v[208:211], v[220:223], v[12:15]
	s_waitcnt vmcnt(0)
	v_mfma_f32_16x16x32_f16 v[20:23], v[200:203], v[224:227], v[20:23]
	v_mfma_f32_16x16x32_f16 v[16:19], v[208:211], v[224:227], v[16:19]
	global_load_dwordx4 v[36:39], v[228:229], off
	v_add_u32_e32 v2, 0, v2
	v_and_b32_e32 v41, 0x1c0, v0
	v_lshl_add_u32 v43, v230, 13, v2
	v_lshl_add_u32 v2, v41, 4, v2
	v_lshl_add_u32 v40, v0, 4, 0
	ds_write_b128 v43, v[24:27]
	ds_write_b128 v43, v[4:7] offset:1024
	ds_write_b128 v43, v[28:31] offset:2048
	ds_write_b128 v43, v[8:11] offset:3072
	ds_write_b128 v43, v[32:35] offset:4096
	ds_write_b128 v43, v[12:15] offset:5120
	ds_write_b128 v43, v[20:23] offset:6144
	ds_write_b128 v43, v[16:19] offset:7168
	s_waitcnt lgkmcnt(0)
	s_barrier
	ds_read_b128 v[4:7], v2 offset:8192
	ds_read_b128 v[8:11], v2 offset:16384
	ds_read_b128 v[12:15], v2 offset:24576
	ds_read_b128 v[16:19], v40
	ds_read_b128 v[20:23], v2 offset:32768
	ds_read_b128 v[24:27], v2 offset:40960
	ds_read_b128 v[28:31], v2 offset:49152
	ds_read_b128 v[32:35], v2 offset:57344
	s_waitcnt lgkmcnt(4)
	v_pk_add_f32 v[4:5], v[16:17], v[4:5]
	v_pk_add_f32 v[6:7], v[18:19], v[6:7]
	v_pk_add_f32 v[4:5], v[4:5], v[8:9]
	v_pk_add_f32 v[6:7], v[6:7], v[10:11]
	v_pk_add_f32 v[4:5], v[4:5], v[12:13]
	v_pk_add_f32 v[6:7], v[6:7], v[14:15]
	s_waitcnt lgkmcnt(3)
	v_pk_add_f32 v[4:5], v[4:5], v[20:21]
	v_pk_add_f32 v[6:7], v[6:7], v[22:23]
	s_waitcnt lgkmcnt(2)
	v_pk_add_f32 v[4:5], v[4:5], v[24:25]
	v_pk_add_f32 v[6:7], v[6:7], v[26:27]
	s_waitcnt lgkmcnt(1)
	v_pk_add_f32 v[4:5], v[4:5], v[28:29]
	v_pk_add_f32 v[6:7], v[6:7], v[30:31]
	s_waitcnt lgkmcnt(0)
	v_pk_add_f32 v[4:5], v[4:5], v[32:33]
	v_pk_add_f32 v[6:7], v[6:7], v[34:35]
	v_lshrrev_b32_e32 v42, 7, v0
	s_waitcnt vmcnt(0)
	v_pk_add_f32 v[4:5], v[36:37], v[4:5]
	v_pk_add_f32 v[6:7], v[38:39], v[6:7]
	v_mul_f32_e32 v2, 0x3d372713, v4
	v_mul_f32_e32 v8, 0x3d372713, v5
	v_mul_f32_e32 v9, 0x3d372713, v6
	v_mul_f32_e32 v2, v4, v2
	v_mul_f32_e32 v8, v5, v8
	v_mul_f32_e32 v9, v6, v9
	v_fma_f32 v2, v4, v2, v4
	v_fma_f32 v8, v5, v8, v5
	v_fma_f32 v9, v6, v9, v6
	v_mul_f32_e32 v2, 0x3f4c422a, v2
	v_mul_f32_e32 v8, 0x3f4c422a, v8
	v_mul_f32_e32 v9, 0x3f4c422a, v9
	v_add_f32_e32 v2, v2, v2
	v_add_f32_e32 v8, v8, v8
	v_add_f32_e32 v9, v9, v9
	v_mul_f32_e32 v2, 0x3fb8aa3b, v2
	v_mul_f32_e32 v11, 0x3fb8aa3b, v8
	v_mul_f32_e32 v10, 0x3d372713, v7
	v_mul_f32_e32 v12, 0x3fb8aa3b, v9
	v_exp_f32_e32 v8, v2
	v_exp_f32_e32 v9, v11
	v_mul_f32_e32 v10, v7, v10
	v_fma_f32 v10, v7, v10, v7
	v_mul_f32_e32 v10, 0x3f4c422a, v10
	v_add_f32_e32 v10, v10, v10
	v_pk_add_f32 v[8:9], v[8:9], 1.0 op_sel_hi:[1,0]
	v_mul_f32_e32 v13, 0x3fb8aa3b, v10
	v_div_scale_f32 v2, s[0:1], v9, v9, 2.0
	v_exp_f32_e32 v10, v12
	v_exp_f32_e32 v11, v13
	v_div_scale_f32 v14, s[0:1], v8, v8, 2.0
	v_rcp_f32_e32 v16, v2
	v_rcp_f32_e32 v17, v14
	v_pk_add_f32 v[10:11], v[10:11], 1.0 op_sel_hi:[1,0]
	v_div_scale_f32 v13, vcc, 2.0, v9, 2.0
	v_fma_f32 v20, -v2, v16, 1.0
	v_div_scale_f32 v15, s[0:1], v11, v11, 2.0
	v_fma_f32 v21, -v14, v17, 1.0
	v_fmac_f32_e32 v16, v20, v16
	v_div_scale_f32 v19, s[0:1], 2.0, v8, 2.0
	v_fmac_f32_e32 v17, v21, v17
	v_mul_f32_e32 v20, v13, v16
	v_mul_f32_e32 v21, v19, v17
	v_fma_f32 v23, -v2, v20, v13
	v_fma_f32 v24, -v14, v21, v19
	v_fmac_f32_e32 v20, v23, v16
	v_fmac_f32_e32 v21, v24, v17
	v_fma_f32 v2, -v2, v20, v13
	v_rcp_f32_e32 v18, v15
	v_fma_f32 v13, -v14, v21, v19
	v_div_fmas_f32 v2, v2, v16, v20
	s_mov_b64 vcc, s[0:1]
	v_div_fixup_f32 v9, v2, v9, 2.0
	v_div_fmas_f32 v2, v13, v17, v21
	v_div_fixup_f32 v8, v2, v8, 2.0
	v_pk_add_f32 v[8:9], v[8:9], 1.0 op_sel_hi:[1,0] neg_lo:[1,0] neg_hi:[1,0]
	v_pk_mul_f32 v[4:5], v[4:5], 0.5 op_sel_hi:[1,0]
	v_fma_f32 v22, -v15, v18, 1.0
	v_pk_add_f32 v[8:9], v[8:9], 1.0 op_sel_hi:[1,0]
	v_fmac_f32_e32 v18, v22, v18
	v_pk_mul_f32 v[4:5], v[4:5], v[8:9]
	v_div_scale_f32 v2, vcc, 2.0, v11, 2.0
	v_cvt_pk_f16_f32 v4, v4, v5
	v_mul_f32_e32 v5, v2, v18
	v_fma_f32 v8, -v15, v5, v2
	v_fmac_f32_e32 v5, v8, v18
	v_div_scale_f32 v8, s[0:1], v10, v10, 2.0
	v_rcp_f32_e32 v13, v8
	v_fma_f32 v2, -v15, v5, v2
	v_div_fmas_f32 v2, v2, v18, v5
	v_div_fixup_f32 v9, v2, v11, 2.0
	v_fma_f32 v2, -v8, v13, 1.0
	v_fmac_f32_e32 v13, v2, v13
	v_div_scale_f32 v2, vcc, 2.0, v10, 2.0
	v_mul_f32_e32 v5, v2, v13
	v_fma_f32 v11, -v8, v5, v2
	v_fmac_f32_e32 v5, v11, v13
	v_fma_f32 v2, -v8, v5, v2
	v_div_fmas_f32 v2, v2, v13, v5
	v_div_fixup_f32 v8, v2, v10, 2.0
	v_pk_add_f32 v[8:9], v[8:9], 1.0 op_sel_hi:[1,0] neg_lo:[1,0] neg_hi:[1,0]
	s_lshl_b32 s0, s2, 3
	v_pk_mul_f32 v[6:7], v[6:7], 0.5 op_sel_hi:[1,0]
	v_pk_add_f32 v[8:9], v[8:9], 1.0 op_sel_hi:[1,0]
	s_add_i32 s0, s0, s12
	v_pk_mul_f32 v[6:7], v[6:7], v[8:9]
	v_or_b32_e32 v2, s0, v42
	v_cvt_pk_f16_f32 v5, v6, v7
	v_lshlrev_b64 v[6:7], 6, v[2:3]
	v_lshrrev_b32_e32 v2, 1, v0
	v_and_b32_e32 v12, 15, v0
	v_and_b32_e32 v0, 16, v2
	v_lshl_or_b32 v0, v1, 5, v0
	v_or3_b32 v6, v6, v0, v12
	v_lshl_add_u64 v[0:1], v[6:7], 4, s[10:11]
	v_and_b32_e32 v2, 8, v2
	v_lshl_add_u64 v[0:1], v[0:1], 0, v[2:3]
	global_store_dwordx2 v[0:1], v[4:5], off
	s_endpgm
	s_nop 0
	s_nop 0
	s_nop 0
	s_nop 0
	s_nop 0
	s_nop 0
	s_nop 0
	s_nop 0
	s_nop 0
	s_nop 0
	s_nop 0
	s_nop 0
	s_nop 0
	s_nop 0
	s_nop 0
	s_nop 0
	s_nop 0
	s_nop 0
	s_nop 0
	s_nop 0
	s_nop 0
	s_nop 0
	s_nop 0
	s_nop 0
	s_nop 0
	s_nop 0
	s_nop 0
	s_nop 0
	s_nop 0
	s_nop 0
	s_nop 0
	s_endpgm

	.amdhsa_kernel _ZN12_GLOBAL__N_110gemm_fullkILi0ELi2EEEvPKDF16_S2_PKfPDF16_PfS6_S4_S4_S4_S4_S4_S5_
		.amdhsa_group_segment_fixed_size 0
		.amdhsa_private_segment_fixed_size 0
		.amdhsa_kernarg_size 96
		.amdhsa_user_sgpr_count 2
		.amdhsa_user_sgpr_dispatch_ptr 0
		.amdhsa_user_sgpr_queue_ptr 0
		.amdhsa_user_sgpr_kernarg_segment_ptr 1
		.amdhsa_user_sgpr_dispatch_id 0
		.amdhsa_user_sgpr_kernarg_preload_length 0
		.amdhsa_user_sgpr_kernarg_preload_offset 0
		.amdhsa_user_sgpr_private_segment_size 0
		.amdhsa_uses_dynamic_stack 0
		.amdhsa_enable_private_segment 0
		.amdhsa_system_sgpr_workgroup_id_x 1
		.amdhsa_system_sgpr_workgroup_id_y 0
		.amdhsa_system_sgpr_workgroup_id_z 0
		.amdhsa_system_sgpr_workgroup_info 0
		.amdhsa_system_vgpr_workitem_id 0
		.amdhsa_next_free_vgpr 231
		.amdhsa_next_free_sgpr 14
		.amdhsa_accum_offset 232
		.amdhsa_reserve_vcc 1
		.amdhsa_float_round_mode_32 0
		.amdhsa_float_round_mode_16_64 0
		.amdhsa_float_denorm_mode_32 3
		.amdhsa_float_denorm_mode_16_64 3
		.amdhsa_dx10_clamp 1
		.amdhsa_ieee_mode 1
		.amdhsa_fp16_overflow 0
		.amdhsa_tg_split 0
		.amdhsa_exception_fp_ieee_invalid_op 0
		.amdhsa_exception_fp_denorm_src 0
		.amdhsa_exception_fp_ieee_div_zero 0
		.amdhsa_exception_fp_ieee_overflow 0
		.amdhsa_exception_fp_ieee_underflow 0
		.amdhsa_exception_fp_ieee_inexact 0
		.amdhsa_exception_int_div_zero 0
	.end_amdhsa_kernel

_ZN12_GLOBAL__N_110gemm_fullkILi1ELi2EEEvPKDF16_S2_PKfPDF16_PfS6_S4_S4_S4_S4_S4_S5_:
	s_load_dwordx2 s[4:5], s[0:1], 0x38
	s_and_b32 s3, s2, 63
	s_lshl_b32 s16, s3, 5
	s_lshl_b32 s6, s3, 13
	v_lshlrev_b32_e32 v1, 4, v0
	s_waitcnt lgkmcnt(0)
	s_add_u32 s4, s4, s6
	s_addc_u32 s5, s5, 0
	global_load_dwordx4 v[2:5], v1, s[4:5]
	v_lshlrev_b32_e32 v1, 2, v0
	v_cmp_lt_u32_e32 vcc, 31, v0
	s_and_saveexec_b64 s[4:5], vcc
	s_xor_b64 s[4:5], exec, s[4:5]
	s_cbranch_execz .LBB13_10
	v_cmp_lt_u32_e32 vcc, 63, v0
	s_and_saveexec_b64 s[6:7], vcc
	s_xor_b64 s[6:7], exec, s[6:7]
	s_cbranch_execz .LBB13_7
	s_movk_i32 s8, 0x47
	v_cmp_lt_u32_e32 vcc, s8, v0
	s_and_saveexec_b64 s[8:9], vcc
	s_xor_b64 s[8:9], exec, s[8:9]
	s_cbranch_execz .LBB13_4
	s_load_dwordx2 s[10:11], s[0:1], 0x10
	s_lshl_b32 s12, s16, 2
	v_lshlrev_b32_e32 v6, 2, v1
	v_mov_b32_e32 v7, 0
	s_movk_i32 s14, 0x50
	s_waitcnt lgkmcnt(0)
	s_add_u32 s10, s10, s12
	s_addc_u32 s11, s11, 0
	s_movk_i32 s12, 0xfb80
	v_lshl_add_u64 v[6:7], s[10:11], 0, v[6:7]
	s_mov_b32 s13, -1
	v_lshl_add_u64 v[6:7], v[6:7], 0, s[12:13]
	v_mov_b32_e32 v8, s11
	v_cmp_gt_u32_e32 vcc, s14, v0
	s_nop 1
	v_cndmask_b32_e32 v7, v8, v7, vcc
	v_mov_b32_e32 v8, s10
	v_cndmask_b32_e32 v6, v8, v6, vcc

.LBB13_10:
	s_or_saveexec_b64 s[14:15], s[4:5]
	s_load_dwordx2 s[12:13], s[0:1], 0x58
	s_load_dwordx4 s[8:11], s[0:1], 0x0
	s_load_dwordx4 s[4:7], s[0:1], 0x20
	s_xor_b64 exec, exec, s[14:15]
	s_cbranch_execz .LBB13_12
	s_load_dwordx2 s[0:1], s[0:1], 0x40
	s_lshl_b32 s17, s3, 9
	v_lshlrev_b32_e32 v6, 2, v1
	v_mov_b32_e32 v7, 0
	s_waitcnt lgkmcnt(0)
	s_add_u32 s0, s0, s17
	s_addc_u32 s1, s1, 0
	v_lshl_add_u64 v[6:7], s[0:1], 0, v[6:7]
.LBB13_12:
	s_or_b64 exec, exec, s[14:15]
	v_lshrrev_b32_e32 v176, 6, v0
	s_lshr_b32 s0, s2, 5
	s_and_b32 s0, s0, 0x7fffffe
	s_mov_b32 s1, 0
	v_lshlrev_b32_e32 v8, 17, v176
	v_mov_b32_e32 v9, 0
	v_and_b32_e32 v14, 63, v0
	s_lshl_b64 s[14:15], s[0:1], 10
	v_lshlrev_b32_e32 v10, 14, v176
	s_waitcnt lgkmcnt(0)
	v_lshl_add_u64 v[12:13], s[8:9], 0, v[8:9]
	v_lshl_or_b32 v10, s3, 18, v10
	v_mov_b32_e32 v11, v9
	v_lshl_add_u64 v[12:13], v[12:13], 0, s[14:15]
	v_lshlrev_b32_e32 v8, 4, v14
	v_lshl_add_u64 v[10:11], s[10:11], 0, v[10:11]
	v_lshl_add_u64 v[20:21], v[12:13], 0, v[8:9]
	v_lshrrev_b32_e32 v12, 2, v0
	v_lshl_add_u64 v[172:173], v[10:11], 0, v[8:9]
	v_lshrrev_b32_e32 v10, 8, v0
	v_lshrrev_b32_e32 v11, 3, v0
	v_and_b32_e32 v12, 12, v12
	v_and_b32_e32 v22, 15, v0
	v_bfe_u32 v26, v0, 6, 1
	v_or_b32_e32 v24, s0, v10
	v_and_or_b32 v25, v11, 16, v12
	v_lshl_or_b32 v10, v24, 4, v22
	v_lshl_or_b32 v23, v26, 1, v25
	v_mov_b32_e32 v11, v9
	v_or_b32_e32 v14, s16, v23
	v_lshlrev_b64 v[12:13], 13, v[10:11]
	v_lshl_add_u64 v[10:11], s[4:5], 0, v[12:13]
	v_lshlrev_b32_e32 v14, 2, v14
	v_mov_b32_e32 v15, v9
	v_lshl_add_u64 v[10:11], v[10:11], 0, v[14:15]
	s_mov_b32 s2, 0x200000
	v_add_co_u32_e32 v16, vcc, s2, v10
	v_lshl_add_u64 v[12:13], s[6:7], 0, v[12:13]
	s_nop 0
	v_addc_co_u32_e32 v17, vcc, 0, v11, vcc
	v_lshl_add_u64 v[18:19], v[12:13], 0, v[14:15]
	s_mov_b32 s0, 0x100000
	v_add_co_u32_e32 v28, vcc, s0, v18
	s_mov_b32 s0, 0x20000
	s_nop 0
	v_addc_co_u32_e32 v29, vcc, 0, v19, vcc
	v_add_co_u32_e32 v80, vcc, s0, v172
	s_mov_b32 s0, 0x21000
	s_nop 0
	v_addc_co_u32_e32 v81, vcc, 0, v173, vcc
	v_add_co_u32_e32 v144, vcc, s0, v172
	s_movk_i32 s0, 0x2000
	s_nop 0
	v_addc_co_u32_e32 v145, vcc, 0, v173, vcc
	v_add_co_u32_e32 v60, vcc, s0, v20
	s_movk_i32 s1, 0x4000
	s_nop 0
	v_addc_co_u32_e32 v61, vcc, 0, v21, vcc
	v_add_co_u32_e32 v82, vcc, s1, v20
	s_movk_i32 s1, 0x6000
	s_nop 0
	v_addc_co_u32_e32 v83, vcc, 0, v21, vcc
	v_add_co_u32_e32 v88, vcc, s1, v20
	s_movk_i32 s1, 0x1000
	s_nop 0
	v_addc_co_u32_e32 v89, vcc, 0, v21, vcc
	v_add_co_u32_e32 v136, vcc, s1, v172
	global_load_dwordx2 v[16:17], v[16:17], off
	s_nop 0
	v_addc_co_u32_e32 v137, vcc, 0, v173, vcc
	v_add_co_u32_e32 v160, vcc, s0, v172
	s_mov_b32 s0, 0x8000
	s_nop 0
	v_addc_co_u32_e32 v161, vcc, 0, v173, vcc
	v_add_co_u32_e32 v104, vcc, s0, v20
	s_mov_b32 s0, 0xa000
	s_nop 0
	v_addc_co_u32_e32 v105, vcc, 0, v21, vcc
	v_add_co_u32_e32 v116, vcc, s0, v20
	s_mov_b32 s0, 0xc000
	s_nop 0
	v_addc_co_u32_e32 v117, vcc, 0, v21, vcc
	global_load_dwordx2 v[12:13], v[18:19], off
	global_load_dwordx2 v[14:15], v[28:29], off
	s_nop 0
	global_load_dwordx4 v[28:31], v[20:21], off
	global_load_dwordx4 v[32:35], v[20:21], off offset:1024
	global_load_dwordx4 v[36:39], v[172:173], off
	global_load_dwordx4 v[40:43], v[172:173], off offset:1024
	global_load_dwordx4 v[44:47], v[60:61], off
	global_load_dwordx4 v[48:51], v[60:61], off offset:1024
	global_load_dwordx4 v[52:55], v[80:81], off offset:1024
	global_load_dwordx4 v[56:59], v[80:81], off offset:2048
	s_nop 0
	global_load_dwordx4 v[60:63], v[82:83], off
	global_load_dwordx4 v[64:67], v[82:83], off offset:1024
	global_load_dwordx4 v[68:71], v[172:173], off offset:2048
	global_load_dwordx4 v[72:75], v[172:173], off offset:3072
	global_load_dwordx4 v[76:79], v[80:81], off offset:3072
	s_nop 0
	global_load_dwordx4 v[80:83], v[88:89], off
	global_load_dwordx4 v[84:87], v[88:89], off offset:1024
	s_nop 0
	global_load_dwordx4 v[88:91], v[144:145], off offset:-4096
	global_load_dwordx4 v[92:95], v[144:145], off
	global_load_dwordx4 v[96:99], v[104:105], off
	global_load_dwordx4 v[100:103], v[104:105], off offset:1024
	s_nop 0
	global_load_dwordx4 v[104:107], v[116:117], off
	global_load_dwordx4 v[108:111], v[116:117], off offset:1024
	global_load_dwordx4 v[112:115], v[136:137], off offset:1024
	s_nop 0
	global_load_dwordx4 v[116:119], v[136:137], off offset:2048
	global_load_dwordx4 v[120:123], v[144:145], off offset:1024
	global_load_dwordx4 v[124:127], v[144:145], off offset:2048
	v_add_co_u32_e32 v132, vcc, s0, v20
	s_mov_b32 s0, 0xe000
	s_nop 0
	v_addc_co_u32_e32 v133, vcc, 0, v21, vcc
	global_load_dwordx4 v[128:131], v[132:133], off
	s_nop 0
	global_load_dwordx4 v[132:135], v[132:133], off offset:1024
	s_nop 0
	global_load_dwordx4 v[136:139], v[136:137], off offset:3072
	s_nop 0
	global_load_dwordx4 v[140:143], v[160:161], off offset:-4096
	s_nop 0
	global_load_dwordx4 v[144:147], v[144:145], off offset:3072
	v_add_co_u32_e32 v152, vcc, s0, v20
	v_lshrrev_b32_e32 v27, 7, v0
	s_nop 0
	v_addc_co_u32_e32 v153, vcc, 0, v21, vcc
	global_load_dwordx4 v[148:151], v[152:153], off
	s_nop 0
	global_load_dwordx4 v[152:155], v[152:153], off offset:1024
	s_waitcnt vmcnt(29)
	v_mfma_f32_16x16x32_f16 v[156:159], v[36:39], v[28:31], 0
	s_waitcnt vmcnt(16)
	v_mfma_f32_16x16x32_f16 v[28:31], v[88:91], v[28:31], 0
	v_mfma_f32_16x16x32_f16 v[36:39], v[36:39], v[32:35], 0
	v_mfma_f32_16x16x32_f16 v[32:35], v[88:91], v[32:35], 0
	v_mfma_f32_16x16x32_f16 v[88:91], v[40:43], v[44:47], v[156:159]
	v_mfma_f32_16x16x32_f16 v[28:31], v[52:55], v[44:47], v[28:31]
	v_mfma_f32_16x16x32_f16 v[36:39], v[40:43], v[48:51], v[36:39]
	v_mfma_f32_16x16x32_f16 v[32:35], v[52:55], v[48:51], v[32:35]
	v_mfma_f32_16x16x32_f16 v[40:43], v[68:71], v[60:63], v[88:91]
	v_mfma_f32_16x16x32_f16 v[28:31], v[56:59], v[60:63], v[28:31]
	v_mfma_f32_16x16x32_f16 v[36:39], v[68:71], v[64:67], v[36:39]
	v_mfma_f32_16x16x32_f16 v[32:35], v[56:59], v[64:67], v[32:35]
	v_mfma_f32_16x16x32_f16 v[40:43], v[72:75], v[80:83], v[40:43]
	v_mfma_f32_16x16x32_f16 v[28:31], v[76:79], v[80:83], v[28:31]
	v_mfma_f32_16x16x32_f16 v[36:39], v[72:75], v[84:87], v[36:39]
	v_mfma_f32_16x16x32_f16 v[32:35], v[76:79], v[84:87], v[32:35]
	s_mov_b32 s0, 0x22000
	v_add_co_u32_e32 v162, vcc, s0, v172
	s_mov_b32 s0, 0x23000
	s_nop 0
	v_addc_co_u32_e32 v163, vcc, 0, v173, vcc
	v_add_co_u32_e32 v174, vcc, s0, v172
	s_mov_b32 s0, 0x10000
	s_nop 0
	v_addc_co_u32_e32 v175, vcc, 0, v173, vcc
	v_add_co_u32_e32 v52, vcc, s0, v20
	s_mov_b32 s0, 0x12000
	s_nop 0
	v_addc_co_u32_e32 v53, vcc, 0, v21, vcc
	v_add_co_u32_e32 v68, vcc, s0, v20
	s_mov_b32 s0, 0x14000
	s_nop 0
	v_addc_co_u32_e32 v69, vcc, 0, v21, vcc
	v_add_co_u32_e32 v84, vcc, s0, v20
	global_load_dwordx4 v[44:47], v[174:175], off offset:-4096
	s_nop 0
	v_addc_co_u32_e32 v85, vcc, 0, v21, vcc
	global_load_dwordx4 v[48:51], v[52:53], off
	s_nop 0
	global_load_dwordx4 v[52:55], v[52:53], off offset:1024
	s_nop 0
	global_load_dwordx4 v[56:59], v[160:161], off
	global_load_dwordx4 v[60:63], v[160:161], off offset:1024
	global_load_dwordx4 v[64:67], v[68:69], off
	s_nop 0
	global_load_dwordx4 v[68:71], v[68:69], off offset:1024
	s_nop 0
	global_load_dwordx4 v[72:75], v[162:163], off offset:1024
	global_load_dwordx4 v[76:79], v[162:163], off offset:2048
	global_load_dwordx4 v[80:83], v[84:85], off
	s_nop 0
	global_load_dwordx4 v[84:87], v[84:85], off offset:1024
	s_nop 0
	global_load_dwordx4 v[88:91], v[160:161], off offset:2048
	global_load_dwordx4 v[156:159], v[160:161], off offset:3072
	s_nop 0
	global_load_dwordx4 v[160:163], v[162:163], off offset:3072
	s_mov_b32 s0, 0x16000
	v_add_co_u32_e32 v168, vcc, s0, v20
	s_nop 1
	v_addc_co_u32_e32 v169, vcc, 0, v21, vcc
	global_load_dwordx4 v[164:167], v[168:169], off
	s_nop 0
	global_load_dwordx4 v[168:171], v[168:169], off offset:1024
	s_waitcnt vmcnt(19)
	v_mfma_f32_16x16x32_f16 v[40:43], v[140:143], v[96:99], v[40:43]
	v_mfma_f32_16x16x32_f16 v[28:31], v[92:95], v[96:99], v[28:31]
	v_mfma_f32_16x16x32_f16 v[36:39], v[140:143], v[100:103], v[36:39]
	v_mfma_f32_16x16x32_f16 v[32:35], v[92:95], v[100:103], v[32:35]
	v_mfma_f32_16x16x32_f16 v[40:43], v[112:115], v[104:107], v[40:43]
	v_mfma_f32_16x16x32_f16 v[28:31], v[120:123], v[104:107], v[28:31]
	v_mfma_f32_16x16x32_f16 v[36:39], v[112:115], v[108:111], v[36:39]
	v_mfma_f32_16x16x32_f16 v[32:35], v[120:123], v[108:111], v[32:35]
	v_mfma_f32_16x16x32_f16 v[40:43], v[116:119], v[128:131], v[40:43]
	v_mfma_f32_16x16x32_f16 v[28:31], v[124:127], v[128:131], v[28:31]
	v_mfma_f32_16x16x32_f16 v[36:39], v[116:119], v[132:135], v[36:39]
	v_mfma_f32_16x16x32_f16 v[32:35], v[124:127], v[132:135], v[32:35]
	s_waitcnt vmcnt(17)
	v_mfma_f32_16x16x32_f16 v[40:43], v[136:139], v[148:151], v[40:43]
	v_mfma_f32_16x16x32_f16 v[28:31], v[144:147], v[148:151], v[28:31]
	s_waitcnt vmcnt(16)
	v_mfma_f32_16x16x32_f16 v[36:39], v[136:139], v[152:155], v[36:39]
	v_mfma_f32_16x16x32_f16 v[32:35], v[144:147], v[152:155], v[32:35]
	s_movk_i32 s0, 0x3000
	v_add_co_u32_e32 v136, vcc, s0, v172
	s_mov_b32 s0, 0x18000
	s_nop 0
	v_addc_co_u32_e32 v137, vcc, 0, v173, vcc
	v_add_co_u32_e32 v104, vcc, s0, v20
	s_mov_b32 s0, 0x1a000
	s_nop 0
	v_addc_co_u32_e32 v105, vcc, 0, v21, vcc
	v_add_co_u32_e32 v120, vcc, s0, v20
	s_mov_b32 s0, 0x1c000
	s_nop 0
	v_addc_co_u32_e32 v121, vcc, 0, v21, vcc
	v_add_co_u32_e32 v128, vcc, s0, v20
	global_load_dwordx4 v[92:95], v[104:105], off
	global_load_dwordx4 v[96:99], v[104:105], off offset:1024
	global_load_dwordx4 v[100:103], v[136:137], off
	s_nop 0
	global_load_dwordx4 v[104:107], v[136:137], off offset:1024
	global_load_dwordx4 v[108:111], v[174:175], off
	global_load_dwordx4 v[112:115], v[174:175], off offset:1024
	v_addc_co_u32_e32 v129, vcc, 0, v21, vcc
	global_load_dwordx4 v[116:119], v[120:121], off
	s_nop 0
	global_load_dwordx4 v[120:123], v[120:121], off offset:1024
	s_nop 0
	global_load_dwordx4 v[124:127], v[128:129], off
	s_nop 0
	global_load_dwordx4 v[128:131], v[128:129], off offset:1024
	s_nop 0
	global_load_dwordx4 v[132:135], v[136:137], off offset:2048
	s_nop 0
	global_load_dwordx4 v[136:139], v[136:137], off offset:3072
	s_nop 0
	global_load_dwordx4 v[140:143], v[174:175], off offset:2048
	global_load_dwordx4 v[144:147], v[174:175], off offset:3072
	s_mov_b32 s0, 0x1e000
	v_add_co_u32_e32 v20, vcc, s0, v20
	s_nop 1
	v_addc_co_u32_e32 v21, vcc, 0, v21, vcc
	global_load_dwordx4 v[148:151], v[20:21], off
	global_load_dwordx4 v[152:155], v[20:21], off offset:1024
	s_waitcnt vmcnt(28)
	v_mfma_f32_16x16x32_f16 v[40:43], v[56:59], v[48:51], v[40:43]
	v_mfma_f32_16x16x32_f16 v[28:31], v[44:47], v[48:51], v[28:31]
	v_mfma_f32_16x16x32_f16 v[36:39], v[56:59], v[52:55], v[36:39]
	v_mfma_f32_16x16x32_f16 v[32:35], v[44:47], v[52:55], v[32:35]
	s_waitcnt vmcnt(26)
	v_mfma_f32_16x16x32_f16 v[40:43], v[60:63], v[64:67], v[40:43]
	s_waitcnt vmcnt(24)
	v_mfma_f32_16x16x32_f16 v[28:31], v[72:75], v[64:67], v[28:31]
	v_mfma_f32_16x16x32_f16 v[36:39], v[60:63], v[68:71], v[36:39]
	v_mfma_f32_16x16x32_f16 v[32:35], v[72:75], v[68:71], v[32:35]
	s_waitcnt vmcnt(20)
	v_mfma_f32_16x16x32_f16 v[40:43], v[88:91], v[80:83], v[40:43]
	v_mfma_f32_16x16x32_f16 v[28:31], v[76:79], v[80:83], v[28:31]
	v_mfma_f32_16x16x32_f16 v[36:39], v[88:91], v[84:87], v[36:39]
	v_mfma_f32_16x16x32_f16 v[32:35], v[76:79], v[84:87], v[32:35]
	s_waitcnt vmcnt(17)
	v_mfma_f32_16x16x32_f16 v[40:43], v[156:159], v[164:167], v[40:43]
	v_mfma_f32_16x16x32_f16 v[28:31], v[160:163], v[164:167], v[28:31]
	s_waitcnt vmcnt(16)
	v_mfma_f32_16x16x32_f16 v[36:39], v[156:159], v[168:171], v[36:39]
	v_mfma_f32_16x16x32_f16 v[32:35], v[160:163], v[168:171], v[32:35]
	s_waitcnt vmcnt(13)
	v_mfma_f32_16x16x32_f16 v[40:43], v[100:103], v[92:95], v[40:43]
	s_waitcnt vmcnt(11)
	v_mfma_f32_16x16x32_f16 v[28:31], v[108:111], v[92:95], v[28:31]
	v_mfma_f32_16x16x32_f16 v[36:39], v[100:103], v[96:99], v[36:39]
	v_mfma_f32_16x16x32_f16 v[32:35], v[108:111], v[96:99], v[32:35]
	s_waitcnt vmcnt(9)
	v_mfma_f32_16x16x32_f16 v[40:43], v[104:107], v[116:119], v[40:43]
	v_mfma_f32_16x16x32_f16 v[28:31], v[112:115], v[116:119], v[28:31]
	s_waitcnt vmcnt(8)
	v_mfma_f32_16x16x32_f16 v[36:39], v[104:107], v[120:123], v[36:39]
	v_mfma_f32_16x16x32_f16 v[32:35], v[112:115], v[120:123], v[32:35]
	s_waitcnt vmcnt(5)
	v_mfma_f32_16x16x32_f16 v[40:43], v[132:135], v[124:127], v[40:43]
	s_waitcnt vmcnt(3)
	v_mfma_f32_16x16x32_f16 v[28:31], v[140:143], v[124:127], v[28:31]
	v_mfma_f32_16x16x32_f16 v[36:39], v[132:135], v[128:131], v[36:39]
	v_mfma_f32_16x16x32_f16 v[32:35], v[140:143], v[128:131], v[32:35]
	s_waitcnt vmcnt(1)
	v_mfma_f32_16x16x32_f16 v[40:43], v[136:139], v[148:151], v[40:43]
	v_mfma_f32_16x16x32_f16 v[28:31], v[144:147], v[148:151], v[28:31]
	s_waitcnt vmcnt(0)
	v_mfma_f32_16x16x32_f16 v[36:39], v[136:139], v[152:155], v[36:39]
	v_mfma_f32_16x16x32_f16 v[32:35], v[144:147], v[152:155], v[32:35]
	v_lshlrev_b32_e32 v20, 12, v176
	v_add3_u32 v20, 0, v8, v20
	s_nop 1
	ds_write_b128 v20, v[40:43]
	ds_write_b128 v20, v[28:31] offset:1024
	s_nop 0
	ds_write_b128 v20, v[36:39] offset:2048
	ds_write_b128 v20, v[32:35] offset:3072
	v_lshrrev_b32_e32 v20, 4, v0
	v_and_b32_e32 v21, 60, v1
	v_mul_u32_u24_e32 v20, 0x110, v20
	v_lshlrev_b32_e32 v21, 2, v21
	s_movk_i32 s0, 0x50
	v_add3_u32 v20, 0, v20, v21
	v_cmp_gt_u32_e32 vcc, s0, v0
	ds_write_b128 v20, v[2:5] offset:32768
	s_and_saveexec_b64 s[0:1], vcc
	s_cbranch_execz .LBB13_14
	global_load_dwordx4 v[2:5], v[6:7], off
	v_lshl_add_u32 v0, v1, 2, 0
	s_waitcnt vmcnt(0)
	ds_write_b128 v0, v[2:5] offset:41472
.LBB13_14:
	s_or_b64 exec, exec, s[0:1]
	v_lshlrev_b32_e32 v0, 10, v27
	v_add3_u32 v8, 0, v0, v8
	s_waitcnt lgkmcnt(0)
	s_barrier
	ds_read_b128 v[0:3], v8
	ds_read_b128 v[4:7], v8 offset:4096
	ds_read_b128 v[28:31], v8 offset:8192
	ds_read_b128 v[32:35], v8 offset:12288
	v_cmp_eq_u32_e32 vcc, 0, v26
	s_waitcnt lgkmcnt(2)
	v_pk_add_f32 v[2:3], v[2:3], v[6:7]
	v_pk_add_f32 v[4:5], v[0:1], v[4:5]
	s_waitcnt lgkmcnt(1)
	v_pk_add_f32 v[6:7], v[2:3], v[30:31]
	ds_read_b128 v[0:3], v8 offset:16384
	v_pk_add_f32 v[4:5], v[4:5], v[28:29]
	s_waitcnt lgkmcnt(1)
	v_pk_add_f32 v[20:21], v[6:7], v[34:35]
	v_pk_add_f32 v[32:33], v[4:5], v[32:33]
	ds_read_b128 v[4:7], v8 offset:20480
	ds_read_b128 v[28:31], v8 offset:24576
	s_waitcnt lgkmcnt(2)
	v_pk_add_f32 v[20:21], v[20:21], v[2:3]
	v_pk_add_f32 v[32:33], v[32:33], v[0:1]
	ds_read_b128 v[0:3], v8 offset:28672
	s_waitcnt lgkmcnt(2)
	v_pk_add_f32 v[6:7], v[20:21], v[6:7]
	v_pk_add_f32 v[4:5], v[32:33], v[4:5]
	s_waitcnt lgkmcnt(1)
	v_pk_add_f32 v[6:7], v[6:7], v[30:31]
	v_pk_add_f32 v[4:5], v[4:5], v[28:29]
	s_waitcnt lgkmcnt(0)
	v_pk_add_f32 v[2:3], v[6:7], v[2:3]
	v_lshl_add_u32 v6, v23, 2, 0
	v_pk_add_f32 v[0:1], v[4:5], v[0:1]
	ds_read_b64 v[4:5], v6 offset:42624
	v_cndmask_b32_e32 v1, v3, v1, vcc
	v_cndmask_b32_e32 v0, v2, v0, vcc
	v_mad_u32_u24 v2, v23, 12, v6
	ds_read_b128 v[26:29], v2 offset:41472
	s_waitcnt lgkmcnt(1)
	v_pk_add_f32 v[0:1], v[0:1], v[4:5]
	v_mad_i32_i24 v4, v23, -12, v2
	v_pk_add_f32 v[54:55], v[16:17], v[0:1]
	v_add_co_u32_e32 v0, vcc, s2, v18
	s_waitcnt lgkmcnt(0)
	v_mov_b32_e32 v58, v26
	v_addc_co_u32_e32 v1, vcc, 0, v19, vcc
	global_store_dwordx2 v[0:1], v[54:55], off
	v_or_b32_e32 v1, 1, v23
	v_lshl_add_u32 v0, v23, 8, v2
	v_lshl_add_u32 v5, v1, 4, 0
	v_lshl_add_u32 v6, v1, 8, v5
	ds_read_b128 v[18:21], v0 offset:32992
	ds_read_b128 v[30:33], v0 offset:33008
	ds_read_b128 v[34:37], v0 offset:32976
	ds_read_b128 v[0:3], v2 offset:41984
	ds_read_b64 v[16:17], v4 offset:42496
	ds_read_b128 v[38:41], v5 offset:41472
	ds_read_b128 v[42:45], v6 offset:32976
	ds_read_b128 v[46:49], v6 offset:32992
	ds_read_b128 v[50:53], v6 offset:33008
	s_waitcnt lgkmcnt(6)
	v_mov_b32_e32 v56, v34
	s_waitcnt lgkmcnt(3)
	v_mov_b32_e32 v59, v38
	s_waitcnt lgkmcnt(2)
	v_mov_b32_e32 v57, v42
	v_pk_fma_f32 v[56:57], v[12:13], v[56:57], v[58:59]
	v_mov_b32_e32 v58, v18
	s_waitcnt lgkmcnt(1)
	v_mov_b32_e32 v59, v46
	v_pk_fma_f32 v[56:57], v[14:15], v[58:59], v[56:57]
	v_mov_b32_e32 v58, v30
	s_waitcnt lgkmcnt(0)
	v_mov_b32_e32 v59, v50
	v_pk_fma_f32 v[56:57], v[54:55], v[58:59], v[56:57]
	v_mov_b32_e32 v42, v35
	v_mul_f32_e32 v8, 0x3d372713, v56
	v_mul_f32_e32 v8, v56, v8
	v_fma_f32 v8, v56, v8, v56
	v_mov_b32_e32 v38, v27
	v_mul_f32_e32 v8, 0x3f4c422a, v8
	v_pk_fma_f32 v[26:27], v[12:13], v[42:43], v[38:39]
	v_mov_b32_e32 v46, v19
	v_add_f32_e32 v8, v8, v8
	v_pk_fma_f32 v[26:27], v[14:15], v[46:47], v[26:27]
	v_mov_b32_e32 v50, v31
	v_mul_f32_e32 v8, 0x3fb8aa3b, v8
	v_pk_fma_f32 v[26:27], v[54:55], v[50:51], v[26:27]
	v_exp_f32_e32 v18, v8
	v_mul_f32_e32 v8, 0x3d372713, v26
	v_mov_b32_e32 v34, v36
	v_mov_b32_e32 v35, v44
	v_mov_b32_e32 v38, v28
	v_mov_b32_e32 v39, v40
	v_mov_b32_e32 v44, v37
	v_mov_b32_e32 v40, v29
	v_mul_f32_e32 v8, v26, v8
	v_pk_fma_f32 v[34:35], v[12:13], v[34:35], v[38:39]
	v_mov_b32_e32 v38, v20
	v_mov_b32_e32 v39, v48
	v_pk_fma_f32 v[12:13], v[12:13], v[44:45], v[40:41]
	v_mov_b32_e32 v48, v21
	v_fma_f32 v8, v26, v8, v26
	v_pk_fma_f32 v[34:35], v[14:15], v[38:39], v[34:35]
	v_pk_fma_f32 v[12:13], v[14:15], v[48:49], v[12:13]
	v_mul_f32_e32 v14, 0x3d372713, v57
	v_mul_f32_e32 v8, 0x3f4c422a, v8
	v_mul_f32_e32 v14, v57, v14
	v_add_f32_e32 v8, v8, v8
	v_mov_b32_e32 v38, v32
	v_mov_b32_e32 v39, v52
	v_fma_f32 v14, v57, v14, v57
	v_mul_f32_e32 v8, 0x3fb8aa3b, v8
	v_pk_fma_f32 v[34:35], v[54:55], v[38:39], v[34:35]
	v_mul_f32_e32 v14, 0x3f4c422a, v14
	v_exp_f32_e32 v30, v8
	v_mul_f32_e32 v8, 0x3d372713, v34
	v_add_f32_e32 v14, v14, v14
	v_mul_f32_e32 v8, v34, v8
	v_mul_f32_e32 v14, 0x3fb8aa3b, v14
	v_fma_f32 v8, v34, v8, v34
	v_exp_f32_e32 v19, v14
	v_mul_f32_e32 v8, 0x3f4c422a, v8
	v_add_f32_e32 v8, v8, v8
	v_mov_b32_e32 v52, v33
	v_mul_f32_e32 v8, 0x3fb8aa3b, v8
	v_pk_fma_f32 v[12:13], v[54:55], v[52:53], v[12:13]
	v_exp_f32_e32 v20, v8
	v_mul_f32_e32 v8, 0x3d372713, v12
	v_pk_add_f32 v[14:15], v[18:19], 1.0 op_sel_hi:[1,0]
	v_mul_f32_e32 v8, v12, v8
	v_div_scale_f32 v19, s[0:1], v15, v15, 2.0
	v_fma_f32 v8, v12, v8, v12
	v_rcp_f32_e32 v21, v19
	v_mul_f32_e32 v8, 0x3f4c422a, v8
	v_add_f32_e32 v8, v8, v8
	v_mul_f32_e32 v8, 0x3fb8aa3b, v8
	v_exp_f32_e32 v18, v8
	v_fma_f32 v8, -v19, v21, 1.0
	v_fmac_f32_e32 v21, v8, v21
	v_div_scale_f32 v8, vcc, 2.0, v15, 2.0
	v_mul_f32_e32 v28, v8, v21
	v_fma_f32 v29, -v19, v28, v8
	v_fmac_f32_e32 v28, v29, v21
	v_fma_f32 v8, -v19, v28, v8
	v_div_scale_f32 v19, s[0:1], v14, v14, 2.0
	v_rcp_f32_e32 v29, v19
	v_div_fmas_f32 v8, v8, v21, v28
	v_div_fixup_f32 v15, v8, v15, 2.0
	ds_read_b128 v[4:7], v5 offset:41984
	v_fma_f32 v8, -v19, v29, 1.0
	v_fmac_f32_e32 v29, v8, v29
	v_div_scale_f32 v8, vcc, 2.0, v14, 2.0
	v_mul_f32_e32 v21, v8, v29
	v_fma_f32 v28, -v19, v21, v8
	v_fmac_f32_e32 v21, v28, v29
	v_fma_f32 v8, -v19, v21, v8
	v_div_fmas_f32 v8, v8, v29, v21
	v_div_fixup_f32 v14, v8, v14, 2.0
	v_mul_f32_e32 v8, 0x3d372713, v27
	v_mul_f32_e32 v8, v27, v8
	v_fma_f32 v8, v27, v8, v27
	v_mul_f32_e32 v8, 0x3f4c422a, v8
	v_add_f32_e32 v8, v8, v8
	v_mul_f32_e32 v8, 0x3fb8aa3b, v8
	v_exp_f32_e32 v31, v8
	v_pk_add_f32 v[14:15], v[14:15], 1.0 op_sel_hi:[1,0] neg_lo:[1,0] neg_hi:[1,0]
	v_pk_mul_f32 v[28:29], v[56:57], 0.5 op_sel_hi:[1,0]
	v_pk_add_f32 v[14:15], v[14:15], 1.0 op_sel_hi:[1,0]
	v_pk_add_f32 v[30:31], v[30:31], 1.0 op_sel_hi:[1,0]
	v_pk_mul_f32 v[14:15], v[28:29], v[14:15]
	v_div_scale_f32 v8, s[0:1], v31, v31, 2.0
	v_rcp_f32_e32 v19, v8
	v_mov_b32_e32 v28, v0
	s_waitcnt lgkmcnt(0)
	v_mov_b32_e32 v29, v4
	v_pk_mul_f32 v[26:27], v[26:27], 0.5 op_sel_hi:[1,0]
	v_fma_f32 v0, -v8, v19, 1.0
	v_fmac_f32_e32 v19, v0, v19
	v_div_scale_f32 v0, vcc, 2.0, v31, 2.0
	v_mul_f32_e32 v4, v0, v19
	v_fma_f32 v21, -v8, v4, v0
	v_fmac_f32_e32 v4, v21, v19
	v_fma_f32 v0, -v8, v4, v0
	v_div_scale_f32 v8, s[0:1], v30, v30, 2.0
	v_rcp_f32_e32 v21, v8
	v_div_fmas_f32 v0, v0, v19, v4
	v_div_fixup_f32 v31, v0, v31, 2.0
	v_fma_f32 v0, -v8, v21, 1.0
	v_fmac_f32_e32 v21, v0, v21
	v_div_scale_f32 v0, vcc, 2.0, v30, 2.0
	v_mul_f32_e32 v4, v0, v21
	v_fma_f32 v19, -v8, v4, v0
	v_fmac_f32_e32 v4, v19, v21
	v_fma_f32 v0, -v8, v4, v0
	v_div_fmas_f32 v0, v0, v21, v4
	v_div_fixup_f32 v30, v0, v30, 2.0
	v_mul_f32_e32 v0, 0x3d372713, v35
	v_mul_f32_e32 v0, v35, v0
	v_fma_f32 v0, v35, v0, v35
	v_mul_f32_e32 v0, 0x3f4c422a, v0
	v_add_f32_e32 v0, v0, v0
	v_mul_f32_e32 v0, 0x3fb8aa3b, v0
	v_exp_f32_e32 v21, v0
	v_pk_add_f32 v[30:31], v[30:31], 1.0 op_sel_hi:[1,0] neg_lo:[1,0] neg_hi:[1,0]
	v_mov_b32_e32 v4, v1
	v_pk_add_f32 v[30:31], v[30:31], 1.0 op_sel_hi:[1,0]
	v_pk_add_f32 v[20:21], v[20:21], 1.0 op_sel_hi:[1,0]
	v_pk_mul_f32 v[26:27], v[26:27], v[30:31]
	v_div_scale_f32 v8, s[0:1], v21, v21, 2.0
	v_rcp_f32_e32 v19, v8
	v_pk_mul_f32 v[0:1], v[26:27], v[4:5]
	v_fma_f32 v4, -v8, v19, 1.0
	v_fmac_f32_e32 v19, v4, v19
	v_div_scale_f32 v4, vcc, 2.0, v21, 2.0
	v_mul_f32_e32 v5, v4, v19
	v_pk_fma_f32 v[0:1], v[14:15], v[28:29], v[0:1]
	v_fma_f32 v14, -v8, v5, v4
	v_fmac_f32_e32 v5, v14, v19
	v_fma_f32 v4, -v8, v5, v4
	v_div_scale_f32 v8, s[0:1], v20, v20, 2.0
	v_rcp_f32_e32 v14, v8
	v_div_fmas_f32 v4, v4, v19, v5
	v_div_fixup_f32 v5, v4, v21, 2.0
	v_fma_f32 v4, -v8, v14, 1.0
	v_fmac_f32_e32 v14, v4, v14
	v_div_scale_f32 v4, vcc, 2.0, v20, 2.0
	v_mul_f32_e32 v15, v4, v14
	v_fma_f32 v19, -v8, v15, v4
	v_fmac_f32_e32 v15, v19, v14
	v_fma_f32 v4, -v8, v15, v4
	v_mul_f32_e32 v8, 0x3d372713, v13
	v_mul_f32_e32 v8, v13, v8
	v_fma_f32 v8, v13, v8, v13
	v_mul_f32_e32 v8, 0x3f4c422a, v8
	v_add_f32_e32 v8, v8, v8
	v_mul_f32_e32 v8, 0x3fb8aa3b, v8
	v_div_fmas_f32 v4, v4, v14, v15
	v_exp_f32_e32 v19, v8
	v_div_fixup_f32 v4, v4, v20, 2.0
	v_pk_add_f32 v[4:5], v[4:5], 1.0 op_sel_hi:[1,0] neg_lo:[1,0] neg_hi:[1,0]
	v_pk_mul_f32 v[14:15], v[34:35], 0.5 op_sel_hi:[1,0]
	v_pk_add_f32 v[4:5], v[4:5], 1.0 op_sel_hi:[1,0]
	v_pk_mul_f32 v[12:13], v[12:13], 0.5 op_sel_hi:[1,0]
	v_pk_mul_f32 v[4:5], v[14:15], v[4:5]
	v_pk_add_f32 v[14:15], v[18:19], 1.0 op_sel_hi:[1,0]
	v_mov_b32_e32 v18, v2
	v_div_scale_f32 v8, s[0:1], v15, v15, 2.0
	v_rcp_f32_e32 v20, v8
	v_mov_b32_e32 v19, v6
	v_pk_fma_f32 v[0:1], v[4:5], v[18:19], v[0:1]
	v_div_scale_f32 v6, s[0:1], v14, v14, 2.0
	v_fma_f32 v2, -v8, v20, 1.0
	v_fmac_f32_e32 v20, v2, v20
	v_div_scale_f32 v2, vcc, 2.0, v15, 2.0
	v_mul_f32_e32 v4, v2, v20
	v_fma_f32 v5, -v8, v4, v2
	v_fmac_f32_e32 v4, v5, v20
	v_fma_f32 v2, -v8, v4, v2
	v_rcp_f32_e32 v8, v6
	v_div_fmas_f32 v2, v2, v20, v4
	v_div_fixup_f32 v5, v2, v15, 2.0
	s_mov_b32 s0, 0x300000
	v_fma_f32 v2, -v6, v8, 1.0
	v_fmac_f32_e32 v8, v2, v8
	v_div_scale_f32 v2, vcc, 2.0, v14, 2.0
	v_mul_f32_e32 v4, v2, v8
	v_fma_f32 v15, -v6, v4, v2
	v_fmac_f32_e32 v4, v15, v8
	v_fma_f32 v2, -v6, v4, v2
	v_div_fmas_f32 v2, v2, v8, v4
	v_div_fixup_f32 v4, v2, v14, 2.0
	v_pk_add_f32 v[4:5], v[4:5], 1.0 op_sel_hi:[1,0] neg_lo:[1,0] neg_hi:[1,0]
	v_mov_b32_e32 v6, v3
	v_pk_add_f32 v[4:5], v[4:5], 1.0 op_sel_hi:[1,0]
	v_add_co_u32_e32 v2, vcc, s0, v10
	v_pk_mul_f32 v[4:5], v[12:13], v[4:5]
	s_lshl_b32 s0, s3, 3
	v_pk_fma_f32 v[0:1], v[4:5], v[6:7], v[0:1]
	v_addc_co_u32_e32 v3, vcc, 0, v11, vcc
	v_pk_add_f32 v[0:1], v[16:17], v[0:1]
	s_addk_i32 s0, 0x100
	global_store_dwordx2 v[2:3], v[0:1], off
	v_add_u32_e32 v8, s0, v24
	v_lshlrev_b32_e32 v3, 1, v25
	v_cvt_pk_f16_f32 v2, v0, v1
	v_lshlrev_b64 v[0:1], 6, v[8:9]
	v_and_b32_e32 v3, 48, v3
	v_or3_b32 v0, v0, v3, v22
	v_and_b32_e32 v3, 6, v23
	v_lshl_add_u64 v[0:1], v[0:1], 4, s[12:13]
	v_lshlrev_b32_e32 v8, 1, v3
	v_lshl_add_u64 v[0:1], v[0:1], 0, v[8:9]
	global_store_dword v[0:1], v2, off
	s_endpgm
	s_nop 0
	s_nop 0
	s_nop 0
	s_nop 0
	s_nop 0
	s_nop 0
	s_endpgm

	.amdhsa_kernel _ZN12_GLOBAL__N_110gemm_fullkILi1ELi2EEEvPKDF16_S2_PKfPDF16_PfS6_S4_S4_S4_S4_S4_S5_
		.amdhsa_group_segment_fixed_size 0
		.amdhsa_private_segment_fixed_size 0
		.amdhsa_kernarg_size 96
		.amdhsa_user_sgpr_count 2
		.amdhsa_user_sgpr_dispatch_ptr 0
		.amdhsa_user_sgpr_queue_ptr 0
		.amdhsa_user_sgpr_kernarg_segment_ptr 1
		.amdhsa_user_sgpr_dispatch_id 0
		.amdhsa_user_sgpr_kernarg_preload_length 0
		.amdhsa_user_sgpr_kernarg_preload_offset 0
		.amdhsa_user_sgpr_private_segment_size 0
		.amdhsa_uses_dynamic_stack 0
		.amdhsa_enable_private_segment 0
		.amdhsa_system_sgpr_workgroup_id_x 1
		.amdhsa_system_sgpr_workgroup_id_y 0
		.amdhsa_system_sgpr_workgroup_id_z 0
		.amdhsa_system_sgpr_workgroup_info 0
		.amdhsa_system_vgpr_workitem_id 0
		.amdhsa_next_free_vgpr 177
		.amdhsa_next_free_sgpr 18
		.amdhsa_accum_offset 180
		.amdhsa_reserve_vcc 1
		.amdhsa_float_round_mode_32 0
		.amdhsa_float_round_mode_16_64 0
		.amdhsa_float_denorm_mode_32 3
		.amdhsa_float_denorm_mode_16_64 3
		.amdhsa_dx10_clamp 1
		.amdhsa_ieee_mode 1
		.amdhsa_fp16_overflow 0
		.amdhsa_tg_split 0
		.amdhsa_exception_fp_ieee_invalid_op 0
		.amdhsa_exception_fp_denorm_src 0
		.amdhsa_exception_fp_ieee_div_zero 0
		.amdhsa_exception_fp_ieee_overflow 0
		.amdhsa_exception_fp_ieee_underflow 0
		.amdhsa_exception_fp_ieee_inexact 0
		.amdhsa_exception_int_div_zero 0
	.end_amdhsa_kernel

_ZN12_GLOBAL__N_110gemm_fullkILi0ELi3EEEvPKDF16_S2_PKfPDF16_PfS6_S4_S4_S4_S4_S4_S5_:
	s_load_dwordx8 s[4:11], s[0:1], 0x0
	s_lshr_b32 s0, s2, 5
	v_lshrrev_b32_e32 v230, 6, v0
	s_and_b32 s12, s0, 0x7fffffc
	s_and_b32 s2, s2, 0x7f
	s_mov_b32 s13, 0
	v_mul_u32_u24_e32 v4, 12, v230
	v_mov_b32_e32 v3, 0
	s_lshl_b64 s[0:1], s[12:13], 10
	s_mul_i32 s13, s2, 0xc0
	v_and_b32_e32 v1, 63, v0
	v_mul_u32_u24_e32 v2, 0x18000, v230
	v_add_lshl_u32 v4, s13, v4, 10
	v_mov_b32_e32 v5, v3
	s_waitcnt lgkmcnt(0)
	v_lshl_add_u64 v[4:5], s[6:7], 0, v[4:5]
	v_lshl_add_u64 v[6:7], s[4:5], 0, v[2:3]
	v_lshlrev_b32_e32 v2, 4, v1
	s_mov_b32 s3, 0x18000
	v_lshl_add_u64 v[208:209], v[4:5], 0, v[2:3]
	v_add_co_u32_e32 v80, vcc, s3, v208
	v_lshl_add_u64 v[6:7], v[6:7], 0, s[0:1]
	s_nop 0
	v_addc_co_u32_e32 v81, vcc, 0, v209, vcc
	s_mov_b32 s0, 0x19000
	v_add_co_u32_e32 v176, vcc, s0, v208
	v_lshl_add_u64 v[212:213], v[6:7], 0, v[2:3]
	s_nop 0
	v_addc_co_u32_e32 v177, vcc, 0, v209, vcc
	s_movk_i32 s0, 0x2000
	v_add_co_u32_e32 v52, vcc, s0, v212
	s_movk_i32 s1, 0x4000
	s_nop 0
	v_addc_co_u32_e32 v53, vcc, 0, v213, vcc
	v_add_co_u32_e32 v82, vcc, s1, v212
	s_movk_i32 s1, 0x6000
	s_nop 0
	v_addc_co_u32_e32 v83, vcc, 0, v213, vcc
	v_add_co_u32_e32 v96, vcc, s1, v212
	s_movk_i32 s1, 0x1000
	s_nop 0
	v_addc_co_u32_e32 v97, vcc, 0, v213, vcc
	v_add_co_u32_e32 v168, vcc, s1, v208
	global_load_dwordx4 v[4:7], v[212:213], off
	global_load_dwordx4 v[8:11], v[212:213], off offset:1024
	global_load_dwordx4 v[12:15], v[212:213], off offset:2048
	global_load_dwordx4 v[16:19], v[212:213], off offset:3072
	global_load_dwordx4 v[20:23], v[208:209], off
	global_load_dwordx4 v[24:27], v[208:209], off offset:1024
	v_addc_co_u32_e32 v169, vcc, 0, v209, vcc
	v_add_co_u32_e32 v210, vcc, s0, v208
	s_mov_b32 s0, 0x8000
	s_nop 0
	v_addc_co_u32_e32 v211, vcc, 0, v209, vcc
	v_add_co_u32_e32 v116, vcc, s0, v212
	s_mov_b32 s0, 0xa000
	s_nop 0
	v_addc_co_u32_e32 v117, vcc, 0, v213, vcc
	v_add_co_u32_e32 v132, vcc, s0, v212
	s_mov_b32 s0, 0xc000
	s_nop 0
	v_addc_co_u32_e32 v133, vcc, 0, v213, vcc
	v_add_co_u32_e32 v164, vcc, s0, v212
	global_load_dwordx4 v[28:31], v[52:53], off
	global_load_dwordx4 v[32:35], v[52:53], off offset:1024
	global_load_dwordx4 v[36:39], v[52:53], off offset:2048
	global_load_dwordx4 v[40:43], v[52:53], off offset:3072
	global_load_dwordx4 v[44:47], v[80:81], off offset:1024
	global_load_dwordx4 v[48:51], v[80:81], off offset:2048
	s_nop 0
	global_load_dwordx4 v[52:55], v[82:83], off
	global_load_dwordx4 v[56:59], v[82:83], off offset:1024
	global_load_dwordx4 v[60:63], v[82:83], off offset:2048
	global_load_dwordx4 v[64:67], v[82:83], off offset:3072
	global_load_dwordx4 v[68:71], v[208:209], off offset:2048
	global_load_dwordx4 v[72:75], v[208:209], off offset:3072
	global_load_dwordx4 v[76:79], v[80:81], off offset:3072
	s_nop 0
	global_load_dwordx4 v[80:83], v[96:97], off
	global_load_dwordx4 v[84:87], v[96:97], off offset:1024
	global_load_dwordx4 v[88:91], v[96:97], off offset:2048
	global_load_dwordx4 v[92:95], v[96:97], off offset:3072
	s_nop 0
	global_load_dwordx4 v[96:99], v[176:177], off offset:-4096
	global_load_dwordx4 v[100:103], v[176:177], off
	global_load_dwordx4 v[104:107], v[116:117], off
	global_load_dwordx4 v[108:111], v[116:117], off offset:1024
	global_load_dwordx4 v[112:115], v[116:117], off offset:2048
	s_nop 0
	global_load_dwordx4 v[116:119], v[116:117], off offset:3072
	s_nop 0
	global_load_dwordx4 v[120:123], v[132:133], off
	global_load_dwordx4 v[124:127], v[132:133], off offset:1024
	global_load_dwordx4 v[128:131], v[132:133], off offset:2048
	s_nop 0
	global_load_dwordx4 v[132:135], v[132:133], off offset:3072
	s_nop 0
	global_load_dwordx4 v[136:139], v[168:169], off offset:1024
	global_load_dwordx4 v[140:143], v[168:169], off offset:2048
	global_load_dwordx4 v[144:147], v[176:177], off offset:1024
	global_load_dwordx4 v[148:151], v[176:177], off offset:2048
	v_addc_co_u32_e32 v165, vcc, 0, v213, vcc
	global_load_dwordx4 v[152:155], v[164:165], off
	global_load_dwordx4 v[156:159], v[164:165], off offset:1024
	global_load_dwordx4 v[160:163], v[164:165], off offset:2048
	s_nop 0
	global_load_dwordx4 v[164:167], v[164:165], off offset:3072
	s_nop 0
	global_load_dwordx4 v[168:171], v[168:169], off offset:3072
	s_nop 0
	global_load_dwordx4 v[172:175], v[210:211], off offset:-4096
	s_nop 0
	global_load_dwordx4 v[176:179], v[176:177], off offset:3072
	s_mov_b32 s0, 0xe000
	v_add_co_u32_e32 v192, vcc, s0, v212
	s_lshl_b32 s0, s2, 7
	s_nop 0
	v_addc_co_u32_e32 v193, vcc, 0, v213, vcc
	global_load_dwordx4 v[180:183], v[192:193], off
	global_load_dwordx4 v[184:187], v[192:193], off offset:1024
	global_load_dwordx4 v[188:191], v[192:193], off offset:2048
	s_nop 0
	global_load_dwordx4 v[192:195], v[192:193], off offset:3072
	v_bfe_u32 v1, v0, 6, 1
	s_add_u32 s0, s8, s0
	s_addc_u32 s1, s9, 0
	v_lshlrev_b32_e32 v196, 6, v1
	v_mov_b32_e32 v197, v3
	v_lshl_add_u64 v[196:197], s[0:1], 0, v[196:197]
	v_and_b32_e32 v198, 48, v0
	v_mov_b32_e32 v199, v3
	v_lshl_add_u64 v[228:229], v[196:197], 0, v[198:199]
	s_waitcnt vmcnt(43)
	v_mfma_f32_16x16x32_f16 v[196:199], v[20:23], v[4:7], 0
	s_waitcnt vmcnt(24)
	v_mfma_f32_16x16x32_f16 v[4:7], v[96:99], v[4:7], 0
	v_mfma_f32_16x16x32_f16 v[200:203], v[20:23], v[8:11], 0
	v_mfma_f32_16x16x32_f16 v[8:11], v[96:99], v[8:11], 0
	v_mfma_f32_16x16x32_f16 v[204:207], v[20:23], v[12:15], 0
	v_mfma_f32_16x16x32_f16 v[12:15], v[96:99], v[12:15], 0
	v_mfma_f32_16x16x32_f16 v[20:23], v[20:23], v[16:19], 0
	v_mfma_f32_16x16x32_f16 v[16:19], v[96:99], v[16:19], 0
	v_mfma_f32_16x16x32_f16 v[96:99], v[24:27], v[28:31], v[196:199]
	v_mfma_f32_16x16x32_f16 v[4:7], v[44:47], v[28:31], v[4:7]
	v_mfma_f32_16x16x32_f16 v[28:31], v[24:27], v[32:35], v[200:203]
	v_mfma_f32_16x16x32_f16 v[8:11], v[44:47], v[32:35], v[8:11]
	v_mfma_f32_16x16x32_f16 v[32:35], v[24:27], v[36:39], v[204:207]
	v_mfma_f32_16x16x32_f16 v[12:15], v[44:47], v[36:39], v[12:15]
	v_mfma_f32_16x16x32_f16 v[20:23], v[24:27], v[40:43], v[20:23]
	v_mfma_f32_16x16x32_f16 v[16:19], v[44:47], v[40:43], v[16:19]
	v_mfma_f32_16x16x32_f16 v[24:27], v[68:71], v[52:55], v[96:99]
	v_mfma_f32_16x16x32_f16 v[4:7], v[48:51], v[52:55], v[4:7]
	v_mfma_f32_16x16x32_f16 v[28:31], v[68:71], v[56:59], v[28:31]
	v_mfma_f32_16x16x32_f16 v[8:11], v[48:51], v[56:59], v[8:11]
	v_mfma_f32_16x16x32_f16 v[32:35], v[68:71], v[60:63], v[32:35]
	v_mfma_f32_16x16x32_f16 v[12:15], v[48:51], v[60:63], v[12:15]
	v_mfma_f32_16x16x32_f16 v[20:23], v[68:71], v[64:67], v[20:23]
	v_mfma_f32_16x16x32_f16 v[16:19], v[48:51], v[64:67], v[16:19]
	v_mfma_f32_16x16x32_f16 v[24:27], v[72:75], v[80:83], v[24:27]
	v_mfma_f32_16x16x32_f16 v[4:7], v[76:79], v[80:83], v[4:7]
	v_mfma_f32_16x16x32_f16 v[28:31], v[72:75], v[84:87], v[28:31]
	v_mfma_f32_16x16x32_f16 v[8:11], v[76:79], v[84:87], v[8:11]
	v_mfma_f32_16x16x32_f16 v[32:35], v[72:75], v[88:91], v[32:35]
	v_mfma_f32_16x16x32_f16 v[12:15], v[76:79], v[88:91], v[12:15]
	v_mfma_f32_16x16x32_f16 v[20:23], v[72:75], v[92:95], v[20:23]
	v_mfma_f32_16x16x32_f16 v[16:19], v[76:79], v[92:95], v[16:19]
	s_mov_b32 s0, 0x1a000
	v_add_co_u32_e32 v208, vcc, s0, v208
	s_mov_b32 s0, 0x10000
	s_nop 0
	v_addc_co_u32_e32 v209, vcc, 0, v209, vcc
	v_add_co_u32_e32 v48, vcc, s0, v212
	s_mov_b32 s0, 0x12000
	s_nop 0
	v_addc_co_u32_e32 v49, vcc, 0, v213, vcc
	v_add_co_u32_e32 v80, vcc, s0, v212
	s_mov_b32 s0, 0x14000
	s_nop 0
	v_addc_co_u32_e32 v81, vcc, 0, v213, vcc
	v_add_co_u32_e32 v96, vcc, s0, v212
	global_load_dwordx4 v[36:39], v[48:49], off
	global_load_dwordx4 v[40:43], v[48:49], off offset:1024
	global_load_dwordx4 v[44:47], v[48:49], off offset:2048
	s_nop 0
	global_load_dwordx4 v[48:51], v[48:49], off offset:3072
	s_nop 0
	global_load_dwordx4 v[52:55], v[210:211], off
	global_load_dwordx4 v[56:59], v[210:211], off offset:1024
	global_load_dwordx4 v[60:63], v[208:209], off
	global_load_dwordx4 v[64:67], v[208:209], off offset:1024
	v_addc_co_u32_e32 v97, vcc, 0, v213, vcc
	global_load_dwordx4 v[68:71], v[80:81], off
	global_load_dwordx4 v[72:75], v[80:81], off offset:1024
	global_load_dwordx4 v[76:79], v[80:81], off offset:2048
	s_nop 0
	global_load_dwordx4 v[80:83], v[80:81], off offset:3072
	s_nop 0
	global_load_dwordx4 v[84:87], v[96:97], off
	global_load_dwordx4 v[88:91], v[96:97], off offset:1024
	global_load_dwordx4 v[92:95], v[96:97], off offset:2048
	s_nop 0
	global_load_dwordx4 v[96:99], v[96:97], off offset:3072
	s_nop 0
	global_load_dwordx4 v[196:199], v[210:211], off offset:2048
	global_load_dwordx4 v[200:203], v[210:211], off offset:3072
	global_load_dwordx4 v[204:207], v[208:209], off offset:2048
	s_nop 0
	global_load_dwordx4 v[208:211], v[208:209], off offset:3072
	s_mov_b32 s0, 0x16000
	v_add_co_u32_e32 v224, vcc, s0, v212
	s_nop 1
	v_addc_co_u32_e32 v225, vcc, 0, v213, vcc
	global_load_dwordx4 v[212:215], v[224:225], off
	global_load_dwordx4 v[216:219], v[224:225], off offset:1024
	global_load_dwordx4 v[220:223], v[224:225], off offset:2048
	s_nop 0
	global_load_dwordx4 v[224:227], v[224:225], off offset:3072
	s_waitcnt vmcnt(29)
	v_mfma_f32_16x16x32_f16 v[24:27], v[172:175], v[104:107], v[24:27]
	v_mfma_f32_16x16x32_f16 v[4:7], v[100:103], v[104:107], v[4:7]
	v_mfma_f32_16x16x32_f16 v[28:31], v[172:175], v[108:111], v[28:31]
	v_mfma_f32_16x16x32_f16 v[8:11], v[100:103], v[108:111], v[8:11]
	v_mfma_f32_16x16x32_f16 v[32:35], v[172:175], v[112:115], v[32:35]
	v_mfma_f32_16x16x32_f16 v[12:15], v[100:103], v[112:115], v[12:15]
	v_mfma_f32_16x16x32_f16 v[20:23], v[172:175], v[116:119], v[20:23]
	v_mfma_f32_16x16x32_f16 v[16:19], v[100:103], v[116:119], v[16:19]
	v_mfma_f32_16x16x32_f16 v[24:27], v[136:139], v[120:123], v[24:27]
	v_mfma_f32_16x16x32_f16 v[4:7], v[144:147], v[120:123], v[4:7]
	v_mfma_f32_16x16x32_f16 v[28:31], v[136:139], v[124:127], v[28:31]
	v_mfma_f32_16x16x32_f16 v[8:11], v[144:147], v[124:127], v[8:11]
	v_mfma_f32_16x16x32_f16 v[32:35], v[136:139], v[128:131], v[32:35]
	v_mfma_f32_16x16x32_f16 v[12:15], v[144:147], v[128:131], v[12:15]
	v_mfma_f32_16x16x32_f16 v[20:23], v[136:139], v[132:135], v[20:23]
	v_mfma_f32_16x16x32_f16 v[16:19], v[144:147], v[132:135], v[16:19]
	v_mfma_f32_16x16x32_f16 v[24:27], v[140:143], v[152:155], v[24:27]
	v_mfma_f32_16x16x32_f16 v[4:7], v[148:151], v[152:155], v[4:7]
	v_mfma_f32_16x16x32_f16 v[28:31], v[140:143], v[156:159], v[28:31]
	v_mfma_f32_16x16x32_f16 v[8:11], v[148:151], v[156:159], v[8:11]
	v_mfma_f32_16x16x32_f16 v[32:35], v[140:143], v[160:163], v[32:35]
	v_mfma_f32_16x16x32_f16 v[12:15], v[148:151], v[160:163], v[12:15]
	v_mfma_f32_16x16x32_f16 v[20:23], v[140:143], v[164:167], v[20:23]
	v_mfma_f32_16x16x32_f16 v[16:19], v[148:151], v[164:167], v[16:19]
	s_waitcnt vmcnt(27)
	v_mfma_f32_16x16x32_f16 v[24:27], v[168:171], v[180:183], v[24:27]
	v_mfma_f32_16x16x32_f16 v[4:7], v[176:179], v[180:183], v[4:7]
	s_waitcnt vmcnt(26)
	v_mfma_f32_16x16x32_f16 v[28:31], v[168:171], v[184:187], v[28:31]
	v_mfma_f32_16x16x32_f16 v[8:11], v[176:179], v[184:187], v[8:11]
	s_waitcnt vmcnt(25)
	v_mfma_f32_16x16x32_f16 v[32:35], v[168:171], v[188:191], v[32:35]
	v_mfma_f32_16x16x32_f16 v[12:15], v[176:179], v[188:191], v[12:15]
	s_waitcnt vmcnt(24)
	v_mfma_f32_16x16x32_f16 v[20:23], v[168:171], v[192:195], v[20:23]
	v_mfma_f32_16x16x32_f16 v[16:19], v[176:179], v[192:195], v[16:19]
	s_waitcnt vmcnt(19)
	v_mfma_f32_16x16x32_f16 v[24:27], v[52:55], v[36:39], v[24:27]
	s_waitcnt vmcnt(17)
	v_mfma_f32_16x16x32_f16 v[4:7], v[60:63], v[36:39], v[4:7]
	v_mfma_f32_16x16x32_f16 v[28:31], v[52:55], v[40:43], v[28:31]
	v_mfma_f32_16x16x32_f16 v[8:11], v[60:63], v[40:43], v[8:11]
	v_mfma_f32_16x16x32_f16 v[32:35], v[52:55], v[44:47], v[32:35]
	v_mfma_f32_16x16x32_f16 v[12:15], v[60:63], v[44:47], v[12:15]
	v_mfma_f32_16x16x32_f16 v[20:23], v[52:55], v[48:51], v[20:23]
	v_mfma_f32_16x16x32_f16 v[16:19], v[60:63], v[48:51], v[16:19]
	s_waitcnt vmcnt(15)
	v_mfma_f32_16x16x32_f16 v[24:27], v[56:59], v[68:71], v[24:27]
	v_mfma_f32_16x16x32_f16 v[4:7], v[64:67], v[68:71], v[4:7]
	s_waitcnt vmcnt(14)
	v_mfma_f32_16x16x32_f16 v[28:31], v[56:59], v[72:75], v[28:31]
	v_mfma_f32_16x16x32_f16 v[8:11], v[64:67], v[72:75], v[8:11]
	s_waitcnt vmcnt(13)
	v_mfma_f32_16x16x32_f16 v[32:35], v[56:59], v[76:79], v[32:35]
	v_mfma_f32_16x16x32_f16 v[12:15], v[64:67], v[76:79], v[12:15]
	s_waitcnt vmcnt(12)
	v_mfma_f32_16x16x32_f16 v[20:23], v[56:59], v[80:83], v[20:23]
	v_mfma_f32_16x16x32_f16 v[16:19], v[64:67], v[80:83], v[16:19]
	s_waitcnt vmcnt(7)
	v_mfma_f32_16x16x32_f16 v[24:27], v[196:199], v[84:87], v[24:27]
	s_waitcnt vmcnt(5)
	v_mfma_f32_16x16x32_f16 v[4:7], v[204:207], v[84:87], v[4:7]
	v_mfma_f32_16x16x32_f16 v[28:31], v[196:199], v[88:91], v[28:31]
	v_mfma_f32_16x16x32_f16 v[8:11], v[204:207], v[88:91], v[8:11]
	v_mfma_f32_16x16x32_f16 v[32:35], v[196:199], v[92:95], v[32:35]
	v_mfma_f32_16x16x32_f16 v[12:15], v[204:207], v[92:95], v[12:15]
	v_mfma_f32_16x16x32_f16 v[20:23], v[196:199], v[96:99], v[20:23]
	v_mfma_f32_16x16x32_f16 v[16:19], v[204:207], v[96:99], v[16:19]
	s_waitcnt vmcnt(3)
	v_mfma_f32_16x16x32_f16 v[24:27], v[200:203], v[212:215], v[24:27]
	v_mfma_f32_16x16x32_f16 v[4:7], v[208:211], v[212:215], v[4:7]
	s_waitcnt vmcnt(2)
	v_mfma_f32_16x16x32_f16 v[28:31], v[200:203], v[216:219], v[28:31]
	v_mfma_f32_16x16x32_f16 v[8:11], v[208:211], v[216:219], v[8:11]
	s_waitcnt vmcnt(1)
	v_mfma_f32_16x16x32_f16 v[32:35], v[200:203], v[220:223], v[32:35]
	v_mfma_f32_16x16x32_f16 v[12:15], v[208:211], v[220:223], v[12:15]
	s_waitcnt vmcnt(0)
	v_mfma_f32_16x16x32_f16 v[20:23], v[200:203], v[224:227], v[20:23]
	v_mfma_f32_16x16x32_f16 v[16:19], v[208:211], v[224:227], v[16:19]
	global_load_dwordx4 v[36:39], v[228:229], off
	v_add_u32_e32 v2, 0, v2
	v_and_b32_e32 v41, 0x1c0, v0
	v_lshl_add_u32 v43, v230, 13, v2
	v_lshl_add_u32 v2, v41, 4, v2
	v_lshl_add_u32 v40, v0, 4, 0
	ds_write_b128 v43, v[24:27]
	ds_write_b128 v43, v[4:7] offset:1024
	ds_write_b128 v43, v[28:31] offset:2048
	ds_write_b128 v43, v[8:11] offset:3072
	ds_write_b128 v43, v[32:35] offset:4096
	ds_write_b128 v43, v[12:15] offset:5120
	ds_write_b128 v43, v[20:23] offset:6144
	ds_write_b128 v43, v[16:19] offset:7168
	s_waitcnt lgkmcnt(0)
	s_barrier
	ds_read_b128 v[4:7], v2 offset:8192
	ds_read_b128 v[8:11], v2 offset:16384
	ds_read_b128 v[12:15], v2 offset:24576
	ds_read_b128 v[16:19], v40
	ds_read_b128 v[20:23], v2 offset:32768
	ds_read_b128 v[24:27], v2 offset:40960
	ds_read_b128 v[28:31], v2 offset:49152
	ds_read_b128 v[32:35], v2 offset:57344
	s_waitcnt lgkmcnt(4)
	v_pk_add_f32 v[4:5], v[16:17], v[4:5]
	v_pk_add_f32 v[6:7], v[18:19], v[6:7]
	v_pk_add_f32 v[4:5], v[4:5], v[8:9]
	v_pk_add_f32 v[6:7], v[6:7], v[10:11]
	v_pk_add_f32 v[4:5], v[4:5], v[12:13]
	v_pk_add_f32 v[6:7], v[6:7], v[14:15]
	s_waitcnt lgkmcnt(3)
	v_pk_add_f32 v[4:5], v[4:5], v[20:21]
	v_pk_add_f32 v[6:7], v[6:7], v[22:23]
	s_waitcnt lgkmcnt(2)
	v_pk_add_f32 v[4:5], v[4:5], v[24:25]
	v_pk_add_f32 v[6:7], v[6:7], v[26:27]
	s_waitcnt lgkmcnt(1)
	v_pk_add_f32 v[4:5], v[4:5], v[28:29]
	v_pk_add_f32 v[6:7], v[6:7], v[30:31]
	s_waitcnt lgkmcnt(0)
	v_pk_add_f32 v[4:5], v[4:5], v[32:33]
	v_pk_add_f32 v[6:7], v[6:7], v[34:35]
	v_lshrrev_b32_e32 v42, 7, v0
	s_waitcnt vmcnt(0)
	v_pk_add_f32 v[4:5], v[36:37], v[4:5]
	v_pk_add_f32 v[6:7], v[38:39], v[6:7]
	v_mul_f32_e32 v2, 0x3d372713, v4
	v_mul_f32_e32 v8, 0x3d372713, v5
	v_mul_f32_e32 v9, 0x3d372713, v6
	v_mul_f32_e32 v2, v4, v2
	v_mul_f32_e32 v8, v5, v8
	v_mul_f32_e32 v9, v6, v9
	v_fma_f32 v2, v4, v2, v4
	v_fma_f32 v8, v5, v8, v5
	v_fma_f32 v9, v6, v9, v6
	v_mul_f32_e32 v2, 0x3f4c422a, v2
	v_mul_f32_e32 v8, 0x3f4c422a, v8
	v_mul_f32_e32 v9, 0x3f4c422a, v9
	v_add_f32_e32 v2, v2, v2
	v_add_f32_e32 v8, v8, v8
	v_add_f32_e32 v9, v9, v9
	v_mul_f32_e32 v2, 0x3fb8aa3b, v2
	v_mul_f32_e32 v11, 0x3fb8aa3b, v8
	v_mul_f32_e32 v10, 0x3d372713, v7
	v_mul_f32_e32 v12, 0x3fb8aa3b, v9
	v_exp_f32_e32 v8, v2
	v_exp_f32_e32 v9, v11
	v_mul_f32_e32 v10, v7, v10
	v_fma_f32 v10, v7, v10, v7
	v_mul_f32_e32 v10, 0x3f4c422a, v10
	v_add_f32_e32 v10, v10, v10
	v_pk_add_f32 v[8:9], v[8:9], 1.0 op_sel_hi:[1,0]
	v_mul_f32_e32 v13, 0x3fb8aa3b, v10
	v_div_scale_f32 v2, s[0:1], v9, v9, 2.0
	v_exp_f32_e32 v10, v12
	v_exp_f32_e32 v11, v13
	v_div_scale_f32 v14, s[0:1], v8, v8, 2.0
	v_rcp_f32_e32 v16, v2
	v_rcp_f32_e32 v17, v14
	v_pk_add_f32 v[10:11], v[10:11], 1.0 op_sel_hi:[1,0]
	v_div_scale_f32 v13, vcc, 2.0, v9, 2.0
	v_fma_f32 v20, -v2, v16, 1.0
	v_div_scale_f32 v15, s[0:1], v11, v11, 2.0
	v_fma_f32 v21, -v14, v17, 1.0
	v_fmac_f32_e32 v16, v20, v16
	v_div_scale_f32 v19, s[0:1], 2.0, v8, 2.0
	v_fmac_f32_e32 v17, v21, v17
	v_mul_f32_e32 v20, v13, v16
	v_mul_f32_e32 v21, v19, v17
	v_fma_f32 v23, -v2, v20, v13
	v_fma_f32 v24, -v14, v21, v19
	v_fmac_f32_e32 v20, v23, v16
	v_fmac_f32_e32 v21, v24, v17
	v_fma_f32 v2, -v2, v20, v13
	v_rcp_f32_e32 v18, v15
	v_fma_f32 v13, -v14, v21, v19
	v_div_fmas_f32 v2, v2, v16, v20
	s_mov_b64 vcc, s[0:1]
	v_div_fixup_f32 v9, v2, v9, 2.0
	v_div_fmas_f32 v2, v13, v17, v21
	v_div_fixup_f32 v8, v2, v8, 2.0
	v_pk_add_f32 v[8:9], v[8:9], 1.0 op_sel_hi:[1,0] neg_lo:[1,0] neg_hi:[1,0]
	v_pk_mul_f32 v[4:5], v[4:5], 0.5 op_sel_hi:[1,0]
	v_fma_f32 v22, -v15, v18, 1.0
	v_pk_add_f32 v[8:9], v[8:9], 1.0 op_sel_hi:[1,0]
	v_fmac_f32_e32 v18, v22, v18
	v_pk_mul_f32 v[4:5], v[4:5], v[8:9]
	v_div_scale_f32 v2, vcc, 2.0, v11, 2.0
	v_cvt_pk_f16_f32 v4, v4, v5
	v_mul_f32_e32 v5, v2, v18
	v_fma_f32 v8, -v15, v5, v2
	v_fmac_f32_e32 v5, v8, v18
	v_div_scale_f32 v8, s[0:1], v10, v10, 2.0
	v_rcp_f32_e32 v13, v8
	v_fma_f32 v2, -v15, v5, v2
	v_div_fmas_f32 v2, v2, v18, v5
	v_div_fixup_f32 v9, v2, v11, 2.0
	v_fma_f32 v2, -v8, v13, 1.0
	v_fmac_f32_e32 v13, v2, v13
	v_div_scale_f32 v2, vcc, 2.0, v10, 2.0
	v_mul_f32_e32 v5, v2, v13
	v_fma_f32 v11, -v8, v5, v2
	v_fmac_f32_e32 v5, v11, v13
	v_fma_f32 v2, -v8, v5, v2
	v_div_fmas_f32 v2, v2, v13, v5
	v_div_fixup_f32 v8, v2, v10, 2.0
	v_pk_add_f32 v[8:9], v[8:9], 1.0 op_sel_hi:[1,0] neg_lo:[1,0] neg_hi:[1,0]
	s_lshl_b32 s0, s2, 3
	v_pk_mul_f32 v[6:7], v[6:7], 0.5 op_sel_hi:[1,0]
	v_pk_add_f32 v[8:9], v[8:9], 1.0 op_sel_hi:[1,0]
	s_add_i32 s0, s0, s12
	v_pk_mul_f32 v[6:7], v[6:7], v[8:9]
	v_or_b32_e32 v2, s0, v42
	v_cvt_pk_f16_f32 v5, v6, v7
	v_lshlrev_b64 v[6:7], 6, v[2:3]
	v_lshrrev_b32_e32 v2, 1, v0
	v_and_b32_e32 v12, 15, v0
	v_and_b32_e32 v0, 16, v2
	v_lshl_or_b32 v0, v1, 5, v0
	v_or3_b32 v6, v6, v0, v12
	v_lshl_add_u64 v[0:1], v[6:7], 4, s[10:11]
	v_and_b32_e32 v2, 8, v2
	v_lshl_add_u64 v[0:1], v[0:1], 0, v[2:3]
	global_store_dwordx2 v[0:1], v[4:5], off
	s_endpgm
	s_nop 0
	s_nop 0
	s_nop 0
	s_nop 0
	s_nop 0
	s_nop 0
	s_nop 0
	s_nop 0
	s_nop 0
	s_nop 0
	s_nop 0
	s_nop 0
	s_nop 0
	s_nop 0
	s_nop 0
	s_nop 0
	s_nop 0
	s_nop 0
	s_nop 0
	s_nop 0
	s_nop 0
	s_nop 0
	s_nop 0
	s_nop 0
	s_nop 0
	s_nop 0
	s_nop 0
	s_nop 0
	s_nop 0
	s_nop 0
	s_nop 0
	s_endpgm

	.amdhsa_kernel _ZN12_GLOBAL__N_110gemm_fullkILi0ELi3EEEvPKDF16_S2_PKfPDF16_PfS6_S4_S4_S4_S4_S4_S5_
		.amdhsa_group_segment_fixed_size 0
		.amdhsa_private_segment_fixed_size 0
		.amdhsa_kernarg_size 96
		.amdhsa_user_sgpr_count 2
		.amdhsa_user_sgpr_dispatch_ptr 0
		.amdhsa_user_sgpr_queue_ptr 0
		.amdhsa_user_sgpr_kernarg_segment_ptr 1
		.amdhsa_user_sgpr_dispatch_id 0
		.amdhsa_user_sgpr_kernarg_preload_length 0
		.amdhsa_user_sgpr_kernarg_preload_offset 0
		.amdhsa_user_sgpr_private_segment_size 0
		.amdhsa_uses_dynamic_stack 0
		.amdhsa_enable_private_segment 0
		.amdhsa_system_sgpr_workgroup_id_x 1
		.amdhsa_system_sgpr_workgroup_id_y 0
		.amdhsa_system_sgpr_workgroup_id_z 0
		.amdhsa_system_sgpr_workgroup_info 0
		.amdhsa_system_vgpr_workitem_id 0
		.amdhsa_next_free_vgpr 231
		.amdhsa_next_free_sgpr 14
		.amdhsa_accum_offset 232
		.amdhsa_reserve_vcc 1
		.amdhsa_float_round_mode_32 0
		.amdhsa_float_round_mode_16_64 0
		.amdhsa_float_denorm_mode_32 3
		.amdhsa_float_denorm_mode_16_64 3
		.amdhsa_dx10_clamp 1
		.amdhsa_ieee_mode 1
		.amdhsa_fp16_overflow 0
		.amdhsa_tg_split 0
		.amdhsa_exception_fp_ieee_invalid_op 0
		.amdhsa_exception_fp_denorm_src 0
		.amdhsa_exception_fp_ieee_div_zero 0
		.amdhsa_exception_fp_ieee_overflow 0
		.amdhsa_exception_fp_ieee_underflow 0
		.amdhsa_exception_fp_ieee_inexact 0
		.amdhsa_exception_int_div_zero 0
	.end_amdhsa_kernel

_ZN12_GLOBAL__N_110gemm_fullkILi1ELi3EEEvPKDF16_S2_PKfPDF16_PfS6_S4_S4_S4_S4_S4_S5_:
	s_load_dwordx2 s[4:5], s[0:1], 0x38
	s_and_b32 s3, s2, 63
	s_lshl_b32 s16, s3, 5
	s_lshl_b32 s6, s3, 13
	v_lshlrev_b32_e32 v1, 4, v0
	s_waitcnt lgkmcnt(0)
	s_add_u32 s4, s4, s6
	s_addc_u32 s5, s5, 0
	global_load_dwordx4 v[2:5], v1, s[4:5]
	v_lshlrev_b32_e32 v1, 2, v0
	v_cmp_lt_u32_e32 vcc, 31, v0
	s_and_saveexec_b64 s[4:5], vcc
	s_xor_b64 s[4:5], exec, s[4:5]
	s_cbranch_execz .LBB15_10
	v_cmp_lt_u32_e32 vcc, 63, v0
	s_and_saveexec_b64 s[6:7], vcc
	s_xor_b64 s[6:7], exec, s[6:7]
	s_cbranch_execz .LBB15_7
	s_movk_i32 s8, 0x47
	v_cmp_lt_u32_e32 vcc, s8, v0
	s_and_saveexec_b64 s[8:9], vcc
	s_xor_b64 s[8:9], exec, s[8:9]
	s_cbranch_execz .LBB15_4
	s_load_dwordx2 s[10:11], s[0:1], 0x10
	s_lshl_b32 s12, s16, 2
	v_lshlrev_b32_e32 v6, 2, v1
	v_mov_b32_e32 v7, 0
	s_movk_i32 s14, 0x50
	s_waitcnt lgkmcnt(0)
	s_add_u32 s10, s10, s12
	s_addc_u32 s11, s11, 0
	s_movk_i32 s12, 0xfb80
	v_lshl_add_u64 v[6:7], s[10:11], 0, v[6:7]
	s_mov_b32 s13, -1
	v_lshl_add_u64 v[6:7], v[6:7], 0, s[12:13]
	v_mov_b32_e32 v8, s11
	v_cmp_gt_u32_e32 vcc, s14, v0
	s_nop 1
	v_cndmask_b32_e32 v7, v8, v7, vcc
	v_mov_b32_e32 v8, s10
	v_cndmask_b32_e32 v6, v8, v6, vcc

.LBB15_12:
	s_or_b64 exec, exec, s[14:15]
	v_lshrrev_b32_e32 v178, 6, v0
	s_lshr_b32 s0, s2, 5
	s_and_b32 s0, s0, 0x7fffffe
	s_mov_b32 s1, 0
	v_lshlrev_b32_e32 v8, 17, v178
	v_mov_b32_e32 v9, 0
	v_and_b32_e32 v14, 63, v0
	s_lshl_b64 s[14:15], s[0:1], 10
	v_lshlrev_b32_e32 v10, 14, v178
	s_waitcnt lgkmcnt(0)
	v_lshl_add_u64 v[12:13], s[8:9], 0, v[8:9]
	v_lshl_or_b32 v10, s3, 18, v10
	v_mov_b32_e32 v11, v9
	v_lshl_add_u64 v[12:13], v[12:13], 0, s[14:15]
	v_lshlrev_b32_e32 v8, 4, v14
	v_lshl_add_u64 v[10:11], s[10:11], 0, v[10:11]
	v_lshl_add_u64 v[22:23], v[12:13], 0, v[8:9]
	v_lshrrev_b32_e32 v12, 2, v0
	v_lshl_add_u64 v[174:175], v[10:11], 0, v[8:9]
	v_lshrrev_b32_e32 v10, 8, v0
	v_lshrrev_b32_e32 v11, 3, v0
	v_and_b32_e32 v12, 12, v12
	v_and_b32_e32 v24, 15, v0
	v_bfe_u32 v28, v0, 6, 1
	v_or_b32_e32 v26, s0, v10
	v_and_or_b32 v27, v11, 16, v12
	v_lshl_or_b32 v10, v26, 4, v24
	v_lshl_or_b32 v25, v28, 1, v27
	v_mov_b32_e32 v11, v9
	v_or_b32_e32 v14, s16, v25
	v_lshlrev_b64 v[12:13], 13, v[10:11]
	v_lshl_add_u64 v[10:11], s[4:5], 0, v[12:13]
	v_lshlrev_b32_e32 v14, 2, v14
	v_mov_b32_e32 v15, v9
	v_lshl_add_u64 v[10:11], v[10:11], 0, v[14:15]
	s_mov_b32 s2, 0x300000
	v_add_co_u32_e32 v16, vcc, s2, v10
	v_lshl_add_u64 v[12:13], s[6:7], 0, v[12:13]
	s_nop 0
	v_addc_co_u32_e32 v17, vcc, 0, v11, vcc
	v_lshl_add_u64 v[20:21], v[12:13], 0, v[14:15]
	s_mov_b32 s0, 0x100000
	v_add_co_u32_e32 v30, vcc, s0, v20
	s_mov_b32 s0, 0x200000
	s_nop 0
	v_addc_co_u32_e32 v31, vcc, 0, v21, vcc
	v_add_co_u32_e32 v32, vcc, s0, v20
	s_mov_b32 s0, 0x20000
	s_nop 0
	v_addc_co_u32_e32 v33, vcc, 0, v21, vcc
	v_add_co_u32_e32 v82, vcc, s0, v174
	s_mov_b32 s0, 0x21000
	s_nop 0
	v_addc_co_u32_e32 v83, vcc, 0, v175, vcc
	v_add_co_u32_e32 v146, vcc, s0, v174
	s_movk_i32 s0, 0x2000
	s_nop 0
	v_addc_co_u32_e32 v147, vcc, 0, v175, vcc
	v_add_co_u32_e32 v62, vcc, s0, v22
	s_movk_i32 s1, 0x4000
	s_nop 0
	v_addc_co_u32_e32 v63, vcc, 0, v23, vcc
	v_add_co_u32_e32 v84, vcc, s1, v22
	s_movk_i32 s1, 0x6000
	s_nop 0
	v_addc_co_u32_e32 v85, vcc, 0, v23, vcc
	v_add_co_u32_e32 v90, vcc, s1, v22
	s_movk_i32 s1, 0x1000
	s_nop 0
	v_addc_co_u32_e32 v91, vcc, 0, v23, vcc
	v_add_co_u32_e32 v138, vcc, s1, v174
	global_load_dwordx2 v[18:19], v[16:17], off
	s_nop 0
	v_addc_co_u32_e32 v139, vcc, 0, v175, vcc
	v_add_co_u32_e32 v162, vcc, s0, v174
	s_mov_b32 s0, 0x8000
	s_nop 0
	v_addc_co_u32_e32 v163, vcc, 0, v175, vcc
	v_add_co_u32_e32 v106, vcc, s0, v22
	s_mov_b32 s0, 0xa000
	s_nop 0
	v_addc_co_u32_e32 v107, vcc, 0, v23, vcc
	v_add_co_u32_e32 v118, vcc, s0, v22
	s_mov_b32 s0, 0xc000
	s_nop 0
	v_addc_co_u32_e32 v119, vcc, 0, v23, vcc
	global_load_dwordx2 v[14:15], v[20:21], off
	global_load_dwordx2 v[12:13], v[30:31], off
	global_load_dwordx2 v[16:17], v[32:33], off
	s_nop 0
	global_load_dwordx4 v[30:33], v[22:23], off
	global_load_dwordx4 v[34:37], v[22:23], off offset:1024
	global_load_dwordx4 v[38:41], v[174:175], off
	global_load_dwordx4 v[42:45], v[174:175], off offset:1024
	global_load_dwordx4 v[46:49], v[62:63], off
	global_load_dwordx4 v[50:53], v[62:63], off offset:1024
	global_load_dwordx4 v[54:57], v[82:83], off offset:1024
	global_load_dwordx4 v[58:61], v[82:83], off offset:2048
	s_nop 0
	global_load_dwordx4 v[62:65], v[84:85], off
	global_load_dwordx4 v[66:69], v[84:85], off offset:1024
	global_load_dwordx4 v[70:73], v[174:175], off offset:2048
	global_load_dwordx4 v[74:77], v[174:175], off offset:3072
	global_load_dwordx4 v[78:81], v[82:83], off offset:3072
	s_nop 0
	global_load_dwordx4 v[82:85], v[90:91], off
	global_load_dwordx4 v[86:89], v[90:91], off offset:1024
	s_nop 0
	global_load_dwordx4 v[90:93], v[146:147], off offset:-4096
	global_load_dwordx4 v[94:97], v[146:147], off
	global_load_dwordx4 v[98:101], v[106:107], off
	global_load_dwordx4 v[102:105], v[106:107], off offset:1024
	s_nop 0
	global_load_dwordx4 v[106:109], v[118:119], off
	global_load_dwordx4 v[110:113], v[118:119], off offset:1024
	global_load_dwordx4 v[114:117], v[138:139], off offset:1024
	s_nop 0
	global_load_dwordx4 v[118:121], v[138:139], off offset:2048
	global_load_dwordx4 v[122:125], v[146:147], off offset:1024
	global_load_dwordx4 v[126:129], v[146:147], off offset:2048
	v_add_co_u32_e32 v134, vcc, s0, v22
	s_mov_b32 s0, 0xe000
	s_nop 0
	v_addc_co_u32_e32 v135, vcc, 0, v23, vcc
	global_load_dwordx4 v[130:133], v[134:135], off
	s_nop 0
	global_load_dwordx4 v[134:137], v[134:135], off offset:1024
	s_nop 0
	global_load_dwordx4 v[138:141], v[138:139], off offset:3072
	s_nop 0
	global_load_dwordx4 v[142:145], v[162:163], off offset:-4096
	s_nop 0
	global_load_dwordx4 v[146:149], v[146:147], off offset:3072
	v_add_co_u32_e32 v154, vcc, s0, v22
	v_lshrrev_b32_e32 v29, 7, v0
	s_nop 0
	v_addc_co_u32_e32 v155, vcc, 0, v23, vcc
	global_load_dwordx4 v[150:153], v[154:155], off
	s_nop 0
	global_load_dwordx4 v[154:157], v[154:155], off offset:1024
	s_waitcnt vmcnt(29)
	v_mfma_f32_16x16x32_f16 v[158:161], v[38:41], v[30:33], 0
	s_waitcnt vmcnt(16)
	v_mfma_f32_16x16x32_f16 v[30:33], v[90:93], v[30:33], 0
	v_mfma_f32_16x16x32_f16 v[38:41], v[38:41], v[34:37], 0
	v_mfma_f32_16x16x32_f16 v[34:37], v[90:93], v[34:37], 0
	v_mfma_f32_16x16x32_f16 v[90:93], v[42:45], v[46:49], v[158:161]
	v_mfma_f32_16x16x32_f16 v[30:33], v[54:57], v[46:49], v[30:33]
	v_mfma_f32_16x16x32_f16 v[38:41], v[42:45], v[50:53], v[38:41]
	v_mfma_f32_16x16x32_f16 v[34:37], v[54:57], v[50:53], v[34:37]
	v_mfma_f32_16x16x32_f16 v[42:45], v[70:73], v[62:65], v[90:93]
	v_mfma_f32_16x16x32_f16 v[30:33], v[58:61], v[62:65], v[30:33]
	v_mfma_f32_16x16x32_f16 v[38:41], v[70:73], v[66:69], v[38:41]
	v_mfma_f32_16x16x32_f16 v[34:37], v[58:61], v[66:69], v[34:37]
	v_mfma_f32_16x16x32_f16 v[42:45], v[74:77], v[82:85], v[42:45]
	v_mfma_f32_16x16x32_f16 v[30:33], v[78:81], v[82:85], v[30:33]
	v_mfma_f32_16x16x32_f16 v[38:41], v[74:77], v[86:89], v[38:41]
	v_mfma_f32_16x16x32_f16 v[34:37], v[78:81], v[86:89], v[34:37]
	s_mov_b32 s0, 0x22000
	v_add_co_u32_e32 v164, vcc, s0, v174
	s_mov_b32 s0, 0x23000
	s_nop 0
	v_addc_co_u32_e32 v165, vcc, 0, v175, vcc
	v_add_co_u32_e32 v176, vcc, s0, v174
	s_mov_b32 s0, 0x10000
	s_nop 0
	v_addc_co_u32_e32 v177, vcc, 0, v175, vcc
	v_add_co_u32_e32 v54, vcc, s0, v22
	s_mov_b32 s0, 0x12000
	s_nop 0
	v_addc_co_u32_e32 v55, vcc, 0, v23, vcc
	v_add_co_u32_e32 v70, vcc, s0, v22
	s_mov_b32 s0, 0x14000
	s_nop 0
	v_addc_co_u32_e32 v71, vcc, 0, v23, vcc
	v_add_co_u32_e32 v86, vcc, s0, v22
	global_load_dwordx4 v[46:49], v[176:177], off offset:-4096
	s_nop 0
	v_addc_co_u32_e32 v87, vcc, 0, v23, vcc
	global_load_dwordx4 v[50:53], v[54:55], off
	s_nop 0
	global_load_dwordx4 v[54:57], v[54:55], off offset:1024
	s_nop 0
	global_load_dwordx4 v[58:61], v[162:163], off
	global_load_dwordx4 v[62:65], v[162:163], off offset:1024
	global_load_dwordx4 v[66:69], v[70:71], off
	s_nop 0
	global_load_dwordx4 v[70:73], v[70:71], off offset:1024
	s_nop 0
	global_load_dwordx4 v[74:77], v[164:165], off offset:1024
	global_load_dwordx4 v[78:81], v[164:165], off offset:2048
	global_load_dwordx4 v[82:85], v[86:87], off
	s_nop 0
	global_load_dwordx4 v[86:89], v[86:87], off offset:1024
	s_nop 0
	global_load_dwordx4 v[90:93], v[162:163], off offset:2048
	global_load_dwordx4 v[158:161], v[162:163], off offset:3072
	s_nop 0
	global_load_dwordx4 v[162:165], v[164:165], off offset:3072
	s_mov_b32 s0, 0x16000
	v_add_co_u32_e32 v170, vcc, s0, v22
	s_nop 1
	v_addc_co_u32_e32 v171, vcc, 0, v23, vcc
	global_load_dwordx4 v[166:169], v[170:171], off
	s_nop 0
	global_load_dwordx4 v[170:173], v[170:171], off offset:1024
	s_waitcnt vmcnt(19)
	v_mfma_f32_16x16x32_f16 v[42:45], v[142:145], v[98:101], v[42:45]
	v_mfma_f32_16x16x32_f16 v[30:33], v[94:97], v[98:101], v[30:33]
	v_mfma_f32_16x16x32_f16 v[38:41], v[142:145], v[102:105], v[38:41]
	v_mfma_f32_16x16x32_f16 v[34:37], v[94:97], v[102:105], v[34:37]
	v_mfma_f32_16x16x32_f16 v[42:45], v[114:117], v[106:109], v[42:45]
	v_mfma_f32_16x16x32_f16 v[30:33], v[122:125], v[106:109], v[30:33]
	v_mfma_f32_16x16x32_f16 v[38:41], v[114:117], v[110:113], v[38:41]
	v_mfma_f32_16x16x32_f16 v[34:37], v[122:125], v[110:113], v[34:37]
	v_mfma_f32_16x16x32_f16 v[42:45], v[118:121], v[130:133], v[42:45]
	v_mfma_f32_16x16x32_f16 v[30:33], v[126:129], v[130:133], v[30:33]
	v_mfma_f32_16x16x32_f16 v[38:41], v[118:121], v[134:137], v[38:41]
	v_mfma_f32_16x16x32_f16 v[34:37], v[126:129], v[134:137], v[34:37]
	s_waitcnt vmcnt(17)
	v_mfma_f32_16x16x32_f16 v[42:45], v[138:141], v[150:153], v[42:45]
	v_mfma_f32_16x16x32_f16 v[30:33], v[146:149], v[150:153], v[30:33]
	s_waitcnt vmcnt(16)
	v_mfma_f32_16x16x32_f16 v[38:41], v[138:141], v[154:157], v[38:41]
	v_mfma_f32_16x16x32_f16 v[34:37], v[146:149], v[154:157], v[34:37]
	s_movk_i32 s0, 0x3000
	v_add_co_u32_e32 v138, vcc, s0, v174
	s_mov_b32 s0, 0x18000
	s_nop 0
	v_addc_co_u32_e32 v139, vcc, 0, v175, vcc
	v_add_co_u32_e32 v98, vcc, s0, v22
	s_mov_b32 s0, 0x1a000
	s_nop 0
	v_addc_co_u32_e32 v99, vcc, 0, v23, vcc
	v_add_co_u32_e32 v122, vcc, s0, v22
	s_mov_b32 s0, 0x1c000
	s_nop 0
	v_addc_co_u32_e32 v123, vcc, 0, v23, vcc
	v_add_co_u32_e32 v130, vcc, s0, v22
	global_load_dwordx4 v[94:97], v[98:99], off
	s_nop 0
	global_load_dwordx4 v[98:101], v[98:99], off offset:1024
	s_nop 0
	global_load_dwordx4 v[102:105], v[138:139], off
	global_load_dwordx4 v[106:109], v[138:139], off offset:1024
	global_load_dwordx4 v[110:113], v[176:177], off
	global_load_dwordx4 v[114:117], v[176:177], off offset:1024
	v_addc_co_u32_e32 v131, vcc, 0, v23, vcc
	global_load_dwordx4 v[118:121], v[122:123], off
	s_nop 0
	global_load_dwordx4 v[122:125], v[122:123], off offset:1024
	s_nop 0
	global_load_dwordx4 v[126:129], v[130:131], off
	s_nop 0
	global_load_dwordx4 v[130:133], v[130:131], off offset:1024
	s_nop 0
	global_load_dwordx4 v[134:137], v[138:139], off offset:2048
	s_nop 0
	global_load_dwordx4 v[138:141], v[138:139], off offset:3072
	s_nop 0
	global_load_dwordx4 v[142:145], v[176:177], off offset:2048
	global_load_dwordx4 v[146:149], v[176:177], off offset:3072
	s_mov_b32 s0, 0x1e000
	v_add_co_u32_e32 v22, vcc, s0, v22
	s_nop 1
	v_addc_co_u32_e32 v23, vcc, 0, v23, vcc
	global_load_dwordx4 v[150:153], v[22:23], off
	global_load_dwordx4 v[154:157], v[22:23], off offset:1024
	s_waitcnt vmcnt(28)
	v_mfma_f32_16x16x32_f16 v[42:45], v[58:61], v[50:53], v[42:45]
	v_mfma_f32_16x16x32_f16 v[30:33], v[46:49], v[50:53], v[30:33]
	v_mfma_f32_16x16x32_f16 v[38:41], v[58:61], v[54:57], v[38:41]
	v_mfma_f32_16x16x32_f16 v[34:37], v[46:49], v[54:57], v[34:37]
	s_waitcnt vmcnt(26)
	v_mfma_f32_16x16x32_f16 v[42:45], v[62:65], v[66:69], v[42:45]
	s_waitcnt vmcnt(24)
	v_mfma_f32_16x16x32_f16 v[30:33], v[74:77], v[66:69], v[30:33]
	v_mfma_f32_16x16x32_f16 v[38:41], v[62:65], v[70:73], v[38:41]
	v_mfma_f32_16x16x32_f16 v[34:37], v[74:77], v[70:73], v[34:37]
	s_waitcnt vmcnt(20)
	v_mfma_f32_16x16x32_f16 v[42:45], v[90:93], v[82:85], v[42:45]
	v_mfma_f32_16x16x32_f16 v[30:33], v[78:81], v[82:85], v[30:33]
	v_mfma_f32_16x16x32_f16 v[38:41], v[90:93], v[86:89], v[38:41]
	v_mfma_f32_16x16x32_f16 v[34:37], v[78:81], v[86:89], v[34:37]
	s_waitcnt vmcnt(17)
	v_mfma_f32_16x16x32_f16 v[42:45], v[158:161], v[166:169], v[42:45]
	v_mfma_f32_16x16x32_f16 v[30:33], v[162:165], v[166:169], v[30:33]
	s_waitcnt vmcnt(16)
	v_mfma_f32_16x16x32_f16 v[38:41], v[158:161], v[170:173], v[38:41]
	v_mfma_f32_16x16x32_f16 v[34:37], v[162:165], v[170:173], v[34:37]
	s_waitcnt vmcnt(13)
	v_mfma_f32_16x16x32_f16 v[42:45], v[102:105], v[94:97], v[42:45]
	s_waitcnt vmcnt(11)
	v_mfma_f32_16x16x32_f16 v[30:33], v[110:113], v[94:97], v[30:33]
	v_mfma_f32_16x16x32_f16 v[38:41], v[102:105], v[98:101], v[38:41]
	v_mfma_f32_16x16x32_f16 v[34:37], v[110:113], v[98:101], v[34:37]
	s_waitcnt vmcnt(9)
	v_mfma_f32_16x16x32_f16 v[42:45], v[106:109], v[118:121], v[42:45]
	v_mfma_f32_16x16x32_f16 v[30:33], v[114:117], v[118:121], v[30:33]
	s_waitcnt vmcnt(8)
	v_mfma_f32_16x16x32_f16 v[38:41], v[106:109], v[122:125], v[38:41]
	v_mfma_f32_16x16x32_f16 v[34:37], v[114:117], v[122:125], v[34:37]
	s_waitcnt vmcnt(5)
	v_mfma_f32_16x16x32_f16 v[42:45], v[134:137], v[126:129], v[42:45]
	s_waitcnt vmcnt(3)
	v_mfma_f32_16x16x32_f16 v[30:33], v[142:145], v[126:129], v[30:33]
	v_mfma_f32_16x16x32_f16 v[38:41], v[134:137], v[130:133], v[38:41]
	v_mfma_f32_16x16x32_f16 v[34:37], v[142:145], v[130:133], v[34:37]
	s_waitcnt vmcnt(1)
	v_mfma_f32_16x16x32_f16 v[42:45], v[138:141], v[150:153], v[42:45]
	v_mfma_f32_16x16x32_f16 v[30:33], v[146:149], v[150:153], v[30:33]
	s_waitcnt vmcnt(0)
	v_mfma_f32_16x16x32_f16 v[38:41], v[138:141], v[154:157], v[38:41]
	v_mfma_f32_16x16x32_f16 v[34:37], v[146:149], v[154:157], v[34:37]
	v_lshlrev_b32_e32 v22, 12, v178
	v_add3_u32 v22, 0, v8, v22
	s_nop 1
	ds_write_b128 v22, v[42:45]
	ds_write_b128 v22, v[30:33] offset:1024
	s_nop 0
	ds_write_b128 v22, v[38:41] offset:2048
	ds_write_b128 v22, v[34:37] offset:3072
	v_lshrrev_b32_e32 v22, 4, v0
	v_and_b32_e32 v23, 60, v1
	v_mul_u32_u24_e32 v22, 0x110, v22
	v_lshlrev_b32_e32 v23, 2, v23
	s_movk_i32 s0, 0x50
	v_add3_u32 v22, 0, v22, v23
	v_cmp_gt_u32_e32 vcc, s0, v0
	ds_write_b128 v22, v[2:5] offset:32768
	s_and_saveexec_b64 s[0:1], vcc
	s_cbranch_execz .LBB15_14
	global_load_dwordx4 v[2:5], v[6:7], off
	v_lshl_add_u32 v0, v1, 2, 0
	s_waitcnt vmcnt(0)
	ds_write_b128 v0, v[2:5] offset:41472
.LBB15_14:
	s_or_b64 exec, exec, s[0:1]
	v_lshlrev_b32_e32 v0, 10, v29
	v_add3_u32 v8, 0, v0, v8
	s_waitcnt lgkmcnt(0)
	s_barrier
	ds_read_b128 v[0:3], v8
	ds_read_b128 v[4:7], v8 offset:4096
	ds_read_b128 v[30:33], v8 offset:8192
	ds_read_b128 v[34:37], v8 offset:12288
	v_cmp_eq_u32_e32 vcc, 0, v28
	s_waitcnt lgkmcnt(2)
	v_pk_add_f32 v[2:3], v[2:3], v[6:7]
	v_pk_add_f32 v[4:5], v[0:1], v[4:5]
	s_waitcnt lgkmcnt(1)
	v_pk_add_f32 v[6:7], v[2:3], v[32:33]
	ds_read_b128 v[0:3], v8 offset:16384
	v_pk_add_f32 v[4:5], v[4:5], v[30:31]
	s_waitcnt lgkmcnt(1)
	v_pk_add_f32 v[22:23], v[6:7], v[36:37]
	v_pk_add_f32 v[34:35], v[4:5], v[34:35]
	ds_read_b128 v[4:7], v8 offset:20480
	ds_read_b128 v[30:33], v8 offset:24576
	s_waitcnt lgkmcnt(2)
	v_pk_add_f32 v[22:23], v[22:23], v[2:3]
	v_pk_add_f32 v[34:35], v[34:35], v[0:1]
	ds_read_b128 v[0:3], v8 offset:28672
	s_waitcnt lgkmcnt(2)
	v_pk_add_f32 v[6:7], v[22:23], v[6:7]
	v_pk_add_f32 v[4:5], v[34:35], v[4:5]
	s_waitcnt lgkmcnt(1)
	v_pk_add_f32 v[6:7], v[6:7], v[32:33]
	v_pk_add_f32 v[4:5], v[4:5], v[30:31]
	s_waitcnt lgkmcnt(0)
	v_pk_add_f32 v[2:3], v[6:7], v[2:3]
	v_lshl_add_u32 v6, v25, 2, 0
	v_pk_add_f32 v[0:1], v[4:5], v[0:1]
	ds_read_b64 v[4:5], v6 offset:42624
	v_cndmask_b32_e32 v1, v3, v1, vcc
	v_cndmask_b32_e32 v0, v2, v0, vcc
	v_mad_u32_u24 v2, v25, 12, v6
	ds_read_b128 v[28:31], v2 offset:41472
	s_waitcnt lgkmcnt(1)
	v_pk_add_f32 v[0:1], v[0:1], v[4:5]
	s_nop 0
	v_pk_add_f32 v[64:65], v[18:19], v[0:1]
	v_add_co_u32_e32 v0, vcc, s2, v20
	s_nop 1
	v_addc_co_u32_e32 v1, vcc, 0, v21, vcc
	global_store_dwordx2 v[0:1], v[64:65], off
	v_lshl_add_u32 v0, v25, 8, v2
	ds_read_b128 v[20:23], v0 offset:32960
	ds_read_b128 v[32:35], v0 offset:32976
	ds_read_b128 v[36:39], v0 offset:32992
	v_mad_i32_i24 v1, v25, -12, v2
	ds_read_b128 v[40:43], v0 offset:33008
	ds_read_b64 v[18:19], v1 offset:42496
	v_or_b32_e32 v0, 1, v25
	v_lshl_add_u32 v4, v0, 4, 0
	v_lshl_add_u32 v0, v0, 8, v4
	ds_read_b128 v[44:47], v0 offset:32960
	ds_read_b128 v[48:51], v0 offset:32976
	ds_read_b128 v[52:55], v0 offset:32992
	ds_read_b128 v[56:59], v0 offset:33008
	ds_read_b128 v[0:3], v2 offset:41984
	ds_read_b128 v[60:63], v4 offset:41472
	s_waitcnt lgkmcnt(10)
	v_mov_b32_e32 v66, v20
	s_waitcnt lgkmcnt(5)
	v_mov_b32_e32 v67, v44
	v_mov_b32_e32 v44, v21
	v_mov_b32_e32 v20, v28
	s_waitcnt lgkmcnt(0)
	v_mov_b32_e32 v21, v60
	v_pk_fma_f32 v[20:21], v[14:15], v[66:67], v[20:21]
	v_mov_b32_e32 v66, v32
	v_mov_b32_e32 v67, v48
	v_pk_fma_f32 v[20:21], v[12:13], v[66:67], v[20:21]
	v_mov_b32_e32 v66, v36
	v_mov_b32_e32 v67, v52
	v_pk_fma_f32 v[20:21], v[16:17], v[66:67], v[20:21]
	v_mov_b32_e32 v66, v40
	v_mov_b32_e32 v67, v56
	v_pk_fma_f32 v[20:21], v[64:65], v[66:67], v[20:21]
	v_mov_b32_e32 v60, v29
	v_mul_f32_e32 v8, 0x3d372713, v20
	v_mul_f32_e32 v8, v20, v8
	v_fma_f32 v8, v20, v8, v20
	v_pk_fma_f32 v[44:45], v[14:15], v[44:45], v[60:61]
	v_mov_b32_e32 v48, v33
	v_mul_f32_e32 v8, 0x3f4c422a, v8
	v_pk_fma_f32 v[32:33], v[12:13], v[48:49], v[44:45]
	v_mov_b32_e32 v52, v37
	v_add_f32_e32 v8, v8, v8
	v_pk_fma_f32 v[32:33], v[16:17], v[52:53], v[32:33]
	v_mov_b32_e32 v56, v41
	v_mul_f32_e32 v8, 0x3fb8aa3b, v8
	v_pk_fma_f32 v[32:33], v[64:65], v[56:57], v[32:33]
	v_exp_f32_e32 v28, v8
	v_mul_f32_e32 v8, 0x3d372713, v32
	v_mov_b32_e32 v40, v22
	v_mov_b32_e32 v41, v46
	v_mov_b32_e32 v44, v30
	v_mov_b32_e32 v45, v62
	v_mov_b32_e32 v46, v23
	v_mov_b32_e32 v62, v31
	v_mul_f32_e32 v8, v32, v8
	v_pk_fma_f32 v[40:41], v[14:15], v[40:41], v[44:45]
	v_mov_b32_e32 v44, v34
	v_mov_b32_e32 v45, v50
	v_pk_fma_f32 v[14:15], v[14:15], v[46:47], v[62:63]
	v_mov_b32_e32 v50, v35
	v_fma_f32 v8, v32, v8, v32
	v_pk_fma_f32 v[40:41], v[12:13], v[44:45], v[40:41]
	v_pk_fma_f32 v[12:13], v[12:13], v[50:51], v[14:15]
	v_mul_f32_e32 v14, 0x3d372713, v21
	v_mul_f32_e32 v8, 0x3f4c422a, v8
	v_mov_b32_e32 v44, v38
	v_mov_b32_e32 v45, v54
	v_mul_f32_e32 v14, v21, v14
	v_add_f32_e32 v8, v8, v8
	v_pk_fma_f32 v[40:41], v[16:17], v[44:45], v[40:41]
	v_mov_b32_e32 v44, v42
	v_mov_b32_e32 v45, v58
	v_fma_f32 v14, v21, v14, v21
	v_mul_f32_e32 v8, 0x3fb8aa3b, v8
	v_pk_fma_f32 v[40:41], v[64:65], v[44:45], v[40:41]
	v_mul_f32_e32 v14, 0x3f4c422a, v14
	v_exp_f32_e32 v36, v8
	v_mul_f32_e32 v8, 0x3d372713, v40
	v_add_f32_e32 v14, v14, v14
	v_mul_f32_e32 v8, v40, v8
	v_mul_f32_e32 v14, 0x3fb8aa3b, v14
	v_fma_f32 v8, v40, v8, v40
	v_exp_f32_e32 v29, v14
	v_mul_f32_e32 v8, 0x3f4c422a, v8
	v_mov_b32_e32 v54, v39
	v_add_f32_e32 v8, v8, v8
	v_pk_fma_f32 v[12:13], v[16:17], v[54:55], v[12:13]
	v_mov_b32_e32 v58, v43
	v_mul_f32_e32 v8, 0x3fb8aa3b, v8
	v_pk_fma_f32 v[12:13], v[64:65], v[58:59], v[12:13]
	v_exp_f32_e32 v22, v8
	v_mul_f32_e32 v8, 0x3d372713, v12
	v_pk_add_f32 v[14:15], v[28:29], 1.0 op_sel_hi:[1,0]
	v_mul_f32_e32 v8, v12, v8
	v_div_scale_f32 v17, s[0:1], v15, v15, 2.0
	v_fma_f32 v8, v12, v8, v12
	v_rcp_f32_e32 v23, v17
	v_mul_f32_e32 v8, 0x3f4c422a, v8
	v_add_f32_e32 v8, v8, v8
	v_mul_f32_e32 v8, 0x3fb8aa3b, v8
	v_exp_f32_e32 v16, v8
	v_fma_f32 v8, -v17, v23, 1.0
	v_fmac_f32_e32 v23, v8, v23
	v_div_scale_f32 v8, vcc, 2.0, v15, 2.0
	v_mul_f32_e32 v28, v8, v23
	v_fma_f32 v29, -v17, v28, v8
	v_fmac_f32_e32 v28, v29, v23
	v_fma_f32 v8, -v17, v28, v8
	v_div_scale_f32 v17, s[0:1], v14, v14, 2.0
	v_rcp_f32_e32 v29, v17
	v_div_fmas_f32 v8, v8, v23, v28
	v_div_fixup_f32 v15, v8, v15, 2.0
	ds_read_b128 v[4:7], v4 offset:41984
	v_fma_f32 v8, -v17, v29, 1.0
	v_fmac_f32_e32 v29, v8, v29
	v_div_scale_f32 v8, vcc, 2.0, v14, 2.0
	v_mul_f32_e32 v23, v8, v29
	v_fma_f32 v28, -v17, v23, v8
	v_fmac_f32_e32 v23, v28, v29
	v_fma_f32 v8, -v17, v23, v8
	v_div_fmas_f32 v8, v8, v29, v23
	v_div_fixup_f32 v14, v8, v14, 2.0
	v_mul_f32_e32 v8, 0x3d372713, v33
	v_mul_f32_e32 v8, v33, v8
	v_fma_f32 v8, v33, v8, v33
	v_mul_f32_e32 v8, 0x3f4c422a, v8
	v_add_f32_e32 v8, v8, v8
	v_mul_f32_e32 v8, 0x3fb8aa3b, v8
	v_exp_f32_e32 v37, v8
	v_pk_add_f32 v[14:15], v[14:15], 1.0 op_sel_hi:[1,0] neg_lo:[1,0] neg_hi:[1,0]
	v_pk_mul_f32 v[20:21], v[20:21], 0.5 op_sel_hi:[1,0]
	v_pk_add_f32 v[14:15], v[14:15], 1.0 op_sel_hi:[1,0]
	v_pk_add_f32 v[28:29], v[36:37], 1.0 op_sel_hi:[1,0]
	v_pk_mul_f32 v[14:15], v[20:21], v[14:15]
	v_div_scale_f32 v8, s[0:1], v29, v29, 2.0
	v_rcp_f32_e32 v17, v8
	v_mov_b32_e32 v20, v0
	s_waitcnt lgkmcnt(0)
	v_mov_b32_e32 v21, v4
	v_pk_mul_f32 v[30:31], v[32:33], 0.5 op_sel_hi:[1,0]
	v_fma_f32 v0, -v8, v17, 1.0
	v_fmac_f32_e32 v17, v0, v17
	v_div_scale_f32 v0, vcc, 2.0, v29, 2.0
	v_mul_f32_e32 v4, v0, v17
	v_fma_f32 v23, -v8, v4, v0
	v_fmac_f32_e32 v4, v23, v17
	v_fma_f32 v0, -v8, v4, v0
	v_div_scale_f32 v8, s[0:1], v28, v28, 2.0
	v_rcp_f32_e32 v23, v8
	v_div_fmas_f32 v0, v0, v17, v4
	v_div_fixup_f32 v29, v0, v29, 2.0
	v_fma_f32 v0, -v8, v23, 1.0
	v_fmac_f32_e32 v23, v0, v23
	v_div_scale_f32 v0, vcc, 2.0, v28, 2.0
	v_mul_f32_e32 v4, v0, v23
	v_fma_f32 v17, -v8, v4, v0
	v_fmac_f32_e32 v4, v17, v23
	v_fma_f32 v0, -v8, v4, v0
	v_div_fmas_f32 v0, v0, v23, v4
	v_div_fixup_f32 v28, v0, v28, 2.0
	v_mul_f32_e32 v0, 0x3d372713, v41
	v_mul_f32_e32 v0, v41, v0
	v_fma_f32 v0, v41, v0, v41
	v_mul_f32_e32 v0, 0x3f4c422a, v0
	v_add_f32_e32 v0, v0, v0
	v_mul_f32_e32 v0, 0x3fb8aa3b, v0
	v_exp_f32_e32 v23, v0
	v_pk_add_f32 v[28:29], v[28:29], 1.0 op_sel_hi:[1,0] neg_lo:[1,0] neg_hi:[1,0]
	v_mov_b32_e32 v4, v1
	v_pk_add_f32 v[28:29], v[28:29], 1.0 op_sel_hi:[1,0]
	v_pk_add_f32 v[22:23], v[22:23], 1.0 op_sel_hi:[1,0]
	v_pk_mul_f32 v[28:29], v[30:31], v[28:29]
	v_div_scale_f32 v8, s[0:1], v23, v23, 2.0
	v_rcp_f32_e32 v17, v8
	v_pk_mul_f32 v[0:1], v[28:29], v[4:5]
	v_fma_f32 v4, -v8, v17, 1.0
	v_fmac_f32_e32 v17, v4, v17
	v_div_scale_f32 v4, vcc, 2.0, v23, 2.0
	v_mul_f32_e32 v5, v4, v17
	v_pk_fma_f32 v[0:1], v[14:15], v[20:21], v[0:1]
	v_fma_f32 v14, -v8, v5, v4
	v_fmac_f32_e32 v5, v14, v17
	v_fma_f32 v4, -v8, v5, v4
	v_div_scale_f32 v8, s[0:1], v22, v22, 2.0
	v_rcp_f32_e32 v14, v8
	v_div_fmas_f32 v4, v4, v17, v5
	v_div_fixup_f32 v5, v4, v23, 2.0
	v_fma_f32 v4, -v8, v14, 1.0
	v_fmac_f32_e32 v14, v4, v14
	v_div_scale_f32 v4, vcc, 2.0, v22, 2.0
	v_mul_f32_e32 v15, v4, v14
	v_fma_f32 v17, -v8, v15, v4
	v_fmac_f32_e32 v15, v17, v14
	v_fma_f32 v4, -v8, v15, v4
	v_mul_f32_e32 v8, 0x3d372713, v13
	v_mul_f32_e32 v8, v13, v8
	v_fma_f32 v8, v13, v8, v13
	v_mul_f32_e32 v8, 0x3f4c422a, v8
	v_add_f32_e32 v8, v8, v8
	v_mul_f32_e32 v8, 0x3fb8aa3b, v8
	v_div_fmas_f32 v4, v4, v14, v15
	v_exp_f32_e32 v17, v8
	v_div_fixup_f32 v4, v4, v22, 2.0
	v_pk_add_f32 v[4:5], v[4:5], 1.0 op_sel_hi:[1,0] neg_lo:[1,0] neg_hi:[1,0]
	v_pk_mul_f32 v[14:15], v[40:41], 0.5 op_sel_hi:[1,0]
	v_pk_add_f32 v[4:5], v[4:5], 1.0 op_sel_hi:[1,0]
	v_pk_mul_f32 v[12:13], v[12:13], 0.5 op_sel_hi:[1,0]
	v_pk_mul_f32 v[4:5], v[14:15], v[4:5]
	v_pk_add_f32 v[14:15], v[16:17], 1.0 op_sel_hi:[1,0]
	v_mov_b32_e32 v16, v2
	v_div_scale_f32 v8, s[0:1], v15, v15, 2.0
	v_rcp_f32_e32 v20, v8
	v_mov_b32_e32 v17, v6
	v_pk_fma_f32 v[0:1], v[4:5], v[16:17], v[0:1]
	v_div_scale_f32 v6, s[0:1], v14, v14, 2.0
	v_fma_f32 v2, -v8, v20, 1.0
	v_fmac_f32_e32 v20, v2, v20
	v_div_scale_f32 v2, vcc, 2.0, v15, 2.0
	v_mul_f32_e32 v4, v2, v20
	v_fma_f32 v5, -v8, v4, v2
	v_fmac_f32_e32 v4, v5, v20
	v_fma_f32 v2, -v8, v4, v2
	v_rcp_f32_e32 v8, v6
	v_div_fmas_f32 v2, v2, v20, v4
	v_div_fixup_f32 v5, v2, v15, 2.0
	s_mov_b32 s0, 0x400000
	v_fma_f32 v2, -v6, v8, 1.0
	v_fmac_f32_e32 v8, v2, v8
	v_div_scale_f32 v2, vcc, 2.0, v14, 2.0
	v_mul_f32_e32 v4, v2, v8
	v_fma_f32 v15, -v6, v4, v2
	v_fmac_f32_e32 v4, v15, v8
	v_fma_f32 v2, -v6, v4, v2
	v_div_fmas_f32 v2, v2, v8, v4
	v_div_fixup_f32 v4, v2, v14, 2.0
	v_pk_add_f32 v[4:5], v[4:5], 1.0 op_sel_hi:[1,0] neg_lo:[1,0] neg_hi:[1,0]
	v_mov_b32_e32 v6, v3
	v_pk_add_f32 v[4:5], v[4:5], 1.0 op_sel_hi:[1,0]
	v_add_co_u32_e32 v2, vcc, s0, v10
	v_pk_mul_f32 v[4:5], v[12:13], v[4:5]
	s_lshl_b32 s0, s3, 3
	v_pk_fma_f32 v[0:1], v[4:5], v[6:7], v[0:1]
	v_addc_co_u32_e32 v3, vcc, 0, v11, vcc
	v_pk_add_f32 v[0:1], v[18:19], v[0:1]
	s_addk_i32 s0, 0x100
	global_store_dwordx2 v[2:3], v[0:1], off
	v_add_u32_e32 v8, s0, v26
	v_lshlrev_b32_e32 v3, 1, v27
	v_cvt_pk_f16_f32 v2, v0, v1
	v_lshlrev_b64 v[0:1], 6, v[8:9]
	v_and_b32_e32 v3, 48, v3
	v_or3_b32 v0, v0, v3, v24
	v_and_b32_e32 v3, 6, v25
	v_lshl_add_u64 v[0:1], v[0:1], 4, s[12:13]
	v_lshlrev_b32_e32 v8, 1, v3
	v_lshl_add_u64 v[0:1], v[0:1], 0, v[8:9]
	global_store_dword v[0:1], v2, off
	s_endpgm
	s_nop 0
	s_nop 0
	s_nop 0
	s_nop 0
	s_nop 0
	s_nop 0
	s_nop 0
	s_nop 0
	s_nop 0
	s_nop 0
	s_nop 0
	s_nop 0
	s_nop 0
	s_nop 0
	s_nop 0
	s_nop 0
	s_nop 0
	s_nop 0
	s_nop 0
	s_nop 0
	s_nop 0
	s_nop 0
	s_nop 0
	s_nop 0
	s_nop 0
	s_nop 0
	s_nop 0
	s_nop 0
	s_nop 0
	s_nop 0
	s_nop 0
	s_nop 0
	s_nop 0
	s_nop 0
	s_nop 0
	s_nop 0
	s_nop 0
	s_nop 0
	s_nop 0
	s_nop 0
	s_nop 0
	s_nop 0
	s_nop 0
	s_nop 0
	s_nop 0
	s_endpgm

	.amdhsa_kernel _ZN12_GLOBAL__N_110gemm_fullkILi1ELi3EEEvPKDF16_S2_PKfPDF16_PfS6_S4_S4_S4_S4_S4_S5_
		.amdhsa_group_segment_fixed_size 0
		.amdhsa_private_segment_fixed_size 0
		.amdhsa_kernarg_size 96
		.amdhsa_user_sgpr_count 2
		.amdhsa_user_sgpr_dispatch_ptr 0
		.amdhsa_user_sgpr_queue_ptr 0
		.amdhsa_user_sgpr_kernarg_segment_ptr 1
		.amdhsa_user_sgpr_dispatch_id 0
		.amdhsa_user_sgpr_kernarg_preload_length 0
		.amdhsa_user_sgpr_kernarg_preload_offset 0
		.amdhsa_user_sgpr_private_segment_size 0
		.amdhsa_uses_dynamic_stack 0
		.amdhsa_enable_private_segment 0
		.amdhsa_system_sgpr_workgroup_id_x 1
		.amdhsa_system_sgpr_workgroup_id_y 0
		.amdhsa_system_sgpr_workgroup_id_z 0
		.amdhsa_system_sgpr_workgroup_info 0
		.amdhsa_system_vgpr_workitem_id 0
		.amdhsa_next_free_vgpr 179
		.amdhsa_next_free_sgpr 18
		.amdhsa_accum_offset 180
		.amdhsa_reserve_vcc 1
		.amdhsa_float_round_mode_32 0
		.amdhsa_float_round_mode_16_64 0
		.amdhsa_float_denorm_mode_32 3
		.amdhsa_float_denorm_mode_16_64 3
		.amdhsa_dx10_clamp 1
		.amdhsa_ieee_mode 1
		.amdhsa_fp16_overflow 0
		.amdhsa_tg_split 0
		.amdhsa_exception_fp_ieee_invalid_op 0
		.amdhsa_exception_fp_denorm_src 0
		.amdhsa_exception_fp_ieee_div_zero 0
		.amdhsa_exception_fp_ieee_overflow 0
		.amdhsa_exception_fp_ieee_underflow 0
		.amdhsa_exception_fp_ieee_inexact 0
		.amdhsa_exception_int_div_zero 0
	.end_amdhsa_kernel

_ZN12_GLOBAL__N_110gemm_fullkILi0ELi4EEEvPKDF16_S2_PKfPDF16_PfS6_S4_S4_S4_S4_S4_S5_:
	s_load_dwordx8 s[4:11], s[0:1], 0x0
	s_lshr_b32 s0, s2, 5
	v_lshrrev_b32_e32 v230, 6, v0
	s_and_b32 s12, s0, 0x7fffffc
	s_and_b32 s2, s2, 0x7f
	s_mov_b32 s13, 0
	v_mul_u32_u24_e32 v4, 12, v230
	v_mov_b32_e32 v3, 0
	s_lshl_b64 s[0:1], s[12:13], 10
	s_mul_i32 s13, s2, 0xc0
	v_and_b32_e32 v1, 63, v0
	v_mul_u32_u24_e32 v2, 0x18000, v230
	v_add_lshl_u32 v4, s13, v4, 10
	v_mov_b32_e32 v5, v3
	s_waitcnt lgkmcnt(0)
	v_lshl_add_u64 v[4:5], s[6:7], 0, v[4:5]
	v_lshl_add_u64 v[6:7], s[4:5], 0, v[2:3]
	v_lshlrev_b32_e32 v2, 4, v1
	s_mov_b32 s3, 0x18000
	v_lshl_add_u64 v[208:209], v[4:5], 0, v[2:3]
	v_add_co_u32_e32 v80, vcc, s3, v208
	v_lshl_add_u64 v[6:7], v[6:7], 0, s[0:1]
	s_nop 0
	v_addc_co_u32_e32 v81, vcc, 0, v209, vcc
	s_mov_b32 s0, 0x19000
	v_add_co_u32_e32 v176, vcc, s0, v208
	v_lshl_add_u64 v[212:213], v[6:7], 0, v[2:3]
	s_nop 0
	v_addc_co_u32_e32 v177, vcc, 0, v209, vcc
	s_movk_i32 s0, 0x2000
	v_add_co_u32_e32 v52, vcc, s0, v212
	s_movk_i32 s1, 0x4000
	s_nop 0
	v_addc_co_u32_e32 v53, vcc, 0, v213, vcc
	v_add_co_u32_e32 v82, vcc, s1, v212
	s_movk_i32 s1, 0x6000
	s_nop 0
	v_addc_co_u32_e32 v83, vcc, 0, v213, vcc
	v_add_co_u32_e32 v96, vcc, s1, v212
	s_movk_i32 s1, 0x1000
	s_nop 0
	v_addc_co_u32_e32 v97, vcc, 0, v213, vcc
	v_add_co_u32_e32 v168, vcc, s1, v208
	global_load_dwordx4 v[4:7], v[212:213], off
	global_load_dwordx4 v[8:11], v[212:213], off offset:1024
	global_load_dwordx4 v[12:15], v[212:213], off offset:2048
	global_load_dwordx4 v[16:19], v[212:213], off offset:3072
	global_load_dwordx4 v[20:23], v[208:209], off
	global_load_dwordx4 v[24:27], v[208:209], off offset:1024
	v_addc_co_u32_e32 v169, vcc, 0, v209, vcc
	v_add_co_u32_e32 v210, vcc, s0, v208
	s_mov_b32 s0, 0x8000
	s_nop 0
	v_addc_co_u32_e32 v211, vcc, 0, v209, vcc
	v_add_co_u32_e32 v116, vcc, s0, v212
	s_mov_b32 s0, 0xa000
	s_nop 0
	v_addc_co_u32_e32 v117, vcc, 0, v213, vcc
	v_add_co_u32_e32 v132, vcc, s0, v212
	s_mov_b32 s0, 0xc000
	s_nop 0
	v_addc_co_u32_e32 v133, vcc, 0, v213, vcc
	v_add_co_u32_e32 v164, vcc, s0, v212
	global_load_dwordx4 v[28:31], v[52:53], off
	global_load_dwordx4 v[32:35], v[52:53], off offset:1024
	global_load_dwordx4 v[36:39], v[52:53], off offset:2048
	global_load_dwordx4 v[40:43], v[52:53], off offset:3072
	global_load_dwordx4 v[44:47], v[80:81], off offset:1024
	global_load_dwordx4 v[48:51], v[80:81], off offset:2048
	s_nop 0
	global_load_dwordx4 v[52:55], v[82:83], off
	global_load_dwordx4 v[56:59], v[82:83], off offset:1024
	global_load_dwordx4 v[60:63], v[82:83], off offset:2048
	global_load_dwordx4 v[64:67], v[82:83], off offset:3072
	global_load_dwordx4 v[68:71], v[208:209], off offset:2048
	global_load_dwordx4 v[72:75], v[208:209], off offset:3072
	global_load_dwordx4 v[76:79], v[80:81], off offset:3072
	s_nop 0
	global_load_dwordx4 v[80:83], v[96:97], off
	global_load_dwordx4 v[84:87], v[96:97], off offset:1024
	global_load_dwordx4 v[88:91], v[96:97], off offset:2048
	global_load_dwordx4 v[92:95], v[96:97], off offset:3072
	s_nop 0
	global_load_dwordx4 v[96:99], v[176:177], off offset:-4096
	global_load_dwordx4 v[100:103], v[176:177], off
	global_load_dwordx4 v[104:107], v[116:117], off
	global_load_dwordx4 v[108:111], v[116:117], off offset:1024
	global_load_dwordx4 v[112:115], v[116:117], off offset:2048
	s_nop 0
	global_load_dwordx4 v[116:119], v[116:117], off offset:3072
	s_nop 0
	global_load_dwordx4 v[120:123], v[132:133], off
	global_load_dwordx4 v[124:127], v[132:133], off offset:1024
	global_load_dwordx4 v[128:131], v[132:133], off offset:2048
	s_nop 0
	global_load_dwordx4 v[132:135], v[132:133], off offset:3072
	s_nop 0
	global_load_dwordx4 v[136:139], v[168:169], off offset:1024
	global_load_dwordx4 v[140:143], v[168:169], off offset:2048
	global_load_dwordx4 v[144:147], v[176:177], off offset:1024
	global_load_dwordx4 v[148:151], v[176:177], off offset:2048
	v_addc_co_u32_e32 v165, vcc, 0, v213, vcc
	global_load_dwordx4 v[152:155], v[164:165], off
	global_load_dwordx4 v[156:159], v[164:165], off offset:1024
	global_load_dwordx4 v[160:163], v[164:165], off offset:2048
	s_nop 0
	global_load_dwordx4 v[164:167], v[164:165], off offset:3072
	s_nop 0
	global_load_dwordx4 v[168:171], v[168:169], off offset:3072
	s_nop 0
	global_load_dwordx4 v[172:175], v[210:211], off offset:-4096
	s_nop 0
	global_load_dwordx4 v[176:179], v[176:177], off offset:3072
	s_mov_b32 s0, 0xe000
	v_add_co_u32_e32 v192, vcc, s0, v212
	s_lshl_b32 s0, s2, 7
	s_nop 0
	v_addc_co_u32_e32 v193, vcc, 0, v213, vcc
	global_load_dwordx4 v[180:183], v[192:193], off
	global_load_dwordx4 v[184:187], v[192:193], off offset:1024
	global_load_dwordx4 v[188:191], v[192:193], off offset:2048
	s_nop 0
	global_load_dwordx4 v[192:195], v[192:193], off offset:3072
	v_bfe_u32 v1, v0, 6, 1
	s_add_u32 s0, s8, s0
	s_addc_u32 s1, s9, 0
	v_lshlrev_b32_e32 v196, 6, v1
	v_mov_b32_e32 v197, v3
	v_lshl_add_u64 v[196:197], s[0:1], 0, v[196:197]
	v_and_b32_e32 v198, 48, v0
	v_mov_b32_e32 v199, v3
	v_lshl_add_u64 v[228:229], v[196:197], 0, v[198:199]
	s_waitcnt vmcnt(43)
	v_mfma_f32_16x16x32_f16 v[196:199], v[20:23], v[4:7], 0
	s_waitcnt vmcnt(24)
	v_mfma_f32_16x16x32_f16 v[4:7], v[96:99], v[4:7], 0
	v_mfma_f32_16x16x32_f16 v[200:203], v[20:23], v[8:11], 0
	v_mfma_f32_16x16x32_f16 v[8:11], v[96:99], v[8:11], 0
	v_mfma_f32_16x16x32_f16 v[204:207], v[20:23], v[12:15], 0
	v_mfma_f32_16x16x32_f16 v[12:15], v[96:99], v[12:15], 0
	v_mfma_f32_16x16x32_f16 v[20:23], v[20:23], v[16:19], 0
	v_mfma_f32_16x16x32_f16 v[16:19], v[96:99], v[16:19], 0
	v_mfma_f32_16x16x32_f16 v[96:99], v[24:27], v[28:31], v[196:199]
	v_mfma_f32_16x16x32_f16 v[4:7], v[44:47], v[28:31], v[4:7]
	v_mfma_f32_16x16x32_f16 v[28:31], v[24:27], v[32:35], v[200:203]
	v_mfma_f32_16x16x32_f16 v[8:11], v[44:47], v[32:35], v[8:11]
	v_mfma_f32_16x16x32_f16 v[32:35], v[24:27], v[36:39], v[204:207]
	v_mfma_f32_16x16x32_f16 v[12:15], v[44:47], v[36:39], v[12:15]
	v_mfma_f32_16x16x32_f16 v[20:23], v[24:27], v[40:43], v[20:23]
	v_mfma_f32_16x16x32_f16 v[16:19], v[44:47], v[40:43], v[16:19]
	v_mfma_f32_16x16x32_f16 v[24:27], v[68:71], v[52:55], v[96:99]
	v_mfma_f32_16x16x32_f16 v[4:7], v[48:51], v[52:55], v[4:7]
	v_mfma_f32_16x16x32_f16 v[28:31], v[68:71], v[56:59], v[28:31]
	v_mfma_f32_16x16x32_f16 v[8:11], v[48:51], v[56:59], v[8:11]
	v_mfma_f32_16x16x32_f16 v[32:35], v[68:71], v[60:63], v[32:35]
	v_mfma_f32_16x16x32_f16 v[12:15], v[48:51], v[60:63], v[12:15]
	v_mfma_f32_16x16x32_f16 v[20:23], v[68:71], v[64:67], v[20:23]
	v_mfma_f32_16x16x32_f16 v[16:19], v[48:51], v[64:67], v[16:19]
	v_mfma_f32_16x16x32_f16 v[24:27], v[72:75], v[80:83], v[24:27]
	v_mfma_f32_16x16x32_f16 v[4:7], v[76:79], v[80:83], v[4:7]
	v_mfma_f32_16x16x32_f16 v[28:31], v[72:75], v[84:87], v[28:31]
	v_mfma_f32_16x16x32_f16 v[8:11], v[76:79], v[84:87], v[8:11]
	v_mfma_f32_16x16x32_f16 v[32:35], v[72:75], v[88:91], v[32:35]
	v_mfma_f32_16x16x32_f16 v[12:15], v[76:79], v[88:91], v[12:15]
	v_mfma_f32_16x16x32_f16 v[20:23], v[72:75], v[92:95], v[20:23]
	v_mfma_f32_16x16x32_f16 v[16:19], v[76:79], v[92:95], v[16:19]
	s_mov_b32 s0, 0x1a000
	v_add_co_u32_e32 v208, vcc, s0, v208
	s_mov_b32 s0, 0x10000
	s_nop 0
	v_addc_co_u32_e32 v209, vcc, 0, v209, vcc
	v_add_co_u32_e32 v48, vcc, s0, v212
	s_mov_b32 s0, 0x12000
	s_nop 0
	v_addc_co_u32_e32 v49, vcc, 0, v213, vcc
	v_add_co_u32_e32 v80, vcc, s0, v212
	s_mov_b32 s0, 0x14000
	s_nop 0
	v_addc_co_u32_e32 v81, vcc, 0, v213, vcc
	v_add_co_u32_e32 v96, vcc, s0, v212
	global_load_dwordx4 v[36:39], v[48:49], off
	global_load_dwordx4 v[40:43], v[48:49], off offset:1024
	global_load_dwordx4 v[44:47], v[48:49], off offset:2048
	s_nop 0
	global_load_dwordx4 v[48:51], v[48:49], off offset:3072
	s_nop 0
	global_load_dwordx4 v[52:55], v[210:211], off
	global_load_dwordx4 v[56:59], v[210:211], off offset:1024
	global_load_dwordx4 v[60:63], v[208:209], off
	global_load_dwordx4 v[64:67], v[208:209], off offset:1024
	v_addc_co_u32_e32 v97, vcc, 0, v213, vcc
	global_load_dwordx4 v[68:71], v[80:81], off
	global_load_dwordx4 v[72:75], v[80:81], off offset:1024
	global_load_dwordx4 v[76:79], v[80:81], off offset:2048
	s_nop 0
	global_load_dwordx4 v[80:83], v[80:81], off offset:3072
	s_nop 0
	global_load_dwordx4 v[84:87], v[96:97], off
	global_load_dwordx4 v[88:91], v[96:97], off offset:1024
	global_load_dwordx4 v[92:95], v[96:97], off offset:2048
	s_nop 0
	global_load_dwordx4 v[96:99], v[96:97], off offset:3072
	s_nop 0
	global_load_dwordx4 v[196:199], v[210:211], off offset:2048
	global_load_dwordx4 v[200:203], v[210:211], off offset:3072
	global_load_dwordx4 v[204:207], v[208:209], off offset:2048
	s_nop 0
	global_load_dwordx4 v[208:211], v[208:209], off offset:3072
	s_mov_b32 s0, 0x16000
	v_add_co_u32_e32 v224, vcc, s0, v212
	s_nop 1
	v_addc_co_u32_e32 v225, vcc, 0, v213, vcc
	global_load_dwordx4 v[212:215], v[224:225], off
	global_load_dwordx4 v[216:219], v[224:225], off offset:1024
	global_load_dwordx4 v[220:223], v[224:225], off offset:2048
	s_nop 0
	global_load_dwordx4 v[224:227], v[224:225], off offset:3072
	s_waitcnt vmcnt(29)
	v_mfma_f32_16x16x32_f16 v[24:27], v[172:175], v[104:107], v[24:27]
	v_mfma_f32_16x16x32_f16 v[4:7], v[100:103], v[104:107], v[4:7]
	v_mfma_f32_16x16x32_f16 v[28:31], v[172:175], v[108:111], v[28:31]
	v_mfma_f32_16x16x32_f16 v[8:11], v[100:103], v[108:111], v[8:11]
	v_mfma_f32_16x16x32_f16 v[32:35], v[172:175], v[112:115], v[32:35]
	v_mfma_f32_16x16x32_f16 v[12:15], v[100:103], v[112:115], v[12:15]
	v_mfma_f32_16x16x32_f16 v[20:23], v[172:175], v[116:119], v[20:23]
	v_mfma_f32_16x16x32_f16 v[16:19], v[100:103], v[116:119], v[16:19]
	v_mfma_f32_16x16x32_f16 v[24:27], v[136:139], v[120:123], v[24:27]
	v_mfma_f32_16x16x32_f16 v[4:7], v[144:147], v[120:123], v[4:7]
	v_mfma_f32_16x16x32_f16 v[28:31], v[136:139], v[124:127], v[28:31]
	v_mfma_f32_16x16x32_f16 v[8:11], v[144:147], v[124:127], v[8:11]
	v_mfma_f32_16x16x32_f16 v[32:35], v[136:139], v[128:131], v[32:35]
	v_mfma_f32_16x16x32_f16 v[12:15], v[144:147], v[128:131], v[12:15]
	v_mfma_f32_16x16x32_f16 v[20:23], v[136:139], v[132:135], v[20:23]
	v_mfma_f32_16x16x32_f16 v[16:19], v[144:147], v[132:135], v[16:19]
	v_mfma_f32_16x16x32_f16 v[24:27], v[140:143], v[152:155], v[24:27]
	v_mfma_f32_16x16x32_f16 v[4:7], v[148:151], v[152:155], v[4:7]
	v_mfma_f32_16x16x32_f16 v[28:31], v[140:143], v[156:159], v[28:31]
	v_mfma_f32_16x16x32_f16 v[8:11], v[148:151], v[156:159], v[8:11]
	v_mfma_f32_16x16x32_f16 v[32:35], v[140:143], v[160:163], v[32:35]
	v_mfma_f32_16x16x32_f16 v[12:15], v[148:151], v[160:163], v[12:15]
	v_mfma_f32_16x16x32_f16 v[20:23], v[140:143], v[164:167], v[20:23]
	v_mfma_f32_16x16x32_f16 v[16:19], v[148:151], v[164:167], v[16:19]
	s_waitcnt vmcnt(27)
	v_mfma_f32_16x16x32_f16 v[24:27], v[168:171], v[180:183], v[24:27]
	v_mfma_f32_16x16x32_f16 v[4:7], v[176:179], v[180:183], v[4:7]
	s_waitcnt vmcnt(26)
	v_mfma_f32_16x16x32_f16 v[28:31], v[168:171], v[184:187], v[28:31]
	v_mfma_f32_16x16x32_f16 v[8:11], v[176:179], v[184:187], v[8:11]
	s_waitcnt vmcnt(25)
	v_mfma_f32_16x16x32_f16 v[32:35], v[168:171], v[188:191], v[32:35]
	v_mfma_f32_16x16x32_f16 v[12:15], v[176:179], v[188:191], v[12:15]
	s_waitcnt vmcnt(24)
	v_mfma_f32_16x16x32_f16 v[20:23], v[168:171], v[192:195], v[20:23]
	v_mfma_f32_16x16x32_f16 v[16:19], v[176:179], v[192:195], v[16:19]
	s_waitcnt vmcnt(19)
	v_mfma_f32_16x16x32_f16 v[24:27], v[52:55], v[36:39], v[24:27]
	s_waitcnt vmcnt(17)
	v_mfma_f32_16x16x32_f16 v[4:7], v[60:63], v[36:39], v[4:7]
	v_mfma_f32_16x16x32_f16 v[28:31], v[52:55], v[40:43], v[28:31]
	v_mfma_f32_16x16x32_f16 v[8:11], v[60:63], v[40:43], v[8:11]
	v_mfma_f32_16x16x32_f16 v[32:35], v[52:55], v[44:47], v[32:35]
	v_mfma_f32_16x16x32_f16 v[12:15], v[60:63], v[44:47], v[12:15]
	v_mfma_f32_16x16x32_f16 v[20:23], v[52:55], v[48:51], v[20:23]
	v_mfma_f32_16x16x32_f16 v[16:19], v[60:63], v[48:51], v[16:19]
	s_waitcnt vmcnt(15)
	v_mfma_f32_16x16x32_f16 v[24:27], v[56:59], v[68:71], v[24:27]
	v_mfma_f32_16x16x32_f16 v[4:7], v[64:67], v[68:71], v[4:7]
	s_waitcnt vmcnt(14)
	v_mfma_f32_16x16x32_f16 v[28:31], v[56:59], v[72:75], v[28:31]
	v_mfma_f32_16x16x32_f16 v[8:11], v[64:67], v[72:75], v[8:11]
	s_waitcnt vmcnt(13)
	v_mfma_f32_16x16x32_f16 v[32:35], v[56:59], v[76:79], v[32:35]
	v_mfma_f32_16x16x32_f16 v[12:15], v[64:67], v[76:79], v[12:15]
	s_waitcnt vmcnt(12)
	v_mfma_f32_16x16x32_f16 v[20:23], v[56:59], v[80:83], v[20:23]
	v_mfma_f32_16x16x32_f16 v[16:19], v[64:67], v[80:83], v[16:19]
	s_waitcnt vmcnt(7)
	v_mfma_f32_16x16x32_f16 v[24:27], v[196:199], v[84:87], v[24:27]
	s_waitcnt vmcnt(5)
	v_mfma_f32_16x16x32_f16 v[4:7], v[204:207], v[84:87], v[4:7]
	v_mfma_f32_16x16x32_f16 v[28:31], v[196:199], v[88:91], v[28:31]
	v_mfma_f32_16x16x32_f16 v[8:11], v[204:207], v[88:91], v[8:11]
	v_mfma_f32_16x16x32_f16 v[32:35], v[196:199], v[92:95], v[32:35]
	v_mfma_f32_16x16x32_f16 v[12:15], v[204:207], v[92:95], v[12:15]
	v_mfma_f32_16x16x32_f16 v[20:23], v[196:199], v[96:99], v[20:23]
	v_mfma_f32_16x16x32_f16 v[16:19], v[204:207], v[96:99], v[16:19]
	s_waitcnt vmcnt(3)
	v_mfma_f32_16x16x32_f16 v[24:27], v[200:203], v[212:215], v[24:27]
	v_mfma_f32_16x16x32_f16 v[4:7], v[208:211], v[212:215], v[4:7]
	s_waitcnt vmcnt(2)
	v_mfma_f32_16x16x32_f16 v[28:31], v[200:203], v[216:219], v[28:31]
	v_mfma_f32_16x16x32_f16 v[8:11], v[208:211], v[216:219], v[8:11]
	s_waitcnt vmcnt(1)
	v_mfma_f32_16x16x32_f16 v[32:35], v[200:203], v[220:223], v[32:35]
	v_mfma_f32_16x16x32_f16 v[12:15], v[208:211], v[220:223], v[12:15]
	s_waitcnt vmcnt(0)
	v_mfma_f32_16x16x32_f16 v[20:23], v[200:203], v[224:227], v[20:23]
	v_mfma_f32_16x16x32_f16 v[16:19], v[208:211], v[224:227], v[16:19]
	global_load_dwordx4 v[36:39], v[228:229], off
	v_add_u32_e32 v2, 0, v2
	v_and_b32_e32 v41, 0x1c0, v0
	v_lshl_add_u32 v43, v230, 13, v2
	v_lshl_add_u32 v2, v41, 4, v2
	v_lshl_add_u32 v40, v0, 4, 0
	ds_write_b128 v43, v[24:27]
	ds_write_b128 v43, v[4:7] offset:1024
	ds_write_b128 v43, v[28:31] offset:2048
	ds_write_b128 v43, v[8:11] offset:3072
	ds_write_b128 v43, v[32:35] offset:4096
	ds_write_b128 v43, v[12:15] offset:5120
	ds_write_b128 v43, v[20:23] offset:6144
	ds_write_b128 v43, v[16:19] offset:7168
	s_waitcnt lgkmcnt(0)
	s_barrier
	ds_read_b128 v[4:7], v2 offset:8192
	ds_read_b128 v[8:11], v2 offset:16384
	ds_read_b128 v[12:15], v2 offset:24576
	ds_read_b128 v[16:19], v40
	ds_read_b128 v[20:23], v2 offset:32768
	ds_read_b128 v[24:27], v2 offset:40960
	ds_read_b128 v[28:31], v2 offset:49152
	ds_read_b128 v[32:35], v2 offset:57344
	s_waitcnt lgkmcnt(4)
	v_pk_add_f32 v[4:5], v[16:17], v[4:5]
	v_pk_add_f32 v[6:7], v[18:19], v[6:7]
	v_pk_add_f32 v[4:5], v[4:5], v[8:9]
	v_pk_add_f32 v[6:7], v[6:7], v[10:11]
	v_pk_add_f32 v[4:5], v[4:5], v[12:13]
	v_pk_add_f32 v[6:7], v[6:7], v[14:15]
	s_waitcnt lgkmcnt(3)
	v_pk_add_f32 v[4:5], v[4:5], v[20:21]
	v_pk_add_f32 v[6:7], v[6:7], v[22:23]
	s_waitcnt lgkmcnt(2)
	v_pk_add_f32 v[4:5], v[4:5], v[24:25]
	v_pk_add_f32 v[6:7], v[6:7], v[26:27]
	s_waitcnt lgkmcnt(1)
	v_pk_add_f32 v[4:5], v[4:5], v[28:29]
	v_pk_add_f32 v[6:7], v[6:7], v[30:31]
	s_waitcnt lgkmcnt(0)
	v_pk_add_f32 v[4:5], v[4:5], v[32:33]
	v_pk_add_f32 v[6:7], v[6:7], v[34:35]
	v_lshrrev_b32_e32 v42, 7, v0
	s_waitcnt vmcnt(0)
	v_pk_add_f32 v[4:5], v[36:37], v[4:5]
	v_pk_add_f32 v[6:7], v[38:39], v[6:7]
	v_mul_f32_e32 v2, 0x3d372713, v4
	v_mul_f32_e32 v8, 0x3d372713, v5
	v_mul_f32_e32 v9, 0x3d372713, v6
	v_mul_f32_e32 v2, v4, v2
	v_mul_f32_e32 v8, v5, v8
	v_mul_f32_e32 v9, v6, v9
	v_fma_f32 v2, v4, v2, v4
	v_fma_f32 v8, v5, v8, v5
	v_fma_f32 v9, v6, v9, v6
	v_mul_f32_e32 v2, 0x3f4c422a, v2
	v_mul_f32_e32 v8, 0x3f4c422a, v8
	v_mul_f32_e32 v9, 0x3f4c422a, v9
	v_add_f32_e32 v2, v2, v2
	v_add_f32_e32 v8, v8, v8
	v_add_f32_e32 v9, v9, v9
	v_mul_f32_e32 v2, 0x3fb8aa3b, v2
	v_mul_f32_e32 v11, 0x3fb8aa3b, v8
	v_mul_f32_e32 v10, 0x3d372713, v7
	v_mul_f32_e32 v12, 0x3fb8aa3b, v9
	v_exp_f32_e32 v8, v2
	v_exp_f32_e32 v9, v11
	v_mul_f32_e32 v10, v7, v10
	v_fma_f32 v10, v7, v10, v7
	v_mul_f32_e32 v10, 0x3f4c422a, v10
	v_add_f32_e32 v10, v10, v10
	v_pk_add_f32 v[8:9], v[8:9], 1.0 op_sel_hi:[1,0]
	v_mul_f32_e32 v13, 0x3fb8aa3b, v10
	v_div_scale_f32 v2, s[0:1], v9, v9, 2.0
	v_exp_f32_e32 v10, v12
	v_exp_f32_e32 v11, v13
	v_div_scale_f32 v14, s[0:1], v8, v8, 2.0
	v_rcp_f32_e32 v16, v2
	v_rcp_f32_e32 v17, v14
	v_pk_add_f32 v[10:11], v[10:11], 1.0 op_sel_hi:[1,0]
	v_div_scale_f32 v13, vcc, 2.0, v9, 2.0
	v_fma_f32 v20, -v2, v16, 1.0
	v_div_scale_f32 v15, s[0:1], v11, v11, 2.0
	v_fma_f32 v21, -v14, v17, 1.0
	v_fmac_f32_e32 v16, v20, v16
	v_div_scale_f32 v19, s[0:1], 2.0, v8, 2.0
	v_fmac_f32_e32 v17, v21, v17
	v_mul_f32_e32 v20, v13, v16
	v_mul_f32_e32 v21, v19, v17
	v_fma_f32 v23, -v2, v20, v13
	v_fma_f32 v24, -v14, v21, v19
	v_fmac_f32_e32 v20, v23, v16
	v_fmac_f32_e32 v21, v24, v17
	v_fma_f32 v2, -v2, v20, v13
	v_rcp_f32_e32 v18, v15
	v_fma_f32 v13, -v14, v21, v19
	v_div_fmas_f32 v2, v2, v16, v20
	s_mov_b64 vcc, s[0:1]
	v_div_fixup_f32 v9, v2, v9, 2.0
	v_div_fmas_f32 v2, v13, v17, v21
	v_div_fixup_f32 v8, v2, v8, 2.0
	v_pk_add_f32 v[8:9], v[8:9], 1.0 op_sel_hi:[1,0] neg_lo:[1,0] neg_hi:[1,0]
	v_pk_mul_f32 v[4:5], v[4:5], 0.5 op_sel_hi:[1,0]
	v_fma_f32 v22, -v15, v18, 1.0
	v_pk_add_f32 v[8:9], v[8:9], 1.0 op_sel_hi:[1,0]
	v_fmac_f32_e32 v18, v22, v18
	v_pk_mul_f32 v[4:5], v[4:5], v[8:9]
	v_div_scale_f32 v2, vcc, 2.0, v11, 2.0
	v_cvt_pk_f16_f32 v4, v4, v5
	v_mul_f32_e32 v5, v2, v18
	v_fma_f32 v8, -v15, v5, v2
	v_fmac_f32_e32 v5, v8, v18
	v_div_scale_f32 v8, s[0:1], v10, v10, 2.0
	v_rcp_f32_e32 v13, v8
	v_fma_f32 v2, -v15, v5, v2
	v_div_fmas_f32 v2, v2, v18, v5
	v_div_fixup_f32 v9, v2, v11, 2.0
	v_fma_f32 v2, -v8, v13, 1.0
	v_fmac_f32_e32 v13, v2, v13
	v_div_scale_f32 v2, vcc, 2.0, v10, 2.0
	v_mul_f32_e32 v5, v2, v13
	v_fma_f32 v11, -v8, v5, v2
	v_fmac_f32_e32 v5, v11, v13
	v_fma_f32 v2, -v8, v5, v2
	v_div_fmas_f32 v2, v2, v13, v5
	v_div_fixup_f32 v8, v2, v10, 2.0
	v_pk_add_f32 v[8:9], v[8:9], 1.0 op_sel_hi:[1,0] neg_lo:[1,0] neg_hi:[1,0]
	s_lshl_b32 s0, s2, 3
	v_pk_mul_f32 v[6:7], v[6:7], 0.5 op_sel_hi:[1,0]
	v_pk_add_f32 v[8:9], v[8:9], 1.0 op_sel_hi:[1,0]
	s_add_i32 s0, s0, s12
	v_pk_mul_f32 v[6:7], v[6:7], v[8:9]
	v_or_b32_e32 v2, s0, v42
	v_cvt_pk_f16_f32 v5, v6, v7
	v_lshlrev_b64 v[6:7], 6, v[2:3]
	v_lshrrev_b32_e32 v2, 1, v0
	v_and_b32_e32 v12, 15, v0
	v_and_b32_e32 v0, 16, v2
	v_lshl_or_b32 v0, v1, 5, v0
	v_or3_b32 v6, v6, v0, v12
	v_lshl_add_u64 v[0:1], v[6:7], 4, s[10:11]
	v_and_b32_e32 v2, 8, v2
	v_lshl_add_u64 v[0:1], v[0:1], 0, v[2:3]
	global_store_dwordx2 v[0:1], v[4:5], off
	s_endpgm
	s_nop 0
	s_nop 0
	s_nop 0
	s_nop 0
	s_nop 0
	s_nop 0
	s_nop 0
	s_nop 0
	s_nop 0
	s_nop 0
	s_nop 0
	s_nop 0
	s_nop 0
	s_nop 0
	s_nop 0
	s_nop 0
	s_nop 0
	s_nop 0
	s_nop 0
	s_nop 0
	s_nop 0
	s_nop 0
	s_nop 0
	s_nop 0
	s_nop 0
	s_nop 0
	s_nop 0
	s_nop 0
	s_nop 0
	s_nop 0
	s_nop 0
	s_endpgm

	.amdhsa_kernel _ZN12_GLOBAL__N_110gemm_fullkILi0ELi4EEEvPKDF16_S2_PKfPDF16_PfS6_S4_S4_S4_S4_S4_S5_
		.amdhsa_group_segment_fixed_size 0
		.amdhsa_private_segment_fixed_size 0
		.amdhsa_kernarg_size 96
		.amdhsa_user_sgpr_count 2
		.amdhsa_user_sgpr_dispatch_ptr 0
		.amdhsa_user_sgpr_queue_ptr 0
		.amdhsa_user_sgpr_kernarg_segment_ptr 1
		.amdhsa_user_sgpr_dispatch_id 0
		.amdhsa_user_sgpr_kernarg_preload_length 0
		.amdhsa_user_sgpr_kernarg_preload_offset 0
		.amdhsa_user_sgpr_private_segment_size 0
		.amdhsa_uses_dynamic_stack 0
		.amdhsa_enable_private_segment 0
		.amdhsa_system_sgpr_workgroup_id_x 1
		.amdhsa_system_sgpr_workgroup_id_y 0
		.amdhsa_system_sgpr_workgroup_id_z 0
		.amdhsa_system_sgpr_workgroup_info 0
		.amdhsa_system_vgpr_workitem_id 0
		.amdhsa_next_free_vgpr 231
		.amdhsa_next_free_sgpr 14
		.amdhsa_accum_offset 232
		.amdhsa_reserve_vcc 1
		.amdhsa_float_round_mode_32 0
		.amdhsa_float_round_mode_16_64 0
		.amdhsa_float_denorm_mode_32 3
		.amdhsa_float_denorm_mode_16_64 3
		.amdhsa_dx10_clamp 1
		.amdhsa_ieee_mode 1
		.amdhsa_fp16_overflow 0
		.amdhsa_tg_split 0
		.amdhsa_exception_fp_ieee_invalid_op 0
		.amdhsa_exception_fp_denorm_src 0
		.amdhsa_exception_fp_ieee_div_zero 0
		.amdhsa_exception_fp_ieee_overflow 0
		.amdhsa_exception_fp_ieee_underflow 0
		.amdhsa_exception_fp_ieee_inexact 0
		.amdhsa_exception_int_div_zero 0
	.end_amdhsa_kernel

_ZN12_GLOBAL__N_110gemm_fullkILi1ELi4EEEvPKDF16_S2_PKfPDF16_PfS6_S4_S4_S4_S4_S4_S5_:
	s_load_dwordx2 s[4:5], s[0:1], 0x38
	s_and_b32 s3, s2, 63
	s_lshl_b32 s16, s3, 5
	s_lshl_b32 s6, s3, 13
	v_lshlrev_b32_e32 v1, 4, v0
	s_waitcnt lgkmcnt(0)
	s_add_u32 s4, s4, s6
	s_addc_u32 s5, s5, 0
	global_load_dwordx4 v[2:5], v1, s[4:5]
	v_lshlrev_b32_e32 v1, 2, v0
	v_cmp_lt_u32_e32 vcc, 31, v0
	s_and_saveexec_b64 s[4:5], vcc
	s_xor_b64 s[4:5], exec, s[4:5]
	s_cbranch_execz .LBB17_10
	v_cmp_lt_u32_e32 vcc, 63, v0
	s_and_saveexec_b64 s[6:7], vcc
	s_xor_b64 s[6:7], exec, s[6:7]
	s_cbranch_execz .LBB17_7
	s_movk_i32 s8, 0x47
	v_cmp_lt_u32_e32 vcc, s8, v0
	s_and_saveexec_b64 s[8:9], vcc
	s_xor_b64 s[8:9], exec, s[8:9]
	s_cbranch_execz .LBB17_4
	s_load_dwordx2 s[10:11], s[0:1], 0x10
	s_lshl_b32 s12, s16, 2
	v_lshlrev_b32_e32 v6, 2, v1
	v_mov_b32_e32 v7, 0
	s_movk_i32 s14, 0x50
	s_waitcnt lgkmcnt(0)
	s_add_u32 s10, s10, s12
	s_addc_u32 s11, s11, 0
	s_movk_i32 s12, 0xfb80
	v_lshl_add_u64 v[6:7], s[10:11], 0, v[6:7]
	s_mov_b32 s13, -1
	v_lshl_add_u64 v[6:7], v[6:7], 0, s[12:13]
	v_mov_b32_e32 v8, s11
	v_cmp_gt_u32_e32 vcc, s14, v0
	s_nop 1
	v_cndmask_b32_e32 v7, v8, v7, vcc
	v_mov_b32_e32 v8, s10
	v_cndmask_b32_e32 v6, v8, v6, vcc

.LBB17_12:
	s_or_b64 exec, exec, s[14:15]
	v_lshrrev_b32_e32 v180, 6, v0
	s_lshr_b32 s0, s2, 5
	s_and_b32 s0, s0, 0x7fffffe
	s_mov_b32 s1, 0
	v_lshlrev_b32_e32 v8, 17, v180
	v_mov_b32_e32 v9, 0
	v_and_b32_e32 v14, 63, v0
	s_lshl_b64 s[14:15], s[0:1], 10
	v_lshlrev_b32_e32 v10, 14, v180
	s_waitcnt lgkmcnt(0)
	v_lshl_add_u64 v[12:13], s[8:9], 0, v[8:9]
	v_lshl_or_b32 v10, s3, 18, v10
	v_mov_b32_e32 v11, v9
	v_lshl_add_u64 v[12:13], v[12:13], 0, s[14:15]
	v_lshlrev_b32_e32 v8, 4, v14
	v_lshl_add_u64 v[10:11], s[10:11], 0, v[10:11]
	v_lshl_add_u64 v[24:25], v[12:13], 0, v[8:9]
	v_lshrrev_b32_e32 v12, 2, v0
	v_lshl_add_u64 v[176:177], v[10:11], 0, v[8:9]
	v_lshrrev_b32_e32 v10, 8, v0
	v_lshrrev_b32_e32 v11, 3, v0
	v_and_b32_e32 v12, 12, v12
	v_and_b32_e32 v26, 15, v0
	v_bfe_u32 v30, v0, 6, 1
	v_or_b32_e32 v28, s0, v10
	v_and_or_b32 v29, v11, 16, v12
	v_lshl_or_b32 v10, v28, 4, v26
	v_lshl_or_b32 v27, v30, 1, v29
	v_mov_b32_e32 v11, v9
	v_or_b32_e32 v14, s16, v27
	v_lshlrev_b64 v[12:13], 13, v[10:11]
	v_lshl_add_u64 v[10:11], s[4:5], 0, v[12:13]
	v_lshlrev_b32_e32 v14, 2, v14
	v_mov_b32_e32 v15, v9
	v_lshl_add_u64 v[10:11], v[10:11], 0, v[14:15]
	s_mov_b32 s2, 0x400000
	v_add_co_u32_e32 v16, vcc, s2, v10
	v_lshl_add_u64 v[12:13], s[6:7], 0, v[12:13]
	s_nop 0
	v_addc_co_u32_e32 v17, vcc, 0, v11, vcc
	v_lshl_add_u64 v[22:23], v[12:13], 0, v[14:15]
	s_mov_b32 s0, 0x100000
	v_add_co_u32_e32 v32, vcc, s0, v22
	s_mov_b32 s0, 0x200000
	s_nop 0
	v_addc_co_u32_e32 v33, vcc, 0, v23, vcc
	v_add_co_u32_e32 v34, vcc, s0, v22
	s_mov_b32 s0, 0x300000
	s_nop 0
	v_addc_co_u32_e32 v35, vcc, 0, v23, vcc
	v_add_co_u32_e32 v36, vcc, s0, v22
	s_mov_b32 s0, 0x20000
	s_nop 0
	v_addc_co_u32_e32 v37, vcc, 0, v23, vcc
	v_add_co_u32_e32 v84, vcc, s0, v176
	s_mov_b32 s0, 0x21000
	s_nop 0
	v_addc_co_u32_e32 v85, vcc, 0, v177, vcc
	v_add_co_u32_e32 v148, vcc, s0, v176
	s_movk_i32 s0, 0x2000
	s_nop 0
	v_addc_co_u32_e32 v149, vcc, 0, v177, vcc
	v_add_co_u32_e32 v64, vcc, s0, v24
	s_movk_i32 s1, 0x4000
	s_nop 0
	v_addc_co_u32_e32 v65, vcc, 0, v25, vcc
	v_add_co_u32_e32 v86, vcc, s1, v24
	s_movk_i32 s1, 0x6000
	s_nop 0
	v_addc_co_u32_e32 v87, vcc, 0, v25, vcc
	v_add_co_u32_e32 v92, vcc, s1, v24
	s_movk_i32 s1, 0x1000
	s_nop 0
	v_addc_co_u32_e32 v93, vcc, 0, v25, vcc
	v_add_co_u32_e32 v140, vcc, s1, v176
	global_load_dwordx2 v[20:21], v[16:17], off
	s_nop 0
	v_addc_co_u32_e32 v141, vcc, 0, v177, vcc
	v_add_co_u32_e32 v164, vcc, s0, v176
	s_mov_b32 s0, 0x8000
	s_nop 0
	v_addc_co_u32_e32 v165, vcc, 0, v177, vcc
	v_add_co_u32_e32 v108, vcc, s0, v24
	s_mov_b32 s0, 0xa000
	s_nop 0
	v_addc_co_u32_e32 v109, vcc, 0, v25, vcc
	v_add_co_u32_e32 v116, vcc, s0, v24
	s_mov_b32 s0, 0xc000
	s_nop 0
	v_addc_co_u32_e32 v117, vcc, 0, v25, vcc
	global_load_dwordx2 v[18:19], v[22:23], off
	global_load_dwordx2 v[14:15], v[32:33], off
	global_load_dwordx2 v[12:13], v[34:35], off
	global_load_dwordx2 v[16:17], v[36:37], off
	s_nop 0
	global_load_dwordx4 v[32:35], v[24:25], off
	global_load_dwordx4 v[36:39], v[24:25], off offset:1024
	global_load_dwordx4 v[40:43], v[176:177], off
	global_load_dwordx4 v[44:47], v[176:177], off offset:1024
	global_load_dwordx4 v[48:51], v[64:65], off
	global_load_dwordx4 v[52:55], v[64:65], off offset:1024
	global_load_dwordx4 v[56:59], v[84:85], off offset:1024
	global_load_dwordx4 v[60:63], v[84:85], off offset:2048
	s_nop 0
	global_load_dwordx4 v[64:67], v[86:87], off
	global_load_dwordx4 v[68:71], v[86:87], off offset:1024
	global_load_dwordx4 v[72:75], v[176:177], off offset:2048
	global_load_dwordx4 v[76:79], v[176:177], off offset:3072
	global_load_dwordx4 v[80:83], v[84:85], off offset:3072
	s_nop 0
	global_load_dwordx4 v[84:87], v[92:93], off
	global_load_dwordx4 v[88:91], v[92:93], off offset:1024
	s_nop 0
	global_load_dwordx4 v[92:95], v[148:149], off offset:-4096
	global_load_dwordx4 v[96:99], v[148:149], off
	global_load_dwordx4 v[100:103], v[108:109], off
	global_load_dwordx4 v[104:107], v[108:109], off offset:1024
	s_nop 0
	global_load_dwordx4 v[108:111], v[116:117], off
	global_load_dwordx4 v[112:115], v[116:117], off offset:1024
	s_nop 0
	global_load_dwordx4 v[116:119], v[140:141], off offset:1024
	global_load_dwordx4 v[120:123], v[140:141], off offset:2048
	global_load_dwordx4 v[124:127], v[148:149], off offset:1024
	global_load_dwordx4 v[128:131], v[148:149], off offset:2048
	v_add_co_u32_e32 v136, vcc, s0, v24
	s_mov_b32 s0, 0xe000
	s_nop 0
	v_addc_co_u32_e32 v137, vcc, 0, v25, vcc
	global_load_dwordx4 v[132:135], v[136:137], off
	s_nop 0
	global_load_dwordx4 v[136:139], v[136:137], off offset:1024
	s_nop 0
	global_load_dwordx4 v[140:143], v[140:141], off offset:3072
	s_nop 0
	global_load_dwordx4 v[144:147], v[164:165], off offset:-4096
	s_nop 0
	global_load_dwordx4 v[148:151], v[148:149], off offset:3072
	v_add_co_u32_e32 v156, vcc, s0, v24
	v_lshrrev_b32_e32 v31, 7, v0
	s_nop 0
	v_addc_co_u32_e32 v157, vcc, 0, v25, vcc
	global_load_dwordx4 v[152:155], v[156:157], off
	s_nop 0
	global_load_dwordx4 v[156:159], v[156:157], off offset:1024
	s_waitcnt vmcnt(29)
	v_mfma_f32_16x16x32_f16 v[160:163], v[40:43], v[32:35], 0
	s_waitcnt vmcnt(16)
	v_mfma_f32_16x16x32_f16 v[32:35], v[92:95], v[32:35], 0
	v_mfma_f32_16x16x32_f16 v[40:43], v[40:43], v[36:39], 0
	v_mfma_f32_16x16x32_f16 v[36:39], v[92:95], v[36:39], 0
	v_mfma_f32_16x16x32_f16 v[92:95], v[44:47], v[48:51], v[160:163]
	v_mfma_f32_16x16x32_f16 v[32:35], v[56:59], v[48:51], v[32:35]
	v_mfma_f32_16x16x32_f16 v[40:43], v[44:47], v[52:55], v[40:43]
	v_mfma_f32_16x16x32_f16 v[36:39], v[56:59], v[52:55], v[36:39]
	v_mfma_f32_16x16x32_f16 v[44:47], v[72:75], v[64:67], v[92:95]
	v_mfma_f32_16x16x32_f16 v[32:35], v[60:63], v[64:67], v[32:35]
	v_mfma_f32_16x16x32_f16 v[40:43], v[72:75], v[68:71], v[40:43]
	v_mfma_f32_16x16x32_f16 v[36:39], v[60:63], v[68:71], v[36:39]
	v_mfma_f32_16x16x32_f16 v[44:47], v[76:79], v[84:87], v[44:47]
	v_mfma_f32_16x16x32_f16 v[32:35], v[80:83], v[84:87], v[32:35]
	v_mfma_f32_16x16x32_f16 v[40:43], v[76:79], v[88:91], v[40:43]
	v_mfma_f32_16x16x32_f16 v[36:39], v[80:83], v[88:91], v[36:39]
	s_mov_b32 s0, 0x22000
	v_add_co_u32_e32 v166, vcc, s0, v176
	s_mov_b32 s0, 0x23000
	s_nop 0
	v_addc_co_u32_e32 v167, vcc, 0, v177, vcc
	v_add_co_u32_e32 v178, vcc, s0, v176
	s_mov_b32 s0, 0x10000
	s_nop 0
	v_addc_co_u32_e32 v179, vcc, 0, v177, vcc
	v_add_co_u32_e32 v56, vcc, s0, v24
	s_mov_b32 s0, 0x12000
	s_nop 0
	v_addc_co_u32_e32 v57, vcc, 0, v25, vcc
	v_add_co_u32_e32 v72, vcc, s0, v24
	s_mov_b32 s0, 0x14000
	s_nop 0
	v_addc_co_u32_e32 v73, vcc, 0, v25, vcc
	v_add_co_u32_e32 v88, vcc, s0, v24
	global_load_dwordx4 v[48:51], v[178:179], off offset:-4096
	s_nop 0
	v_addc_co_u32_e32 v89, vcc, 0, v25, vcc
	global_load_dwordx4 v[52:55], v[56:57], off
	s_nop 0
	global_load_dwordx4 v[56:59], v[56:57], off offset:1024
	s_nop 0
	global_load_dwordx4 v[60:63], v[164:165], off
	global_load_dwordx4 v[64:67], v[164:165], off offset:1024
	global_load_dwordx4 v[68:71], v[72:73], off
	s_nop 0
	global_load_dwordx4 v[72:75], v[72:73], off offset:1024
	s_nop 0
	global_load_dwordx4 v[76:79], v[166:167], off offset:1024
	global_load_dwordx4 v[80:83], v[166:167], off offset:2048
	global_load_dwordx4 v[84:87], v[88:89], off
	s_nop 0
	global_load_dwordx4 v[88:91], v[88:89], off offset:1024
	s_nop 0
	global_load_dwordx4 v[92:95], v[164:165], off offset:2048
	global_load_dwordx4 v[160:163], v[164:165], off offset:3072
	s_nop 0
	global_load_dwordx4 v[164:167], v[166:167], off offset:3072
	s_mov_b32 s0, 0x16000
	v_add_co_u32_e32 v172, vcc, s0, v24
	s_nop 1
	v_addc_co_u32_e32 v173, vcc, 0, v25, vcc
	global_load_dwordx4 v[168:171], v[172:173], off
	s_nop 0
	global_load_dwordx4 v[172:175], v[172:173], off offset:1024
	s_waitcnt vmcnt(19)
	v_mfma_f32_16x16x32_f16 v[44:47], v[144:147], v[100:103], v[44:47]
	v_mfma_f32_16x16x32_f16 v[32:35], v[96:99], v[100:103], v[32:35]
	v_mfma_f32_16x16x32_f16 v[40:43], v[144:147], v[104:107], v[40:43]
	v_mfma_f32_16x16x32_f16 v[36:39], v[96:99], v[104:107], v[36:39]
	v_mfma_f32_16x16x32_f16 v[44:47], v[116:119], v[108:111], v[44:47]
	v_mfma_f32_16x16x32_f16 v[32:35], v[124:127], v[108:111], v[32:35]
	v_mfma_f32_16x16x32_f16 v[40:43], v[116:119], v[112:115], v[40:43]
	v_mfma_f32_16x16x32_f16 v[36:39], v[124:127], v[112:115], v[36:39]
	v_mfma_f32_16x16x32_f16 v[44:47], v[120:123], v[132:135], v[44:47]
	v_mfma_f32_16x16x32_f16 v[32:35], v[128:131], v[132:135], v[32:35]
	v_mfma_f32_16x16x32_f16 v[40:43], v[120:123], v[136:139], v[40:43]
	v_mfma_f32_16x16x32_f16 v[36:39], v[128:131], v[136:139], v[36:39]
	s_waitcnt vmcnt(17)
	v_mfma_f32_16x16x32_f16 v[44:47], v[140:143], v[152:155], v[44:47]
	v_mfma_f32_16x16x32_f16 v[32:35], v[148:151], v[152:155], v[32:35]
	s_waitcnt vmcnt(16)
	v_mfma_f32_16x16x32_f16 v[40:43], v[140:143], v[156:159], v[40:43]
	v_mfma_f32_16x16x32_f16 v[36:39], v[148:151], v[156:159], v[36:39]
	s_movk_i32 s0, 0x3000
	v_add_co_u32_e32 v140, vcc, s0, v176
	s_mov_b32 s0, 0x18000
	s_nop 0
	v_addc_co_u32_e32 v141, vcc, 0, v177, vcc
	v_add_co_u32_e32 v100, vcc, s0, v24
	s_mov_b32 s0, 0x1a000
	s_nop 0
	v_addc_co_u32_e32 v101, vcc, 0, v25, vcc
	v_add_co_u32_e32 v124, vcc, s0, v24
	s_mov_b32 s0, 0x1c000
	s_nop 0
	v_addc_co_u32_e32 v125, vcc, 0, v25, vcc
	v_add_co_u32_e32 v132, vcc, s0, v24
	global_load_dwordx4 v[96:99], v[100:101], off
	s_nop 0
	global_load_dwordx4 v[100:103], v[100:101], off offset:1024
	s_nop 0
	global_load_dwordx4 v[104:107], v[140:141], off
	global_load_dwordx4 v[108:111], v[140:141], off offset:1024
	global_load_dwordx4 v[112:115], v[178:179], off
	global_load_dwordx4 v[116:119], v[178:179], off offset:1024
	v_addc_co_u32_e32 v133, vcc, 0, v25, vcc
	global_load_dwordx4 v[120:123], v[124:125], off
	s_nop 0
	global_load_dwordx4 v[124:127], v[124:125], off offset:1024
	s_nop 0
	global_load_dwordx4 v[128:131], v[132:133], off
	s_nop 0
	global_load_dwordx4 v[132:135], v[132:133], off offset:1024
	s_nop 0
	global_load_dwordx4 v[136:139], v[140:141], off offset:2048
	s_nop 0
	global_load_dwordx4 v[140:143], v[140:141], off offset:3072
	s_nop 0
	global_load_dwordx4 v[144:147], v[178:179], off offset:2048
	global_load_dwordx4 v[148:151], v[178:179], off offset:3072
	s_mov_b32 s0, 0x1e000
	v_add_co_u32_e32 v24, vcc, s0, v24
	s_nop 1
	v_addc_co_u32_e32 v25, vcc, 0, v25, vcc
	global_load_dwordx4 v[152:155], v[24:25], off
	global_load_dwordx4 v[156:159], v[24:25], off offset:1024
	s_waitcnt vmcnt(28)
	v_mfma_f32_16x16x32_f16 v[44:47], v[60:63], v[52:55], v[44:47]
	v_mfma_f32_16x16x32_f16 v[32:35], v[48:51], v[52:55], v[32:35]
	v_mfma_f32_16x16x32_f16 v[40:43], v[60:63], v[56:59], v[40:43]
	v_mfma_f32_16x16x32_f16 v[36:39], v[48:51], v[56:59], v[36:39]
	s_waitcnt vmcnt(26)
	v_mfma_f32_16x16x32_f16 v[44:47], v[64:67], v[68:71], v[44:47]
	s_waitcnt vmcnt(24)
	v_mfma_f32_16x16x32_f16 v[32:35], v[76:79], v[68:71], v[32:35]
	v_mfma_f32_16x16x32_f16 v[40:43], v[64:67], v[72:75], v[40:43]
	v_mfma_f32_16x16x32_f16 v[36:39], v[76:79], v[72:75], v[36:39]
	s_waitcnt vmcnt(20)
	v_mfma_f32_16x16x32_f16 v[44:47], v[92:95], v[84:87], v[44:47]
	v_mfma_f32_16x16x32_f16 v[32:35], v[80:83], v[84:87], v[32:35]
	v_mfma_f32_16x16x32_f16 v[40:43], v[92:95], v[88:91], v[40:43]
	v_mfma_f32_16x16x32_f16 v[36:39], v[80:83], v[88:91], v[36:39]
	s_waitcnt vmcnt(17)
	v_mfma_f32_16x16x32_f16 v[44:47], v[160:163], v[168:171], v[44:47]
	v_mfma_f32_16x16x32_f16 v[32:35], v[164:167], v[168:171], v[32:35]
	s_waitcnt vmcnt(16)
	v_mfma_f32_16x16x32_f16 v[40:43], v[160:163], v[172:175], v[40:43]
	v_mfma_f32_16x16x32_f16 v[36:39], v[164:167], v[172:175], v[36:39]
	s_waitcnt vmcnt(13)
	v_mfma_f32_16x16x32_f16 v[44:47], v[104:107], v[96:99], v[44:47]
	s_waitcnt vmcnt(11)
	v_mfma_f32_16x16x32_f16 v[32:35], v[112:115], v[96:99], v[32:35]
	v_mfma_f32_16x16x32_f16 v[40:43], v[104:107], v[100:103], v[40:43]
	v_mfma_f32_16x16x32_f16 v[36:39], v[112:115], v[100:103], v[36:39]
	s_waitcnt vmcnt(9)
	v_mfma_f32_16x16x32_f16 v[44:47], v[108:111], v[120:123], v[44:47]
	v_mfma_f32_16x16x32_f16 v[32:35], v[116:119], v[120:123], v[32:35]
	s_waitcnt vmcnt(8)
	v_mfma_f32_16x16x32_f16 v[40:43], v[108:111], v[124:127], v[40:43]
	v_mfma_f32_16x16x32_f16 v[36:39], v[116:119], v[124:127], v[36:39]
	s_waitcnt vmcnt(5)
	v_mfma_f32_16x16x32_f16 v[44:47], v[136:139], v[128:131], v[44:47]
	s_waitcnt vmcnt(3)
	v_mfma_f32_16x16x32_f16 v[32:35], v[144:147], v[128:131], v[32:35]
	v_mfma_f32_16x16x32_f16 v[40:43], v[136:139], v[132:135], v[40:43]
	v_mfma_f32_16x16x32_f16 v[36:39], v[144:147], v[132:135], v[36:39]
	s_waitcnt vmcnt(1)
	v_mfma_f32_16x16x32_f16 v[44:47], v[140:143], v[152:155], v[44:47]
	v_mfma_f32_16x16x32_f16 v[32:35], v[148:151], v[152:155], v[32:35]
	s_waitcnt vmcnt(0)
	v_mfma_f32_16x16x32_f16 v[40:43], v[140:143], v[156:159], v[40:43]
	v_mfma_f32_16x16x32_f16 v[36:39], v[148:151], v[156:159], v[36:39]
	v_lshlrev_b32_e32 v24, 12, v180
	v_add3_u32 v24, 0, v8, v24
	s_nop 1
	ds_write_b128 v24, v[44:47]
	ds_write_b128 v24, v[32:35] offset:1024
	s_nop 0
	ds_write_b128 v24, v[40:43] offset:2048
	ds_write_b128 v24, v[36:39] offset:3072
	v_lshrrev_b32_e32 v24, 4, v0
	v_and_b32_e32 v25, 60, v1
	v_mul_u32_u24_e32 v24, 0x110, v24
	v_lshlrev_b32_e32 v25, 2, v25
	s_movk_i32 s0, 0x50
	v_add3_u32 v24, 0, v24, v25
	v_cmp_gt_u32_e32 vcc, s0, v0
	ds_write_b128 v24, v[2:5] offset:32768
	s_and_saveexec_b64 s[0:1], vcc
	s_cbranch_execz .LBB17_14
	global_load_dwordx4 v[2:5], v[6:7], off
	v_lshl_add_u32 v0, v1, 2, 0
	s_waitcnt vmcnt(0)
	ds_write_b128 v0, v[2:5] offset:41472
.LBB17_14:
	s_or_b64 exec, exec, s[0:1]
	v_lshlrev_b32_e32 v0, 10, v31
	v_add3_u32 v8, 0, v0, v8
	s_waitcnt lgkmcnt(0)
	s_barrier
	ds_read_b128 v[0:3], v8
	ds_read_b128 v[4:7], v8 offset:4096
	ds_read_b128 v[32:35], v8 offset:8192
	ds_read_b128 v[36:39], v8 offset:12288
	v_cmp_eq_u32_e32 vcc, 0, v30
	s_waitcnt lgkmcnt(2)
	v_pk_add_f32 v[2:3], v[2:3], v[6:7]
	v_pk_add_f32 v[4:5], v[0:1], v[4:5]
	s_waitcnt lgkmcnt(1)
	v_pk_add_f32 v[6:7], v[2:3], v[34:35]
	ds_read_b128 v[0:3], v8 offset:16384
	v_pk_add_f32 v[4:5], v[4:5], v[32:33]
	s_waitcnt lgkmcnt(1)
	v_pk_add_f32 v[24:25], v[6:7], v[38:39]
	v_pk_add_f32 v[36:37], v[4:5], v[36:37]
	ds_read_b128 v[4:7], v8 offset:20480
	ds_read_b128 v[32:35], v8 offset:24576
	s_waitcnt lgkmcnt(2)
	v_pk_add_f32 v[24:25], v[24:25], v[2:3]
	v_pk_add_f32 v[36:37], v[36:37], v[0:1]
	ds_read_b128 v[0:3], v8 offset:28672
	s_waitcnt lgkmcnt(2)
	v_pk_add_f32 v[6:7], v[24:25], v[6:7]
	v_pk_add_f32 v[4:5], v[36:37], v[4:5]
	s_waitcnt lgkmcnt(1)
	v_pk_add_f32 v[6:7], v[6:7], v[34:35]
	v_pk_add_f32 v[4:5], v[4:5], v[32:33]
	s_waitcnt lgkmcnt(0)
	v_pk_add_f32 v[2:3], v[6:7], v[2:3]
	v_lshl_add_u32 v6, v27, 2, 0
	v_pk_add_f32 v[0:1], v[4:5], v[0:1]
	ds_read_b64 v[4:5], v6 offset:42624
	v_cndmask_b32_e32 v1, v3, v1, vcc
	v_cndmask_b32_e32 v0, v2, v0, vcc
	v_mad_u32_u24 v2, v27, 12, v6
	ds_read_b128 v[30:33], v2 offset:41472
	s_waitcnt lgkmcnt(1)
	v_pk_add_f32 v[0:1], v[0:1], v[4:5]
	v_lshl_add_u32 v8, v27, 8, v2
	v_pk_add_f32 v[74:75], v[20:21], v[0:1]
	v_add_co_u32_e32 v0, vcc, s2, v22
	s_waitcnt lgkmcnt(0)
	v_mov_b32_e32 v60, v30
	v_addc_co_u32_e32 v1, vcc, 0, v23, vcc
	global_store_dwordx2 v[0:1], v[74:75], off
	v_mad_i32_i24 v0, v27, -12, v2
	v_or_b32_e32 v1, 1, v27
	ds_read_b128 v[22:25], v8 offset:32944
	ds_read_b128 v[34:37], v8 offset:32960
	ds_read_b128 v[38:41], v8 offset:32976
	v_lshl_add_u32 v4, v1, 4, 0
	ds_read_b64 v[20:21], v0 offset:42496
	ds_read_b128 v[42:45], v4 offset:41472
	v_lshl_add_u32 v70, v1, 8, v4
	ds_read_b128 v[46:49], v70 offset:32944
	ds_read_b128 v[50:53], v70 offset:32960
	ds_read_b128 v[54:57], v70 offset:32976
	ds_read_b128 v[0:3], v2 offset:41984
	s_waitcnt lgkmcnt(8)
	v_mov_b32_e32 v58, v22
	s_waitcnt lgkmcnt(3)
	v_mov_b32_e32 v59, v46
	v_mov_b32_e32 v61, v42
	ds_read_b128 v[4:7], v4 offset:41984
	v_pk_fma_f32 v[76:77], v[18:19], v[58:59], v[60:61]
	ds_read_b128 v[58:61], v8 offset:32992
	ds_read_b128 v[62:65], v8 offset:33008
	ds_read_b128 v[66:69], v70 offset:32992
	ds_read_b128 v[70:73], v70 offset:33008
	v_mov_b32_e32 v78, v34
	s_waitcnt lgkmcnt(7)
	v_mov_b32_e32 v79, v50
	v_mov_b32_e32 v46, v23
	v_mov_b32_e32 v42, v31
	v_pk_fma_f32 v[22:23], v[18:19], v[46:47], v[42:43]
	v_mov_b32_e32 v50, v35
	v_pk_fma_f32 v[34:35], v[14:15], v[78:79], v[76:77]
	v_mov_b32_e32 v42, v38
	s_waitcnt lgkmcnt(6)
	v_mov_b32_e32 v43, v54
	v_pk_fma_f32 v[34:35], v[12:13], v[42:43], v[34:35]
	s_waitcnt lgkmcnt(3)
	v_mov_b32_e32 v42, v58
	s_waitcnt lgkmcnt(1)
	v_mov_b32_e32 v43, v66
	v_pk_fma_f32 v[34:35], v[16:17], v[42:43], v[34:35]
	v_mov_b32_e32 v42, v62
	s_waitcnt lgkmcnt(0)
	v_mov_b32_e32 v43, v70
	v_pk_fma_f32 v[34:35], v[74:75], v[42:43], v[34:35]
	v_pk_fma_f32 v[22:23], v[14:15], v[50:51], v[22:23]
	v_mul_f32_e32 v8, 0x3d372713, v34
	v_mul_f32_e32 v8, v34, v8
	v_fma_f32 v8, v34, v8, v34
	v_mov_b32_e32 v54, v39
	v_mul_f32_e32 v8, 0x3f4c422a, v8
	v_pk_fma_f32 v[22:23], v[12:13], v[54:55], v[22:23]
	v_mov_b32_e32 v66, v59
	v_add_f32_e32 v8, v8, v8
	v_pk_fma_f32 v[22:23], v[16:17], v[66:67], v[22:23]
	v_mov_b32_e32 v70, v63
	v_mov_b32_e32 v30, v24
	v_mov_b32_e32 v31, v48
	v_mul_f32_e32 v8, 0x3fb8aa3b, v8
	v_pk_fma_f32 v[22:23], v[74:75], v[70:71], v[22:23]
	v_mov_b32_e32 v42, v32
	v_mov_b32_e32 v43, v44
	v_mov_b32_e32 v48, v25
	v_mov_b32_e32 v44, v33
	v_exp_f32_e32 v24, v8
	v_mul_f32_e32 v8, 0x3d372713, v22
	v_pk_fma_f32 v[30:31], v[18:19], v[30:31], v[42:43]
	v_mov_b32_e32 v42, v36
	v_mov_b32_e32 v43, v52
	v_pk_fma_f32 v[18:19], v[18:19], v[48:49], v[44:45]
	v_mov_b32_e32 v52, v37
	v_mul_f32_e32 v8, v22, v8
	v_pk_fma_f32 v[30:31], v[14:15], v[42:43], v[30:31]
	v_mov_b32_e32 v42, v40
	v_mov_b32_e32 v43, v56
	v_pk_fma_f32 v[14:15], v[14:15], v[52:53], v[18:19]
	v_mov_b32_e32 v56, v41
	v_fma_f32 v8, v22, v8, v22
	v_pk_fma_f32 v[30:31], v[12:13], v[42:43], v[30:31]
	v_pk_fma_f32 v[12:13], v[12:13], v[56:57], v[14:15]
	v_mul_f32_e32 v14, 0x3d372713, v35
	v_mul_f32_e32 v8, 0x3f4c422a, v8
	v_mov_b32_e32 v42, v60
	v_mov_b32_e32 v43, v68
	v_mul_f32_e32 v14, v35, v14
	v_add_f32_e32 v8, v8, v8
	v_pk_fma_f32 v[30:31], v[16:17], v[42:43], v[30:31]
	v_mov_b32_e32 v42, v64
	v_mov_b32_e32 v43, v72
	v_fma_f32 v14, v35, v14, v35
	v_mul_f32_e32 v8, 0x3fb8aa3b, v8
	v_pk_fma_f32 v[30:31], v[74:75], v[42:43], v[30:31]
	v_mul_f32_e32 v14, 0x3f4c422a, v14
	v_exp_f32_e32 v38, v8
	v_mul_f32_e32 v8, 0x3d372713, v30
	v_add_f32_e32 v14, v14, v14
	v_mul_f32_e32 v8, v30, v8
	v_mul_f32_e32 v14, 0x3fb8aa3b, v14
	v_fma_f32 v8, v30, v8, v30
	v_exp_f32_e32 v25, v14
	v_mul_f32_e32 v8, 0x3f4c422a, v8
	v_mov_b32_e32 v68, v61
	v_add_f32_e32 v8, v8, v8
	v_pk_fma_f32 v[12:13], v[16:17], v[68:69], v[12:13]
	v_mov_b32_e32 v72, v65
	v_mul_f32_e32 v8, 0x3fb8aa3b, v8
	v_pk_fma_f32 v[12:13], v[74:75], v[72:73], v[12:13]
	v_exp_f32_e32 v32, v8
	v_mul_f32_e32 v8, 0x3d372713, v12
	v_pk_add_f32 v[14:15], v[24:25], 1.0 op_sel_hi:[1,0]
	v_mul_f32_e32 v8, v12, v8
	v_div_scale_f32 v17, s[0:1], v15, v15, 2.0
	v_fma_f32 v8, v12, v8, v12
	v_rcp_f32_e32 v18, v17
	v_mul_f32_e32 v8, 0x3f4c422a, v8
	v_add_f32_e32 v8, v8, v8
	v_mul_f32_e32 v8, 0x3fb8aa3b, v8
	v_exp_f32_e32 v16, v8
	v_fma_f32 v8, -v17, v18, 1.0
	v_fmac_f32_e32 v18, v8, v18
	v_div_scale_f32 v8, vcc, 2.0, v15, 2.0
	v_mul_f32_e32 v19, v8, v18
	v_fma_f32 v24, -v17, v19, v8
	v_fmac_f32_e32 v19, v24, v18
	v_fma_f32 v8, -v17, v19, v8
	v_div_scale_f32 v17, s[0:1], v14, v14, 2.0
	v_rcp_f32_e32 v24, v17
	v_div_fmas_f32 v8, v8, v18, v19
	v_div_fixup_f32 v15, v8, v15, 2.0
	v_fma_f32 v8, -v17, v24, 1.0
	v_fmac_f32_e32 v24, v8, v24
	v_div_scale_f32 v8, vcc, 2.0, v14, 2.0
	v_mul_f32_e32 v18, v8, v24
	v_fma_f32 v19, -v17, v18, v8
	v_fmac_f32_e32 v18, v19, v24
	v_fma_f32 v8, -v17, v18, v8
	v_div_fmas_f32 v8, v8, v24, v18
	v_div_fixup_f32 v14, v8, v14, 2.0
	v_mul_f32_e32 v8, 0x3d372713, v23
	v_mul_f32_e32 v8, v23, v8
	v_fma_f32 v8, v23, v8, v23
	v_mul_f32_e32 v8, 0x3f4c422a, v8
	v_add_f32_e32 v8, v8, v8
	v_mul_f32_e32 v8, 0x3fb8aa3b, v8
	v_exp_f32_e32 v39, v8
	v_pk_add_f32 v[14:15], v[14:15], 1.0 op_sel_hi:[1,0] neg_lo:[1,0] neg_hi:[1,0]
	v_pk_mul_f32 v[18:19], v[34:35], 0.5 op_sel_hi:[1,0]
	v_pk_add_f32 v[14:15], v[14:15], 1.0 op_sel_hi:[1,0]
	v_pk_add_f32 v[24:25], v[38:39], 1.0 op_sel_hi:[1,0]
	v_pk_mul_f32 v[14:15], v[18:19], v[14:15]
	v_div_scale_f32 v8, s[0:1], v25, v25, 2.0
	v_rcp_f32_e32 v17, v8
	v_mov_b32_e32 v18, v0
	v_mov_b32_e32 v19, v4
	v_pk_mul_f32 v[22:23], v[22:23], 0.5 op_sel_hi:[1,0]
	v_fma_f32 v0, -v8, v17, 1.0
	v_fmac_f32_e32 v17, v0, v17
	v_div_scale_f32 v0, vcc, 2.0, v25, 2.0
	v_mul_f32_e32 v4, v0, v17
	v_fma_f32 v33, -v8, v4, v0
	v_fmac_f32_e32 v4, v33, v17
	v_fma_f32 v0, -v8, v4, v0
	v_div_scale_f32 v8, s[0:1], v24, v24, 2.0
	v_rcp_f32_e32 v33, v8
	v_div_fmas_f32 v0, v0, v17, v4
	v_div_fixup_f32 v25, v0, v25, 2.0
	v_fma_f32 v0, -v8, v33, 1.0
	v_fmac_f32_e32 v33, v0, v33
	v_div_scale_f32 v0, vcc, 2.0, v24, 2.0
	v_mul_f32_e32 v4, v0, v33
	v_fma_f32 v17, -v8, v4, v0
	v_fmac_f32_e32 v4, v17, v33
	v_fma_f32 v0, -v8, v4, v0
	v_div_fmas_f32 v0, v0, v33, v4
	v_div_fixup_f32 v24, v0, v24, 2.0
	v_mul_f32_e32 v0, 0x3d372713, v31
	v_mul_f32_e32 v0, v31, v0
	v_fma_f32 v0, v31, v0, v31
	v_mul_f32_e32 v0, 0x3f4c422a, v0
	v_add_f32_e32 v0, v0, v0
	v_mul_f32_e32 v0, 0x3fb8aa3b, v0
	v_exp_f32_e32 v33, v0
	v_pk_add_f32 v[24:25], v[24:25], 1.0 op_sel_hi:[1,0] neg_lo:[1,0] neg_hi:[1,0]
	v_mov_b32_e32 v4, v1
	v_pk_add_f32 v[24:25], v[24:25], 1.0 op_sel_hi:[1,0]
	s_nop 0
	v_pk_mul_f32 v[22:23], v[22:23], v[24:25]
	v_pk_add_f32 v[24:25], v[32:33], 1.0 op_sel_hi:[1,0]
	v_pk_mul_f32 v[0:1], v[22:23], v[4:5]
	v_div_scale_f32 v8, s[0:1], v25, v25, 2.0
	v_rcp_f32_e32 v17, v8
	v_pk_fma_f32 v[0:1], v[14:15], v[18:19], v[0:1]
	v_fma_f32 v4, -v8, v17, 1.0
	v_fmac_f32_e32 v17, v4, v17
	v_div_scale_f32 v4, vcc, 2.0, v25, 2.0
	v_mul_f32_e32 v5, v4, v17
	v_fma_f32 v14, -v8, v5, v4
	v_fmac_f32_e32 v5, v14, v17
	v_fma_f32 v4, -v8, v5, v4
	v_div_scale_f32 v8, s[0:1], v24, v24, 2.0
	v_rcp_f32_e32 v14, v8
	v_div_fmas_f32 v4, v4, v17, v5
	v_div_fixup_f32 v5, v4, v25, 2.0
	v_fma_f32 v4, -v8, v14, 1.0
	v_fmac_f32_e32 v14, v4, v14
	v_div_scale_f32 v4, vcc, 2.0, v24, 2.0
	v_mul_f32_e32 v15, v4, v14
	v_fma_f32 v17, -v8, v15, v4
	v_fmac_f32_e32 v15, v17, v14
	v_fma_f32 v4, -v8, v15, v4
	v_mul_f32_e32 v8, 0x3d372713, v13
	v_mul_f32_e32 v8, v13, v8
	v_fma_f32 v8, v13, v8, v13
	v_mul_f32_e32 v8, 0x3f4c422a, v8
	v_add_f32_e32 v8, v8, v8
	v_mul_f32_e32 v8, 0x3fb8aa3b, v8
	v_div_fmas_f32 v4, v4, v14, v15
	v_exp_f32_e32 v17, v8
	v_div_fixup_f32 v4, v4, v24, 2.0
	v_pk_add_f32 v[4:5], v[4:5], 1.0 op_sel_hi:[1,0] neg_lo:[1,0] neg_hi:[1,0]
	v_pk_mul_f32 v[14:15], v[30:31], 0.5 op_sel_hi:[1,0]
	v_pk_add_f32 v[4:5], v[4:5], 1.0 op_sel_hi:[1,0]
	v_pk_mul_f32 v[12:13], v[12:13], 0.5 op_sel_hi:[1,0]
	v_pk_mul_f32 v[4:5], v[14:15], v[4:5]
	v_pk_add_f32 v[14:15], v[16:17], 1.0 op_sel_hi:[1,0]
	v_mov_b32_e32 v16, v2
	v_div_scale_f32 v8, s[0:1], v15, v15, 2.0
	v_rcp_f32_e32 v18, v8
	v_mov_b32_e32 v17, v6
	v_pk_fma_f32 v[0:1], v[4:5], v[16:17], v[0:1]
	v_div_scale_f32 v6, s[0:1], v14, v14, 2.0
	v_fma_f32 v2, -v8, v18, 1.0
	v_fmac_f32_e32 v18, v2, v18
	v_div_scale_f32 v2, vcc, 2.0, v15, 2.0
	v_mul_f32_e32 v4, v2, v18
	v_fma_f32 v5, -v8, v4, v2
	v_fmac_f32_e32 v4, v5, v18
	v_fma_f32 v2, -v8, v4, v2
	v_rcp_f32_e32 v8, v6
	v_div_fmas_f32 v2, v2, v18, v4
	v_div_fixup_f32 v5, v2, v15, 2.0
	s_mov_b32 s0, 0x500000
	v_fma_f32 v2, -v6, v8, 1.0
	v_fmac_f32_e32 v8, v2, v8
	v_div_scale_f32 v2, vcc, 2.0, v14, 2.0
	v_mul_f32_e32 v4, v2, v8
	v_fma_f32 v15, -v6, v4, v2
	v_fmac_f32_e32 v4, v15, v8
	v_fma_f32 v2, -v6, v4, v2
	v_div_fmas_f32 v2, v2, v8, v4
	v_div_fixup_f32 v4, v2, v14, 2.0
	v_pk_add_f32 v[4:5], v[4:5], 1.0 op_sel_hi:[1,0] neg_lo:[1,0] neg_hi:[1,0]
	v_mov_b32_e32 v6, v3
	v_pk_add_f32 v[4:5], v[4:5], 1.0 op_sel_hi:[1,0]
	v_add_co_u32_e32 v2, vcc, s0, v10
	v_pk_mul_f32 v[4:5], v[12:13], v[4:5]
	s_lshl_b32 s0, s3, 3
	v_pk_fma_f32 v[0:1], v[4:5], v[6:7], v[0:1]
	v_addc_co_u32_e32 v3, vcc, 0, v11, vcc
	v_pk_add_f32 v[0:1], v[20:21], v[0:1]
	s_addk_i32 s0, 0x100
	global_store_dwordx2 v[2:3], v[0:1], off
	v_add_u32_e32 v8, s0, v28
	v_lshlrev_b32_e32 v3, 1, v29
	v_cvt_pk_f16_f32 v2, v0, v1
	v_lshlrev_b64 v[0:1], 6, v[8:9]
	v_and_b32_e32 v3, 48, v3
	v_or3_b32 v0, v0, v3, v26
	v_and_b32_e32 v3, 6, v27
	v_lshl_add_u64 v[0:1], v[0:1], 4, s[12:13]
	v_lshlrev_b32_e32 v8, 1, v3
	v_lshl_add_u64 v[0:1], v[0:1], 0, v[8:9]
	global_store_dword v[0:1], v2, off
	s_endpgm
	s_nop 0
	s_nop 0
	s_nop 0
	s_nop 0
	s_nop 0
	s_nop 0
	s_nop 0
	s_nop 0
	s_nop 0
	s_nop 0
	s_nop 0
	s_nop 0
	s_nop 0
	s_nop 0
	s_nop 0
	s_nop 0
	s_nop 0
	s_endpgm

	.amdhsa_kernel _ZN12_GLOBAL__N_110gemm_fullkILi1ELi4EEEvPKDF16_S2_PKfPDF16_PfS6_S4_S4_S4_S4_S4_S5_
		.amdhsa_group_segment_fixed_size 0
		.amdhsa_private_segment_fixed_size 0
		.amdhsa_kernarg_size 96
		.amdhsa_user_sgpr_count 2
		.amdhsa_user_sgpr_dispatch_ptr 0
		.amdhsa_user_sgpr_queue_ptr 0
		.amdhsa_user_sgpr_kernarg_segment_ptr 1
		.amdhsa_user_sgpr_dispatch_id 0
		.amdhsa_user_sgpr_kernarg_preload_length 0
		.amdhsa_user_sgpr_kernarg_preload_offset 0
		.amdhsa_user_sgpr_private_segment_size 0
		.amdhsa_uses_dynamic_stack 0
		.amdhsa_enable_private_segment 0
		.amdhsa_system_sgpr_workgroup_id_x 1
		.amdhsa_system_sgpr_workgroup_id_y 0
		.amdhsa_system_sgpr_workgroup_id_z 0
		.amdhsa_system_sgpr_workgroup_info 0
		.amdhsa_system_vgpr_workitem_id 0
		.amdhsa_next_free_vgpr 181
		.amdhsa_next_free_sgpr 18
		.amdhsa_accum_offset 184
		.amdhsa_reserve_vcc 1
		.amdhsa_float_round_mode_32 0
		.amdhsa_float_round_mode_16_64 0
		.amdhsa_float_denorm_mode_32 3
		.amdhsa_float_denorm_mode_16_64 3
		.amdhsa_dx10_clamp 1
		.amdhsa_ieee_mode 1
		.amdhsa_fp16_overflow 0
		.amdhsa_tg_split 0
		.amdhsa_exception_fp_ieee_invalid_op 0
		.amdhsa_exception_fp_denorm_src 0
		.amdhsa_exception_fp_ieee_div_zero 0
		.amdhsa_exception_fp_ieee_overflow 0
		.amdhsa_exception_fp_ieee_underflow 0
		.amdhsa_exception_fp_ieee_inexact 0
		.amdhsa_exception_int_div_zero 0
	.end_amdhsa_kernel

_ZN12_GLOBAL__N_110gemm_fullkILi0ELi5EEEvPKDF16_S2_PKfPDF16_PfS6_S4_S4_S4_S4_S4_S5_:
	s_load_dwordx8 s[4:11], s[0:1], 0x0
	s_lshr_b32 s0, s2, 5
	v_lshrrev_b32_e32 v230, 6, v0
	s_and_b32 s12, s0, 0x7fffffc
	s_and_b32 s2, s2, 0x7f
	s_mov_b32 s13, 0
	v_mul_u32_u24_e32 v4, 12, v230
	v_mov_b32_e32 v3, 0
	s_lshl_b64 s[0:1], s[12:13], 10
	s_mul_i32 s13, s2, 0xc0
	v_and_b32_e32 v1, 63, v0
	v_mul_u32_u24_e32 v2, 0x18000, v230
	v_add_lshl_u32 v4, s13, v4, 10
	v_mov_b32_e32 v5, v3
	s_waitcnt lgkmcnt(0)
	v_lshl_add_u64 v[4:5], s[6:7], 0, v[4:5]
	v_lshl_add_u64 v[6:7], s[4:5], 0, v[2:3]
	v_lshlrev_b32_e32 v2, 4, v1
	s_mov_b32 s3, 0x18000
	v_lshl_add_u64 v[208:209], v[4:5], 0, v[2:3]
	v_add_co_u32_e32 v80, vcc, s3, v208
	v_lshl_add_u64 v[6:7], v[6:7], 0, s[0:1]
	s_nop 0
	v_addc_co_u32_e32 v81, vcc, 0, v209, vcc
	s_mov_b32 s0, 0x19000
	v_add_co_u32_e32 v176, vcc, s0, v208
	v_lshl_add_u64 v[212:213], v[6:7], 0, v[2:3]
	s_nop 0
	v_addc_co_u32_e32 v177, vcc, 0, v209, vcc
	s_movk_i32 s0, 0x2000
	v_add_co_u32_e32 v52, vcc, s0, v212
	s_movk_i32 s1, 0x4000
	s_nop 0
	v_addc_co_u32_e32 v53, vcc, 0, v213, vcc
	v_add_co_u32_e32 v82, vcc, s1, v212
	s_movk_i32 s1, 0x6000
	s_nop 0
	v_addc_co_u32_e32 v83, vcc, 0, v213, vcc
	v_add_co_u32_e32 v96, vcc, s1, v212
	s_movk_i32 s1, 0x1000
	s_nop 0
	v_addc_co_u32_e32 v97, vcc, 0, v213, vcc
	v_add_co_u32_e32 v168, vcc, s1, v208
	global_load_dwordx4 v[4:7], v[212:213], off
	global_load_dwordx4 v[8:11], v[212:213], off offset:1024
	global_load_dwordx4 v[12:15], v[212:213], off offset:2048
	global_load_dwordx4 v[16:19], v[212:213], off offset:3072
	global_load_dwordx4 v[20:23], v[208:209], off
	global_load_dwordx4 v[24:27], v[208:209], off offset:1024
	v_addc_co_u32_e32 v169, vcc, 0, v209, vcc
	v_add_co_u32_e32 v210, vcc, s0, v208
	s_mov_b32 s0, 0x8000
	s_nop 0
	v_addc_co_u32_e32 v211, vcc, 0, v209, vcc
	v_add_co_u32_e32 v116, vcc, s0, v212
	s_mov_b32 s0, 0xa000
	s_nop 0
	v_addc_co_u32_e32 v117, vcc, 0, v213, vcc
	v_add_co_u32_e32 v132, vcc, s0, v212
	s_mov_b32 s0, 0xc000
	s_nop 0
	v_addc_co_u32_e32 v133, vcc, 0, v213, vcc
	v_add_co_u32_e32 v164, vcc, s0, v212
	global_load_dwordx4 v[28:31], v[52:53], off
	global_load_dwordx4 v[32:35], v[52:53], off offset:1024
	global_load_dwordx4 v[36:39], v[52:53], off offset:2048
	global_load_dwordx4 v[40:43], v[52:53], off offset:3072
	global_load_dwordx4 v[44:47], v[80:81], off offset:1024
	global_load_dwordx4 v[48:51], v[80:81], off offset:2048
	s_nop 0
	global_load_dwordx4 v[52:55], v[82:83], off
	global_load_dwordx4 v[56:59], v[82:83], off offset:1024
	global_load_dwordx4 v[60:63], v[82:83], off offset:2048
	global_load_dwordx4 v[64:67], v[82:83], off offset:3072
	global_load_dwordx4 v[68:71], v[208:209], off offset:2048
	global_load_dwordx4 v[72:75], v[208:209], off offset:3072
	global_load_dwordx4 v[76:79], v[80:81], off offset:3072
	s_nop 0
	global_load_dwordx4 v[80:83], v[96:97], off
	global_load_dwordx4 v[84:87], v[96:97], off offset:1024
	global_load_dwordx4 v[88:91], v[96:97], off offset:2048
	global_load_dwordx4 v[92:95], v[96:97], off offset:3072
	s_nop 0
	global_load_dwordx4 v[96:99], v[176:177], off offset:-4096
	global_load_dwordx4 v[100:103], v[176:177], off
	global_load_dwordx4 v[104:107], v[116:117], off
	global_load_dwordx4 v[108:111], v[116:117], off offset:1024
	global_load_dwordx4 v[112:115], v[116:117], off offset:2048
	s_nop 0
	global_load_dwordx4 v[116:119], v[116:117], off offset:3072
	s_nop 0
	global_load_dwordx4 v[120:123], v[132:133], off
	global_load_dwordx4 v[124:127], v[132:133], off offset:1024
	global_load_dwordx4 v[128:131], v[132:133], off offset:2048
	s_nop 0
	global_load_dwordx4 v[132:135], v[132:133], off offset:3072
	s_nop 0
	global_load_dwordx4 v[136:139], v[168:169], off offset:1024
	global_load_dwordx4 v[140:143], v[168:169], off offset:2048
	global_load_dwordx4 v[144:147], v[176:177], off offset:1024
	global_load_dwordx4 v[148:151], v[176:177], off offset:2048
	v_addc_co_u32_e32 v165, vcc, 0, v213, vcc
	global_load_dwordx4 v[152:155], v[164:165], off
	global_load_dwordx4 v[156:159], v[164:165], off offset:1024
	global_load_dwordx4 v[160:163], v[164:165], off offset:2048
	s_nop 0
	global_load_dwordx4 v[164:167], v[164:165], off offset:3072
	s_nop 0
	global_load_dwordx4 v[168:171], v[168:169], off offset:3072
	s_nop 0
	global_load_dwordx4 v[172:175], v[210:211], off offset:-4096
	s_nop 0
	global_load_dwordx4 v[176:179], v[176:177], off offset:3072
	s_mov_b32 s0, 0xe000
	v_add_co_u32_e32 v192, vcc, s0, v212
	s_lshl_b32 s0, s2, 7
	s_nop 0
	v_addc_co_u32_e32 v193, vcc, 0, v213, vcc
	global_load_dwordx4 v[180:183], v[192:193], off
	global_load_dwordx4 v[184:187], v[192:193], off offset:1024
	global_load_dwordx4 v[188:191], v[192:193], off offset:2048
	s_nop 0
	global_load_dwordx4 v[192:195], v[192:193], off offset:3072
	v_bfe_u32 v1, v0, 6, 1
	s_add_u32 s0, s8, s0
	s_addc_u32 s1, s9, 0
	v_lshlrev_b32_e32 v196, 6, v1
	v_mov_b32_e32 v197, v3
	v_lshl_add_u64 v[196:197], s[0:1], 0, v[196:197]
	v_and_b32_e32 v198, 48, v0
	v_mov_b32_e32 v199, v3
	v_lshl_add_u64 v[228:229], v[196:197], 0, v[198:199]
	s_waitcnt vmcnt(43)
	v_mfma_f32_16x16x32_f16 v[196:199], v[20:23], v[4:7], 0
	s_waitcnt vmcnt(24)
	v_mfma_f32_16x16x32_f16 v[4:7], v[96:99], v[4:7], 0
	v_mfma_f32_16x16x32_f16 v[200:203], v[20:23], v[8:11], 0
	v_mfma_f32_16x16x32_f16 v[8:11], v[96:99], v[8:11], 0
	v_mfma_f32_16x16x32_f16 v[204:207], v[20:23], v[12:15], 0
	v_mfma_f32_16x16x32_f16 v[12:15], v[96:99], v[12:15], 0
	v_mfma_f32_16x16x32_f16 v[20:23], v[20:23], v[16:19], 0
	v_mfma_f32_16x16x32_f16 v[16:19], v[96:99], v[16:19], 0
	v_mfma_f32_16x16x32_f16 v[96:99], v[24:27], v[28:31], v[196:199]
	v_mfma_f32_16x16x32_f16 v[4:7], v[44:47], v[28:31], v[4:7]
	v_mfma_f32_16x16x32_f16 v[28:31], v[24:27], v[32:35], v[200:203]
	v_mfma_f32_16x16x32_f16 v[8:11], v[44:47], v[32:35], v[8:11]
	v_mfma_f32_16x16x32_f16 v[32:35], v[24:27], v[36:39], v[204:207]
	v_mfma_f32_16x16x32_f16 v[12:15], v[44:47], v[36:39], v[12:15]
	v_mfma_f32_16x16x32_f16 v[20:23], v[24:27], v[40:43], v[20:23]
	v_mfma_f32_16x16x32_f16 v[16:19], v[44:47], v[40:43], v[16:19]
	v_mfma_f32_16x16x32_f16 v[24:27], v[68:71], v[52:55], v[96:99]
	v_mfma_f32_16x16x32_f16 v[4:7], v[48:51], v[52:55], v[4:7]
	v_mfma_f32_16x16x32_f16 v[28:31], v[68:71], v[56:59], v[28:31]
	v_mfma_f32_16x16x32_f16 v[8:11], v[48:51], v[56:59], v[8:11]
	v_mfma_f32_16x16x32_f16 v[32:35], v[68:71], v[60:63], v[32:35]
	v_mfma_f32_16x16x32_f16 v[12:15], v[48:51], v[60:63], v[12:15]
	v_mfma_f32_16x16x32_f16 v[20:23], v[68:71], v[64:67], v[20:23]
	v_mfma_f32_16x16x32_f16 v[16:19], v[48:51], v[64:67], v[16:19]
	v_mfma_f32_16x16x32_f16 v[24:27], v[72:75], v[80:83], v[24:27]
	v_mfma_f32_16x16x32_f16 v[4:7], v[76:79], v[80:83], v[4:7]
	v_mfma_f32_16x16x32_f16 v[28:31], v[72:75], v[84:87], v[28:31]
	v_mfma_f32_16x16x32_f16 v[8:11], v[76:79], v[84:87], v[8:11]
	v_mfma_f32_16x16x32_f16 v[32:35], v[72:75], v[88:91], v[32:35]
	v_mfma_f32_16x16x32_f16 v[12:15], v[76:79], v[88:91], v[12:15]
	v_mfma_f32_16x16x32_f16 v[20:23], v[72:75], v[92:95], v[20:23]
	v_mfma_f32_16x16x32_f16 v[16:19], v[76:79], v[92:95], v[16:19]
	s_mov_b32 s0, 0x1a000
	v_add_co_u32_e32 v208, vcc, s0, v208
	s_mov_b32 s0, 0x10000
	s_nop 0
	v_addc_co_u32_e32 v209, vcc, 0, v209, vcc
	v_add_co_u32_e32 v48, vcc, s0, v212
	s_mov_b32 s0, 0x12000
	s_nop 0
	v_addc_co_u32_e32 v49, vcc, 0, v213, vcc
	v_add_co_u32_e32 v80, vcc, s0, v212
	s_mov_b32 s0, 0x14000
	s_nop 0
	v_addc_co_u32_e32 v81, vcc, 0, v213, vcc
	v_add_co_u32_e32 v96, vcc, s0, v212
	global_load_dwordx4 v[36:39], v[48:49], off
	global_load_dwordx4 v[40:43], v[48:49], off offset:1024
	global_load_dwordx4 v[44:47], v[48:49], off offset:2048
	s_nop 0
	global_load_dwordx4 v[48:51], v[48:49], off offset:3072
	s_nop 0
	global_load_dwordx4 v[52:55], v[210:211], off
	global_load_dwordx4 v[56:59], v[210:211], off offset:1024
	global_load_dwordx4 v[60:63], v[208:209], off
	global_load_dwordx4 v[64:67], v[208:209], off offset:1024
	v_addc_co_u32_e32 v97, vcc, 0, v213, vcc
	global_load_dwordx4 v[68:71], v[80:81], off
	global_load_dwordx4 v[72:75], v[80:81], off offset:1024
	global_load_dwordx4 v[76:79], v[80:81], off offset:2048
	s_nop 0
	global_load_dwordx4 v[80:83], v[80:81], off offset:3072
	s_nop 0
	global_load_dwordx4 v[84:87], v[96:97], off
	global_load_dwordx4 v[88:91], v[96:97], off offset:1024
	global_load_dwordx4 v[92:95], v[96:97], off offset:2048
	s_nop 0
	global_load_dwordx4 v[96:99], v[96:97], off offset:3072
	s_nop 0
	global_load_dwordx4 v[196:199], v[210:211], off offset:2048
	global_load_dwordx4 v[200:203], v[210:211], off offset:3072
	global_load_dwordx4 v[204:207], v[208:209], off offset:2048
	s_nop 0
	global_load_dwordx4 v[208:211], v[208:209], off offset:3072
	s_mov_b32 s0, 0x16000
	v_add_co_u32_e32 v224, vcc, s0, v212
	s_nop 1
	v_addc_co_u32_e32 v225, vcc, 0, v213, vcc
	global_load_dwordx4 v[212:215], v[224:225], off
	global_load_dwordx4 v[216:219], v[224:225], off offset:1024
	global_load_dwordx4 v[220:223], v[224:225], off offset:2048
	s_nop 0
	global_load_dwordx4 v[224:227], v[224:225], off offset:3072
	s_waitcnt vmcnt(29)
	v_mfma_f32_16x16x32_f16 v[24:27], v[172:175], v[104:107], v[24:27]
	v_mfma_f32_16x16x32_f16 v[4:7], v[100:103], v[104:107], v[4:7]
	v_mfma_f32_16x16x32_f16 v[28:31], v[172:175], v[108:111], v[28:31]
	v_mfma_f32_16x16x32_f16 v[8:11], v[100:103], v[108:111], v[8:11]
	v_mfma_f32_16x16x32_f16 v[32:35], v[172:175], v[112:115], v[32:35]
	v_mfma_f32_16x16x32_f16 v[12:15], v[100:103], v[112:115], v[12:15]
	v_mfma_f32_16x16x32_f16 v[20:23], v[172:175], v[116:119], v[20:23]
	v_mfma_f32_16x16x32_f16 v[16:19], v[100:103], v[116:119], v[16:19]
	v_mfma_f32_16x16x32_f16 v[24:27], v[136:139], v[120:123], v[24:27]
	v_mfma_f32_16x16x32_f16 v[4:7], v[144:147], v[120:123], v[4:7]
	v_mfma_f32_16x16x32_f16 v[28:31], v[136:139], v[124:127], v[28:31]
	v_mfma_f32_16x16x32_f16 v[8:11], v[144:147], v[124:127], v[8:11]
	v_mfma_f32_16x16x32_f16 v[32:35], v[136:139], v[128:131], v[32:35]
	v_mfma_f32_16x16x32_f16 v[12:15], v[144:147], v[128:131], v[12:15]
	v_mfma_f32_16x16x32_f16 v[20:23], v[136:139], v[132:135], v[20:23]
	v_mfma_f32_16x16x32_f16 v[16:19], v[144:147], v[132:135], v[16:19]
	v_mfma_f32_16x16x32_f16 v[24:27], v[140:143], v[152:155], v[24:27]
	v_mfma_f32_16x16x32_f16 v[4:7], v[148:151], v[152:155], v[4:7]
	v_mfma_f32_16x16x32_f16 v[28:31], v[140:143], v[156:159], v[28:31]
	v_mfma_f32_16x16x32_f16 v[8:11], v[148:151], v[156:159], v[8:11]
	v_mfma_f32_16x16x32_f16 v[32:35], v[140:143], v[160:163], v[32:35]
	v_mfma_f32_16x16x32_f16 v[12:15], v[148:151], v[160:163], v[12:15]
	v_mfma_f32_16x16x32_f16 v[20:23], v[140:143], v[164:167], v[20:23]
	v_mfma_f32_16x16x32_f16 v[16:19], v[148:151], v[164:167], v[16:19]
	s_waitcnt vmcnt(27)
	v_mfma_f32_16x16x32_f16 v[24:27], v[168:171], v[180:183], v[24:27]
	v_mfma_f32_16x16x32_f16 v[4:7], v[176:179], v[180:183], v[4:7]
	s_waitcnt vmcnt(26)
	v_mfma_f32_16x16x32_f16 v[28:31], v[168:171], v[184:187], v[28:31]
	v_mfma_f32_16x16x32_f16 v[8:11], v[176:179], v[184:187], v[8:11]
	s_waitcnt vmcnt(25)
	v_mfma_f32_16x16x32_f16 v[32:35], v[168:171], v[188:191], v[32:35]
	v_mfma_f32_16x16x32_f16 v[12:15], v[176:179], v[188:191], v[12:15]
	s_waitcnt vmcnt(24)
	v_mfma_f32_16x16x32_f16 v[20:23], v[168:171], v[192:195], v[20:23]
	v_mfma_f32_16x16x32_f16 v[16:19], v[176:179], v[192:195], v[16:19]
	s_waitcnt vmcnt(19)
	v_mfma_f32_16x16x32_f16 v[24:27], v[52:55], v[36:39], v[24:27]
	s_waitcnt vmcnt(17)
	v_mfma_f32_16x16x32_f16 v[4:7], v[60:63], v[36:39], v[4:7]
	v_mfma_f32_16x16x32_f16 v[28:31], v[52:55], v[40:43], v[28:31]
	v_mfma_f32_16x16x32_f16 v[8:11], v[60:63], v[40:43], v[8:11]
	v_mfma_f32_16x16x32_f16 v[32:35], v[52:55], v[44:47], v[32:35]
	v_mfma_f32_16x16x32_f16 v[12:15], v[60:63], v[44:47], v[12:15]
	v_mfma_f32_16x16x32_f16 v[20:23], v[52:55], v[48:51], v[20:23]
	v_mfma_f32_16x16x32_f16 v[16:19], v[60:63], v[48:51], v[16:19]
	s_waitcnt vmcnt(15)
	v_mfma_f32_16x16x32_f16 v[24:27], v[56:59], v[68:71], v[24:27]
	v_mfma_f32_16x16x32_f16 v[4:7], v[64:67], v[68:71], v[4:7]
	s_waitcnt vmcnt(14)
	v_mfma_f32_16x16x32_f16 v[28:31], v[56:59], v[72:75], v[28:31]
	v_mfma_f32_16x16x32_f16 v[8:11], v[64:67], v[72:75], v[8:11]
	s_waitcnt vmcnt(13)
	v_mfma_f32_16x16x32_f16 v[32:35], v[56:59], v[76:79], v[32:35]
	v_mfma_f32_16x16x32_f16 v[12:15], v[64:67], v[76:79], v[12:15]
	s_waitcnt vmcnt(12)
	v_mfma_f32_16x16x32_f16 v[20:23], v[56:59], v[80:83], v[20:23]
	v_mfma_f32_16x16x32_f16 v[16:19], v[64:67], v[80:83], v[16:19]
	s_waitcnt vmcnt(7)
	v_mfma_f32_16x16x32_f16 v[24:27], v[196:199], v[84:87], v[24:27]
	s_waitcnt vmcnt(5)
	v_mfma_f32_16x16x32_f16 v[4:7], v[204:207], v[84:87], v[4:7]
	v_mfma_f32_16x16x32_f16 v[28:31], v[196:199], v[88:91], v[28:31]
	v_mfma_f32_16x16x32_f16 v[8:11], v[204:207], v[88:91], v[8:11]
	v_mfma_f32_16x16x32_f16 v[32:35], v[196:199], v[92:95], v[32:35]
	v_mfma_f32_16x16x32_f16 v[12:15], v[204:207], v[92:95], v[12:15]
	v_mfma_f32_16x16x32_f16 v[20:23], v[196:199], v[96:99], v[20:23]
	v_mfma_f32_16x16x32_f16 v[16:19], v[204:207], v[96:99], v[16:19]
	s_waitcnt vmcnt(3)
	v_mfma_f32_16x16x32_f16 v[24:27], v[200:203], v[212:215], v[24:27]
	v_mfma_f32_16x16x32_f16 v[4:7], v[208:211], v[212:215], v[4:7]
	s_waitcnt vmcnt(2)
	v_mfma_f32_16x16x32_f16 v[28:31], v[200:203], v[216:219], v[28:31]
	v_mfma_f32_16x16x32_f16 v[8:11], v[208:211], v[216:219], v[8:11]
	s_waitcnt vmcnt(1)
	v_mfma_f32_16x16x32_f16 v[32:35], v[200:203], v[220:223], v[32:35]
	v_mfma_f32_16x16x32_f16 v[12:15], v[208:211], v[220:223], v[12:15]
	s_waitcnt vmcnt(0)
	v_mfma_f32_16x16x32_f16 v[20:23], v[200:203], v[224:227], v[20:23]
	v_mfma_f32_16x16x32_f16 v[16:19], v[208:211], v[224:227], v[16:19]
	global_load_dwordx4 v[36:39], v[228:229], off
	v_add_u32_e32 v2, 0, v2
	v_and_b32_e32 v41, 0x1c0, v0
	v_lshl_add_u32 v43, v230, 13, v2
	v_lshl_add_u32 v2, v41, 4, v2
	v_lshl_add_u32 v40, v0, 4, 0
	ds_write_b128 v43, v[24:27]
	ds_write_b128 v43, v[4:7] offset:1024
	ds_write_b128 v43, v[28:31] offset:2048
	ds_write_b128 v43, v[8:11] offset:3072
	ds_write_b128 v43, v[32:35] offset:4096
	ds_write_b128 v43, v[12:15] offset:5120
	ds_write_b128 v43, v[20:23] offset:6144
	ds_write_b128 v43, v[16:19] offset:7168
	s_waitcnt lgkmcnt(0)
	s_barrier
	ds_read_b128 v[4:7], v2 offset:8192
	ds_read_b128 v[8:11], v2 offset:16384
	ds_read_b128 v[12:15], v2 offset:24576
	ds_read_b128 v[16:19], v40
	ds_read_b128 v[20:23], v2 offset:32768
	ds_read_b128 v[24:27], v2 offset:40960
	ds_read_b128 v[28:31], v2 offset:49152
	ds_read_b128 v[32:35], v2 offset:57344
	s_waitcnt lgkmcnt(4)
	v_pk_add_f32 v[4:5], v[16:17], v[4:5]
	v_pk_add_f32 v[6:7], v[18:19], v[6:7]
	v_pk_add_f32 v[4:5], v[4:5], v[8:9]
	v_pk_add_f32 v[6:7], v[6:7], v[10:11]
	v_pk_add_f32 v[4:5], v[4:5], v[12:13]
	v_pk_add_f32 v[6:7], v[6:7], v[14:15]
	s_waitcnt lgkmcnt(3)
	v_pk_add_f32 v[4:5], v[4:5], v[20:21]
	v_pk_add_f32 v[6:7], v[6:7], v[22:23]
	s_waitcnt lgkmcnt(2)
	v_pk_add_f32 v[4:5], v[4:5], v[24:25]
	v_pk_add_f32 v[6:7], v[6:7], v[26:27]
	s_waitcnt lgkmcnt(1)
	v_pk_add_f32 v[4:5], v[4:5], v[28:29]
	v_pk_add_f32 v[6:7], v[6:7], v[30:31]
	s_waitcnt lgkmcnt(0)
	v_pk_add_f32 v[4:5], v[4:5], v[32:33]
	v_pk_add_f32 v[6:7], v[6:7], v[34:35]
	v_lshrrev_b32_e32 v42, 7, v0
	s_waitcnt vmcnt(0)
	v_pk_add_f32 v[4:5], v[36:37], v[4:5]
	v_pk_add_f32 v[6:7], v[38:39], v[6:7]
	v_mul_f32_e32 v2, 0x3d372713, v4
	v_mul_f32_e32 v8, 0x3d372713, v5
	v_mul_f32_e32 v9, 0x3d372713, v6
	v_mul_f32_e32 v2, v4, v2
	v_mul_f32_e32 v8, v5, v8
	v_mul_f32_e32 v9, v6, v9
	v_fma_f32 v2, v4, v2, v4
	v_fma_f32 v8, v5, v8, v5
	v_fma_f32 v9, v6, v9, v6
	v_mul_f32_e32 v2, 0x3f4c422a, v2
	v_mul_f32_e32 v8, 0x3f4c422a, v8
	v_mul_f32_e32 v9, 0x3f4c422a, v9
	v_add_f32_e32 v2, v2, v2
	v_add_f32_e32 v8, v8, v8
	v_add_f32_e32 v9, v9, v9
	v_mul_f32_e32 v2, 0x3fb8aa3b, v2
	v_mul_f32_e32 v11, 0x3fb8aa3b, v8
	v_mul_f32_e32 v10, 0x3d372713, v7
	v_mul_f32_e32 v12, 0x3fb8aa3b, v9
	v_exp_f32_e32 v8, v2
	v_exp_f32_e32 v9, v11
	v_mul_f32_e32 v10, v7, v10
	v_fma_f32 v10, v7, v10, v7
	v_mul_f32_e32 v10, 0x3f4c422a, v10
	v_add_f32_e32 v10, v10, v10
	v_pk_add_f32 v[8:9], v[8:9], 1.0 op_sel_hi:[1,0]
	v_mul_f32_e32 v13, 0x3fb8aa3b, v10
	v_div_scale_f32 v2, s[0:1], v9, v9, 2.0
	v_exp_f32_e32 v10, v12
	v_exp_f32_e32 v11, v13
	v_div_scale_f32 v14, s[0:1], v8, v8, 2.0
	v_rcp_f32_e32 v16, v2
	v_rcp_f32_e32 v17, v14
	v_pk_add_f32 v[10:11], v[10:11], 1.0 op_sel_hi:[1,0]
	v_div_scale_f32 v13, vcc, 2.0, v9, 2.0
	v_fma_f32 v20, -v2, v16, 1.0
	v_div_scale_f32 v15, s[0:1], v11, v11, 2.0
	v_fma_f32 v21, -v14, v17, 1.0
	v_fmac_f32_e32 v16, v20, v16
	v_div_scale_f32 v19, s[0:1], 2.0, v8, 2.0
	v_fmac_f32_e32 v17, v21, v17
	v_mul_f32_e32 v20, v13, v16
	v_mul_f32_e32 v21, v19, v17
	v_fma_f32 v23, -v2, v20, v13
	v_fma_f32 v24, -v14, v21, v19
	v_fmac_f32_e32 v20, v23, v16
	v_fmac_f32_e32 v21, v24, v17
	v_fma_f32 v2, -v2, v20, v13
	v_rcp_f32_e32 v18, v15
	v_fma_f32 v13, -v14, v21, v19
	v_div_fmas_f32 v2, v2, v16, v20
	s_mov_b64 vcc, s[0:1]
	v_div_fixup_f32 v9, v2, v9, 2.0
	v_div_fmas_f32 v2, v13, v17, v21
	v_div_fixup_f32 v8, v2, v8, 2.0
	v_pk_add_f32 v[8:9], v[8:9], 1.0 op_sel_hi:[1,0] neg_lo:[1,0] neg_hi:[1,0]
	v_pk_mul_f32 v[4:5], v[4:5], 0.5 op_sel_hi:[1,0]
	v_fma_f32 v22, -v15, v18, 1.0
	v_pk_add_f32 v[8:9], v[8:9], 1.0 op_sel_hi:[1,0]
	v_fmac_f32_e32 v18, v22, v18
	v_pk_mul_f32 v[4:5], v[4:5], v[8:9]
	v_div_scale_f32 v2, vcc, 2.0, v11, 2.0
	v_cvt_pk_f16_f32 v4, v4, v5
	v_mul_f32_e32 v5, v2, v18
	v_fma_f32 v8, -v15, v5, v2
	v_fmac_f32_e32 v5, v8, v18
	v_div_scale_f32 v8, s[0:1], v10, v10, 2.0
	v_rcp_f32_e32 v13, v8
	v_fma_f32 v2, -v15, v5, v2
	v_div_fmas_f32 v2, v2, v18, v5
	v_div_fixup_f32 v9, v2, v11, 2.0
	v_fma_f32 v2, -v8, v13, 1.0
	v_fmac_f32_e32 v13, v2, v13
	v_div_scale_f32 v2, vcc, 2.0, v10, 2.0
	v_mul_f32_e32 v5, v2, v13
	v_fma_f32 v11, -v8, v5, v2
	v_fmac_f32_e32 v5, v11, v13
	v_fma_f32 v2, -v8, v5, v2
	v_div_fmas_f32 v2, v2, v13, v5
	v_div_fixup_f32 v8, v2, v10, 2.0
	v_pk_add_f32 v[8:9], v[8:9], 1.0 op_sel_hi:[1,0] neg_lo:[1,0] neg_hi:[1,0]
	s_lshl_b32 s0, s2, 3
	v_pk_mul_f32 v[6:7], v[6:7], 0.5 op_sel_hi:[1,0]
	v_pk_add_f32 v[8:9], v[8:9], 1.0 op_sel_hi:[1,0]
	s_add_i32 s0, s0, s12
	v_pk_mul_f32 v[6:7], v[6:7], v[8:9]
	v_or_b32_e32 v2, s0, v42
	v_cvt_pk_f16_f32 v5, v6, v7
	v_lshlrev_b64 v[6:7], 6, v[2:3]
	v_lshrrev_b32_e32 v2, 1, v0
	v_and_b32_e32 v12, 15, v0
	v_and_b32_e32 v0, 16, v2
	v_lshl_or_b32 v0, v1, 5, v0
	v_or3_b32 v6, v6, v0, v12
	v_lshl_add_u64 v[0:1], v[6:7], 4, s[10:11]
	v_and_b32_e32 v2, 8, v2
	v_lshl_add_u64 v[0:1], v[0:1], 0, v[2:3]
	global_store_dwordx2 v[0:1], v[4:5], off
	s_endpgm
	s_nop 0
	s_nop 0
	s_nop 0
	s_nop 0
	s_nop 0
	s_nop 0
	s_nop 0
	s_nop 0
	s_nop 0
	s_nop 0
	s_nop 0
	s_nop 0
	s_nop 0
	s_nop 0
	s_nop 0
	s_nop 0
	s_nop 0
	s_nop 0
	s_nop 0
	s_nop 0
	s_nop 0
	s_nop 0
	s_nop 0
	s_nop 0
	s_nop 0
	s_nop 0
	s_nop 0
	s_nop 0
	s_nop 0
	s_nop 0
	s_nop 0
	s_endpgm

	.amdhsa_kernel _ZN12_GLOBAL__N_110gemm_fullkILi0ELi5EEEvPKDF16_S2_PKfPDF16_PfS6_S4_S4_S4_S4_S4_S5_
		.amdhsa_group_segment_fixed_size 0
		.amdhsa_private_segment_fixed_size 0
		.amdhsa_kernarg_size 96
		.amdhsa_user_sgpr_count 2
		.amdhsa_user_sgpr_dispatch_ptr 0
		.amdhsa_user_sgpr_queue_ptr 0
		.amdhsa_user_sgpr_kernarg_segment_ptr 1
		.amdhsa_user_sgpr_dispatch_id 0
		.amdhsa_user_sgpr_kernarg_preload_length 0
		.amdhsa_user_sgpr_kernarg_preload_offset 0
		.amdhsa_user_sgpr_private_segment_size 0
		.amdhsa_uses_dynamic_stack 0
		.amdhsa_enable_private_segment 0
		.amdhsa_system_sgpr_workgroup_id_x 1
		.amdhsa_system_sgpr_workgroup_id_y 0
		.amdhsa_system_sgpr_workgroup_id_z 0
		.amdhsa_system_sgpr_workgroup_info 0
		.amdhsa_system_vgpr_workitem_id 0
		.amdhsa_next_free_vgpr 231
		.amdhsa_next_free_sgpr 14
		.amdhsa_accum_offset 232
		.amdhsa_reserve_vcc 1
		.amdhsa_float_round_mode_32 0
		.amdhsa_float_round_mode_16_64 0
		.amdhsa_float_denorm_mode_32 3
		.amdhsa_float_denorm_mode_16_64 3
		.amdhsa_dx10_clamp 1
		.amdhsa_ieee_mode 1
		.amdhsa_fp16_overflow 0
		.amdhsa_tg_split 0
		.amdhsa_exception_fp_ieee_invalid_op 0
		.amdhsa_exception_fp_denorm_src 0
		.amdhsa_exception_fp_ieee_div_zero 0
		.amdhsa_exception_fp_ieee_overflow 0
		.amdhsa_exception_fp_ieee_underflow 0
		.amdhsa_exception_fp_ieee_inexact 0
		.amdhsa_exception_int_div_zero 0
	.end_amdhsa_kernel

_ZN12_GLOBAL__N_110gemm_fullkILi1ELi5EEEvPKDF16_S2_PKfPDF16_PfS6_S4_S4_S4_S4_S4_S5_:
	s_load_dwordx2 s[4:5], s[0:1], 0x38
	s_and_b32 s3, s2, 63
	s_lshl_b32 s16, s3, 5
	s_lshl_b32 s6, s3, 13
	v_lshlrev_b32_e32 v1, 4, v0
	s_waitcnt lgkmcnt(0)
	s_add_u32 s4, s4, s6
	s_addc_u32 s5, s5, 0
	global_load_dwordx4 v[2:5], v1, s[4:5]
	v_lshlrev_b32_e32 v1, 2, v0
	v_cmp_lt_u32_e32 vcc, 31, v0
	s_and_saveexec_b64 s[4:5], vcc
	s_xor_b64 s[4:5], exec, s[4:5]
	s_cbranch_execz .LBB19_10
	v_cmp_lt_u32_e32 vcc, 63, v0
	s_and_saveexec_b64 s[6:7], vcc
	s_xor_b64 s[6:7], exec, s[6:7]
	s_cbranch_execz .LBB19_7
	s_movk_i32 s8, 0x47
	v_cmp_lt_u32_e32 vcc, s8, v0
	s_and_saveexec_b64 s[8:9], vcc
	s_xor_b64 s[8:9], exec, s[8:9]
	s_cbranch_execz .LBB19_4
	s_load_dwordx2 s[10:11], s[0:1], 0x10
	s_lshl_b32 s12, s16, 2
	v_lshlrev_b32_e32 v6, 2, v1
	v_mov_b32_e32 v7, 0
	s_movk_i32 s14, 0x50
	s_waitcnt lgkmcnt(0)
	s_add_u32 s10, s10, s12
	s_addc_u32 s11, s11, 0
	s_movk_i32 s12, 0xfb80
	v_lshl_add_u64 v[6:7], s[10:11], 0, v[6:7]
	s_mov_b32 s13, -1
	v_lshl_add_u64 v[6:7], v[6:7], 0, s[12:13]
	v_mov_b32_e32 v8, s11
	v_cmp_gt_u32_e32 vcc, s14, v0
	s_nop 1
	v_cndmask_b32_e32 v25, v8, v7, vcc
	v_mov_b32_e32 v7, s10
	v_cndmask_b32_e32 v24, v7, v6, vcc
.LBB19_4:
	s_andn2_saveexec_b64 s[8:9], s[8:9]
	s_cbranch_execz .LBB19_6
	s_load_dwordx2 s[10:11], s[0:1], 0x50
	s_lshl_b32 s12, s16, 2
	v_lshlrev_b32_e32 v6, 2, v1
	v_mov_b32_e32 v7, 0
	s_waitcnt lgkmcnt(0)
	s_add_u32 s10, s10, s12
	s_addc_u32 s11, s11, 0
	v_lshl_add_u64 v[6:7], s[10:11], 0, v[6:7]
	s_movk_i32 s10, 0xfc00
	s_mov_b32 s11, -1
	v_lshl_add_u64 v[24:25], v[6:7], 0, s[10:11]

.LBB19_7:
	s_andn2_saveexec_b64 s[6:7], s[6:7]
	s_cbranch_execz .LBB19_9
	s_load_dwordx2 s[8:9], s[0:1], 0x48
	s_lshl_b32 s10, s3, 9
	v_lshlrev_b32_e32 v6, 2, v1
	v_mov_b32_e32 v7, 0
	s_waitcnt lgkmcnt(0)
	s_add_u32 s8, s8, s10
	s_addc_u32 s9, s9, 0
	v_lshl_add_u64 v[6:7], s[8:9], 0, v[6:7]
	s_movk_i32 s8, 0xfe00
	s_mov_b32 s9, -1
	v_lshl_add_u64 v[24:25], v[6:7], 0, s[8:9]

.LBB19_10:
	s_or_saveexec_b64 s[14:15], s[4:5]
	s_load_dwordx2 s[12:13], s[0:1], 0x58
	s_load_dwordx4 s[8:11], s[0:1], 0x0
	s_load_dwordx4 s[4:7], s[0:1], 0x20
	s_xor_b64 exec, exec, s[14:15]
	s_cbranch_execz .LBB19_12
	s_load_dwordx2 s[0:1], s[0:1], 0x40
	s_lshl_b32 s17, s3, 9
	v_lshlrev_b32_e32 v6, 2, v1
	v_mov_b32_e32 v7, 0
	s_waitcnt lgkmcnt(0)
	s_add_u32 s0, s0, s17
	s_addc_u32 s1, s1, 0
	v_lshl_add_u64 v[24:25], s[0:1], 0, v[6:7]
.LBB19_12:
	s_or_b64 exec, exec, s[14:15]
	v_lshrrev_b32_e32 v182, 6, v0
	s_lshr_b32 s0, s2, 5
	s_and_b32 s0, s0, 0x7fffffe
	s_mov_b32 s1, 0
	v_lshlrev_b32_e32 v8, 17, v182
	v_mov_b32_e32 v9, 0
	v_and_b32_e32 v12, 63, v0
	s_lshl_b64 s[14:15], s[0:1], 10
	v_lshlrev_b32_e32 v6, 14, v182
	s_waitcnt lgkmcnt(0)
	v_lshl_add_u64 v[10:11], s[8:9], 0, v[8:9]
	v_lshl_or_b32 v6, s3, 18, v6
	v_mov_b32_e32 v7, v9
	v_lshl_add_u64 v[10:11], v[10:11], 0, s[14:15]
	v_lshlrev_b32_e32 v8, 4, v12
	v_lshl_add_u64 v[6:7], s[10:11], 0, v[6:7]
	v_lshl_add_u64 v[26:27], v[10:11], 0, v[8:9]
	v_lshrrev_b32_e32 v10, 2, v0
	v_lshl_add_u64 v[178:179], v[6:7], 0, v[8:9]
	v_lshrrev_b32_e32 v6, 8, v0
	v_lshrrev_b32_e32 v7, 3, v0
	v_and_b32_e32 v10, 12, v10
	v_and_b32_e32 v28, 15, v0
	v_bfe_u32 v32, v0, 6, 1
	v_or_b32_e32 v30, s0, v6
	v_and_or_b32 v31, v7, 16, v10
	v_lshl_or_b32 v6, v30, 4, v28
	v_lshl_or_b32 v29, v32, 1, v31
	v_mov_b32_e32 v7, v9
	v_or_b32_e32 v10, s16, v29
	v_lshlrev_b64 v[12:13], 13, v[6:7]
	v_lshl_add_u64 v[6:7], s[4:5], 0, v[12:13]
	v_lshlrev_b32_e32 v14, 2, v10
	v_mov_b32_e32 v15, v9
	v_lshl_add_u64 v[10:11], v[6:7], 0, v[14:15]
	s_mov_b32 s2, 0x500000
	v_add_co_u32_e32 v6, vcc, s2, v10
	v_lshl_add_u64 v[12:13], s[6:7], 0, v[12:13]
	s_nop 0
	v_addc_co_u32_e32 v7, vcc, 0, v11, vcc
	v_lshl_add_u64 v[22:23], v[12:13], 0, v[14:15]
	s_mov_b32 s0, 0x100000
	v_add_co_u32_e32 v20, vcc, s0, v22
	s_mov_b32 s0, 0x200000
	s_nop 0
	v_addc_co_u32_e32 v21, vcc, 0, v23, vcc
	v_add_co_u32_e32 v34, vcc, s0, v22
	s_mov_b32 s0, 0x300000
	s_nop 0
	v_addc_co_u32_e32 v35, vcc, 0, v23, vcc
	v_add_co_u32_e32 v36, vcc, s0, v22
	s_mov_b32 s0, 0x400000
	s_nop 0
	v_addc_co_u32_e32 v37, vcc, 0, v23, vcc
	global_load_dwordx2 v[6:7], v[6:7], off
	s_nop 0
	global_load_dwordx2 v[18:19], v[22:23], off
	global_load_dwordx2 v[14:15], v[20:21], off
	global_load_dwordx2 v[12:13], v[34:35], off
	global_load_dwordx2 v[16:17], v[36:37], off
	v_add_co_u32_e32 v20, vcc, s0, v22
	s_mov_b32 s0, 0x20000
	s_nop 0
	v_addc_co_u32_e32 v21, vcc, 0, v23, vcc
	v_add_co_u32_e32 v86, vcc, s0, v178
	s_mov_b32 s0, 0x21000
	s_nop 0
	v_addc_co_u32_e32 v87, vcc, 0, v179, vcc
	v_add_co_u32_e32 v150, vcc, s0, v178
	s_movk_i32 s0, 0x2000
	s_nop 0
	v_addc_co_u32_e32 v151, vcc, 0, v179, vcc
	v_add_co_u32_e32 v66, vcc, s0, v26
	s_movk_i32 s1, 0x4000
	s_nop 0
	v_addc_co_u32_e32 v67, vcc, 0, v27, vcc
	v_add_co_u32_e32 v88, vcc, s1, v26
	s_movk_i32 s1, 0x6000
	s_nop 0
	v_addc_co_u32_e32 v89, vcc, 0, v27, vcc
	v_add_co_u32_e32 v94, vcc, s1, v26
	s_movk_i32 s1, 0x1000
	s_nop 0
	v_addc_co_u32_e32 v95, vcc, 0, v27, vcc
	v_add_co_u32_e32 v142, vcc, s1, v178
	global_load_dwordx2 v[20:21], v[20:21], off
	s_nop 0
	v_addc_co_u32_e32 v143, vcc, 0, v179, vcc
	v_add_co_u32_e32 v166, vcc, s0, v178
	s_mov_b32 s0, 0x8000
	s_nop 0
	v_addc_co_u32_e32 v167, vcc, 0, v179, vcc
	v_add_co_u32_e32 v110, vcc, s0, v26
	s_mov_b32 s0, 0xa000
	s_nop 0
	v_addc_co_u32_e32 v111, vcc, 0, v27, vcc
	v_add_co_u32_e32 v118, vcc, s0, v26
	s_mov_b32 s0, 0xc000
	s_nop 0
	v_addc_co_u32_e32 v119, vcc, 0, v27, vcc
	global_load_dwordx4 v[34:37], v[26:27], off
	global_load_dwordx4 v[38:41], v[26:27], off offset:1024
	global_load_dwordx4 v[42:45], v[178:179], off
	global_load_dwordx4 v[46:49], v[178:179], off offset:1024
	global_load_dwordx4 v[50:53], v[66:67], off
	global_load_dwordx4 v[54:57], v[66:67], off offset:1024
	global_load_dwordx4 v[58:61], v[86:87], off offset:1024
	global_load_dwordx4 v[62:65], v[86:87], off offset:2048
	s_nop 0
	global_load_dwordx4 v[66:69], v[88:89], off
	global_load_dwordx4 v[70:73], v[88:89], off offset:1024
	global_load_dwordx4 v[74:77], v[178:179], off offset:2048
	global_load_dwordx4 v[78:81], v[178:179], off offset:3072
	global_load_dwordx4 v[82:85], v[86:87], off offset:3072
	s_nop 0
	global_load_dwordx4 v[86:89], v[94:95], off
	global_load_dwordx4 v[90:93], v[94:95], off offset:1024
	s_nop 0
	global_load_dwordx4 v[94:97], v[150:151], off offset:-4096
	global_load_dwordx4 v[98:101], v[150:151], off
	global_load_dwordx4 v[102:105], v[110:111], off
	global_load_dwordx4 v[106:109], v[110:111], off offset:1024
	s_nop 0
	global_load_dwordx4 v[110:113], v[118:119], off
	global_load_dwordx4 v[114:117], v[118:119], off offset:1024
	s_nop 0
	global_load_dwordx4 v[118:121], v[142:143], off offset:1024
	global_load_dwordx4 v[122:125], v[142:143], off offset:2048
	global_load_dwordx4 v[126:129], v[150:151], off offset:1024
	global_load_dwordx4 v[130:133], v[150:151], off offset:2048
	v_add_co_u32_e32 v138, vcc, s0, v26
	s_mov_b32 s0, 0xe000
	s_nop 0
	v_addc_co_u32_e32 v139, vcc, 0, v27, vcc
	global_load_dwordx4 v[134:137], v[138:139], off
	s_nop 0
	global_load_dwordx4 v[138:141], v[138:139], off offset:1024
	s_nop 0
	global_load_dwordx4 v[142:145], v[142:143], off offset:3072
	s_nop 0
	global_load_dwordx4 v[146:149], v[166:167], off offset:-4096
	s_nop 0
	global_load_dwordx4 v[150:153], v[150:151], off offset:3072
	v_add_co_u32_e32 v158, vcc, s0, v26
	v_lshrrev_b32_e32 v33, 7, v0
	s_nop 0
	v_addc_co_u32_e32 v159, vcc, 0, v27, vcc
	global_load_dwordx4 v[154:157], v[158:159], off
	s_nop 0
	global_load_dwordx4 v[158:161], v[158:159], off offset:1024
	s_waitcnt vmcnt(29)
	v_mfma_f32_16x16x32_f16 v[162:165], v[42:45], v[34:37], 0
	s_waitcnt vmcnt(16)
	v_mfma_f32_16x16x32_f16 v[34:37], v[94:97], v[34:37], 0
	v_mfma_f32_16x16x32_f16 v[42:45], v[42:45], v[38:41], 0
	v_mfma_f32_16x16x32_f16 v[38:41], v[94:97], v[38:41], 0
	v_mfma_f32_16x16x32_f16 v[94:97], v[46:49], v[50:53], v[162:165]
	v_mfma_f32_16x16x32_f16 v[34:37], v[58:61], v[50:53], v[34:37]
	v_mfma_f32_16x16x32_f16 v[42:45], v[46:49], v[54:57], v[42:45]
	v_mfma_f32_16x16x32_f16 v[38:41], v[58:61], v[54:57], v[38:41]
	v_mfma_f32_16x16x32_f16 v[46:49], v[74:77], v[66:69], v[94:97]
	v_mfma_f32_16x16x32_f16 v[34:37], v[62:65], v[66:69], v[34:37]
	v_mfma_f32_16x16x32_f16 v[42:45], v[74:77], v[70:73], v[42:45]
	v_mfma_f32_16x16x32_f16 v[38:41], v[62:65], v[70:73], v[38:41]
	v_mfma_f32_16x16x32_f16 v[46:49], v[78:81], v[86:89], v[46:49]
	v_mfma_f32_16x16x32_f16 v[34:37], v[82:85], v[86:89], v[34:37]
	v_mfma_f32_16x16x32_f16 v[42:45], v[78:81], v[90:93], v[42:45]
	v_mfma_f32_16x16x32_f16 v[38:41], v[82:85], v[90:93], v[38:41]
	s_mov_b32 s0, 0x22000
	v_add_co_u32_e32 v168, vcc, s0, v178
	s_mov_b32 s0, 0x23000
	s_nop 0
	v_addc_co_u32_e32 v169, vcc, 0, v179, vcc
	v_add_co_u32_e32 v180, vcc, s0, v178
	s_mov_b32 s0, 0x10000
	s_nop 0
	v_addc_co_u32_e32 v181, vcc, 0, v179, vcc
	v_add_co_u32_e32 v58, vcc, s0, v26
	s_mov_b32 s0, 0x12000
	s_nop 0
	v_addc_co_u32_e32 v59, vcc, 0, v27, vcc
	v_add_co_u32_e32 v74, vcc, s0, v26
	s_mov_b32 s0, 0x14000
	s_nop 0
	v_addc_co_u32_e32 v75, vcc, 0, v27, vcc
	v_add_co_u32_e32 v90, vcc, s0, v26
	global_load_dwordx4 v[50:53], v[180:181], off offset:-4096
	s_nop 0
	v_addc_co_u32_e32 v91, vcc, 0, v27, vcc
	global_load_dwordx4 v[54:57], v[58:59], off
	s_nop 0
	global_load_dwordx4 v[58:61], v[58:59], off offset:1024
	s_nop 0
	global_load_dwordx4 v[62:65], v[166:167], off
	global_load_dwordx4 v[66:69], v[166:167], off offset:1024
	global_load_dwordx4 v[70:73], v[74:75], off
	s_nop 0
	global_load_dwordx4 v[74:77], v[74:75], off offset:1024
	s_nop 0
	global_load_dwordx4 v[78:81], v[168:169], off offset:1024
	global_load_dwordx4 v[82:85], v[168:169], off offset:2048
	global_load_dwordx4 v[86:89], v[90:91], off
	s_nop 0
	global_load_dwordx4 v[90:93], v[90:91], off offset:1024
	s_nop 0
	global_load_dwordx4 v[94:97], v[166:167], off offset:2048
	global_load_dwordx4 v[162:165], v[166:167], off offset:3072
	s_nop 0
	global_load_dwordx4 v[166:169], v[168:169], off offset:3072
	s_mov_b32 s0, 0x16000
	v_add_co_u32_e32 v174, vcc, s0, v26
	s_nop 1
	v_addc_co_u32_e32 v175, vcc, 0, v27, vcc
	global_load_dwordx4 v[170:173], v[174:175], off
	s_nop 0
	global_load_dwordx4 v[174:177], v[174:175], off offset:1024
	s_waitcnt vmcnt(19)
	v_mfma_f32_16x16x32_f16 v[46:49], v[146:149], v[102:105], v[46:49]
	v_mfma_f32_16x16x32_f16 v[34:37], v[98:101], v[102:105], v[34:37]
	v_mfma_f32_16x16x32_f16 v[42:45], v[146:149], v[106:109], v[42:45]
	v_mfma_f32_16x16x32_f16 v[38:41], v[98:101], v[106:109], v[38:41]
	v_mfma_f32_16x16x32_f16 v[46:49], v[118:121], v[110:113], v[46:49]
	v_mfma_f32_16x16x32_f16 v[34:37], v[126:129], v[110:113], v[34:37]
	v_mfma_f32_16x16x32_f16 v[42:45], v[118:121], v[114:117], v[42:45]
	v_mfma_f32_16x16x32_f16 v[38:41], v[126:129], v[114:117], v[38:41]
	v_mfma_f32_16x16x32_f16 v[46:49], v[122:125], v[134:137], v[46:49]
	v_mfma_f32_16x16x32_f16 v[34:37], v[130:133], v[134:137], v[34:37]
	v_mfma_f32_16x16x32_f16 v[42:45], v[122:125], v[138:141], v[42:45]
	v_mfma_f32_16x16x32_f16 v[38:41], v[130:133], v[138:141], v[38:41]
	s_waitcnt vmcnt(17)
	v_mfma_f32_16x16x32_f16 v[46:49], v[142:145], v[154:157], v[46:49]
	v_mfma_f32_16x16x32_f16 v[34:37], v[150:153], v[154:157], v[34:37]
	s_waitcnt vmcnt(16)
	v_mfma_f32_16x16x32_f16 v[42:45], v[142:145], v[158:161], v[42:45]
	v_mfma_f32_16x16x32_f16 v[38:41], v[150:153], v[158:161], v[38:41]
	s_movk_i32 s0, 0x3000
	v_add_co_u32_e32 v142, vcc, s0, v178
	s_mov_b32 s0, 0x18000
	s_nop 0
	v_addc_co_u32_e32 v143, vcc, 0, v179, vcc
	v_add_co_u32_e32 v102, vcc, s0, v26
	s_mov_b32 s0, 0x1a000
	s_nop 0
	v_addc_co_u32_e32 v103, vcc, 0, v27, vcc
	v_add_co_u32_e32 v126, vcc, s0, v26
	s_mov_b32 s0, 0x1c000
	s_nop 0
	v_addc_co_u32_e32 v127, vcc, 0, v27, vcc
	v_add_co_u32_e32 v134, vcc, s0, v26
	global_load_dwordx4 v[98:101], v[102:103], off
	s_nop 0
	global_load_dwordx4 v[102:105], v[102:103], off offset:1024
	s_nop 0
	global_load_dwordx4 v[106:109], v[142:143], off
	global_load_dwordx4 v[110:113], v[142:143], off offset:1024
	global_load_dwordx4 v[114:117], v[180:181], off
	global_load_dwordx4 v[118:121], v[180:181], off offset:1024
	v_addc_co_u32_e32 v135, vcc, 0, v27, vcc
	global_load_dwordx4 v[122:125], v[126:127], off
	s_nop 0
	global_load_dwordx4 v[126:129], v[126:127], off offset:1024
	s_nop 0
	global_load_dwordx4 v[130:133], v[134:135], off
	s_nop 0
	global_load_dwordx4 v[134:137], v[134:135], off offset:1024
	s_nop 0
	global_load_dwordx4 v[138:141], v[142:143], off offset:2048
	s_nop 0
	global_load_dwordx4 v[142:145], v[142:143], off offset:3072
	s_nop 0
	global_load_dwordx4 v[146:149], v[180:181], off offset:2048
	global_load_dwordx4 v[150:153], v[180:181], off offset:3072
	s_mov_b32 s0, 0x1e000
	v_add_co_u32_e32 v26, vcc, s0, v26
	s_nop 1
	v_addc_co_u32_e32 v27, vcc, 0, v27, vcc
	global_load_dwordx4 v[154:157], v[26:27], off
	global_load_dwordx4 v[158:161], v[26:27], off offset:1024
	s_waitcnt vmcnt(28)
	v_mfma_f32_16x16x32_f16 v[46:49], v[62:65], v[54:57], v[46:49]
	v_mfma_f32_16x16x32_f16 v[34:37], v[50:53], v[54:57], v[34:37]
	v_mfma_f32_16x16x32_f16 v[42:45], v[62:65], v[58:61], v[42:45]
	v_mfma_f32_16x16x32_f16 v[38:41], v[50:53], v[58:61], v[38:41]
	s_waitcnt vmcnt(26)
	v_mfma_f32_16x16x32_f16 v[46:49], v[66:69], v[70:73], v[46:49]
	s_waitcnt vmcnt(24)
	v_mfma_f32_16x16x32_f16 v[34:37], v[78:81], v[70:73], v[34:37]
	v_mfma_f32_16x16x32_f16 v[42:45], v[66:69], v[74:77], v[42:45]
	v_mfma_f32_16x16x32_f16 v[38:41], v[78:81], v[74:77], v[38:41]
	s_waitcnt vmcnt(20)
	v_mfma_f32_16x16x32_f16 v[46:49], v[94:97], v[86:89], v[46:49]
	v_mfma_f32_16x16x32_f16 v[34:37], v[82:85], v[86:89], v[34:37]
	v_mfma_f32_16x16x32_f16 v[42:45], v[94:97], v[90:93], v[42:45]
	v_mfma_f32_16x16x32_f16 v[38:41], v[82:85], v[90:93], v[38:41]
	s_waitcnt vmcnt(17)
	v_mfma_f32_16x16x32_f16 v[46:49], v[162:165], v[170:173], v[46:49]
	v_mfma_f32_16x16x32_f16 v[34:37], v[166:169], v[170:173], v[34:37]
	s_waitcnt vmcnt(16)
	v_mfma_f32_16x16x32_f16 v[42:45], v[162:165], v[174:177], v[42:45]
	v_mfma_f32_16x16x32_f16 v[38:41], v[166:169], v[174:177], v[38:41]
	s_waitcnt vmcnt(13)
	v_mfma_f32_16x16x32_f16 v[46:49], v[106:109], v[98:101], v[46:49]
	s_waitcnt vmcnt(11)
	v_mfma_f32_16x16x32_f16 v[34:37], v[114:117], v[98:101], v[34:37]
	v_mfma_f32_16x16x32_f16 v[42:45], v[106:109], v[102:105], v[42:45]
	v_mfma_f32_16x16x32_f16 v[38:41], v[114:117], v[102:105], v[38:41]
	s_waitcnt vmcnt(9)
	v_mfma_f32_16x16x32_f16 v[46:49], v[110:113], v[122:125], v[46:49]
	v_mfma_f32_16x16x32_f16 v[34:37], v[118:121], v[122:125], v[34:37]
	s_waitcnt vmcnt(8)
	v_mfma_f32_16x16x32_f16 v[42:45], v[110:113], v[126:129], v[42:45]
	v_mfma_f32_16x16x32_f16 v[38:41], v[118:121], v[126:129], v[38:41]
	s_waitcnt vmcnt(5)
	v_mfma_f32_16x16x32_f16 v[46:49], v[138:141], v[130:133], v[46:49]
	s_waitcnt vmcnt(3)
	v_mfma_f32_16x16x32_f16 v[34:37], v[146:149], v[130:133], v[34:37]
	v_mfma_f32_16x16x32_f16 v[42:45], v[138:141], v[134:137], v[42:45]
	v_mfma_f32_16x16x32_f16 v[38:41], v[146:149], v[134:137], v[38:41]
	s_waitcnt vmcnt(1)
	v_mfma_f32_16x16x32_f16 v[46:49], v[142:145], v[154:157], v[46:49]
	v_mfma_f32_16x16x32_f16 v[34:37], v[150:153], v[154:157], v[34:37]
	s_waitcnt vmcnt(0)
	v_mfma_f32_16x16x32_f16 v[42:45], v[142:145], v[158:161], v[42:45]
	v_mfma_f32_16x16x32_f16 v[38:41], v[150:153], v[158:161], v[38:41]
	v_lshlrev_b32_e32 v26, 12, v182
	v_add3_u32 v26, 0, v8, v26
	s_nop 1
	ds_write_b128 v26, v[46:49]
	ds_write_b128 v26, v[34:37] offset:1024
	s_nop 0
	ds_write_b128 v26, v[42:45] offset:2048
	ds_write_b128 v26, v[38:41] offset:3072
	v_lshrrev_b32_e32 v26, 4, v0
	v_and_b32_e32 v27, 60, v1
	v_mul_u32_u24_e32 v26, 0x110, v26
	v_lshlrev_b32_e32 v27, 2, v27
	s_movk_i32 s0, 0x50
	v_add3_u32 v26, 0, v26, v27
	v_cmp_gt_u32_e32 vcc, s0, v0
	ds_write_b128 v26, v[2:5] offset:32768
	s_and_saveexec_b64 s[0:1], vcc
	s_cbranch_execz .LBB19_14
	global_load_dwordx4 v[2:5], v[24:25], off
	v_lshl_add_u32 v0, v1, 2, 0
	s_waitcnt vmcnt(0)
	ds_write_b128 v0, v[2:5] offset:41472
.LBB19_14:
	s_or_b64 exec, exec, s[0:1]
	v_lshlrev_b32_e32 v0, 10, v33
	v_add3_u32 v8, 0, v0, v8
	s_waitcnt lgkmcnt(0)
	s_barrier
	ds_read_b128 v[0:3], v8
	ds_read_b128 v[24:27], v8 offset:4096
	ds_read_b128 v[34:37], v8 offset:8192
	v_cmp_eq_u32_e32 vcc, 0, v32
	s_waitcnt lgkmcnt(1)
	v_pk_add_f32 v[26:27], v[2:3], v[26:27]
	ds_read_b128 v[2:5], v8 offset:12288
	v_pk_add_f32 v[0:1], v[0:1], v[24:25]
	s_waitcnt lgkmcnt(1)
	v_pk_add_f32 v[36:37], v[26:27], v[36:37]
	ds_read_b128 v[24:27], v8 offset:16384
	v_pk_add_f32 v[0:1], v[0:1], v[34:35]
	s_waitcnt lgkmcnt(1)
	v_pk_add_f32 v[4:5], v[36:37], v[4:5]
	v_pk_add_f32 v[38:39], v[0:1], v[2:3]
	ds_read_b128 v[0:3], v8 offset:20480
	ds_read_b128 v[34:37], v8 offset:24576
	s_waitcnt lgkmcnt(2)
	v_pk_add_f32 v[4:5], v[4:5], v[26:27]
	v_pk_add_f32 v[38:39], v[38:39], v[24:25]
	ds_read_b128 v[24:27], v8 offset:28672
	v_lshl_add_u32 v8, v29, 2, 0
	s_waitcnt lgkmcnt(2)
	v_pk_add_f32 v[2:3], v[4:5], v[2:3]
	ds_read_b64 v[4:5], v8 offset:42624
	v_pk_add_f32 v[0:1], v[38:39], v[0:1]
	s_waitcnt lgkmcnt(2)
	v_pk_add_f32 v[2:3], v[2:3], v[36:37]
	v_pk_add_f32 v[0:1], v[0:1], v[34:35]
	s_waitcnt lgkmcnt(1)
	v_pk_add_f32 v[2:3], v[2:3], v[26:27]
	v_pk_add_f32 v[0:1], v[0:1], v[24:25]
	ds_read_b32 v25, v8 offset:42500
	v_cndmask_b32_e32 v1, v3, v1, vcc
	v_cndmask_b32_e32 v0, v2, v0, vcc
	s_waitcnt lgkmcnt(1)
	v_pk_add_f32 v[0:1], v[0:1], v[4:5]
	v_mad_u32_u24 v4, v29, 12, v8
	v_pk_add_f32 v[26:27], v[6:7], v[0:1]
	v_add_co_u32_e32 v0, vcc, s2, v22
	ds_read_b128 v[32:35], v4 offset:41472
	s_nop 0
	v_addc_co_u32_e32 v1, vcc, 0, v23, vcc
	global_store_dwordx2 v[0:1], v[26:27], off
	v_lshl_add_u32 v8, v29, 8, v4
	v_mad_i32_i24 v0, v29, -12, v4
	v_or_b32_e32 v1, 1, v29
	ds_read_b128 v[36:39], v8 offset:32928
	ds_read_b128 v[40:43], v8 offset:32944
	ds_read_b128 v[44:47], v8 offset:32960
	ds_read_b128 v[48:51], v8 offset:32976
	v_lshl_add_u32 v2, v1, 4, 0
	ds_read_b32 v24, v0 offset:42496
	ds_read_b128 v[52:55], v2 offset:41472
	v_lshl_add_u32 v80, v1, 8, v2
	ds_read_b128 v[56:59], v80 offset:32928
	ds_read_b128 v[60:63], v80 offset:32944
	ds_read_b128 v[64:67], v80 offset:32960
	s_waitcnt lgkmcnt(8)
	v_mov_b32_e32 v22, v36
	v_mov_b32_e32 v68, v32
	s_waitcnt lgkmcnt(2)
	v_mov_b32_e32 v23, v56
	v_mov_b32_e32 v69, v52
	v_pk_fma_f32 v[22:23], v[18:19], v[22:23], v[68:69]
	v_mov_b32_e32 v68, v40
	s_waitcnt lgkmcnt(1)
	v_mov_b32_e32 v69, v60
	v_mov_b32_e32 v56, v37
	v_mov_b32_e32 v60, v41
	v_mov_b32_e32 v36, v38
	v_mov_b32_e32 v37, v58
	v_mov_b32_e32 v40, v34
	v_mov_b32_e32 v41, v54
	ds_read_b128 v[0:3], v2 offset:41984
	ds_read_b128 v[4:7], v4 offset:41984
	v_pk_fma_f32 v[22:23], v[14:15], v[68:69], v[22:23]
	v_pk_fma_f32 v[40:41], v[18:19], v[36:37], v[40:41]
	v_mov_b32_e32 v58, v39
	ds_read_b128 v[36:39], v8 offset:32992
	ds_read_b128 v[68:71], v8 offset:33008
	ds_read_b128 v[72:75], v80 offset:32976
	ds_read_b128 v[76:79], v80 offset:32992
	ds_read_b128 v[80:83], v80 offset:33008
	v_mov_b32_e32 v84, v44
	s_waitcnt lgkmcnt(7)
	v_mov_b32_e32 v85, v64
	v_mov_b32_e32 v52, v33
	v_pk_fma_f32 v[32:33], v[18:19], v[56:57], v[52:53]
	v_pk_fma_f32 v[22:23], v[12:13], v[84:85], v[22:23]
	v_mov_b32_e32 v52, v48
	s_waitcnt lgkmcnt(2)
	v_mov_b32_e32 v53, v72
	v_pk_fma_f32 v[22:23], v[16:17], v[52:53], v[22:23]
	v_mov_b32_e32 v52, v36
	s_waitcnt lgkmcnt(1)
	v_mov_b32_e32 v53, v76
	v_pk_fma_f32 v[22:23], v[20:21], v[52:53], v[22:23]
	v_mov_b32_e32 v52, v68
	s_waitcnt lgkmcnt(0)
	v_mov_b32_e32 v53, v80
	v_pk_fma_f32 v[22:23], v[26:27], v[52:53], v[22:23]
	v_pk_fma_f32 v[32:33], v[14:15], v[60:61], v[32:33]
	v_mul_f32_e32 v8, 0x3d372713, v22
	v_mov_b32_e32 v64, v45
	v_mul_f32_e32 v8, v22, v8
	v_fma_f32 v8, v22, v8, v22
	v_pk_fma_f32 v[32:33], v[12:13], v[64:65], v[32:33]
	v_mov_b32_e32 v72, v49
	v_mul_f32_e32 v8, 0x3f4c422a, v8
	v_pk_fma_f32 v[32:33], v[16:17], v[72:73], v[32:33]
	v_mov_b32_e32 v76, v37
	v_add_f32_e32 v8, v8, v8
	v_pk_fma_f32 v[32:33], v[20:21], v[76:77], v[32:33]
	v_mov_b32_e32 v80, v69
	v_mul_f32_e32 v8, 0x3fb8aa3b, v8
	v_pk_fma_f32 v[32:33], v[26:27], v[80:81], v[32:33]
	v_mov_b32_e32 v54, v35
	v_mov_b32_e32 v44, v42
	v_mov_b32_e32 v45, v62
	v_exp_f32_e32 v34, v8
	v_mul_f32_e32 v8, 0x3d372713, v32
	v_pk_fma_f32 v[18:19], v[18:19], v[58:59], v[54:55]
	v_mov_b32_e32 v62, v43
	v_mul_f32_e32 v8, v32, v8
	v_pk_fma_f32 v[40:41], v[14:15], v[44:45], v[40:41]
	v_mov_b32_e32 v44, v46
	v_mov_b32_e32 v45, v66
	v_pk_fma_f32 v[14:15], v[14:15], v[62:63], v[18:19]
	v_mov_b32_e32 v66, v47
	v_fma_f32 v8, v32, v8, v32
	v_pk_fma_f32 v[40:41], v[12:13], v[44:45], v[40:41]
	v_mov_b32_e32 v44, v50
	v_mov_b32_e32 v45, v74
	v_pk_fma_f32 v[12:13], v[12:13], v[66:67], v[14:15]
	v_mul_f32_e32 v14, 0x3d372713, v23
	v_mul_f32_e32 v8, 0x3f4c422a, v8
	v_pk_fma_f32 v[40:41], v[16:17], v[44:45], v[40:41]
	v_mov_b32_e32 v44, v38
	v_mov_b32_e32 v45, v78
	v_mul_f32_e32 v14, v23, v14
	v_add_f32_e32 v8, v8, v8
	v_pk_fma_f32 v[40:41], v[20:21], v[44:45], v[40:41]
	v_mov_b32_e32 v44, v70
	v_mov_b32_e32 v45, v82
	v_fma_f32 v14, v23, v14, v23
	v_mul_f32_e32 v8, 0x3fb8aa3b, v8
	v_pk_fma_f32 v[40:41], v[26:27], v[44:45], v[40:41]
	v_mul_f32_e32 v14, 0x3f4c422a, v14
	v_exp_f32_e32 v36, v8
	v_mul_f32_e32 v8, 0x3d372713, v40
	v_add_f32_e32 v14, v14, v14
	v_mul_f32_e32 v8, v40, v8
	v_mul_f32_e32 v14, 0x3fb8aa3b, v14
	v_fma_f32 v8, v40, v8, v40
	v_mov_b32_e32 v74, v51
	v_exp_f32_e32 v35, v14
	v_mul_f32_e32 v8, 0x3f4c422a, v8
	v_pk_fma_f32 v[12:13], v[16:17], v[74:75], v[12:13]
	v_mov_b32_e32 v78, v39
	v_add_f32_e32 v8, v8, v8
	v_pk_fma_f32 v[12:13], v[20:21], v[78:79], v[12:13]
	v_mov_b32_e32 v82, v71
	v_mul_f32_e32 v8, 0x3fb8aa3b, v8
	v_pk_fma_f32 v[12:13], v[26:27], v[82:83], v[12:13]
	v_exp_f32_e32 v38, v8
	v_mul_f32_e32 v8, 0x3d372713, v12
	v_pk_add_f32 v[14:15], v[34:35], 1.0 op_sel_hi:[1,0]
	v_mul_f32_e32 v8, v12, v8
	v_div_scale_f32 v17, s[0:1], v15, v15, 2.0
	v_fma_f32 v8, v12, v8, v12
	v_rcp_f32_e32 v18, v17
	v_mul_f32_e32 v8, 0x3f4c422a, v8
	v_add_f32_e32 v8, v8, v8
	v_mul_f32_e32 v8, 0x3fb8aa3b, v8
	v_exp_f32_e32 v16, v8
	v_fma_f32 v8, -v17, v18, 1.0
	v_fmac_f32_e32 v18, v8, v18
	v_div_scale_f32 v8, vcc, 2.0, v15, 2.0
	v_mul_f32_e32 v19, v8, v18
	v_fma_f32 v20, -v17, v19, v8
	v_fmac_f32_e32 v19, v20, v18
	v_fma_f32 v8, -v17, v19, v8
	v_div_scale_f32 v17, s[0:1], v14, v14, 2.0
	v_rcp_f32_e32 v20, v17
	v_div_fmas_f32 v8, v8, v18, v19
	v_div_fixup_f32 v15, v8, v15, 2.0
	v_fma_f32 v8, -v17, v20, 1.0
	v_fmac_f32_e32 v20, v8, v20
	v_div_scale_f32 v8, vcc, 2.0, v14, 2.0
	v_mul_f32_e32 v18, v8, v20
	v_fma_f32 v19, -v17, v18, v8
	v_fmac_f32_e32 v18, v19, v20
	v_fma_f32 v8, -v17, v18, v8
	v_div_fmas_f32 v8, v8, v20, v18
	v_div_fixup_f32 v14, v8, v14, 2.0
	v_mul_f32_e32 v8, 0x3d372713, v33
	v_mul_f32_e32 v8, v33, v8
	v_fma_f32 v8, v33, v8, v33
	v_mul_f32_e32 v8, 0x3f4c422a, v8
	v_add_f32_e32 v8, v8, v8
	v_mul_f32_e32 v8, 0x3fb8aa3b, v8
	v_exp_f32_e32 v37, v8
	v_pk_add_f32 v[14:15], v[14:15], 1.0 op_sel_hi:[1,0] neg_lo:[1,0] neg_hi:[1,0]
	v_pk_mul_f32 v[18:19], v[22:23], 0.5 op_sel_hi:[1,0]
	v_pk_add_f32 v[14:15], v[14:15], 1.0 op_sel_hi:[1,0]
	v_pk_add_f32 v[20:21], v[36:37], 1.0 op_sel_hi:[1,0]
	v_pk_mul_f32 v[14:15], v[18:19], v[14:15]
	v_div_scale_f32 v8, s[0:1], v21, v21, 2.0
	v_rcp_f32_e32 v17, v8
	v_mov_b32_e32 v19, v0
	v_mov_b32_e32 v18, v4
	v_fma_f32 v0, -v8, v17, 1.0
	v_fmac_f32_e32 v17, v0, v17
	v_div_scale_f32 v0, vcc, 2.0, v21, 2.0
	v_mul_f32_e32 v4, v0, v17
	v_fma_f32 v22, -v8, v4, v0
	v_fmac_f32_e32 v4, v22, v17
	v_fma_f32 v0, -v8, v4, v0
	v_div_scale_f32 v8, s[0:1], v20, v20, 2.0
	v_rcp_f32_e32 v22, v8
	v_div_fmas_f32 v0, v0, v17, v4
	v_div_fixup_f32 v21, v0, v21, 2.0
	v_fma_f32 v0, -v8, v22, 1.0
	v_fmac_f32_e32 v22, v0, v22
	v_div_scale_f32 v0, vcc, 2.0, v20, 2.0
	v_mul_f32_e32 v4, v0, v22
	v_fma_f32 v17, -v8, v4, v0
	v_fmac_f32_e32 v4, v17, v22
	v_fma_f32 v0, -v8, v4, v0
	v_div_fmas_f32 v0, v0, v22, v4
	v_div_fixup_f32 v20, v0, v20, 2.0
	v_mul_f32_e32 v0, 0x3d372713, v41
	v_mul_f32_e32 v0, v41, v0
	v_fma_f32 v0, v41, v0, v41
	v_mul_f32_e32 v0, 0x3f4c422a, v0
	v_add_f32_e32 v0, v0, v0
	v_mul_f32_e32 v0, 0x3fb8aa3b, v0
	v_exp_f32_e32 v39, v0
	v_pk_add_f32 v[20:21], v[20:21], 1.0 op_sel_hi:[1,0] neg_lo:[1,0] neg_hi:[1,0]
	v_pk_mul_f32 v[22:23], v[32:33], 0.5 op_sel_hi:[1,0]
	v_pk_add_f32 v[20:21], v[20:21], 1.0 op_sel_hi:[1,0]
	v_mov_b32_e32 v0, v5
	v_pk_mul_f32 v[20:21], v[22:23], v[20:21]
	v_pk_add_f32 v[22:23], v[38:39], 1.0 op_sel_hi:[1,0]
	v_pk_mul_f32 v[0:1], v[20:21], v[0:1]
	v_div_scale_f32 v4, s[0:1], v23, v23, 2.0
	v_rcp_f32_e32 v8, v4
	v_pk_fma_f32 v[0:1], v[14:15], v[18:19], v[0:1]
	v_fma_f32 v5, -v4, v8, 1.0
	v_fmac_f32_e32 v8, v5, v8
	v_div_scale_f32 v5, vcc, 2.0, v23, 2.0
	v_mul_f32_e32 v14, v5, v8
	v_fma_f32 v15, -v4, v14, v5
	v_fmac_f32_e32 v14, v15, v8
	v_div_scale_f32 v15, s[0:1], v22, v22, 2.0
	v_rcp_f32_e32 v17, v15
	v_fma_f32 v4, -v4, v14, v5
	v_div_fmas_f32 v4, v4, v8, v14
	v_div_fixup_f32 v5, v4, v23, 2.0
	v_fma_f32 v4, -v15, v17, 1.0
	v_fmac_f32_e32 v17, v4, v17
	v_div_scale_f32 v4, vcc, 2.0, v22, 2.0
	v_mul_f32_e32 v8, v4, v17
	v_fma_f32 v14, -v15, v8, v4
	v_fmac_f32_e32 v8, v14, v17
	v_fma_f32 v4, -v15, v8, v4
	v_div_fmas_f32 v4, v4, v17, v8
	v_mul_f32_e32 v8, 0x3d372713, v13
	v_mul_f32_e32 v8, v13, v8
	v_fma_f32 v8, v13, v8, v13
	v_mul_f32_e32 v8, 0x3f4c422a, v8
	v_add_f32_e32 v8, v8, v8
	v_mul_f32_e32 v8, 0x3fb8aa3b, v8
	v_exp_f32_e32 v17, v8
	v_div_fixup_f32 v4, v4, v22, 2.0
	v_pk_add_f32 v[4:5], v[4:5], 1.0 op_sel_hi:[1,0] neg_lo:[1,0] neg_hi:[1,0]
	v_pk_mul_f32 v[14:15], v[40:41], 0.5 op_sel_hi:[1,0]
	v_pk_add_f32 v[4:5], v[4:5], 1.0 op_sel_hi:[1,0]
	v_pk_mul_f32 v[12:13], v[12:13], 0.5 op_sel_hi:[1,0]
	v_pk_mul_f32 v[4:5], v[14:15], v[4:5]
	v_pk_add_f32 v[14:15], v[16:17], 1.0 op_sel_hi:[1,0]
	v_mov_b32_e32 v17, v2
	v_div_scale_f32 v8, s[0:1], v15, v15, 2.0
	v_rcp_f32_e32 v18, v8
	v_mov_b32_e32 v16, v6
	v_pk_fma_f32 v[0:1], v[4:5], v[16:17], v[0:1]
	v_div_scale_f32 v6, s[0:1], v14, v14, 2.0
	v_fma_f32 v2, -v8, v18, 1.0
	v_fmac_f32_e32 v18, v2, v18
	v_div_scale_f32 v2, vcc, 2.0, v15, 2.0
	v_mul_f32_e32 v4, v2, v18
	v_fma_f32 v5, -v8, v4, v2
	v_fmac_f32_e32 v4, v5, v18
	v_fma_f32 v2, -v8, v4, v2
	v_rcp_f32_e32 v8, v6
	v_div_fmas_f32 v2, v2, v18, v4
	v_div_fixup_f32 v5, v2, v15, 2.0
	s_mov_b32 s0, 0x600000
	v_fma_f32 v2, -v6, v8, 1.0
	v_fmac_f32_e32 v8, v2, v8
	v_div_scale_f32 v2, vcc, 2.0, v14, 2.0
	v_mul_f32_e32 v4, v2, v8
	v_fma_f32 v15, -v6, v4, v2
	v_fmac_f32_e32 v4, v15, v8
	v_fma_f32 v2, -v6, v4, v2
	v_div_fmas_f32 v2, v2, v8, v4
	v_div_fixup_f32 v4, v2, v14, 2.0
	v_pk_add_f32 v[4:5], v[4:5], 1.0 op_sel_hi:[1,0] neg_lo:[1,0] neg_hi:[1,0]
	v_mov_b32_e32 v2, v7
	v_pk_add_f32 v[4:5], v[4:5], 1.0 op_sel_hi:[1,0]
	s_nop 0
	v_pk_mul_f32 v[4:5], v[12:13], v[4:5]
	s_nop 0
	v_pk_fma_f32 v[0:1], v[4:5], v[2:3], v[0:1]
	v_add_co_u32_e32 v2, vcc, s0, v10
	s_lshl_b32 s0, s3, 3
	v_pk_add_f32 v[0:1], v[24:25], v[0:1]
	v_addc_co_u32_e32 v3, vcc, 0, v11, vcc
	s_addk_i32 s0, 0x100
	global_store_dwordx2 v[2:3], v[0:1], off
	v_add_u32_e32 v8, s0, v30
	v_lshlrev_b32_e32 v3, 1, v31
	v_cvt_pk_f16_f32 v2, v0, v1
	v_lshlrev_b64 v[0:1], 6, v[8:9]
	v_and_b32_e32 v3, 48, v3
	v_or3_b32 v0, v0, v3, v28
	v_and_b32_e32 v3, 6, v29
	v_lshl_add_u64 v[0:1], v[0:1], 4, s[12:13]
	v_lshlrev_b32_e32 v8, 1, v3
	v_lshl_add_u64 v[0:1], v[0:1], 0, v[8:9]
	global_store_dword v[0:1], v2, off
	s_endpgm
	s_nop 0
	s_nop 0
	s_nop 0
	s_nop 0
	s_nop 0
	s_nop 0
	s_nop 0
	s_nop 0
	s_nop 0
	s_nop 0
	s_nop 0
	s_nop 0
	s_nop 0
	s_nop 0
	s_nop 0
	s_nop 0
	s_nop 0
	s_nop 0
	s_nop 0
	s_nop 0
	s_nop 0
	s_nop 0
	s_nop 0
	s_nop 0
	s_nop 0
	s_nop 0
	s_nop 0
	s_nop 0
	s_nop 0
	s_nop 0
	s_nop 0
	s_nop 0
	s_nop 0
	s_nop 0
	s_nop 0
	s_nop 0
	s_nop 0
	s_nop 0
	s_nop 0
	s_nop 0
	s_nop 0
	s_nop 0
	s_nop 0
	s_nop 0
	s_nop 0
	s_nop 0
	s_nop 0
	s_nop 0
	s_nop 0
	s_nop 0
	s_nop 0
	s_nop 0
	s_nop 0
	s_endpgm

	.amdhsa_kernel _ZN12_GLOBAL__N_110gemm_fullkILi1ELi5EEEvPKDF16_S2_PKfPDF16_PfS6_S4_S4_S4_S4_S4_S5_
		.amdhsa_group_segment_fixed_size 0
		.amdhsa_private_segment_fixed_size 0
		.amdhsa_kernarg_size 96
		.amdhsa_user_sgpr_count 2
		.amdhsa_user_sgpr_dispatch_ptr 0
		.amdhsa_user_sgpr_queue_ptr 0
		.amdhsa_user_sgpr_kernarg_segment_ptr 1
		.amdhsa_user_sgpr_dispatch_id 0
		.amdhsa_user_sgpr_kernarg_preload_length 0
		.amdhsa_user_sgpr_kernarg_preload_offset 0
		.amdhsa_user_sgpr_private_segment_size 0
		.amdhsa_uses_dynamic_stack 0
		.amdhsa_enable_private_segment 0
		.amdhsa_system_sgpr_workgroup_id_x 1
		.amdhsa_system_sgpr_workgroup_id_y 0
		.amdhsa_system_sgpr_workgroup_id_z 0
		.amdhsa_system_sgpr_workgroup_info 0
		.amdhsa_system_vgpr_workitem_id 0
		.amdhsa_next_free_vgpr 183
		.amdhsa_next_free_sgpr 18
		.amdhsa_accum_offset 184
		.amdhsa_reserve_vcc 1
		.amdhsa_float_round_mode_32 0
		.amdhsa_float_round_mode_16_64 0
		.amdhsa_float_denorm_mode_32 3
		.amdhsa_float_denorm_mode_16_64 3
		.amdhsa_dx10_clamp 1
		.amdhsa_ieee_mode 1
		.amdhsa_fp16_overflow 0
		.amdhsa_tg_split 0
		.amdhsa_exception_fp_ieee_invalid_op 0
		.amdhsa_exception_fp_denorm_src 0
		.amdhsa_exception_fp_ieee_div_zero 0
		.amdhsa_exception_fp_ieee_overflow 0
		.amdhsa_exception_fp_ieee_underflow 0
		.amdhsa_exception_fp_ieee_inexact 0
		.amdhsa_exception_int_div_zero 0
	.end_amdhsa_kernel

_ZN12_GLOBAL__N_110gemm_fullkILi0ELi6EEEvPKDF16_S2_PKfPDF16_PfS6_S4_S4_S4_S4_S4_S5_:
	s_load_dwordx8 s[4:11], s[0:1], 0x0
	s_lshr_b32 s0, s2, 5
	v_lshrrev_b32_e32 v230, 6, v0
	s_and_b32 s12, s0, 0x7fffffc
	s_and_b32 s2, s2, 0x7f
	s_mov_b32 s13, 0
	v_mul_u32_u24_e32 v4, 12, v230
	v_mov_b32_e32 v3, 0
	s_lshl_b64 s[0:1], s[12:13], 10
	s_mul_i32 s13, s2, 0xc0
	v_and_b32_e32 v1, 63, v0
	v_mul_u32_u24_e32 v2, 0x18000, v230
	v_add_lshl_u32 v4, s13, v4, 10
	v_mov_b32_e32 v5, v3
	s_waitcnt lgkmcnt(0)
	v_lshl_add_u64 v[4:5], s[6:7], 0, v[4:5]
	v_lshl_add_u64 v[6:7], s[4:5], 0, v[2:3]
	v_lshlrev_b32_e32 v2, 4, v1
	s_mov_b32 s3, 0x18000
	v_lshl_add_u64 v[208:209], v[4:5], 0, v[2:3]
	v_add_co_u32_e32 v80, vcc, s3, v208
	v_lshl_add_u64 v[6:7], v[6:7], 0, s[0:1]
	s_nop 0
	v_addc_co_u32_e32 v81, vcc, 0, v209, vcc
	s_mov_b32 s0, 0x19000
	v_add_co_u32_e32 v176, vcc, s0, v208
	v_lshl_add_u64 v[212:213], v[6:7], 0, v[2:3]
	s_nop 0
	v_addc_co_u32_e32 v177, vcc, 0, v209, vcc
	s_movk_i32 s0, 0x2000
	v_add_co_u32_e32 v52, vcc, s0, v212
	s_movk_i32 s1, 0x4000
	s_nop 0
	v_addc_co_u32_e32 v53, vcc, 0, v213, vcc
	v_add_co_u32_e32 v82, vcc, s1, v212
	s_movk_i32 s1, 0x6000
	s_nop 0
	v_addc_co_u32_e32 v83, vcc, 0, v213, vcc
	v_add_co_u32_e32 v96, vcc, s1, v212
	s_movk_i32 s1, 0x1000
	s_nop 0
	v_addc_co_u32_e32 v97, vcc, 0, v213, vcc
	v_add_co_u32_e32 v168, vcc, s1, v208
	global_load_dwordx4 v[4:7], v[212:213], off
	global_load_dwordx4 v[8:11], v[212:213], off offset:1024
	global_load_dwordx4 v[12:15], v[212:213], off offset:2048
	global_load_dwordx4 v[16:19], v[212:213], off offset:3072
	global_load_dwordx4 v[20:23], v[208:209], off
	global_load_dwordx4 v[24:27], v[208:209], off offset:1024
	v_addc_co_u32_e32 v169, vcc, 0, v209, vcc
	v_add_co_u32_e32 v210, vcc, s0, v208
	s_mov_b32 s0, 0x8000
	s_nop 0
	v_addc_co_u32_e32 v211, vcc, 0, v209, vcc
	v_add_co_u32_e32 v116, vcc, s0, v212
	s_mov_b32 s0, 0xa000
	s_nop 0
	v_addc_co_u32_e32 v117, vcc, 0, v213, vcc
	v_add_co_u32_e32 v132, vcc, s0, v212
	s_mov_b32 s0, 0xc000
	s_nop 0
	v_addc_co_u32_e32 v133, vcc, 0, v213, vcc
	v_add_co_u32_e32 v164, vcc, s0, v212
	global_load_dwordx4 v[28:31], v[52:53], off
	global_load_dwordx4 v[32:35], v[52:53], off offset:1024
	global_load_dwordx4 v[36:39], v[52:53], off offset:2048
	global_load_dwordx4 v[40:43], v[52:53], off offset:3072
	global_load_dwordx4 v[44:47], v[80:81], off offset:1024
	global_load_dwordx4 v[48:51], v[80:81], off offset:2048
	s_nop 0
	global_load_dwordx4 v[52:55], v[82:83], off
	global_load_dwordx4 v[56:59], v[82:83], off offset:1024
	global_load_dwordx4 v[60:63], v[82:83], off offset:2048
	global_load_dwordx4 v[64:67], v[82:83], off offset:3072
	global_load_dwordx4 v[68:71], v[208:209], off offset:2048
	global_load_dwordx4 v[72:75], v[208:209], off offset:3072
	global_load_dwordx4 v[76:79], v[80:81], off offset:3072
	s_nop 0
	global_load_dwordx4 v[80:83], v[96:97], off
	global_load_dwordx4 v[84:87], v[96:97], off offset:1024
	global_load_dwordx4 v[88:91], v[96:97], off offset:2048
	global_load_dwordx4 v[92:95], v[96:97], off offset:3072
	s_nop 0
	global_load_dwordx4 v[96:99], v[176:177], off offset:-4096
	global_load_dwordx4 v[100:103], v[176:177], off
	global_load_dwordx4 v[104:107], v[116:117], off
	global_load_dwordx4 v[108:111], v[116:117], off offset:1024
	global_load_dwordx4 v[112:115], v[116:117], off offset:2048
	s_nop 0
	global_load_dwordx4 v[116:119], v[116:117], off offset:3072
	s_nop 0
	global_load_dwordx4 v[120:123], v[132:133], off
	global_load_dwordx4 v[124:127], v[132:133], off offset:1024
	global_load_dwordx4 v[128:131], v[132:133], off offset:2048
	s_nop 0
	global_load_dwordx4 v[132:135], v[132:133], off offset:3072
	s_nop 0
	global_load_dwordx4 v[136:139], v[168:169], off offset:1024
	global_load_dwordx4 v[140:143], v[168:169], off offset:2048
	global_load_dwordx4 v[144:147], v[176:177], off offset:1024
	global_load_dwordx4 v[148:151], v[176:177], off offset:2048
	v_addc_co_u32_e32 v165, vcc, 0, v213, vcc
	global_load_dwordx4 v[152:155], v[164:165], off
	global_load_dwordx4 v[156:159], v[164:165], off offset:1024
	global_load_dwordx4 v[160:163], v[164:165], off offset:2048
	s_nop 0
	global_load_dwordx4 v[164:167], v[164:165], off offset:3072
	s_nop 0
	global_load_dwordx4 v[168:171], v[168:169], off offset:3072
	s_nop 0
	global_load_dwordx4 v[172:175], v[210:211], off offset:-4096
	s_nop 0
	global_load_dwordx4 v[176:179], v[176:177], off offset:3072
	s_mov_b32 s0, 0xe000
	v_add_co_u32_e32 v192, vcc, s0, v212
	s_lshl_b32 s0, s2, 7
	s_nop 0
	v_addc_co_u32_e32 v193, vcc, 0, v213, vcc
	global_load_dwordx4 v[180:183], v[192:193], off
	global_load_dwordx4 v[184:187], v[192:193], off offset:1024
	global_load_dwordx4 v[188:191], v[192:193], off offset:2048
	s_nop 0
	global_load_dwordx4 v[192:195], v[192:193], off offset:3072
	v_bfe_u32 v1, v0, 6, 1
	s_add_u32 s0, s8, s0
	s_addc_u32 s1, s9, 0
	v_lshlrev_b32_e32 v196, 6, v1
	v_mov_b32_e32 v197, v3
	v_lshl_add_u64 v[196:197], s[0:1], 0, v[196:197]
	v_and_b32_e32 v198, 48, v0
	v_mov_b32_e32 v199, v3
	v_lshl_add_u64 v[228:229], v[196:197], 0, v[198:199]
	s_waitcnt vmcnt(43)
	v_mfma_f32_16x16x32_f16 v[196:199], v[20:23], v[4:7], 0
	s_waitcnt vmcnt(24)
	v_mfma_f32_16x16x32_f16 v[4:7], v[96:99], v[4:7], 0
	v_mfma_f32_16x16x32_f16 v[200:203], v[20:23], v[8:11], 0
	v_mfma_f32_16x16x32_f16 v[8:11], v[96:99], v[8:11], 0
	v_mfma_f32_16x16x32_f16 v[204:207], v[20:23], v[12:15], 0
	v_mfma_f32_16x16x32_f16 v[12:15], v[96:99], v[12:15], 0
	v_mfma_f32_16x16x32_f16 v[20:23], v[20:23], v[16:19], 0
	v_mfma_f32_16x16x32_f16 v[16:19], v[96:99], v[16:19], 0
	v_mfma_f32_16x16x32_f16 v[96:99], v[24:27], v[28:31], v[196:199]
	v_mfma_f32_16x16x32_f16 v[4:7], v[44:47], v[28:31], v[4:7]
	v_mfma_f32_16x16x32_f16 v[28:31], v[24:27], v[32:35], v[200:203]
	v_mfma_f32_16x16x32_f16 v[8:11], v[44:47], v[32:35], v[8:11]
	v_mfma_f32_16x16x32_f16 v[32:35], v[24:27], v[36:39], v[204:207]
	v_mfma_f32_16x16x32_f16 v[12:15], v[44:47], v[36:39], v[12:15]
	v_mfma_f32_16x16x32_f16 v[20:23], v[24:27], v[40:43], v[20:23]
	v_mfma_f32_16x16x32_f16 v[16:19], v[44:47], v[40:43], v[16:19]
	v_mfma_f32_16x16x32_f16 v[24:27], v[68:71], v[52:55], v[96:99]
	v_mfma_f32_16x16x32_f16 v[4:7], v[48:51], v[52:55], v[4:7]
	v_mfma_f32_16x16x32_f16 v[28:31], v[68:71], v[56:59], v[28:31]
	v_mfma_f32_16x16x32_f16 v[8:11], v[48:51], v[56:59], v[8:11]
	v_mfma_f32_16x16x32_f16 v[32:35], v[68:71], v[60:63], v[32:35]
	v_mfma_f32_16x16x32_f16 v[12:15], v[48:51], v[60:63], v[12:15]
	v_mfma_f32_16x16x32_f16 v[20:23], v[68:71], v[64:67], v[20:23]
	v_mfma_f32_16x16x32_f16 v[16:19], v[48:51], v[64:67], v[16:19]
	v_mfma_f32_16x16x32_f16 v[24:27], v[72:75], v[80:83], v[24:27]
	v_mfma_f32_16x16x32_f16 v[4:7], v[76:79], v[80:83], v[4:7]
	v_mfma_f32_16x16x32_f16 v[28:31], v[72:75], v[84:87], v[28:31]
	v_mfma_f32_16x16x32_f16 v[8:11], v[76:79], v[84:87], v[8:11]
	v_mfma_f32_16x16x32_f16 v[32:35], v[72:75], v[88:91], v[32:35]
	v_mfma_f32_16x16x32_f16 v[12:15], v[76:79], v[88:91], v[12:15]
	v_mfma_f32_16x16x32_f16 v[20:23], v[72:75], v[92:95], v[20:23]
	v_mfma_f32_16x16x32_f16 v[16:19], v[76:79], v[92:95], v[16:19]
	s_mov_b32 s0, 0x1a000
	v_add_co_u32_e32 v208, vcc, s0, v208
	s_mov_b32 s0, 0x10000
	s_nop 0
	v_addc_co_u32_e32 v209, vcc, 0, v209, vcc
	v_add_co_u32_e32 v48, vcc, s0, v212
	s_mov_b32 s0, 0x12000
	s_nop 0
	v_addc_co_u32_e32 v49, vcc, 0, v213, vcc
	v_add_co_u32_e32 v80, vcc, s0, v212
	s_mov_b32 s0, 0x14000
	s_nop 0
	v_addc_co_u32_e32 v81, vcc, 0, v213, vcc
	v_add_co_u32_e32 v96, vcc, s0, v212
	global_load_dwordx4 v[36:39], v[48:49], off
	global_load_dwordx4 v[40:43], v[48:49], off offset:1024
	global_load_dwordx4 v[44:47], v[48:49], off offset:2048
	s_nop 0
	global_load_dwordx4 v[48:51], v[48:49], off offset:3072
	s_nop 0
	global_load_dwordx4 v[52:55], v[210:211], off
	global_load_dwordx4 v[56:59], v[210:211], off offset:1024
	global_load_dwordx4 v[60:63], v[208:209], off
	global_load_dwordx4 v[64:67], v[208:209], off offset:1024
	v_addc_co_u32_e32 v97, vcc, 0, v213, vcc
	global_load_dwordx4 v[68:71], v[80:81], off
	global_load_dwordx4 v[72:75], v[80:81], off offset:1024
	global_load_dwordx4 v[76:79], v[80:81], off offset:2048
	s_nop 0
	global_load_dwordx4 v[80:83], v[80:81], off offset:3072
	s_nop 0
	global_load_dwordx4 v[84:87], v[96:97], off
	global_load_dwordx4 v[88:91], v[96:97], off offset:1024
	global_load_dwordx4 v[92:95], v[96:97], off offset:2048
	s_nop 0
	global_load_dwordx4 v[96:99], v[96:97], off offset:3072
	s_nop 0
	global_load_dwordx4 v[196:199], v[210:211], off offset:2048
	global_load_dwordx4 v[200:203], v[210:211], off offset:3072
	global_load_dwordx4 v[204:207], v[208:209], off offset:2048
	s_nop 0
	global_load_dwordx4 v[208:211], v[208:209], off offset:3072
	s_mov_b32 s0, 0x16000
	v_add_co_u32_e32 v224, vcc, s0, v212
	s_nop 1
	v_addc_co_u32_e32 v225, vcc, 0, v213, vcc
	global_load_dwordx4 v[212:215], v[224:225], off
	global_load_dwordx4 v[216:219], v[224:225], off offset:1024
	global_load_dwordx4 v[220:223], v[224:225], off offset:2048
	s_nop 0
	global_load_dwordx4 v[224:227], v[224:225], off offset:3072
	s_waitcnt vmcnt(29)
	v_mfma_f32_16x16x32_f16 v[24:27], v[172:175], v[104:107], v[24:27]
	v_mfma_f32_16x16x32_f16 v[4:7], v[100:103], v[104:107], v[4:7]
	v_mfma_f32_16x16x32_f16 v[28:31], v[172:175], v[108:111], v[28:31]
	v_mfma_f32_16x16x32_f16 v[8:11], v[100:103], v[108:111], v[8:11]
	v_mfma_f32_16x16x32_f16 v[32:35], v[172:175], v[112:115], v[32:35]
	v_mfma_f32_16x16x32_f16 v[12:15], v[100:103], v[112:115], v[12:15]
	v_mfma_f32_16x16x32_f16 v[20:23], v[172:175], v[116:119], v[20:23]
	v_mfma_f32_16x16x32_f16 v[16:19], v[100:103], v[116:119], v[16:19]
	v_mfma_f32_16x16x32_f16 v[24:27], v[136:139], v[120:123], v[24:27]
	v_mfma_f32_16x16x32_f16 v[4:7], v[144:147], v[120:123], v[4:7]
	v_mfma_f32_16x16x32_f16 v[28:31], v[136:139], v[124:127], v[28:31]
	v_mfma_f32_16x16x32_f16 v[8:11], v[144:147], v[124:127], v[8:11]
	v_mfma_f32_16x16x32_f16 v[32:35], v[136:139], v[128:131], v[32:35]
	v_mfma_f32_16x16x32_f16 v[12:15], v[144:147], v[128:131], v[12:15]
	v_mfma_f32_16x16x32_f16 v[20:23], v[136:139], v[132:135], v[20:23]
	v_mfma_f32_16x16x32_f16 v[16:19], v[144:147], v[132:135], v[16:19]
	v_mfma_f32_16x16x32_f16 v[24:27], v[140:143], v[152:155], v[24:27]
	v_mfma_f32_16x16x32_f16 v[4:7], v[148:151], v[152:155], v[4:7]
	v_mfma_f32_16x16x32_f16 v[28:31], v[140:143], v[156:159], v[28:31]
	v_mfma_f32_16x16x32_f16 v[8:11], v[148:151], v[156:159], v[8:11]
	v_mfma_f32_16x16x32_f16 v[32:35], v[140:143], v[160:163], v[32:35]
	v_mfma_f32_16x16x32_f16 v[12:15], v[148:151], v[160:163], v[12:15]
	v_mfma_f32_16x16x32_f16 v[20:23], v[140:143], v[164:167], v[20:23]
	v_mfma_f32_16x16x32_f16 v[16:19], v[148:151], v[164:167], v[16:19]
	s_waitcnt vmcnt(27)
	v_mfma_f32_16x16x32_f16 v[24:27], v[168:171], v[180:183], v[24:27]
	v_mfma_f32_16x16x32_f16 v[4:7], v[176:179], v[180:183], v[4:7]
	s_waitcnt vmcnt(26)
	v_mfma_f32_16x16x32_f16 v[28:31], v[168:171], v[184:187], v[28:31]
	v_mfma_f32_16x16x32_f16 v[8:11], v[176:179], v[184:187], v[8:11]
	s_waitcnt vmcnt(25)
	v_mfma_f32_16x16x32_f16 v[32:35], v[168:171], v[188:191], v[32:35]
	v_mfma_f32_16x16x32_f16 v[12:15], v[176:179], v[188:191], v[12:15]
	s_waitcnt vmcnt(24)
	v_mfma_f32_16x16x32_f16 v[20:23], v[168:171], v[192:195], v[20:23]
	v_mfma_f32_16x16x32_f16 v[16:19], v[176:179], v[192:195], v[16:19]
	s_waitcnt vmcnt(19)
	v_mfma_f32_16x16x32_f16 v[24:27], v[52:55], v[36:39], v[24:27]
	s_waitcnt vmcnt(17)
	v_mfma_f32_16x16x32_f16 v[4:7], v[60:63], v[36:39], v[4:7]
	v_mfma_f32_16x16x32_f16 v[28:31], v[52:55], v[40:43], v[28:31]
	v_mfma_f32_16x16x32_f16 v[8:11], v[60:63], v[40:43], v[8:11]
	v_mfma_f32_16x16x32_f16 v[32:35], v[52:55], v[44:47], v[32:35]
	v_mfma_f32_16x16x32_f16 v[12:15], v[60:63], v[44:47], v[12:15]
	v_mfma_f32_16x16x32_f16 v[20:23], v[52:55], v[48:51], v[20:23]
	v_mfma_f32_16x16x32_f16 v[16:19], v[60:63], v[48:51], v[16:19]
	s_waitcnt vmcnt(15)
	v_mfma_f32_16x16x32_f16 v[24:27], v[56:59], v[68:71], v[24:27]
	v_mfma_f32_16x16x32_f16 v[4:7], v[64:67], v[68:71], v[4:7]
	s_waitcnt vmcnt(14)
	v_mfma_f32_16x16x32_f16 v[28:31], v[56:59], v[72:75], v[28:31]
	v_mfma_f32_16x16x32_f16 v[8:11], v[64:67], v[72:75], v[8:11]
	s_waitcnt vmcnt(13)
	v_mfma_f32_16x16x32_f16 v[32:35], v[56:59], v[76:79], v[32:35]
	v_mfma_f32_16x16x32_f16 v[12:15], v[64:67], v[76:79], v[12:15]
	s_waitcnt vmcnt(12)
	v_mfma_f32_16x16x32_f16 v[20:23], v[56:59], v[80:83], v[20:23]
	v_mfma_f32_16x16x32_f16 v[16:19], v[64:67], v[80:83], v[16:19]
	s_waitcnt vmcnt(7)
	v_mfma_f32_16x16x32_f16 v[24:27], v[196:199], v[84:87], v[24:27]
	s_waitcnt vmcnt(5)
	v_mfma_f32_16x16x32_f16 v[4:7], v[204:207], v[84:87], v[4:7]
	v_mfma_f32_16x16x32_f16 v[28:31], v[196:199], v[88:91], v[28:31]
	v_mfma_f32_16x16x32_f16 v[8:11], v[204:207], v[88:91], v[8:11]
	v_mfma_f32_16x16x32_f16 v[32:35], v[196:199], v[92:95], v[32:35]
	v_mfma_f32_16x16x32_f16 v[12:15], v[204:207], v[92:95], v[12:15]
	v_mfma_f32_16x16x32_f16 v[20:23], v[196:199], v[96:99], v[20:23]
	v_mfma_f32_16x16x32_f16 v[16:19], v[204:207], v[96:99], v[16:19]
	s_waitcnt vmcnt(3)
	v_mfma_f32_16x16x32_f16 v[24:27], v[200:203], v[212:215], v[24:27]
	v_mfma_f32_16x16x32_f16 v[4:7], v[208:211], v[212:215], v[4:7]
	s_waitcnt vmcnt(2)
	v_mfma_f32_16x16x32_f16 v[28:31], v[200:203], v[216:219], v[28:31]
	v_mfma_f32_16x16x32_f16 v[8:11], v[208:211], v[216:219], v[8:11]
	s_waitcnt vmcnt(1)
	v_mfma_f32_16x16x32_f16 v[32:35], v[200:203], v[220:223], v[32:35]
	v_mfma_f32_16x16x32_f16 v[12:15], v[208:211], v[220:223], v[12:15]
	s_waitcnt vmcnt(0)
	v_mfma_f32_16x16x32_f16 v[20:23], v[200:203], v[224:227], v[20:23]
	v_mfma_f32_16x16x32_f16 v[16:19], v[208:211], v[224:227], v[16:19]
	global_load_dwordx4 v[36:39], v[228:229], off
	v_add_u32_e32 v2, 0, v2
	v_and_b32_e32 v41, 0x1c0, v0
	v_lshl_add_u32 v43, v230, 13, v2
	v_lshl_add_u32 v2, v41, 4, v2
	v_lshl_add_u32 v40, v0, 4, 0
	ds_write_b128 v43, v[24:27]
	ds_write_b128 v43, v[4:7] offset:1024
	ds_write_b128 v43, v[28:31] offset:2048
	ds_write_b128 v43, v[8:11] offset:3072
	ds_write_b128 v43, v[32:35] offset:4096
	ds_write_b128 v43, v[12:15] offset:5120
	ds_write_b128 v43, v[20:23] offset:6144
	ds_write_b128 v43, v[16:19] offset:7168
	s_waitcnt lgkmcnt(0)
	s_barrier
	ds_read_b128 v[4:7], v2 offset:8192
	ds_read_b128 v[8:11], v2 offset:16384
	ds_read_b128 v[12:15], v2 offset:24576
	ds_read_b128 v[16:19], v40
	ds_read_b128 v[20:23], v2 offset:32768
	ds_read_b128 v[24:27], v2 offset:40960
	ds_read_b128 v[28:31], v2 offset:49152
	ds_read_b128 v[32:35], v2 offset:57344
	s_waitcnt lgkmcnt(4)
	v_pk_add_f32 v[4:5], v[16:17], v[4:5]
	v_pk_add_f32 v[6:7], v[18:19], v[6:7]
	v_pk_add_f32 v[4:5], v[4:5], v[8:9]
	v_pk_add_f32 v[6:7], v[6:7], v[10:11]
	v_pk_add_f32 v[4:5], v[4:5], v[12:13]
	v_pk_add_f32 v[6:7], v[6:7], v[14:15]
	s_waitcnt lgkmcnt(3)
	v_pk_add_f32 v[4:5], v[4:5], v[20:21]
	v_pk_add_f32 v[6:7], v[6:7], v[22:23]
	s_waitcnt lgkmcnt(2)
	v_pk_add_f32 v[4:5], v[4:5], v[24:25]
	v_pk_add_f32 v[6:7], v[6:7], v[26:27]
	s_waitcnt lgkmcnt(1)
	v_pk_add_f32 v[4:5], v[4:5], v[28:29]
	v_pk_add_f32 v[6:7], v[6:7], v[30:31]
	s_waitcnt lgkmcnt(0)
	v_pk_add_f32 v[4:5], v[4:5], v[32:33]
	v_pk_add_f32 v[6:7], v[6:7], v[34:35]
	v_lshrrev_b32_e32 v42, 7, v0
	s_waitcnt vmcnt(0)
	v_pk_add_f32 v[4:5], v[36:37], v[4:5]
	v_pk_add_f32 v[6:7], v[38:39], v[6:7]
	v_mul_f32_e32 v2, 0x3d372713, v4
	v_mul_f32_e32 v8, 0x3d372713, v5
	v_mul_f32_e32 v9, 0x3d372713, v6
	v_mul_f32_e32 v2, v4, v2
	v_mul_f32_e32 v8, v5, v8
	v_mul_f32_e32 v9, v6, v9
	v_fma_f32 v2, v4, v2, v4
	v_fma_f32 v8, v5, v8, v5
	v_fma_f32 v9, v6, v9, v6
	v_mul_f32_e32 v2, 0x3f4c422a, v2
	v_mul_f32_e32 v8, 0x3f4c422a, v8
	v_mul_f32_e32 v9, 0x3f4c422a, v9
	v_add_f32_e32 v2, v2, v2
	v_add_f32_e32 v8, v8, v8
	v_add_f32_e32 v9, v9, v9
	v_mul_f32_e32 v2, 0x3fb8aa3b, v2
	v_mul_f32_e32 v11, 0x3fb8aa3b, v8
	v_mul_f32_e32 v10, 0x3d372713, v7
	v_mul_f32_e32 v12, 0x3fb8aa3b, v9
	v_exp_f32_e32 v8, v2
	v_exp_f32_e32 v9, v11
	v_mul_f32_e32 v10, v7, v10
	v_fma_f32 v10, v7, v10, v7
	v_mul_f32_e32 v10, 0x3f4c422a, v10
	v_add_f32_e32 v10, v10, v10
	v_pk_add_f32 v[8:9], v[8:9], 1.0 op_sel_hi:[1,0]
	v_mul_f32_e32 v13, 0x3fb8aa3b, v10
	v_div_scale_f32 v2, s[0:1], v9, v9, 2.0
	v_exp_f32_e32 v10, v12
	v_exp_f32_e32 v11, v13
	v_div_scale_f32 v14, s[0:1], v8, v8, 2.0
	v_rcp_f32_e32 v16, v2
	v_rcp_f32_e32 v17, v14
	v_pk_add_f32 v[10:11], v[10:11], 1.0 op_sel_hi:[1,0]
	v_div_scale_f32 v13, vcc, 2.0, v9, 2.0
	v_fma_f32 v20, -v2, v16, 1.0
	v_div_scale_f32 v15, s[0:1], v11, v11, 2.0
	v_fma_f32 v21, -v14, v17, 1.0
	v_fmac_f32_e32 v16, v20, v16
	v_div_scale_f32 v19, s[0:1], 2.0, v8, 2.0
	v_fmac_f32_e32 v17, v21, v17
	v_mul_f32_e32 v20, v13, v16
	v_mul_f32_e32 v21, v19, v17
	v_fma_f32 v23, -v2, v20, v13
	v_fma_f32 v24, -v14, v21, v19
	v_fmac_f32_e32 v20, v23, v16
	v_fmac_f32_e32 v21, v24, v17
	v_fma_f32 v2, -v2, v20, v13
	v_rcp_f32_e32 v18, v15
	v_fma_f32 v13, -v14, v21, v19
	v_div_fmas_f32 v2, v2, v16, v20
	s_mov_b64 vcc, s[0:1]
	v_div_fixup_f32 v9, v2, v9, 2.0
	v_div_fmas_f32 v2, v13, v17, v21
	v_div_fixup_f32 v8, v2, v8, 2.0
	v_pk_add_f32 v[8:9], v[8:9], 1.0 op_sel_hi:[1,0] neg_lo:[1,0] neg_hi:[1,0]
	v_pk_mul_f32 v[4:5], v[4:5], 0.5 op_sel_hi:[1,0]
	v_fma_f32 v22, -v15, v18, 1.0
	v_pk_add_f32 v[8:9], v[8:9], 1.0 op_sel_hi:[1,0]
	v_fmac_f32_e32 v18, v22, v18
	v_pk_mul_f32 v[4:5], v[4:5], v[8:9]
	v_div_scale_f32 v2, vcc, 2.0, v11, 2.0
	v_cvt_pk_f16_f32 v4, v4, v5
	v_mul_f32_e32 v5, v2, v18
	v_fma_f32 v8, -v15, v5, v2
	v_fmac_f32_e32 v5, v8, v18
	v_div_scale_f32 v8, s[0:1], v10, v10, 2.0
	v_rcp_f32_e32 v13, v8
	v_fma_f32 v2, -v15, v5, v2
	v_div_fmas_f32 v2, v2, v18, v5
	v_div_fixup_f32 v9, v2, v11, 2.0
	v_fma_f32 v2, -v8, v13, 1.0
	v_fmac_f32_e32 v13, v2, v13
	v_div_scale_f32 v2, vcc, 2.0, v10, 2.0
	v_mul_f32_e32 v5, v2, v13
	v_fma_f32 v11, -v8, v5, v2
	v_fmac_f32_e32 v5, v11, v13
	v_fma_f32 v2, -v8, v5, v2
	v_div_fmas_f32 v2, v2, v13, v5
	v_div_fixup_f32 v8, v2, v10, 2.0
	v_pk_add_f32 v[8:9], v[8:9], 1.0 op_sel_hi:[1,0] neg_lo:[1,0] neg_hi:[1,0]
	s_lshl_b32 s0, s2, 3
	v_pk_mul_f32 v[6:7], v[6:7], 0.5 op_sel_hi:[1,0]
	v_pk_add_f32 v[8:9], v[8:9], 1.0 op_sel_hi:[1,0]
	s_add_i32 s0, s0, s12
	v_pk_mul_f32 v[6:7], v[6:7], v[8:9]
	v_or_b32_e32 v2, s0, v42
	v_cvt_pk_f16_f32 v5, v6, v7
	v_lshlrev_b64 v[6:7], 6, v[2:3]
	v_lshrrev_b32_e32 v2, 1, v0
	v_and_b32_e32 v12, 15, v0
	v_and_b32_e32 v0, 16, v2
	v_lshl_or_b32 v0, v1, 5, v0
	v_or3_b32 v6, v6, v0, v12
	v_lshl_add_u64 v[0:1], v[6:7], 4, s[10:11]
	v_and_b32_e32 v2, 8, v2
	v_lshl_add_u64 v[0:1], v[0:1], 0, v[2:3]
	global_store_dwordx2 v[0:1], v[4:5], off
	s_endpgm
	s_nop 0
	s_nop 0
	s_nop 0
	s_nop 0
	s_nop 0
	s_nop 0
	s_nop 0
	s_nop 0
	s_nop 0
	s_nop 0
	s_nop 0
	s_nop 0
	s_nop 0
	s_nop 0
	s_nop 0
	s_nop 0
	s_nop 0
	s_nop 0
	s_nop 0
	s_nop 0
	s_nop 0
	s_nop 0
	s_nop 0
	s_nop 0
	s_nop 0
	s_nop 0
	s_nop 0
	s_nop 0
	s_nop 0
	s_nop 0
	s_nop 0
	s_endpgm

	.amdhsa_kernel _ZN12_GLOBAL__N_110gemm_fullkILi0ELi6EEEvPKDF16_S2_PKfPDF16_PfS6_S4_S4_S4_S4_S4_S5_
		.amdhsa_group_segment_fixed_size 0
		.amdhsa_private_segment_fixed_size 0
		.amdhsa_kernarg_size 96
		.amdhsa_user_sgpr_count 2
		.amdhsa_user_sgpr_dispatch_ptr 0
		.amdhsa_user_sgpr_queue_ptr 0
		.amdhsa_user_sgpr_kernarg_segment_ptr 1
		.amdhsa_user_sgpr_dispatch_id 0
		.amdhsa_user_sgpr_kernarg_preload_length 0
		.amdhsa_user_sgpr_kernarg_preload_offset 0
		.amdhsa_user_sgpr_private_segment_size 0
		.amdhsa_uses_dynamic_stack 0
		.amdhsa_enable_private_segment 0
		.amdhsa_system_sgpr_workgroup_id_x 1
		.amdhsa_system_sgpr_workgroup_id_y 0
		.amdhsa_system_sgpr_workgroup_id_z 0
		.amdhsa_system_sgpr_workgroup_info 0
		.amdhsa_system_vgpr_workitem_id 0
		.amdhsa_next_free_vgpr 231
		.amdhsa_next_free_sgpr 14
		.amdhsa_accum_offset 232
		.amdhsa_reserve_vcc 1
		.amdhsa_float_round_mode_32 0
		.amdhsa_float_round_mode_16_64 0
		.amdhsa_float_denorm_mode_32 3
		.amdhsa_float_denorm_mode_16_64 3
		.amdhsa_dx10_clamp 1
		.amdhsa_ieee_mode 1
		.amdhsa_fp16_overflow 0
		.amdhsa_tg_split 0
		.amdhsa_exception_fp_ieee_invalid_op 0
		.amdhsa_exception_fp_denorm_src 0
		.amdhsa_exception_fp_ieee_div_zero 0
		.amdhsa_exception_fp_ieee_overflow 0
		.amdhsa_exception_fp_ieee_underflow 0
		.amdhsa_exception_fp_ieee_inexact 0
		.amdhsa_exception_int_div_zero 0
	.end_amdhsa_kernel

_ZN12_GLOBAL__N_110gemm_fullkILi1ELi6EEEvPKDF16_S2_PKfPDF16_PfS6_S4_S4_S4_S4_S4_S5_:
	s_load_dwordx2 s[4:5], s[0:1], 0x38
	s_and_b32 s3, s2, 63
	s_lshl_b32 s16, s3, 5
	s_lshl_b32 s6, s3, 13
	v_lshlrev_b32_e32 v1, 4, v0
	s_waitcnt lgkmcnt(0)
	s_add_u32 s4, s4, s6
	s_addc_u32 s5, s5, 0
	global_load_dwordx4 v[2:5], v1, s[4:5]
	v_lshlrev_b32_e32 v1, 2, v0
	v_cmp_lt_u32_e32 vcc, 31, v0
	s_and_saveexec_b64 s[4:5], vcc
	s_xor_b64 s[4:5], exec, s[4:5]
	s_cbranch_execz .LBB21_10
	v_cmp_lt_u32_e32 vcc, 63, v0
	s_and_saveexec_b64 s[6:7], vcc
	s_xor_b64 s[6:7], exec, s[6:7]
	s_cbranch_execz .LBB21_7
	s_movk_i32 s8, 0x47
	v_cmp_lt_u32_e32 vcc, s8, v0
	s_and_saveexec_b64 s[8:9], vcc
	s_xor_b64 s[8:9], exec, s[8:9]
	s_cbranch_execz .LBB21_4
	s_load_dwordx2 s[10:11], s[0:1], 0x10
	s_lshl_b32 s12, s16, 2
	v_lshlrev_b32_e32 v6, 2, v1
	v_mov_b32_e32 v7, 0
	s_movk_i32 s14, 0x50
	s_waitcnt lgkmcnt(0)
	s_add_u32 s10, s10, s12
	s_addc_u32 s11, s11, 0
	s_movk_i32 s12, 0xfb80
	v_lshl_add_u64 v[6:7], s[10:11], 0, v[6:7]
	s_mov_b32 s13, -1
	v_lshl_add_u64 v[6:7], v[6:7], 0, s[12:13]
	v_mov_b32_e32 v8, s11
	v_cmp_gt_u32_e32 vcc, s14, v0
	s_nop 1
	v_cndmask_b32_e32 v27, v8, v7, vcc
	v_mov_b32_e32 v7, s10
	v_cndmask_b32_e32 v26, v7, v6, vcc
.LBB21_4:
	s_andn2_saveexec_b64 s[8:9], s[8:9]
	s_cbranch_execz .LBB21_6
	s_load_dwordx2 s[10:11], s[0:1], 0x50
	s_lshl_b32 s12, s16, 2
	v_lshlrev_b32_e32 v6, 2, v1
	v_mov_b32_e32 v7, 0
	s_waitcnt lgkmcnt(0)
	s_add_u32 s10, s10, s12
	s_addc_u32 s11, s11, 0
	v_lshl_add_u64 v[6:7], s[10:11], 0, v[6:7]
	s_movk_i32 s10, 0xfc00
	s_mov_b32 s11, -1
	v_lshl_add_u64 v[26:27], v[6:7], 0, s[10:11]

.LBB21_7:
	s_andn2_saveexec_b64 s[6:7], s[6:7]
	s_cbranch_execz .LBB21_9
	s_load_dwordx2 s[8:9], s[0:1], 0x48
	s_lshl_b32 s10, s3, 9
	v_lshlrev_b32_e32 v6, 2, v1
	v_mov_b32_e32 v7, 0
	s_waitcnt lgkmcnt(0)
	s_add_u32 s8, s8, s10
	s_addc_u32 s9, s9, 0
	v_lshl_add_u64 v[6:7], s[8:9], 0, v[6:7]
	s_movk_i32 s8, 0xfe00
	s_mov_b32 s9, -1
	v_lshl_add_u64 v[26:27], v[6:7], 0, s[8:9]

.LBB21_10:
	s_or_saveexec_b64 s[14:15], s[4:5]
	s_load_dwordx2 s[12:13], s[0:1], 0x58
	s_load_dwordx4 s[8:11], s[0:1], 0x0
	s_load_dwordx4 s[4:7], s[0:1], 0x20
	s_xor_b64 exec, exec, s[14:15]
	s_cbranch_execz .LBB21_12
	s_load_dwordx2 s[0:1], s[0:1], 0x40
	s_lshl_b32 s17, s3, 9
	v_lshlrev_b32_e32 v6, 2, v1
	v_mov_b32_e32 v7, 0
	s_waitcnt lgkmcnt(0)
	s_add_u32 s0, s0, s17
	s_addc_u32 s1, s1, 0
	v_lshl_add_u64 v[26:27], s[0:1], 0, v[6:7]
.LBB21_12:
	s_or_b64 exec, exec, s[14:15]
	v_lshrrev_b32_e32 v184, 6, v0
	s_lshr_b32 s0, s2, 5
	s_and_b32 s0, s0, 0x7fffffe
	s_mov_b32 s1, 0
	v_lshlrev_b32_e32 v8, 17, v184
	v_mov_b32_e32 v9, 0
	v_and_b32_e32 v12, 63, v0
	s_lshl_b64 s[14:15], s[0:1], 10
	v_lshlrev_b32_e32 v6, 14, v184
	s_waitcnt lgkmcnt(0)
	v_lshl_add_u64 v[10:11], s[8:9], 0, v[8:9]
	v_lshl_or_b32 v6, s3, 18, v6
	v_mov_b32_e32 v7, v9
	v_lshl_add_u64 v[10:11], v[10:11], 0, s[14:15]
	v_lshlrev_b32_e32 v8, 4, v12
	v_lshl_add_u64 v[6:7], s[10:11], 0, v[6:7]
	v_lshl_add_u64 v[28:29], v[10:11], 0, v[8:9]
	v_lshrrev_b32_e32 v10, 2, v0
	v_lshl_add_u64 v[180:181], v[6:7], 0, v[8:9]
	v_lshrrev_b32_e32 v6, 8, v0
	v_lshrrev_b32_e32 v7, 3, v0
	v_and_b32_e32 v10, 12, v10
	v_and_b32_e32 v30, 15, v0
	v_bfe_u32 v34, v0, 6, 1
	v_or_b32_e32 v32, s0, v6
	v_and_or_b32 v33, v7, 16, v10
	v_lshl_or_b32 v6, v32, 4, v30
	v_lshl_or_b32 v31, v34, 1, v33
	v_mov_b32_e32 v7, v9
	v_or_b32_e32 v10, s16, v31
	v_lshlrev_b64 v[12:13], 13, v[6:7]
	v_lshl_add_u64 v[6:7], s[4:5], 0, v[12:13]
	v_lshlrev_b32_e32 v14, 2, v10
	v_mov_b32_e32 v15, v9
	v_lshl_add_u64 v[10:11], v[6:7], 0, v[14:15]
	s_mov_b32 s2, 0x600000
	v_add_co_u32_e32 v6, vcc, s2, v10
	v_lshl_add_u64 v[12:13], s[6:7], 0, v[12:13]
	s_nop 0
	v_addc_co_u32_e32 v7, vcc, 0, v11, vcc
	v_lshl_add_u64 v[24:25], v[12:13], 0, v[14:15]
	s_mov_b32 s0, 0x100000
	v_add_co_u32_e32 v18, vcc, s0, v24
	s_mov_b32 s0, 0x200000
	s_nop 0
	v_addc_co_u32_e32 v19, vcc, 0, v25, vcc
	v_add_co_u32_e32 v20, vcc, s0, v24
	s_mov_b32 s0, 0x300000
	s_nop 0
	v_addc_co_u32_e32 v21, vcc, 0, v25, vcc
	v_add_co_u32_e32 v36, vcc, s0, v24
	s_mov_b32 s0, 0x400000
	s_nop 0
	v_addc_co_u32_e32 v37, vcc, 0, v25, vcc
	global_load_dwordx2 v[6:7], v[6:7], off
	s_nop 0
	global_load_dwordx2 v[22:23], v[24:25], off
	global_load_dwordx2 v[14:15], v[18:19], off
	global_load_dwordx2 v[12:13], v[20:21], off
	global_load_dwordx2 v[16:17], v[36:37], off
	v_add_co_u32_e32 v36, vcc, s0, v24
	s_mov_b32 s0, 0x500000
	s_nop 0
	v_addc_co_u32_e32 v37, vcc, 0, v25, vcc
	v_add_co_u32_e32 v38, vcc, s0, v24
	s_mov_b32 s0, 0x20000
	s_nop 0
	v_addc_co_u32_e32 v39, vcc, 0, v25, vcc
	v_add_co_u32_e32 v88, vcc, s0, v180
	s_mov_b32 s0, 0x21000
	s_nop 0
	v_addc_co_u32_e32 v89, vcc, 0, v181, vcc
	v_add_co_u32_e32 v152, vcc, s0, v180
	s_movk_i32 s0, 0x2000
	s_nop 0
	v_addc_co_u32_e32 v153, vcc, 0, v181, vcc
	v_add_co_u32_e32 v68, vcc, s0, v28
	s_movk_i32 s1, 0x4000
	s_nop 0
	v_addc_co_u32_e32 v69, vcc, 0, v29, vcc
	v_add_co_u32_e32 v90, vcc, s1, v28
	s_movk_i32 s1, 0x6000
	s_nop 0
	v_addc_co_u32_e32 v91, vcc, 0, v29, vcc
	v_add_co_u32_e32 v96, vcc, s1, v28
	s_movk_i32 s1, 0x1000
	s_nop 0
	v_addc_co_u32_e32 v97, vcc, 0, v29, vcc
	v_add_co_u32_e32 v144, vcc, s1, v180
	global_load_dwordx2 v[18:19], v[36:37], off
	global_load_dwordx2 v[20:21], v[38:39], off
	v_addc_co_u32_e32 v145, vcc, 0, v181, vcc
	v_add_co_u32_e32 v168, vcc, s0, v180
	s_mov_b32 s0, 0x8000
	s_nop 0
	v_addc_co_u32_e32 v169, vcc, 0, v181, vcc
	v_add_co_u32_e32 v112, vcc, s0, v28
	s_mov_b32 s0, 0xa000
	s_nop 0
	v_addc_co_u32_e32 v113, vcc, 0, v29, vcc
	v_add_co_u32_e32 v116, vcc, s0, v28
	s_mov_b32 s0, 0xc000
	s_nop 0
	v_addc_co_u32_e32 v117, vcc, 0, v29, vcc
	v_add_co_u32_e32 v140, vcc, s0, v28
	global_load_dwordx4 v[36:39], v[28:29], off
	global_load_dwordx4 v[40:43], v[28:29], off offset:1024
	global_load_dwordx4 v[44:47], v[180:181], off
	global_load_dwordx4 v[48:51], v[180:181], off offset:1024
	global_load_dwordx4 v[52:55], v[68:69], off
	global_load_dwordx4 v[56:59], v[68:69], off offset:1024
	global_load_dwordx4 v[60:63], v[88:89], off offset:1024
	global_load_dwordx4 v[64:67], v[88:89], off offset:2048
	s_nop 0
	global_load_dwordx4 v[68:71], v[90:91], off
	global_load_dwordx4 v[72:75], v[90:91], off offset:1024
	global_load_dwordx4 v[76:79], v[180:181], off offset:2048
	global_load_dwordx4 v[80:83], v[180:181], off offset:3072
	global_load_dwordx4 v[84:87], v[88:89], off offset:3072
	s_nop 0
	global_load_dwordx4 v[88:91], v[96:97], off
	global_load_dwordx4 v[92:95], v[96:97], off offset:1024
	s_nop 0
	global_load_dwordx4 v[96:99], v[152:153], off offset:-4096
	global_load_dwordx4 v[100:103], v[152:153], off
	global_load_dwordx4 v[104:107], v[112:113], off
	global_load_dwordx4 v[108:111], v[112:113], off offset:1024
	s_nop 0
	global_load_dwordx4 v[112:115], v[116:117], off
	s_nop 0
	global_load_dwordx4 v[116:119], v[116:117], off offset:1024
	s_nop 0
	global_load_dwordx4 v[120:123], v[144:145], off offset:1024
	global_load_dwordx4 v[124:127], v[144:145], off offset:2048
	global_load_dwordx4 v[128:131], v[152:153], off offset:1024
	global_load_dwordx4 v[132:135], v[152:153], off offset:2048
	v_addc_co_u32_e32 v141, vcc, 0, v29, vcc
	global_load_dwordx4 v[136:139], v[140:141], off
	s_nop 0
	global_load_dwordx4 v[140:143], v[140:141], off offset:1024
	s_nop 0
	global_load_dwordx4 v[144:147], v[144:145], off offset:3072
	s_nop 0
	global_load_dwordx4 v[148:151], v[168:169], off offset:-4096
	s_nop 0
	global_load_dwordx4 v[152:155], v[152:153], off offset:3072
	s_mov_b32 s0, 0xe000
	v_add_co_u32_e32 v160, vcc, s0, v28
	v_lshrrev_b32_e32 v35, 7, v0
	s_nop 0
	v_addc_co_u32_e32 v161, vcc, 0, v29, vcc
	global_load_dwordx4 v[156:159], v[160:161], off
	s_nop 0
	global_load_dwordx4 v[160:163], v[160:161], off offset:1024
	s_waitcnt vmcnt(29)
	v_mfma_f32_16x16x32_f16 v[164:167], v[44:47], v[36:39], 0
	s_waitcnt vmcnt(16)
	v_mfma_f32_16x16x32_f16 v[36:39], v[96:99], v[36:39], 0
	v_mfma_f32_16x16x32_f16 v[44:47], v[44:47], v[40:43], 0
	v_mfma_f32_16x16x32_f16 v[40:43], v[96:99], v[40:43], 0
	v_mfma_f32_16x16x32_f16 v[96:99], v[48:51], v[52:55], v[164:167]
	v_mfma_f32_16x16x32_f16 v[36:39], v[60:63], v[52:55], v[36:39]
	v_mfma_f32_16x16x32_f16 v[44:47], v[48:51], v[56:59], v[44:47]
	v_mfma_f32_16x16x32_f16 v[40:43], v[60:63], v[56:59], v[40:43]
	v_mfma_f32_16x16x32_f16 v[48:51], v[76:79], v[68:71], v[96:99]
	v_mfma_f32_16x16x32_f16 v[36:39], v[64:67], v[68:71], v[36:39]
	v_mfma_f32_16x16x32_f16 v[44:47], v[76:79], v[72:75], v[44:47]
	v_mfma_f32_16x16x32_f16 v[40:43], v[64:67], v[72:75], v[40:43]
	v_mfma_f32_16x16x32_f16 v[48:51], v[80:83], v[88:91], v[48:51]
	v_mfma_f32_16x16x32_f16 v[36:39], v[84:87], v[88:91], v[36:39]
	v_mfma_f32_16x16x32_f16 v[44:47], v[80:83], v[92:95], v[44:47]
	v_mfma_f32_16x16x32_f16 v[40:43], v[84:87], v[92:95], v[40:43]
	s_mov_b32 s0, 0x22000
	v_add_co_u32_e32 v170, vcc, s0, v180
	s_mov_b32 s0, 0x23000
	s_nop 0
	v_addc_co_u32_e32 v171, vcc, 0, v181, vcc
	v_add_co_u32_e32 v182, vcc, s0, v180
	s_mov_b32 s0, 0x10000
	s_nop 0
	v_addc_co_u32_e32 v183, vcc, 0, v181, vcc
	v_add_co_u32_e32 v60, vcc, s0, v28
	s_mov_b32 s0, 0x12000
	s_nop 0
	v_addc_co_u32_e32 v61, vcc, 0, v29, vcc
	v_add_co_u32_e32 v76, vcc, s0, v28
	s_mov_b32 s0, 0x14000
	s_nop 0
	v_addc_co_u32_e32 v77, vcc, 0, v29, vcc
	v_add_co_u32_e32 v92, vcc, s0, v28
	global_load_dwordx4 v[52:55], v[182:183], off offset:-4096
	s_nop 0
	v_addc_co_u32_e32 v93, vcc, 0, v29, vcc
	global_load_dwordx4 v[56:59], v[60:61], off
	s_nop 0
	global_load_dwordx4 v[60:63], v[60:61], off offset:1024
	s_nop 0
	global_load_dwordx4 v[64:67], v[168:169], off
	global_load_dwordx4 v[68:71], v[168:169], off offset:1024
	global_load_dwordx4 v[72:75], v[76:77], off
	s_nop 0
	global_load_dwordx4 v[76:79], v[76:77], off offset:1024
	s_nop 0
	global_load_dwordx4 v[80:83], v[170:171], off offset:1024
	global_load_dwordx4 v[84:87], v[170:171], off offset:2048
	global_load_dwordx4 v[88:91], v[92:93], off
	s_nop 0
	global_load_dwordx4 v[92:95], v[92:93], off offset:1024
	s_nop 0
	global_load_dwordx4 v[96:99], v[168:169], off offset:2048
	global_load_dwordx4 v[164:167], v[168:169], off offset:3072
	s_nop 0
	global_load_dwordx4 v[168:171], v[170:171], off offset:3072
	s_mov_b32 s0, 0x16000
	v_add_co_u32_e32 v176, vcc, s0, v28
	s_nop 1
	v_addc_co_u32_e32 v177, vcc, 0, v29, vcc
	global_load_dwordx4 v[172:175], v[176:177], off
	s_nop 0
	global_load_dwordx4 v[176:179], v[176:177], off offset:1024
	s_waitcnt vmcnt(19)
	v_mfma_f32_16x16x32_f16 v[48:51], v[148:151], v[104:107], v[48:51]
	v_mfma_f32_16x16x32_f16 v[36:39], v[100:103], v[104:107], v[36:39]
	v_mfma_f32_16x16x32_f16 v[44:47], v[148:151], v[108:111], v[44:47]
	v_mfma_f32_16x16x32_f16 v[40:43], v[100:103], v[108:111], v[40:43]
	v_mfma_f32_16x16x32_f16 v[48:51], v[120:123], v[112:115], v[48:51]
	v_mfma_f32_16x16x32_f16 v[36:39], v[128:131], v[112:115], v[36:39]
	v_mfma_f32_16x16x32_f16 v[44:47], v[120:123], v[116:119], v[44:47]
	v_mfma_f32_16x16x32_f16 v[40:43], v[128:131], v[116:119], v[40:43]
	v_mfma_f32_16x16x32_f16 v[48:51], v[124:127], v[136:139], v[48:51]
	v_mfma_f32_16x16x32_f16 v[36:39], v[132:135], v[136:139], v[36:39]
	v_mfma_f32_16x16x32_f16 v[44:47], v[124:127], v[140:143], v[44:47]
	v_mfma_f32_16x16x32_f16 v[40:43], v[132:135], v[140:143], v[40:43]
	s_waitcnt vmcnt(17)
	v_mfma_f32_16x16x32_f16 v[48:51], v[144:147], v[156:159], v[48:51]
	v_mfma_f32_16x16x32_f16 v[36:39], v[152:155], v[156:159], v[36:39]
	s_waitcnt vmcnt(16)
	v_mfma_f32_16x16x32_f16 v[44:47], v[144:147], v[160:163], v[44:47]
	v_mfma_f32_16x16x32_f16 v[40:43], v[152:155], v[160:163], v[40:43]
	s_movk_i32 s0, 0x3000
	v_add_co_u32_e32 v144, vcc, s0, v180
	s_mov_b32 s0, 0x18000
	s_nop 0
	v_addc_co_u32_e32 v145, vcc, 0, v181, vcc
	v_add_co_u32_e32 v104, vcc, s0, v28
	s_mov_b32 s0, 0x1a000
	s_nop 0
	v_addc_co_u32_e32 v105, vcc, 0, v29, vcc
	v_add_co_u32_e32 v128, vcc, s0, v28
	s_mov_b32 s0, 0x1c000
	s_nop 0
	v_addc_co_u32_e32 v129, vcc, 0, v29, vcc
	v_add_co_u32_e32 v136, vcc, s0, v28
	global_load_dwordx4 v[100:103], v[104:105], off
	s_nop 0
	global_load_dwordx4 v[104:107], v[104:105], off offset:1024
	s_nop 0
	global_load_dwordx4 v[108:111], v[144:145], off
	global_load_dwordx4 v[112:115], v[144:145], off offset:1024
	global_load_dwordx4 v[116:119], v[182:183], off
	global_load_dwordx4 v[120:123], v[182:183], off offset:1024
	v_addc_co_u32_e32 v137, vcc, 0, v29, vcc
	global_load_dwordx4 v[124:127], v[128:129], off
	s_nop 0
	global_load_dwordx4 v[128:131], v[128:129], off offset:1024
	s_nop 0
	global_load_dwordx4 v[132:135], v[136:137], off
	s_nop 0
	global_load_dwordx4 v[136:139], v[136:137], off offset:1024
	s_nop 0
	global_load_dwordx4 v[140:143], v[144:145], off offset:2048
	s_nop 0
	global_load_dwordx4 v[144:147], v[144:145], off offset:3072
	s_nop 0
	global_load_dwordx4 v[148:151], v[182:183], off offset:2048
	global_load_dwordx4 v[152:155], v[182:183], off offset:3072
	s_mov_b32 s0, 0x1e000
	v_add_co_u32_e32 v28, vcc, s0, v28
	s_nop 1
	v_addc_co_u32_e32 v29, vcc, 0, v29, vcc
	global_load_dwordx4 v[156:159], v[28:29], off
	global_load_dwordx4 v[160:163], v[28:29], off offset:1024
	s_waitcnt vmcnt(28)
	v_mfma_f32_16x16x32_f16 v[48:51], v[64:67], v[56:59], v[48:51]
	v_mfma_f32_16x16x32_f16 v[36:39], v[52:55], v[56:59], v[36:39]
	v_mfma_f32_16x16x32_f16 v[44:47], v[64:67], v[60:63], v[44:47]
	v_mfma_f32_16x16x32_f16 v[40:43], v[52:55], v[60:63], v[40:43]
	s_waitcnt vmcnt(26)
	v_mfma_f32_16x16x32_f16 v[48:51], v[68:71], v[72:75], v[48:51]
	s_waitcnt vmcnt(24)
	v_mfma_f32_16x16x32_f16 v[36:39], v[80:83], v[72:75], v[36:39]
	v_mfma_f32_16x16x32_f16 v[44:47], v[68:71], v[76:79], v[44:47]
	v_mfma_f32_16x16x32_f16 v[40:43], v[80:83], v[76:79], v[40:43]
	s_waitcnt vmcnt(20)
	v_mfma_f32_16x16x32_f16 v[48:51], v[96:99], v[88:91], v[48:51]
	v_mfma_f32_16x16x32_f16 v[36:39], v[84:87], v[88:91], v[36:39]
	v_mfma_f32_16x16x32_f16 v[44:47], v[96:99], v[92:95], v[44:47]
	v_mfma_f32_16x16x32_f16 v[40:43], v[84:87], v[92:95], v[40:43]
	s_waitcnt vmcnt(17)
	v_mfma_f32_16x16x32_f16 v[48:51], v[164:167], v[172:175], v[48:51]
	v_mfma_f32_16x16x32_f16 v[36:39], v[168:171], v[172:175], v[36:39]
	s_waitcnt vmcnt(16)
	v_mfma_f32_16x16x32_f16 v[44:47], v[164:167], v[176:179], v[44:47]
	v_mfma_f32_16x16x32_f16 v[40:43], v[168:171], v[176:179], v[40:43]
	s_waitcnt vmcnt(13)
	v_mfma_f32_16x16x32_f16 v[48:51], v[108:111], v[100:103], v[48:51]
	s_waitcnt vmcnt(11)
	v_mfma_f32_16x16x32_f16 v[36:39], v[116:119], v[100:103], v[36:39]
	v_mfma_f32_16x16x32_f16 v[44:47], v[108:111], v[104:107], v[44:47]
	v_mfma_f32_16x16x32_f16 v[40:43], v[116:119], v[104:107], v[40:43]
	s_waitcnt vmcnt(9)
	v_mfma_f32_16x16x32_f16 v[48:51], v[112:115], v[124:127], v[48:51]
	v_mfma_f32_16x16x32_f16 v[36:39], v[120:123], v[124:127], v[36:39]
	s_waitcnt vmcnt(8)
	v_mfma_f32_16x16x32_f16 v[44:47], v[112:115], v[128:131], v[44:47]
	v_mfma_f32_16x16x32_f16 v[40:43], v[120:123], v[128:131], v[40:43]
	s_waitcnt vmcnt(5)
	v_mfma_f32_16x16x32_f16 v[48:51], v[140:143], v[132:135], v[48:51]
	s_waitcnt vmcnt(3)
	v_mfma_f32_16x16x32_f16 v[36:39], v[148:151], v[132:135], v[36:39]
	v_mfma_f32_16x16x32_f16 v[44:47], v[140:143], v[136:139], v[44:47]
	v_mfma_f32_16x16x32_f16 v[40:43], v[148:151], v[136:139], v[40:43]
	s_waitcnt vmcnt(1)
	v_mfma_f32_16x16x32_f16 v[48:51], v[144:147], v[156:159], v[48:51]
	v_mfma_f32_16x16x32_f16 v[36:39], v[152:155], v[156:159], v[36:39]
	s_waitcnt vmcnt(0)
	v_mfma_f32_16x16x32_f16 v[44:47], v[144:147], v[160:163], v[44:47]
	v_mfma_f32_16x16x32_f16 v[40:43], v[152:155], v[160:163], v[40:43]
	v_lshlrev_b32_e32 v28, 12, v184
	v_add3_u32 v28, 0, v8, v28
	s_nop 1
	ds_write_b128 v28, v[48:51]
	ds_write_b128 v28, v[36:39] offset:1024
	s_nop 0
	ds_write_b128 v28, v[44:47] offset:2048
	ds_write_b128 v28, v[40:43] offset:3072
	v_lshrrev_b32_e32 v28, 4, v0
	v_and_b32_e32 v29, 60, v1
	v_mul_u32_u24_e32 v28, 0x110, v28
	v_lshlrev_b32_e32 v29, 2, v29
	s_movk_i32 s0, 0x50
	v_add3_u32 v28, 0, v28, v29
	v_cmp_gt_u32_e32 vcc, s0, v0
	ds_write_b128 v28, v[2:5] offset:32768
	s_and_saveexec_b64 s[0:1], vcc
	s_cbranch_execz .LBB21_14
	global_load_dwordx4 v[2:5], v[26:27], off
	v_lshl_add_u32 v0, v1, 2, 0
	s_waitcnt vmcnt(0)
	ds_write_b128 v0, v[2:5] offset:41472
.LBB21_14:
	s_or_b64 exec, exec, s[0:1]
	v_lshlrev_b32_e32 v0, 10, v35
	v_add3_u32 v8, 0, v0, v8
	s_waitcnt lgkmcnt(0)
	s_barrier
	ds_read_b128 v[0:3], v8
	ds_read_b128 v[26:29], v8 offset:4096
	ds_read_b128 v[36:39], v8 offset:8192
	v_cmp_eq_u32_e32 vcc, 0, v34
	s_waitcnt lgkmcnt(1)
	v_pk_add_f32 v[28:29], v[2:3], v[28:29]
	ds_read_b128 v[2:5], v8 offset:12288
	v_pk_add_f32 v[0:1], v[0:1], v[26:27]
	s_waitcnt lgkmcnt(1)
	v_pk_add_f32 v[38:39], v[28:29], v[38:39]
	ds_read_b128 v[26:29], v8 offset:16384
	v_pk_add_f32 v[0:1], v[0:1], v[36:37]
	s_waitcnt lgkmcnt(1)
	v_pk_add_f32 v[4:5], v[38:39], v[4:5]
	v_pk_add_f32 v[40:41], v[0:1], v[2:3]
	ds_read_b128 v[0:3], v8 offset:20480
	ds_read_b128 v[36:39], v8 offset:24576
	s_waitcnt lgkmcnt(2)
	v_pk_add_f32 v[4:5], v[4:5], v[28:29]
	v_pk_add_f32 v[40:41], v[40:41], v[26:27]
	ds_read_b128 v[26:29], v8 offset:28672
	v_lshl_add_u32 v8, v31, 2, 0
	s_waitcnt lgkmcnt(2)
	v_pk_add_f32 v[2:3], v[4:5], v[2:3]
	ds_read_b64 v[4:5], v8 offset:42624
	v_pk_add_f32 v[0:1], v[40:41], v[0:1]
	s_waitcnt lgkmcnt(2)
	v_pk_add_f32 v[2:3], v[2:3], v[38:39]
	v_pk_add_f32 v[0:1], v[0:1], v[36:37]
	s_waitcnt lgkmcnt(1)
	v_pk_add_f32 v[2:3], v[2:3], v[28:29]
	v_pk_add_f32 v[0:1], v[0:1], v[26:27]
	ds_read_b32 v27, v8 offset:42500
	v_cndmask_b32_e32 v1, v3, v1, vcc
	v_cndmask_b32_e32 v0, v2, v0, vcc
	s_waitcnt lgkmcnt(1)
	v_pk_add_f32 v[0:1], v[0:1], v[4:5]
	s_nop 0
	v_pk_add_f32 v[28:29], v[6:7], v[0:1]
	v_add_co_u32_e32 v0, vcc, s2, v24
	s_nop 1
	v_addc_co_u32_e32 v1, vcc, 0, v25, vcc
	global_store_dwordx2 v[0:1], v[28:29], off
	v_mad_u32_u24 v0, v31, 12, v8
	v_or_b32_e32 v1, 1, v31
	ds_read_b128 v[34:37], v0 offset:41472
	v_lshl_add_u32 v8, v31, 8, v0
	v_lshl_add_u32 v4, v1, 4, 0
	ds_read_b128 v[38:41], v8 offset:32912
	ds_read_b128 v[42:45], v8 offset:32928
	ds_read_b128 v[46:49], v8 offset:32944
	ds_read_b128 v[50:53], v8 offset:32960
	ds_read_b128 v[54:57], v4 offset:41472
	v_lshl_add_u32 v78, v1, 8, v4
	ds_read_b128 v[58:61], v78 offset:32912
	ds_read_b128 v[62:65], v78 offset:32928
	ds_read_b128 v[66:69], v78 offset:32944
	ds_read_b128 v[70:73], v78 offset:32960
	s_waitcnt lgkmcnt(8)
	v_mov_b32_e32 v24, v38
	s_waitcnt lgkmcnt(3)
	v_mov_b32_e32 v25, v58
	v_mov_b32_e32 v74, v34
	v_mov_b32_e32 v75, v54
	v_pk_fma_f32 v[24:25], v[22:23], v[24:25], v[74:75]
	v_mov_b32_e32 v74, v42
	s_waitcnt lgkmcnt(2)
	v_mov_b32_e32 v75, v62
	v_pk_fma_f32 v[24:25], v[14:15], v[74:75], v[24:25]
	v_mov_b32_e32 v74, v46
	s_waitcnt lgkmcnt(1)
	v_mov_b32_e32 v75, v66
	v_mov_b32_e32 v58, v39
	v_mov_b32_e32 v54, v35
	v_pk_fma_f32 v[74:75], v[12:13], v[74:75], v[24:25]
	v_pk_fma_f32 v[24:25], v[22:23], v[58:59], v[54:55]
	v_mov_b32_e32 v62, v43
	v_pk_fma_f32 v[24:25], v[14:15], v[62:63], v[24:25]
	v_mov_b32_e32 v66, v47
	v_pk_fma_f32 v[46:47], v[12:13], v[66:67], v[24:25]
	v_mov_b32_e32 v24, v40
	v_mov_b32_e32 v25, v60
	v_mov_b32_e32 v34, v36
	v_mov_b32_e32 v35, v56
	v_mad_i32_i24 v26, v31, -12, v0
	v_pk_fma_f32 v[24:25], v[22:23], v[24:25], v[34:35]
	v_mov_b32_e32 v34, v44
	v_mov_b32_e32 v35, v64
	v_mov_b32_e32 v60, v41
	v_mov_b32_e32 v56, v37
	ds_read_b128 v[0:3], v0 offset:41984
	ds_read_b128 v[4:7], v4 offset:41984
	v_mov_b32_e32 v76, v50
	s_waitcnt lgkmcnt(2)
	v_mov_b32_e32 v77, v70
	v_mov_b32_e32 v70, v51
	v_pk_fma_f32 v[50:51], v[14:15], v[34:35], v[24:25]
	v_pk_fma_f32 v[66:67], v[22:23], v[60:61], v[56:57]
	v_mov_b32_e32 v64, v45
	ds_read_b128 v[22:25], v8 offset:32976
	ds_read_b128 v[34:37], v8 offset:32992
	ds_read_b32 v26, v26 offset:42496
	ds_read_b128 v[38:41], v8 offset:33008
	ds_read_b128 v[42:45], v78 offset:32976
	ds_read_b128 v[54:57], v78 offset:32992
	ds_read_b128 v[58:61], v78 offset:33008
	v_pk_fma_f32 v[74:75], v[16:17], v[76:77], v[74:75]
	s_waitcnt lgkmcnt(6)
	v_mov_b32_e32 v76, v22
	s_waitcnt lgkmcnt(2)
	v_mov_b32_e32 v77, v42
	v_pk_fma_f32 v[74:75], v[18:19], v[76:77], v[74:75]
	v_mov_b32_e32 v76, v34
	s_waitcnt lgkmcnt(1)
	v_mov_b32_e32 v77, v54
	v_pk_fma_f32 v[74:75], v[20:21], v[76:77], v[74:75]
	v_mov_b32_e32 v76, v38
	s_waitcnt lgkmcnt(0)
	v_mov_b32_e32 v77, v58
	v_pk_fma_f32 v[74:75], v[28:29], v[76:77], v[74:75]
	v_pk_fma_f32 v[46:47], v[16:17], v[70:71], v[46:47]
	v_mul_f32_e32 v8, 0x3d372713, v74
	v_mul_f32_e32 v8, v74, v8
	v_fma_f32 v8, v74, v8, v74
	v_mov_b32_e32 v42, v23
	v_mul_f32_e32 v8, 0x3f4c422a, v8
	v_pk_fma_f32 v[42:43], v[18:19], v[42:43], v[46:47]
	v_mov_b32_e32 v54, v35
	v_add_f32_e32 v8, v8, v8
	v_pk_fma_f32 v[34:35], v[20:21], v[54:55], v[42:43]
	v_mov_b32_e32 v58, v39
	v_mul_f32_e32 v8, 0x3fb8aa3b, v8
	v_pk_fma_f32 v[34:35], v[28:29], v[58:59], v[34:35]
	v_mov_b32_e32 v62, v48
	v_mov_b32_e32 v63, v68
	v_exp_f32_e32 v22, v8
	v_mul_f32_e32 v8, 0x3d372713, v34
	v_mul_f32_e32 v8, v34, v8
	v_pk_fma_f32 v[42:43], v[12:13], v[62:63], v[50:51]
	v_mov_b32_e32 v46, v52
	v_mov_b32_e32 v47, v72
	v_pk_fma_f32 v[14:15], v[14:15], v[64:65], v[66:67]
	v_mov_b32_e32 v68, v49
	v_fma_f32 v8, v34, v8, v34
	v_pk_fma_f32 v[42:43], v[16:17], v[46:47], v[42:43]
	v_mov_b32_e32 v46, v24
	v_mov_b32_e32 v47, v44
	v_pk_fma_f32 v[12:13], v[12:13], v[68:69], v[14:15]
	v_mul_f32_e32 v14, 0x3d372713, v75
	v_mul_f32_e32 v8, 0x3f4c422a, v8
	v_pk_fma_f32 v[42:43], v[18:19], v[46:47], v[42:43]
	v_mov_b32_e32 v46, v36
	v_mov_b32_e32 v47, v56
	v_mul_f32_e32 v14, v75, v14
	v_add_f32_e32 v8, v8, v8
	v_pk_fma_f32 v[42:43], v[20:21], v[46:47], v[42:43]
	v_mov_b32_e32 v46, v40
	v_mov_b32_e32 v47, v60
	v_fma_f32 v14, v75, v14, v75
	v_mul_f32_e32 v8, 0x3fb8aa3b, v8
	v_pk_fma_f32 v[42:43], v[28:29], v[46:47], v[42:43]
	v_mul_f32_e32 v14, 0x3f4c422a, v14
	v_exp_f32_e32 v38, v8
	v_mul_f32_e32 v8, 0x3d372713, v42
	v_add_f32_e32 v14, v14, v14
	v_mul_f32_e32 v8, v42, v8
	v_mov_b32_e32 v72, v53
	v_mul_f32_e32 v14, 0x3fb8aa3b, v14
	v_fma_f32 v8, v42, v8, v42
	v_pk_fma_f32 v[12:13], v[16:17], v[72:73], v[12:13]
	v_mov_b32_e32 v44, v25
	v_exp_f32_e32 v23, v14
	v_mul_f32_e32 v8, 0x3f4c422a, v8
	v_pk_fma_f32 v[12:13], v[18:19], v[44:45], v[12:13]
	v_mov_b32_e32 v56, v37
	v_add_f32_e32 v8, v8, v8
	v_pk_fma_f32 v[12:13], v[20:21], v[56:57], v[12:13]
	v_mov_b32_e32 v60, v41
	v_mul_f32_e32 v8, 0x3fb8aa3b, v8
	v_pk_fma_f32 v[12:13], v[28:29], v[60:61], v[12:13]
	v_exp_f32_e32 v24, v8
	v_mul_f32_e32 v8, 0x3d372713, v12
	v_pk_add_f32 v[14:15], v[22:23], 1.0 op_sel_hi:[1,0]
	v_mul_f32_e32 v8, v12, v8
	v_div_scale_f32 v17, s[0:1], v15, v15, 2.0
	v_fma_f32 v8, v12, v8, v12
	v_rcp_f32_e32 v18, v17
	v_mul_f32_e32 v8, 0x3f4c422a, v8
	v_add_f32_e32 v8, v8, v8
	v_mul_f32_e32 v8, 0x3fb8aa3b, v8
	v_exp_f32_e32 v16, v8
	v_fma_f32 v8, -v17, v18, 1.0
	v_fmac_f32_e32 v18, v8, v18
	v_div_scale_f32 v8, vcc, 2.0, v15, 2.0
	v_mul_f32_e32 v19, v8, v18
	v_fma_f32 v20, -v17, v19, v8
	v_fmac_f32_e32 v19, v20, v18
	v_fma_f32 v8, -v17, v19, v8
	v_div_scale_f32 v17, s[0:1], v14, v14, 2.0
	v_rcp_f32_e32 v20, v17
	v_div_fmas_f32 v8, v8, v18, v19
	v_div_fixup_f32 v15, v8, v15, 2.0
	v_fma_f32 v8, -v17, v20, 1.0
	v_fmac_f32_e32 v20, v8, v20
	v_div_scale_f32 v8, vcc, 2.0, v14, 2.0
	v_mul_f32_e32 v18, v8, v20
	v_fma_f32 v19, -v17, v18, v8
	v_fmac_f32_e32 v18, v19, v20
	v_fma_f32 v8, -v17, v18, v8
	v_div_fmas_f32 v8, v8, v20, v18
	v_div_fixup_f32 v14, v8, v14, 2.0
	v_mul_f32_e32 v8, 0x3d372713, v35
	v_mul_f32_e32 v8, v35, v8
	v_fma_f32 v8, v35, v8, v35
	v_mul_f32_e32 v8, 0x3f4c422a, v8
	v_add_f32_e32 v8, v8, v8
	v_mul_f32_e32 v8, 0x3fb8aa3b, v8
	v_exp_f32_e32 v39, v8
	v_pk_add_f32 v[14:15], v[14:15], 1.0 op_sel_hi:[1,0] neg_lo:[1,0] neg_hi:[1,0]
	v_pk_mul_f32 v[18:19], v[74:75], 0.5 op_sel_hi:[1,0]
	v_pk_add_f32 v[14:15], v[14:15], 1.0 op_sel_hi:[1,0]
	v_pk_add_f32 v[20:21], v[38:39], 1.0 op_sel_hi:[1,0]
	v_pk_mul_f32 v[14:15], v[18:19], v[14:15]
	v_div_scale_f32 v8, s[0:1], v21, v21, 2.0
	v_rcp_f32_e32 v17, v8
	v_mov_b32_e32 v18, v0
	v_mov_b32_e32 v19, v4
	v_fma_f32 v0, -v8, v17, 1.0
	v_fmac_f32_e32 v17, v0, v17
	v_div_scale_f32 v0, vcc, 2.0, v21, 2.0
	v_mul_f32_e32 v4, v0, v17
	v_fma_f32 v22, -v8, v4, v0
	v_fmac_f32_e32 v4, v22, v17
	v_fma_f32 v0, -v8, v4, v0
	v_div_scale_f32 v8, s[0:1], v20, v20, 2.0
	v_rcp_f32_e32 v22, v8
	v_div_fmas_f32 v0, v0, v17, v4
	v_div_fixup_f32 v21, v0, v21, 2.0
	v_fma_f32 v0, -v8, v22, 1.0
	v_fmac_f32_e32 v22, v0, v22
	v_div_scale_f32 v0, vcc, 2.0, v20, 2.0
	v_mul_f32_e32 v4, v0, v22
	v_fma_f32 v17, -v8, v4, v0
	v_fmac_f32_e32 v4, v17, v22
	v_fma_f32 v0, -v8, v4, v0
	v_div_fmas_f32 v0, v0, v22, v4
	v_div_fixup_f32 v20, v0, v20, 2.0
	v_mul_f32_e32 v0, 0x3d372713, v43
	v_mul_f32_e32 v0, v43, v0
	v_fma_f32 v0, v43, v0, v43
	v_mul_f32_e32 v0, 0x3f4c422a, v0
	v_add_f32_e32 v0, v0, v0
	v_mul_f32_e32 v0, 0x3fb8aa3b, v0
	v_exp_f32_e32 v25, v0
	v_pk_add_f32 v[20:21], v[20:21], 1.0 op_sel_hi:[1,0] neg_lo:[1,0] neg_hi:[1,0]
	v_pk_mul_f32 v[22:23], v[34:35], 0.5 op_sel_hi:[1,0]
	v_pk_add_f32 v[20:21], v[20:21], 1.0 op_sel_hi:[1,0]
	v_mov_b32_e32 v4, v1
	v_pk_mul_f32 v[20:21], v[22:23], v[20:21]
	v_pk_add_f32 v[22:23], v[24:25], 1.0 op_sel_hi:[1,0]
	v_pk_mul_f32 v[0:1], v[20:21], v[4:5]
	v_div_scale_f32 v8, s[0:1], v23, v23, 2.0
	v_rcp_f32_e32 v17, v8
	v_pk_fma_f32 v[0:1], v[14:15], v[18:19], v[0:1]
	v_fma_f32 v4, -v8, v17, 1.0
	v_fmac_f32_e32 v17, v4, v17
	v_div_scale_f32 v4, vcc, 2.0, v23, 2.0
	v_mul_f32_e32 v5, v4, v17
	v_fma_f32 v14, -v8, v5, v4
	v_fmac_f32_e32 v5, v14, v17
	v_fma_f32 v4, -v8, v5, v4
	v_div_scale_f32 v8, s[0:1], v22, v22, 2.0
	v_rcp_f32_e32 v14, v8
	v_div_fmas_f32 v4, v4, v17, v5
	v_div_fixup_f32 v5, v4, v23, 2.0
	v_fma_f32 v4, -v8, v14, 1.0
	v_fmac_f32_e32 v14, v4, v14
	v_div_scale_f32 v4, vcc, 2.0, v22, 2.0
	v_mul_f32_e32 v15, v4, v14
	v_fma_f32 v17, -v8, v15, v4
	v_fmac_f32_e32 v15, v17, v14
	v_fma_f32 v4, -v8, v15, v4
	v_mul_f32_e32 v8, 0x3d372713, v13
	v_mul_f32_e32 v8, v13, v8
	v_fma_f32 v8, v13, v8, v13
	v_mul_f32_e32 v8, 0x3f4c422a, v8
	v_add_f32_e32 v8, v8, v8
	v_mul_f32_e32 v8, 0x3fb8aa3b, v8
	v_div_fmas_f32 v4, v4, v14, v15
	v_exp_f32_e32 v17, v8
	v_div_fixup_f32 v4, v4, v22, 2.0
	v_pk_add_f32 v[4:5], v[4:5], 1.0 op_sel_hi:[1,0] neg_lo:[1,0] neg_hi:[1,0]
	v_pk_mul_f32 v[14:15], v[42:43], 0.5 op_sel_hi:[1,0]
	v_pk_add_f32 v[4:5], v[4:5], 1.0 op_sel_hi:[1,0]
	v_pk_mul_f32 v[12:13], v[12:13], 0.5 op_sel_hi:[1,0]
	v_pk_mul_f32 v[4:5], v[14:15], v[4:5]
	v_pk_add_f32 v[14:15], v[16:17], 1.0 op_sel_hi:[1,0]
	v_mov_b32_e32 v16, v2
	v_div_scale_f32 v8, s[0:1], v15, v15, 2.0
	v_rcp_f32_e32 v18, v8
	v_mov_b32_e32 v17, v6
	v_pk_fma_f32 v[0:1], v[4:5], v[16:17], v[0:1]
	v_div_scale_f32 v6, s[0:1], v14, v14, 2.0
	v_fma_f32 v2, -v8, v18, 1.0
	v_fmac_f32_e32 v18, v2, v18
	v_div_scale_f32 v2, vcc, 2.0, v15, 2.0
	v_mul_f32_e32 v4, v2, v18
	v_fma_f32 v5, -v8, v4, v2
	v_fmac_f32_e32 v4, v5, v18
	v_fma_f32 v2, -v8, v4, v2
	v_rcp_f32_e32 v8, v6
	v_div_fmas_f32 v2, v2, v18, v4
	v_div_fixup_f32 v5, v2, v15, 2.0
	s_mov_b32 s0, 0x700000
	v_fma_f32 v2, -v6, v8, 1.0
	v_fmac_f32_e32 v8, v2, v8
	v_div_scale_f32 v2, vcc, 2.0, v14, 2.0
	v_mul_f32_e32 v4, v2, v8
	v_fma_f32 v15, -v6, v4, v2
	v_fmac_f32_e32 v4, v15, v8
	v_fma_f32 v2, -v6, v4, v2
	v_div_fmas_f32 v2, v2, v8, v4
	v_div_fixup_f32 v4, v2, v14, 2.0
	v_pk_add_f32 v[4:5], v[4:5], 1.0 op_sel_hi:[1,0] neg_lo:[1,0] neg_hi:[1,0]
	v_mov_b32_e32 v6, v3
	v_pk_add_f32 v[4:5], v[4:5], 1.0 op_sel_hi:[1,0]
	v_add_co_u32_e32 v2, vcc, s0, v10
	v_pk_mul_f32 v[4:5], v[12:13], v[4:5]
	s_lshl_b32 s0, s3, 3
	v_pk_fma_f32 v[0:1], v[4:5], v[6:7], v[0:1]
	v_addc_co_u32_e32 v3, vcc, 0, v11, vcc
	v_pk_add_f32 v[0:1], v[26:27], v[0:1]
	s_addk_i32 s0, 0x100
	global_store_dwordx2 v[2:3], v[0:1], off
	v_add_u32_e32 v8, s0, v32
	v_lshlrev_b32_e32 v3, 1, v33
	v_cvt_pk_f16_f32 v2, v0, v1
	v_lshlrev_b64 v[0:1], 6, v[8:9]
	v_and_b32_e32 v3, 48, v3
	v_or3_b32 v0, v0, v3, v30
	v_and_b32_e32 v3, 6, v31
	v_lshl_add_u64 v[0:1], v[0:1], 4, s[12:13]
	v_lshlrev_b32_e32 v8, 1, v3
	v_lshl_add_u64 v[0:1], v[0:1], 0, v[8:9]
	global_store_dword v[0:1], v2, off
	s_endpgm
	s_nop 0
	s_nop 0
	s_nop 0
	s_nop 0
	s_nop 0
	s_nop 0
	s_nop 0
	s_nop 0
	s_nop 0
	s_nop 0
	s_nop 0
	s_nop 0
	s_nop 0
	s_nop 0
	s_nop 0
	s_nop 0
	s_nop 0
	s_nop 0
	s_nop 0
	s_nop 0
	s_nop 0
	s_nop 0
	s_nop 0
	s_nop 0
	s_nop 0
	s_nop 0
	s_nop 0
	s_nop 0
	s_endpgm

	.amdhsa_kernel _ZN12_GLOBAL__N_110gemm_fullkILi1ELi6EEEvPKDF16_S2_PKfPDF16_PfS6_S4_S4_S4_S4_S4_S5_
		.amdhsa_group_segment_fixed_size 0
		.amdhsa_private_segment_fixed_size 0
		.amdhsa_kernarg_size 96
		.amdhsa_user_sgpr_count 2
		.amdhsa_user_sgpr_dispatch_ptr 0
		.amdhsa_user_sgpr_queue_ptr 0
		.amdhsa_user_sgpr_kernarg_segment_ptr 1
		.amdhsa_user_sgpr_dispatch_id 0
		.amdhsa_user_sgpr_kernarg_preload_length 0
		.amdhsa_user_sgpr_kernarg_preload_offset 0
		.amdhsa_user_sgpr_private_segment_size 0
		.amdhsa_uses_dynamic_stack 0
		.amdhsa_enable_private_segment 0
		.amdhsa_system_sgpr_workgroup_id_x 1
		.amdhsa_system_sgpr_workgroup_id_y 0
		.amdhsa_system_sgpr_workgroup_id_z 0
		.amdhsa_system_sgpr_workgroup_info 0
		.amdhsa_system_vgpr_workitem_id 0
		.amdhsa_next_free_vgpr 185
		.amdhsa_next_free_sgpr 18
		.amdhsa_accum_offset 188
		.amdhsa_reserve_vcc 1
		.amdhsa_float_round_mode_32 0
		.amdhsa_float_round_mode_16_64 0
		.amdhsa_float_denorm_mode_32 3
		.amdhsa_float_denorm_mode_16_64 3
		.amdhsa_dx10_clamp 1
		.amdhsa_ieee_mode 1
		.amdhsa_fp16_overflow 0
		.amdhsa_tg_split 0
		.amdhsa_exception_fp_ieee_invalid_op 0
		.amdhsa_exception_fp_denorm_src 0
		.amdhsa_exception_fp_ieee_div_zero 0
		.amdhsa_exception_fp_ieee_overflow 0
		.amdhsa_exception_fp_ieee_underflow 0
		.amdhsa_exception_fp_ieee_inexact 0
		.amdhsa_exception_int_div_zero 0
	.end_amdhsa_kernel

_ZN12_GLOBAL__N_110gemm_fullkILi0ELi7EEEvPKDF16_S2_PKfPDF16_PfS6_S4_S4_S4_S4_S4_S5_:
	s_load_dwordx8 s[4:11], s[0:1], 0x0
	s_lshr_b32 s0, s2, 5
	v_lshrrev_b32_e32 v230, 6, v0
	s_and_b32 s12, s0, 0x7fffffc
	s_and_b32 s2, s2, 0x7f
	s_mov_b32 s13, 0
	v_mul_u32_u24_e32 v4, 12, v230
	v_mov_b32_e32 v3, 0
	s_lshl_b64 s[0:1], s[12:13], 10
	s_mul_i32 s13, s2, 0xc0
	v_and_b32_e32 v1, 63, v0
	v_mul_u32_u24_e32 v2, 0x18000, v230
	v_add_lshl_u32 v4, s13, v4, 10
	v_mov_b32_e32 v5, v3
	s_waitcnt lgkmcnt(0)
	v_lshl_add_u64 v[4:5], s[6:7], 0, v[4:5]
	v_lshl_add_u64 v[6:7], s[4:5], 0, v[2:3]
	v_lshlrev_b32_e32 v2, 4, v1
	s_mov_b32 s3, 0x18000
	v_lshl_add_u64 v[208:209], v[4:5], 0, v[2:3]
	v_add_co_u32_e32 v80, vcc, s3, v208
	v_lshl_add_u64 v[6:7], v[6:7], 0, s[0:1]
	s_nop 0
	v_addc_co_u32_e32 v81, vcc, 0, v209, vcc
	s_mov_b32 s0, 0x19000
	v_add_co_u32_e32 v176, vcc, s0, v208
	v_lshl_add_u64 v[212:213], v[6:7], 0, v[2:3]
	s_nop 0
	v_addc_co_u32_e32 v177, vcc, 0, v209, vcc
	s_movk_i32 s0, 0x2000
	v_add_co_u32_e32 v52, vcc, s0, v212
	s_movk_i32 s1, 0x4000
	s_nop 0
	v_addc_co_u32_e32 v53, vcc, 0, v213, vcc
	v_add_co_u32_e32 v82, vcc, s1, v212
	s_movk_i32 s1, 0x6000
	s_nop 0
	v_addc_co_u32_e32 v83, vcc, 0, v213, vcc
	v_add_co_u32_e32 v96, vcc, s1, v212
	s_movk_i32 s1, 0x1000
	s_nop 0
	v_addc_co_u32_e32 v97, vcc, 0, v213, vcc
	v_add_co_u32_e32 v168, vcc, s1, v208
	global_load_dwordx4 v[4:7], v[212:213], off
	global_load_dwordx4 v[8:11], v[212:213], off offset:1024
	global_load_dwordx4 v[12:15], v[212:213], off offset:2048
	global_load_dwordx4 v[16:19], v[212:213], off offset:3072
	global_load_dwordx4 v[20:23], v[208:209], off
	global_load_dwordx4 v[24:27], v[208:209], off offset:1024
	v_addc_co_u32_e32 v169, vcc, 0, v209, vcc
	v_add_co_u32_e32 v210, vcc, s0, v208
	s_mov_b32 s0, 0x8000
	s_nop 0
	v_addc_co_u32_e32 v211, vcc, 0, v209, vcc
	v_add_co_u32_e32 v116, vcc, s0, v212
	s_mov_b32 s0, 0xa000
	s_nop 0
	v_addc_co_u32_e32 v117, vcc, 0, v213, vcc
	v_add_co_u32_e32 v132, vcc, s0, v212
	s_mov_b32 s0, 0xc000
	s_nop 0
	v_addc_co_u32_e32 v133, vcc, 0, v213, vcc
	v_add_co_u32_e32 v164, vcc, s0, v212
	global_load_dwordx4 v[28:31], v[52:53], off
	global_load_dwordx4 v[32:35], v[52:53], off offset:1024
	global_load_dwordx4 v[36:39], v[52:53], off offset:2048
	global_load_dwordx4 v[40:43], v[52:53], off offset:3072
	global_load_dwordx4 v[44:47], v[80:81], off offset:1024
	global_load_dwordx4 v[48:51], v[80:81], off offset:2048
	s_nop 0
	global_load_dwordx4 v[52:55], v[82:83], off
	global_load_dwordx4 v[56:59], v[82:83], off offset:1024
	global_load_dwordx4 v[60:63], v[82:83], off offset:2048
	global_load_dwordx4 v[64:67], v[82:83], off offset:3072
	global_load_dwordx4 v[68:71], v[208:209], off offset:2048
	global_load_dwordx4 v[72:75], v[208:209], off offset:3072
	global_load_dwordx4 v[76:79], v[80:81], off offset:3072
	s_nop 0
	global_load_dwordx4 v[80:83], v[96:97], off
	global_load_dwordx4 v[84:87], v[96:97], off offset:1024
	global_load_dwordx4 v[88:91], v[96:97], off offset:2048
	global_load_dwordx4 v[92:95], v[96:97], off offset:3072
	s_nop 0
	global_load_dwordx4 v[96:99], v[176:177], off offset:-4096
	global_load_dwordx4 v[100:103], v[176:177], off
	global_load_dwordx4 v[104:107], v[116:117], off
	global_load_dwordx4 v[108:111], v[116:117], off offset:1024
	global_load_dwordx4 v[112:115], v[116:117], off offset:2048
	s_nop 0
	global_load_dwordx4 v[116:119], v[116:117], off offset:3072
	s_nop 0
	global_load_dwordx4 v[120:123], v[132:133], off
	global_load_dwordx4 v[124:127], v[132:133], off offset:1024
	global_load_dwordx4 v[128:131], v[132:133], off offset:2048
	s_nop 0
	global_load_dwordx4 v[132:135], v[132:133], off offset:3072
	s_nop 0
	global_load_dwordx4 v[136:139], v[168:169], off offset:1024
	global_load_dwordx4 v[140:143], v[168:169], off offset:2048
	global_load_dwordx4 v[144:147], v[176:177], off offset:1024
	global_load_dwordx4 v[148:151], v[176:177], off offset:2048
	v_addc_co_u32_e32 v165, vcc, 0, v213, vcc
	global_load_dwordx4 v[152:155], v[164:165], off
	global_load_dwordx4 v[156:159], v[164:165], off offset:1024
	global_load_dwordx4 v[160:163], v[164:165], off offset:2048
	s_nop 0
	global_load_dwordx4 v[164:167], v[164:165], off offset:3072
	s_nop 0
	global_load_dwordx4 v[168:171], v[168:169], off offset:3072
	s_nop 0
	global_load_dwordx4 v[172:175], v[210:211], off offset:-4096
	s_nop 0
	global_load_dwordx4 v[176:179], v[176:177], off offset:3072
	s_mov_b32 s0, 0xe000
	v_add_co_u32_e32 v192, vcc, s0, v212
	s_lshl_b32 s0, s2, 7
	s_nop 0
	v_addc_co_u32_e32 v193, vcc, 0, v213, vcc
	global_load_dwordx4 v[180:183], v[192:193], off
	global_load_dwordx4 v[184:187], v[192:193], off offset:1024
	global_load_dwordx4 v[188:191], v[192:193], off offset:2048
	s_nop 0
	global_load_dwordx4 v[192:195], v[192:193], off offset:3072
	v_bfe_u32 v1, v0, 6, 1
	s_add_u32 s0, s8, s0
	s_addc_u32 s1, s9, 0
	v_lshlrev_b32_e32 v196, 6, v1
	v_mov_b32_e32 v197, v3
	v_lshl_add_u64 v[196:197], s[0:1], 0, v[196:197]
	v_and_b32_e32 v198, 48, v0
	v_mov_b32_e32 v199, v3
	v_lshl_add_u64 v[228:229], v[196:197], 0, v[198:199]
	s_waitcnt vmcnt(43)
	v_mfma_f32_16x16x32_f16 v[196:199], v[20:23], v[4:7], 0
	s_waitcnt vmcnt(24)
	v_mfma_f32_16x16x32_f16 v[4:7], v[96:99], v[4:7], 0
	v_mfma_f32_16x16x32_f16 v[200:203], v[20:23], v[8:11], 0
	v_mfma_f32_16x16x32_f16 v[8:11], v[96:99], v[8:11], 0
	v_mfma_f32_16x16x32_f16 v[204:207], v[20:23], v[12:15], 0
	v_mfma_f32_16x16x32_f16 v[12:15], v[96:99], v[12:15], 0
	v_mfma_f32_16x16x32_f16 v[20:23], v[20:23], v[16:19], 0
	v_mfma_f32_16x16x32_f16 v[16:19], v[96:99], v[16:19], 0
	v_mfma_f32_16x16x32_f16 v[96:99], v[24:27], v[28:31], v[196:199]
	v_mfma_f32_16x16x32_f16 v[4:7], v[44:47], v[28:31], v[4:7]
	v_mfma_f32_16x16x32_f16 v[28:31], v[24:27], v[32:35], v[200:203]
	v_mfma_f32_16x16x32_f16 v[8:11], v[44:47], v[32:35], v[8:11]
	v_mfma_f32_16x16x32_f16 v[32:35], v[24:27], v[36:39], v[204:207]
	v_mfma_f32_16x16x32_f16 v[12:15], v[44:47], v[36:39], v[12:15]
	v_mfma_f32_16x16x32_f16 v[20:23], v[24:27], v[40:43], v[20:23]
	v_mfma_f32_16x16x32_f16 v[16:19], v[44:47], v[40:43], v[16:19]
	v_mfma_f32_16x16x32_f16 v[24:27], v[68:71], v[52:55], v[96:99]
	v_mfma_f32_16x16x32_f16 v[4:7], v[48:51], v[52:55], v[4:7]
	v_mfma_f32_16x16x32_f16 v[28:31], v[68:71], v[56:59], v[28:31]
	v_mfma_f32_16x16x32_f16 v[8:11], v[48:51], v[56:59], v[8:11]
	v_mfma_f32_16x16x32_f16 v[32:35], v[68:71], v[60:63], v[32:35]
	v_mfma_f32_16x16x32_f16 v[12:15], v[48:51], v[60:63], v[12:15]
	v_mfma_f32_16x16x32_f16 v[20:23], v[68:71], v[64:67], v[20:23]
	v_mfma_f32_16x16x32_f16 v[16:19], v[48:51], v[64:67], v[16:19]
	v_mfma_f32_16x16x32_f16 v[24:27], v[72:75], v[80:83], v[24:27]
	v_mfma_f32_16x16x32_f16 v[4:7], v[76:79], v[80:83], v[4:7]
	v_mfma_f32_16x16x32_f16 v[28:31], v[72:75], v[84:87], v[28:31]
	v_mfma_f32_16x16x32_f16 v[8:11], v[76:79], v[84:87], v[8:11]
	v_mfma_f32_16x16x32_f16 v[32:35], v[72:75], v[88:91], v[32:35]
	v_mfma_f32_16x16x32_f16 v[12:15], v[76:79], v[88:91], v[12:15]
	v_mfma_f32_16x16x32_f16 v[20:23], v[72:75], v[92:95], v[20:23]
	v_mfma_f32_16x16x32_f16 v[16:19], v[76:79], v[92:95], v[16:19]
	s_mov_b32 s0, 0x1a000
	v_add_co_u32_e32 v208, vcc, s0, v208
	s_mov_b32 s0, 0x10000
	s_nop 0
	v_addc_co_u32_e32 v209, vcc, 0, v209, vcc
	v_add_co_u32_e32 v48, vcc, s0, v212
	s_mov_b32 s0, 0x12000
	s_nop 0
	v_addc_co_u32_e32 v49, vcc, 0, v213, vcc
	v_add_co_u32_e32 v80, vcc, s0, v212
	s_mov_b32 s0, 0x14000
	s_nop 0
	v_addc_co_u32_e32 v81, vcc, 0, v213, vcc
	v_add_co_u32_e32 v96, vcc, s0, v212
	global_load_dwordx4 v[36:39], v[48:49], off
	global_load_dwordx4 v[40:43], v[48:49], off offset:1024
	global_load_dwordx4 v[44:47], v[48:49], off offset:2048
	s_nop 0
	global_load_dwordx4 v[48:51], v[48:49], off offset:3072
	s_nop 0
	global_load_dwordx4 v[52:55], v[210:211], off
	global_load_dwordx4 v[56:59], v[210:211], off offset:1024
	global_load_dwordx4 v[60:63], v[208:209], off
	global_load_dwordx4 v[64:67], v[208:209], off offset:1024
	v_addc_co_u32_e32 v97, vcc, 0, v213, vcc
	global_load_dwordx4 v[68:71], v[80:81], off
	global_load_dwordx4 v[72:75], v[80:81], off offset:1024
	global_load_dwordx4 v[76:79], v[80:81], off offset:2048
	s_nop 0
	global_load_dwordx4 v[80:83], v[80:81], off offset:3072
	s_nop 0
	global_load_dwordx4 v[84:87], v[96:97], off
	global_load_dwordx4 v[88:91], v[96:97], off offset:1024
	global_load_dwordx4 v[92:95], v[96:97], off offset:2048
	s_nop 0
	global_load_dwordx4 v[96:99], v[96:97], off offset:3072
	s_nop 0
	global_load_dwordx4 v[196:199], v[210:211], off offset:2048
	global_load_dwordx4 v[200:203], v[210:211], off offset:3072
	global_load_dwordx4 v[204:207], v[208:209], off offset:2048
	s_nop 0
	global_load_dwordx4 v[208:211], v[208:209], off offset:3072
	s_mov_b32 s0, 0x16000
	v_add_co_u32_e32 v224, vcc, s0, v212
	s_nop 1
	v_addc_co_u32_e32 v225, vcc, 0, v213, vcc
	global_load_dwordx4 v[212:215], v[224:225], off
	global_load_dwordx4 v[216:219], v[224:225], off offset:1024
	global_load_dwordx4 v[220:223], v[224:225], off offset:2048
	s_nop 0
	global_load_dwordx4 v[224:227], v[224:225], off offset:3072
	s_waitcnt vmcnt(29)
	v_mfma_f32_16x16x32_f16 v[24:27], v[172:175], v[104:107], v[24:27]
	v_mfma_f32_16x16x32_f16 v[4:7], v[100:103], v[104:107], v[4:7]
	v_mfma_f32_16x16x32_f16 v[28:31], v[172:175], v[108:111], v[28:31]
	v_mfma_f32_16x16x32_f16 v[8:11], v[100:103], v[108:111], v[8:11]
	v_mfma_f32_16x16x32_f16 v[32:35], v[172:175], v[112:115], v[32:35]
	v_mfma_f32_16x16x32_f16 v[12:15], v[100:103], v[112:115], v[12:15]
	v_mfma_f32_16x16x32_f16 v[20:23], v[172:175], v[116:119], v[20:23]
	v_mfma_f32_16x16x32_f16 v[16:19], v[100:103], v[116:119], v[16:19]
	v_mfma_f32_16x16x32_f16 v[24:27], v[136:139], v[120:123], v[24:27]
	v_mfma_f32_16x16x32_f16 v[4:7], v[144:147], v[120:123], v[4:7]
	v_mfma_f32_16x16x32_f16 v[28:31], v[136:139], v[124:127], v[28:31]
	v_mfma_f32_16x16x32_f16 v[8:11], v[144:147], v[124:127], v[8:11]
	v_mfma_f32_16x16x32_f16 v[32:35], v[136:139], v[128:131], v[32:35]
	v_mfma_f32_16x16x32_f16 v[12:15], v[144:147], v[128:131], v[12:15]
	v_mfma_f32_16x16x32_f16 v[20:23], v[136:139], v[132:135], v[20:23]
	v_mfma_f32_16x16x32_f16 v[16:19], v[144:147], v[132:135], v[16:19]
	v_mfma_f32_16x16x32_f16 v[24:27], v[140:143], v[152:155], v[24:27]
	v_mfma_f32_16x16x32_f16 v[4:7], v[148:151], v[152:155], v[4:7]
	v_mfma_f32_16x16x32_f16 v[28:31], v[140:143], v[156:159], v[28:31]
	v_mfma_f32_16x16x32_f16 v[8:11], v[148:151], v[156:159], v[8:11]
	v_mfma_f32_16x16x32_f16 v[32:35], v[140:143], v[160:163], v[32:35]
	v_mfma_f32_16x16x32_f16 v[12:15], v[148:151], v[160:163], v[12:15]
	v_mfma_f32_16x16x32_f16 v[20:23], v[140:143], v[164:167], v[20:23]
	v_mfma_f32_16x16x32_f16 v[16:19], v[148:151], v[164:167], v[16:19]
	s_waitcnt vmcnt(27)
	v_mfma_f32_16x16x32_f16 v[24:27], v[168:171], v[180:183], v[24:27]
	v_mfma_f32_16x16x32_f16 v[4:7], v[176:179], v[180:183], v[4:7]
	s_waitcnt vmcnt(26)
	v_mfma_f32_16x16x32_f16 v[28:31], v[168:171], v[184:187], v[28:31]
	v_mfma_f32_16x16x32_f16 v[8:11], v[176:179], v[184:187], v[8:11]
	s_waitcnt vmcnt(25)
	v_mfma_f32_16x16x32_f16 v[32:35], v[168:171], v[188:191], v[32:35]
	v_mfma_f32_16x16x32_f16 v[12:15], v[176:179], v[188:191], v[12:15]
	s_waitcnt vmcnt(24)
	v_mfma_f32_16x16x32_f16 v[20:23], v[168:171], v[192:195], v[20:23]
	v_mfma_f32_16x16x32_f16 v[16:19], v[176:179], v[192:195], v[16:19]
	s_waitcnt vmcnt(19)
	v_mfma_f32_16x16x32_f16 v[24:27], v[52:55], v[36:39], v[24:27]
	s_waitcnt vmcnt(17)
	v_mfma_f32_16x16x32_f16 v[4:7], v[60:63], v[36:39], v[4:7]
	v_mfma_f32_16x16x32_f16 v[28:31], v[52:55], v[40:43], v[28:31]
	v_mfma_f32_16x16x32_f16 v[8:11], v[60:63], v[40:43], v[8:11]
	v_mfma_f32_16x16x32_f16 v[32:35], v[52:55], v[44:47], v[32:35]
	v_mfma_f32_16x16x32_f16 v[12:15], v[60:63], v[44:47], v[12:15]
	v_mfma_f32_16x16x32_f16 v[20:23], v[52:55], v[48:51], v[20:23]
	v_mfma_f32_16x16x32_f16 v[16:19], v[60:63], v[48:51], v[16:19]
	s_waitcnt vmcnt(15)
	v_mfma_f32_16x16x32_f16 v[24:27], v[56:59], v[68:71], v[24:27]
	v_mfma_f32_16x16x32_f16 v[4:7], v[64:67], v[68:71], v[4:7]
	s_waitcnt vmcnt(14)
	v_mfma_f32_16x16x32_f16 v[28:31], v[56:59], v[72:75], v[28:31]
	v_mfma_f32_16x16x32_f16 v[8:11], v[64:67], v[72:75], v[8:11]
	s_waitcnt vmcnt(13)
	v_mfma_f32_16x16x32_f16 v[32:35], v[56:59], v[76:79], v[32:35]
	v_mfma_f32_16x16x32_f16 v[12:15], v[64:67], v[76:79], v[12:15]
	s_waitcnt vmcnt(12)
	v_mfma_f32_16x16x32_f16 v[20:23], v[56:59], v[80:83], v[20:23]
	v_mfma_f32_16x16x32_f16 v[16:19], v[64:67], v[80:83], v[16:19]
	s_waitcnt vmcnt(7)
	v_mfma_f32_16x16x32_f16 v[24:27], v[196:199], v[84:87], v[24:27]
	s_waitcnt vmcnt(5)
	v_mfma_f32_16x16x32_f16 v[4:7], v[204:207], v[84:87], v[4:7]
	v_mfma_f32_16x16x32_f16 v[28:31], v[196:199], v[88:91], v[28:31]
	v_mfma_f32_16x16x32_f16 v[8:11], v[204:207], v[88:91], v[8:11]
	v_mfma_f32_16x16x32_f16 v[32:35], v[196:199], v[92:95], v[32:35]
	v_mfma_f32_16x16x32_f16 v[12:15], v[204:207], v[92:95], v[12:15]
	v_mfma_f32_16x16x32_f16 v[20:23], v[196:199], v[96:99], v[20:23]
	v_mfma_f32_16x16x32_f16 v[16:19], v[204:207], v[96:99], v[16:19]
	s_waitcnt vmcnt(3)
	v_mfma_f32_16x16x32_f16 v[24:27], v[200:203], v[212:215], v[24:27]
	v_mfma_f32_16x16x32_f16 v[4:7], v[208:211], v[212:215], v[4:7]
	s_waitcnt vmcnt(2)
	v_mfma_f32_16x16x32_f16 v[28:31], v[200:203], v[216:219], v[28:31]
	v_mfma_f32_16x16x32_f16 v[8:11], v[208:211], v[216:219], v[8:11]
	s_waitcnt vmcnt(1)
	v_mfma_f32_16x16x32_f16 v[32:35], v[200:203], v[220:223], v[32:35]
	v_mfma_f32_16x16x32_f16 v[12:15], v[208:211], v[220:223], v[12:15]
	s_waitcnt vmcnt(0)
	v_mfma_f32_16x16x32_f16 v[20:23], v[200:203], v[224:227], v[20:23]
	v_mfma_f32_16x16x32_f16 v[16:19], v[208:211], v[224:227], v[16:19]
	global_load_dwordx4 v[36:39], v[228:229], off
	v_add_u32_e32 v2, 0, v2
	v_and_b32_e32 v41, 0x1c0, v0
	v_lshl_add_u32 v43, v230, 13, v2
	v_lshl_add_u32 v2, v41, 4, v2
	v_lshl_add_u32 v40, v0, 4, 0
	ds_write_b128 v43, v[24:27]
	ds_write_b128 v43, v[4:7] offset:1024
	ds_write_b128 v43, v[28:31] offset:2048
	ds_write_b128 v43, v[8:11] offset:3072
	ds_write_b128 v43, v[32:35] offset:4096
	ds_write_b128 v43, v[12:15] offset:5120
	ds_write_b128 v43, v[20:23] offset:6144
	ds_write_b128 v43, v[16:19] offset:7168
	s_waitcnt lgkmcnt(0)
	s_barrier
	ds_read_b128 v[4:7], v2 offset:8192
	ds_read_b128 v[8:11], v2 offset:16384
	ds_read_b128 v[12:15], v2 offset:24576
	ds_read_b128 v[16:19], v40
	ds_read_b128 v[20:23], v2 offset:32768
	ds_read_b128 v[24:27], v2 offset:40960
	ds_read_b128 v[28:31], v2 offset:49152
	ds_read_b128 v[32:35], v2 offset:57344
	s_waitcnt lgkmcnt(4)
	v_pk_add_f32 v[4:5], v[16:17], v[4:5]
	v_pk_add_f32 v[6:7], v[18:19], v[6:7]
	v_pk_add_f32 v[4:5], v[4:5], v[8:9]
	v_pk_add_f32 v[6:7], v[6:7], v[10:11]
	v_pk_add_f32 v[4:5], v[4:5], v[12:13]
	v_pk_add_f32 v[6:7], v[6:7], v[14:15]
	s_waitcnt lgkmcnt(3)
	v_pk_add_f32 v[4:5], v[4:5], v[20:21]
	v_pk_add_f32 v[6:7], v[6:7], v[22:23]
	s_waitcnt lgkmcnt(2)
	v_pk_add_f32 v[4:5], v[4:5], v[24:25]
	v_pk_add_f32 v[6:7], v[6:7], v[26:27]
	s_waitcnt lgkmcnt(1)
	v_pk_add_f32 v[4:5], v[4:5], v[28:29]
	v_pk_add_f32 v[6:7], v[6:7], v[30:31]
	s_waitcnt lgkmcnt(0)
	v_pk_add_f32 v[4:5], v[4:5], v[32:33]
	v_pk_add_f32 v[6:7], v[6:7], v[34:35]
	v_lshrrev_b32_e32 v42, 7, v0
	s_waitcnt vmcnt(0)
	v_pk_add_f32 v[4:5], v[36:37], v[4:5]
	v_pk_add_f32 v[6:7], v[38:39], v[6:7]
	v_mul_f32_e32 v2, 0x3d372713, v4
	v_mul_f32_e32 v8, 0x3d372713, v5
	v_mul_f32_e32 v9, 0x3d372713, v6
	v_mul_f32_e32 v2, v4, v2
	v_mul_f32_e32 v8, v5, v8
	v_mul_f32_e32 v9, v6, v9
	v_fma_f32 v2, v4, v2, v4
	v_fma_f32 v8, v5, v8, v5
	v_fma_f32 v9, v6, v9, v6
	v_mul_f32_e32 v2, 0x3f4c422a, v2
	v_mul_f32_e32 v8, 0x3f4c422a, v8
	v_mul_f32_e32 v9, 0x3f4c422a, v9
	v_add_f32_e32 v2, v2, v2
	v_add_f32_e32 v8, v8, v8
	v_add_f32_e32 v9, v9, v9
	v_mul_f32_e32 v2, 0x3fb8aa3b, v2
	v_mul_f32_e32 v11, 0x3fb8aa3b, v8
	v_mul_f32_e32 v10, 0x3d372713, v7
	v_mul_f32_e32 v12, 0x3fb8aa3b, v9
	v_exp_f32_e32 v8, v2
	v_exp_f32_e32 v9, v11
	v_mul_f32_e32 v10, v7, v10
	v_fma_f32 v10, v7, v10, v7
	v_mul_f32_e32 v10, 0x3f4c422a, v10
	v_add_f32_e32 v10, v10, v10
	v_pk_add_f32 v[8:9], v[8:9], 1.0 op_sel_hi:[1,0]
	v_mul_f32_e32 v13, 0x3fb8aa3b, v10
	v_div_scale_f32 v2, s[0:1], v9, v9, 2.0
	v_exp_f32_e32 v10, v12
	v_exp_f32_e32 v11, v13
	v_div_scale_f32 v14, s[0:1], v8, v8, 2.0
	v_rcp_f32_e32 v16, v2
	v_rcp_f32_e32 v17, v14
	v_pk_add_f32 v[10:11], v[10:11], 1.0 op_sel_hi:[1,0]
	v_div_scale_f32 v13, vcc, 2.0, v9, 2.0
	v_fma_f32 v20, -v2, v16, 1.0
	v_div_scale_f32 v15, s[0:1], v11, v11, 2.0
	v_fma_f32 v21, -v14, v17, 1.0
	v_fmac_f32_e32 v16, v20, v16
	v_div_scale_f32 v19, s[0:1], 2.0, v8, 2.0
	v_fmac_f32_e32 v17, v21, v17
	v_mul_f32_e32 v20, v13, v16
	v_mul_f32_e32 v21, v19, v17
	v_fma_f32 v23, -v2, v20, v13
	v_fma_f32 v24, -v14, v21, v19
	v_fmac_f32_e32 v20, v23, v16
	v_fmac_f32_e32 v21, v24, v17
	v_fma_f32 v2, -v2, v20, v13
	v_rcp_f32_e32 v18, v15
	v_fma_f32 v13, -v14, v21, v19
	v_div_fmas_f32 v2, v2, v16, v20
	s_mov_b64 vcc, s[0:1]
	v_div_fixup_f32 v9, v2, v9, 2.0
	v_div_fmas_f32 v2, v13, v17, v21
	v_div_fixup_f32 v8, v2, v8, 2.0
	v_pk_add_f32 v[8:9], v[8:9], 1.0 op_sel_hi:[1,0] neg_lo:[1,0] neg_hi:[1,0]
	v_pk_mul_f32 v[4:5], v[4:5], 0.5 op_sel_hi:[1,0]
	v_fma_f32 v22, -v15, v18, 1.0
	v_pk_add_f32 v[8:9], v[8:9], 1.0 op_sel_hi:[1,0]
	v_fmac_f32_e32 v18, v22, v18
	v_pk_mul_f32 v[4:5], v[4:5], v[8:9]
	v_div_scale_f32 v2, vcc, 2.0, v11, 2.0
	v_cvt_pk_f16_f32 v4, v4, v5
	v_mul_f32_e32 v5, v2, v18
	v_fma_f32 v8, -v15, v5, v2
	v_fmac_f32_e32 v5, v8, v18
	v_div_scale_f32 v8, s[0:1], v10, v10, 2.0
	v_rcp_f32_e32 v13, v8
	v_fma_f32 v2, -v15, v5, v2
	v_div_fmas_f32 v2, v2, v18, v5
	v_div_fixup_f32 v9, v2, v11, 2.0
	v_fma_f32 v2, -v8, v13, 1.0
	v_fmac_f32_e32 v13, v2, v13
	v_div_scale_f32 v2, vcc, 2.0, v10, 2.0
	v_mul_f32_e32 v5, v2, v13
	v_fma_f32 v11, -v8, v5, v2
	v_fmac_f32_e32 v5, v11, v13
	v_fma_f32 v2, -v8, v5, v2
	v_div_fmas_f32 v2, v2, v13, v5
	v_div_fixup_f32 v8, v2, v10, 2.0
	v_pk_add_f32 v[8:9], v[8:9], 1.0 op_sel_hi:[1,0] neg_lo:[1,0] neg_hi:[1,0]
	s_lshl_b32 s0, s2, 3
	v_pk_mul_f32 v[6:7], v[6:7], 0.5 op_sel_hi:[1,0]
	v_pk_add_f32 v[8:9], v[8:9], 1.0 op_sel_hi:[1,0]
	s_add_i32 s0, s0, s12
	v_pk_mul_f32 v[6:7], v[6:7], v[8:9]
	v_or_b32_e32 v2, s0, v42
	v_cvt_pk_f16_f32 v5, v6, v7
	v_lshlrev_b64 v[6:7], 6, v[2:3]
	v_lshrrev_b32_e32 v2, 1, v0
	v_and_b32_e32 v12, 15, v0
	v_and_b32_e32 v0, 16, v2
	v_lshl_or_b32 v0, v1, 5, v0
	v_or3_b32 v6, v6, v0, v12
	v_lshl_add_u64 v[0:1], v[6:7], 4, s[10:11]
	v_and_b32_e32 v2, 8, v2
	v_lshl_add_u64 v[0:1], v[0:1], 0, v[2:3]
	global_store_dwordx2 v[0:1], v[4:5], off
	s_endpgm
	s_nop 0
	s_nop 0
	s_nop 0
	s_nop 0
	s_nop 0
	s_nop 0
	s_nop 0
	s_nop 0
	s_nop 0
	s_nop 0
	s_nop 0
	s_nop 0
	s_nop 0
	s_nop 0
	s_nop 0
	s_nop 0
	s_nop 0
	s_nop 0
	s_nop 0
	s_nop 0
	s_nop 0
	s_nop 0
	s_nop 0
	s_nop 0
	s_nop 0
	s_nop 0
	s_nop 0
	s_nop 0
	s_nop 0
	s_nop 0
	s_nop 0
	s_endpgm

	.amdhsa_kernel _ZN12_GLOBAL__N_110gemm_fullkILi0ELi7EEEvPKDF16_S2_PKfPDF16_PfS6_S4_S4_S4_S4_S4_S5_
		.amdhsa_group_segment_fixed_size 0
		.amdhsa_private_segment_fixed_size 0
		.amdhsa_kernarg_size 96
		.amdhsa_user_sgpr_count 2
		.amdhsa_user_sgpr_dispatch_ptr 0
		.amdhsa_user_sgpr_queue_ptr 0
		.amdhsa_user_sgpr_kernarg_segment_ptr 1
		.amdhsa_user_sgpr_dispatch_id 0
		.amdhsa_user_sgpr_kernarg_preload_length 0
		.amdhsa_user_sgpr_kernarg_preload_offset 0
		.amdhsa_user_sgpr_private_segment_size 0
		.amdhsa_uses_dynamic_stack 0
		.amdhsa_enable_private_segment 0
		.amdhsa_system_sgpr_workgroup_id_x 1
		.amdhsa_system_sgpr_workgroup_id_y 0
		.amdhsa_system_sgpr_workgroup_id_z 0
		.amdhsa_system_sgpr_workgroup_info 0
		.amdhsa_system_vgpr_workitem_id 0
		.amdhsa_next_free_vgpr 231
		.amdhsa_next_free_sgpr 14
		.amdhsa_accum_offset 232
		.amdhsa_reserve_vcc 1
		.amdhsa_float_round_mode_32 0
		.amdhsa_float_round_mode_16_64 0
		.amdhsa_float_denorm_mode_32 3
		.amdhsa_float_denorm_mode_16_64 3
		.amdhsa_dx10_clamp 1
		.amdhsa_ieee_mode 1
		.amdhsa_fp16_overflow 0
		.amdhsa_tg_split 0
		.amdhsa_exception_fp_ieee_invalid_op 0
		.amdhsa_exception_fp_denorm_src 0
		.amdhsa_exception_fp_ieee_div_zero 0
		.amdhsa_exception_fp_ieee_overflow 0
		.amdhsa_exception_fp_ieee_underflow 0
		.amdhsa_exception_fp_ieee_inexact 0
		.amdhsa_exception_int_div_zero 0
	.end_amdhsa_kernel

_ZN12_GLOBAL__N_110gemm_fullkILi1ELi7EEEvPKDF16_S2_PKfPDF16_PfS6_S4_S4_S4_S4_S4_S5_:
	s_load_dwordx2 s[4:5], s[0:1], 0x38
	s_and_b32 s3, s2, 63
	s_lshl_b32 s16, s3, 5
	s_lshl_b32 s6, s3, 13
	v_lshlrev_b32_e32 v1, 4, v0
	s_waitcnt lgkmcnt(0)
	s_add_u32 s4, s4, s6
	s_addc_u32 s5, s5, 0
	global_load_dwordx4 v[2:5], v1, s[4:5]
	v_lshlrev_b32_e32 v1, 2, v0
	v_cmp_lt_u32_e32 vcc, 31, v0
	s_and_saveexec_b64 s[4:5], vcc
	s_xor_b64 s[4:5], exec, s[4:5]
	s_cbranch_execz .LBB23_10
	v_cmp_lt_u32_e32 vcc, 63, v0
	s_and_saveexec_b64 s[6:7], vcc
	s_xor_b64 s[6:7], exec, s[6:7]
	s_cbranch_execz .LBB23_7
	s_movk_i32 s8, 0x47
	v_cmp_lt_u32_e32 vcc, s8, v0
	s_and_saveexec_b64 s[8:9], vcc
	s_xor_b64 s[8:9], exec, s[8:9]
	s_cbranch_execz .LBB23_4
	s_load_dwordx2 s[10:11], s[0:1], 0x10
	s_lshl_b32 s12, s16, 2
	v_lshlrev_b32_e32 v6, 2, v1
	v_mov_b32_e32 v7, 0
	s_movk_i32 s14, 0x50
	s_waitcnt lgkmcnt(0)
	s_add_u32 s10, s10, s12
	s_addc_u32 s11, s11, 0
	s_movk_i32 s12, 0xfb80
	v_lshl_add_u64 v[6:7], s[10:11], 0, v[6:7]
	s_mov_b32 s13, -1
	v_lshl_add_u64 v[6:7], v[6:7], 0, s[12:13]
	v_mov_b32_e32 v8, s11
	v_cmp_gt_u32_e32 vcc, s14, v0
	s_nop 1
	v_cndmask_b32_e32 v29, v8, v7, vcc
	v_mov_b32_e32 v7, s10
	v_cndmask_b32_e32 v28, v7, v6, vcc
.LBB23_4:
	s_andn2_saveexec_b64 s[8:9], s[8:9]
	s_cbranch_execz .LBB23_6
	s_load_dwordx2 s[10:11], s[0:1], 0x50
	s_lshl_b32 s12, s16, 2
	v_lshlrev_b32_e32 v6, 2, v1
	v_mov_b32_e32 v7, 0
	s_waitcnt lgkmcnt(0)
	s_add_u32 s10, s10, s12
	s_addc_u32 s11, s11, 0
	v_lshl_add_u64 v[6:7], s[10:11], 0, v[6:7]
	s_movk_i32 s10, 0xfc00
	s_mov_b32 s11, -1
	v_lshl_add_u64 v[28:29], v[6:7], 0, s[10:11]

.LBB23_7:
	s_andn2_saveexec_b64 s[6:7], s[6:7]
	s_cbranch_execz .LBB23_9
	s_load_dwordx2 s[8:9], s[0:1], 0x48
	s_lshl_b32 s10, s3, 9
	v_lshlrev_b32_e32 v6, 2, v1
	v_mov_b32_e32 v7, 0
	s_waitcnt lgkmcnt(0)
	s_add_u32 s8, s8, s10
	s_addc_u32 s9, s9, 0
	v_lshl_add_u64 v[6:7], s[8:9], 0, v[6:7]
	s_movk_i32 s8, 0xfe00
	s_mov_b32 s9, -1
	v_lshl_add_u64 v[28:29], v[6:7], 0, s[8:9]

.LBB23_10:
	s_or_saveexec_b64 s[14:15], s[4:5]
	s_load_dwordx2 s[12:13], s[0:1], 0x58
	s_load_dwordx4 s[8:11], s[0:1], 0x0
	s_load_dwordx4 s[4:7], s[0:1], 0x20
	s_xor_b64 exec, exec, s[14:15]
	s_cbranch_execz .LBB23_12
	s_load_dwordx2 s[0:1], s[0:1], 0x40
	s_lshl_b32 s17, s3, 9
	v_lshlrev_b32_e32 v6, 2, v1
	v_mov_b32_e32 v7, 0
	s_waitcnt lgkmcnt(0)
	s_add_u32 s0, s0, s17
	s_addc_u32 s1, s1, 0
	v_lshl_add_u64 v[28:29], s[0:1], 0, v[6:7]
.LBB23_12:
	s_or_b64 exec, exec, s[14:15]
	v_lshrrev_b32_e32 v186, 6, v0
	s_lshr_b32 s0, s2, 5
	s_and_b32 s0, s0, 0x7fffffe
	s_mov_b32 s1, 0
	v_lshlrev_b32_e32 v8, 17, v186
	v_mov_b32_e32 v9, 0
	v_and_b32_e32 v12, 63, v0
	s_lshl_b64 s[14:15], s[0:1], 10
	v_lshlrev_b32_e32 v6, 14, v186
	s_waitcnt lgkmcnt(0)
	v_lshl_add_u64 v[10:11], s[8:9], 0, v[8:9]
	v_lshl_or_b32 v6, s3, 18, v6
	v_mov_b32_e32 v7, v9
	v_lshl_add_u64 v[10:11], v[10:11], 0, s[14:15]
	v_lshlrev_b32_e32 v8, 4, v12
	v_lshl_add_u64 v[6:7], s[10:11], 0, v[6:7]
	v_lshl_add_u64 v[30:31], v[10:11], 0, v[8:9]
	v_lshrrev_b32_e32 v10, 2, v0
	v_lshl_add_u64 v[32:33], v[6:7], 0, v[8:9]
	v_lshrrev_b32_e32 v6, 8, v0
	v_lshrrev_b32_e32 v7, 3, v0
	v_and_b32_e32 v10, 12, v10
	v_and_b32_e32 v34, 15, v0
	v_bfe_u32 v38, v0, 6, 1
	v_or_b32_e32 v36, s0, v6
	v_and_or_b32 v37, v7, 16, v10
	v_lshl_or_b32 v6, v36, 4, v34
	v_lshl_or_b32 v35, v38, 1, v37
	v_mov_b32_e32 v7, v9
	v_or_b32_e32 v12, s16, v35
	v_lshlrev_b64 v[6:7], 13, v[6:7]
	v_lshl_add_u64 v[10:11], s[4:5], 0, v[6:7]
	v_lshlrev_b32_e32 v12, 2, v12
	v_mov_b32_e32 v13, v9
	v_lshl_add_u64 v[10:11], v[10:11], 0, v[12:13]
	s_mov_b32 s2, 0x700000
	v_add_co_u32_e32 v14, vcc, s2, v10
	v_lshl_add_u64 v[6:7], s[6:7], 0, v[6:7]
	s_nop 0
	v_addc_co_u32_e32 v15, vcc, 0, v11, vcc
	v_lshl_add_u64 v[26:27], v[6:7], 0, v[12:13]
	s_mov_b32 s0, 0x100000
	v_add_co_u32_e32 v16, vcc, s0, v26
	s_mov_b32 s0, 0x200000
	s_nop 0
	v_addc_co_u32_e32 v17, vcc, 0, v27, vcc
	v_add_co_u32_e32 v18, vcc, s0, v26
	s_mov_b32 s0, 0x300000
	s_nop 0
	v_addc_co_u32_e32 v19, vcc, 0, v27, vcc
	v_add_co_u32_e32 v20, vcc, s0, v26
	s_mov_b32 s0, 0x400000
	s_nop 0
	v_addc_co_u32_e32 v21, vcc, 0, v27, vcc
	v_add_co_u32_e32 v40, vcc, s0, v26
	s_mov_b32 s0, 0x500000
	s_nop 0
	v_addc_co_u32_e32 v41, vcc, 0, v27, vcc
	v_add_co_u32_e32 v42, vcc, s0, v26
	s_mov_b32 s0, 0x600000
	s_nop 0
	v_addc_co_u32_e32 v43, vcc, 0, v27, vcc
	v_add_co_u32_e32 v44, vcc, s0, v26
	s_mov_b32 s0, 0x20000
	s_nop 0
	v_addc_co_u32_e32 v45, vcc, 0, v27, vcc
	v_add_co_u32_e32 v92, vcc, s0, v32
	s_mov_b32 s0, 0x21000
	s_nop 0
	v_addc_co_u32_e32 v93, vcc, 0, v33, vcc
	v_add_co_u32_e32 v156, vcc, s0, v32
	s_movk_i32 s0, 0x2000
	s_nop 0
	v_addc_co_u32_e32 v157, vcc, 0, v33, vcc
	v_add_co_u32_e32 v72, vcc, s0, v30
	s_movk_i32 s1, 0x4000
	s_nop 0
	v_addc_co_u32_e32 v73, vcc, 0, v31, vcc
	v_add_co_u32_e32 v94, vcc, s1, v30
	s_movk_i32 s1, 0x6000
	s_nop 0
	v_addc_co_u32_e32 v95, vcc, 0, v31, vcc
	v_add_co_u32_e32 v100, vcc, s1, v30
	s_movk_i32 s1, 0x1000
	s_nop 0
	v_addc_co_u32_e32 v101, vcc, 0, v31, vcc
	v_add_co_u32_e32 v148, vcc, s1, v32
	global_load_dwordx2 v[24:25], v[14:15], off
	s_nop 0
	v_addc_co_u32_e32 v149, vcc, 0, v33, vcc
	v_add_co_u32_e32 v172, vcc, s0, v32
	s_mov_b32 s0, 0x8000
	s_nop 0
	v_addc_co_u32_e32 v173, vcc, 0, v33, vcc
	v_add_co_u32_e32 v116, vcc, s0, v30
	s_mov_b32 s0, 0xa000
	s_nop 0
	v_addc_co_u32_e32 v117, vcc, 0, v31, vcc
	v_add_co_u32_e32 v120, vcc, s0, v30
	s_mov_b32 s0, 0xc000
	s_nop 0
	v_addc_co_u32_e32 v121, vcc, 0, v31, vcc
	v_add_co_u32_e32 v144, vcc, s0, v30
	global_load_dwordx2 v[22:23], v[26:27], off
	global_load_dwordx2 v[6:7], v[16:17], off
	global_load_dwordx2 v[12:13], v[18:19], off
	global_load_dwordx2 v[14:15], v[20:21], off
	s_nop 0
	global_load_dwordx2 v[18:19], v[40:41], off
	global_load_dwordx2 v[16:17], v[42:43], off
	global_load_dwordx2 v[20:21], v[44:45], off
	s_nop 0
	global_load_dwordx4 v[40:43], v[30:31], off
	global_load_dwordx4 v[44:47], v[30:31], off offset:1024
	global_load_dwordx4 v[48:51], v[32:33], off
	global_load_dwordx4 v[52:55], v[32:33], off offset:1024
	global_load_dwordx4 v[56:59], v[72:73], off
	global_load_dwordx4 v[60:63], v[72:73], off offset:1024
	global_load_dwordx4 v[64:67], v[92:93], off offset:1024
	global_load_dwordx4 v[68:71], v[92:93], off offset:2048
	s_nop 0
	global_load_dwordx4 v[72:75], v[94:95], off
	global_load_dwordx4 v[76:79], v[94:95], off offset:1024
	global_load_dwordx4 v[80:83], v[32:33], off offset:2048
	global_load_dwordx4 v[84:87], v[32:33], off offset:3072
	global_load_dwordx4 v[88:91], v[92:93], off offset:3072
	s_nop 0
	global_load_dwordx4 v[92:95], v[100:101], off
	global_load_dwordx4 v[96:99], v[100:101], off offset:1024
	s_nop 0
	global_load_dwordx4 v[100:103], v[156:157], off offset:-4096
	global_load_dwordx4 v[104:107], v[156:157], off
	global_load_dwordx4 v[108:111], v[116:117], off
	global_load_dwordx4 v[112:115], v[116:117], off offset:1024
	s_nop 0
	global_load_dwordx4 v[116:119], v[120:121], off
	s_nop 0
	global_load_dwordx4 v[120:123], v[120:121], off offset:1024
	s_nop 0
	global_load_dwordx4 v[124:127], v[148:149], off offset:1024
	global_load_dwordx4 v[128:131], v[148:149], off offset:2048
	global_load_dwordx4 v[132:135], v[156:157], off offset:1024
	global_load_dwordx4 v[136:139], v[156:157], off offset:2048
	v_addc_co_u32_e32 v145, vcc, 0, v31, vcc
	global_load_dwordx4 v[140:143], v[144:145], off
	s_nop 0
	global_load_dwordx4 v[144:147], v[144:145], off offset:1024
	s_nop 0
	global_load_dwordx4 v[148:151], v[148:149], off offset:3072
	s_nop 0
	global_load_dwordx4 v[152:155], v[172:173], off offset:-4096
	s_nop 0
	global_load_dwordx4 v[156:159], v[156:157], off offset:3072
	s_mov_b32 s0, 0xe000
	v_add_co_u32_e32 v164, vcc, s0, v30
	v_lshrrev_b32_e32 v39, 7, v0
	s_nop 0
	v_addc_co_u32_e32 v165, vcc, 0, v31, vcc
	global_load_dwordx4 v[160:163], v[164:165], off
	s_nop 0
	global_load_dwordx4 v[164:167], v[164:165], off offset:1024
	s_waitcnt vmcnt(29)
	v_mfma_f32_16x16x32_f16 v[168:171], v[48:51], v[40:43], 0
	s_waitcnt vmcnt(16)
	v_mfma_f32_16x16x32_f16 v[40:43], v[100:103], v[40:43], 0
	v_mfma_f32_16x16x32_f16 v[48:51], v[48:51], v[44:47], 0
	v_mfma_f32_16x16x32_f16 v[44:47], v[100:103], v[44:47], 0
	v_mfma_f32_16x16x32_f16 v[100:103], v[52:55], v[56:59], v[168:171]
	v_mfma_f32_16x16x32_f16 v[40:43], v[64:67], v[56:59], v[40:43]
	v_mfma_f32_16x16x32_f16 v[48:51], v[52:55], v[60:63], v[48:51]
	v_mfma_f32_16x16x32_f16 v[44:47], v[64:67], v[60:63], v[44:47]
	v_mfma_f32_16x16x32_f16 v[52:55], v[80:83], v[72:75], v[100:103]
	v_mfma_f32_16x16x32_f16 v[40:43], v[68:71], v[72:75], v[40:43]
	v_mfma_f32_16x16x32_f16 v[48:51], v[80:83], v[76:79], v[48:51]
	v_mfma_f32_16x16x32_f16 v[44:47], v[68:71], v[76:79], v[44:47]
	v_mfma_f32_16x16x32_f16 v[52:55], v[84:87], v[92:95], v[52:55]
	v_mfma_f32_16x16x32_f16 v[40:43], v[88:91], v[92:95], v[40:43]
	v_mfma_f32_16x16x32_f16 v[48:51], v[84:87], v[96:99], v[48:51]
	v_mfma_f32_16x16x32_f16 v[44:47], v[88:91], v[96:99], v[44:47]
	s_mov_b32 s0, 0x22000
	v_add_co_u32_e32 v174, vcc, s0, v32
	s_mov_b32 s0, 0x23000
	s_nop 0
	v_addc_co_u32_e32 v175, vcc, 0, v33, vcc
	v_add_co_u32_e32 v184, vcc, s0, v32
	s_mov_b32 s0, 0x10000
	s_nop 0
	v_addc_co_u32_e32 v185, vcc, 0, v33, vcc
	v_add_co_u32_e32 v64, vcc, s0, v30
	s_mov_b32 s0, 0x12000
	s_nop 0
	v_addc_co_u32_e32 v65, vcc, 0, v31, vcc
	v_add_co_u32_e32 v80, vcc, s0, v30
	s_mov_b32 s0, 0x14000
	s_nop 0
	v_addc_co_u32_e32 v81, vcc, 0, v31, vcc
	v_add_co_u32_e32 v96, vcc, s0, v30
	global_load_dwordx4 v[56:59], v[184:185], off offset:-4096
	s_nop 0
	v_addc_co_u32_e32 v97, vcc, 0, v31, vcc
	global_load_dwordx4 v[60:63], v[64:65], off
	s_nop 0
	global_load_dwordx4 v[64:67], v[64:65], off offset:1024
	s_nop 0
	global_load_dwordx4 v[68:71], v[172:173], off
	global_load_dwordx4 v[72:75], v[172:173], off offset:1024
	global_load_dwordx4 v[76:79], v[80:81], off
	s_nop 0
	global_load_dwordx4 v[80:83], v[80:81], off offset:1024
	s_nop 0
	global_load_dwordx4 v[84:87], v[174:175], off offset:1024
	global_load_dwordx4 v[88:91], v[174:175], off offset:2048
	global_load_dwordx4 v[92:95], v[96:97], off
	s_nop 0
	global_load_dwordx4 v[96:99], v[96:97], off offset:1024
	s_nop 0
	global_load_dwordx4 v[100:103], v[172:173], off offset:2048
	global_load_dwordx4 v[168:171], v[172:173], off offset:3072
	s_nop 0
	global_load_dwordx4 v[172:175], v[174:175], off offset:3072
	s_mov_b32 s0, 0x16000
	v_add_co_u32_e32 v180, vcc, s0, v30
	s_nop 1
	v_addc_co_u32_e32 v181, vcc, 0, v31, vcc
	global_load_dwordx4 v[176:179], v[180:181], off
	s_nop 0
	global_load_dwordx4 v[180:183], v[180:181], off offset:1024
	s_waitcnt vmcnt(19)
	v_mfma_f32_16x16x32_f16 v[52:55], v[152:155], v[108:111], v[52:55]
	v_mfma_f32_16x16x32_f16 v[40:43], v[104:107], v[108:111], v[40:43]
	v_mfma_f32_16x16x32_f16 v[48:51], v[152:155], v[112:115], v[48:51]
	v_mfma_f32_16x16x32_f16 v[44:47], v[104:107], v[112:115], v[44:47]
	v_mfma_f32_16x16x32_f16 v[52:55], v[124:127], v[116:119], v[52:55]
	v_mfma_f32_16x16x32_f16 v[40:43], v[132:135], v[116:119], v[40:43]
	v_mfma_f32_16x16x32_f16 v[48:51], v[124:127], v[120:123], v[48:51]
	v_mfma_f32_16x16x32_f16 v[44:47], v[132:135], v[120:123], v[44:47]
	v_mfma_f32_16x16x32_f16 v[52:55], v[128:131], v[140:143], v[52:55]
	v_mfma_f32_16x16x32_f16 v[40:43], v[136:139], v[140:143], v[40:43]
	v_mfma_f32_16x16x32_f16 v[48:51], v[128:131], v[144:147], v[48:51]
	v_mfma_f32_16x16x32_f16 v[44:47], v[136:139], v[144:147], v[44:47]
	s_waitcnt vmcnt(17)
	v_mfma_f32_16x16x32_f16 v[52:55], v[148:151], v[160:163], v[52:55]
	v_mfma_f32_16x16x32_f16 v[40:43], v[156:159], v[160:163], v[40:43]
	s_waitcnt vmcnt(16)
	v_mfma_f32_16x16x32_f16 v[48:51], v[148:151], v[164:167], v[48:51]
	v_mfma_f32_16x16x32_f16 v[44:47], v[156:159], v[164:167], v[44:47]
	s_movk_i32 s0, 0x3000
	v_add_co_u32_e32 v32, vcc, s0, v32
	s_mov_b32 s0, 0x18000
	s_nop 0
	v_addc_co_u32_e32 v33, vcc, 0, v33, vcc
	v_add_co_u32_e32 v108, vcc, s0, v30
	s_mov_b32 s0, 0x1a000
	s_nop 0
	v_addc_co_u32_e32 v109, vcc, 0, v31, vcc
	v_add_co_u32_e32 v132, vcc, s0, v30
	s_mov_b32 s0, 0x1c000
	s_nop 0
	v_addc_co_u32_e32 v133, vcc, 0, v31, vcc
	v_add_co_u32_e32 v140, vcc, s0, v30
	global_load_dwordx4 v[104:107], v[108:109], off
	s_nop 0
	global_load_dwordx4 v[108:111], v[108:109], off offset:1024
	s_nop 0
	global_load_dwordx4 v[112:115], v[32:33], off
	global_load_dwordx4 v[116:119], v[32:33], off offset:1024
	global_load_dwordx4 v[120:123], v[184:185], off
	global_load_dwordx4 v[124:127], v[184:185], off offset:1024
	v_addc_co_u32_e32 v141, vcc, 0, v31, vcc
	global_load_dwordx4 v[128:131], v[132:133], off
	s_nop 0
	global_load_dwordx4 v[132:135], v[132:133], off offset:1024
	s_nop 0
	global_load_dwordx4 v[136:139], v[140:141], off
	s_nop 0
	global_load_dwordx4 v[140:143], v[140:141], off offset:1024
	s_nop 0
	global_load_dwordx4 v[144:147], v[32:33], off offset:2048
	global_load_dwordx4 v[148:151], v[32:33], off offset:3072
	global_load_dwordx4 v[152:155], v[184:185], off offset:2048
	global_load_dwordx4 v[156:159], v[184:185], off offset:3072
	s_mov_b32 s0, 0x1e000
	v_add_co_u32_e32 v160, vcc, s0, v30
	s_nop 1
	v_addc_co_u32_e32 v161, vcc, 0, v31, vcc
	global_load_dwordx4 v[30:33], v[160:161], off
	s_nop 0
	global_load_dwordx4 v[160:163], v[160:161], off offset:1024
	s_waitcnt vmcnt(28)
	v_mfma_f32_16x16x32_f16 v[52:55], v[68:71], v[60:63], v[52:55]
	v_mfma_f32_16x16x32_f16 v[40:43], v[56:59], v[60:63], v[40:43]
	v_mfma_f32_16x16x32_f16 v[48:51], v[68:71], v[64:67], v[48:51]
	v_mfma_f32_16x16x32_f16 v[44:47], v[56:59], v[64:67], v[44:47]
	s_waitcnt vmcnt(26)
	v_mfma_f32_16x16x32_f16 v[52:55], v[72:75], v[76:79], v[52:55]
	s_waitcnt vmcnt(24)
	v_mfma_f32_16x16x32_f16 v[40:43], v[84:87], v[76:79], v[40:43]
	v_mfma_f32_16x16x32_f16 v[48:51], v[72:75], v[80:83], v[48:51]
	v_mfma_f32_16x16x32_f16 v[44:47], v[84:87], v[80:83], v[44:47]
	s_waitcnt vmcnt(20)
	v_mfma_f32_16x16x32_f16 v[52:55], v[100:103], v[92:95], v[52:55]
	v_mfma_f32_16x16x32_f16 v[40:43], v[88:91], v[92:95], v[40:43]
	v_mfma_f32_16x16x32_f16 v[48:51], v[100:103], v[96:99], v[48:51]
	v_mfma_f32_16x16x32_f16 v[44:47], v[88:91], v[96:99], v[44:47]
	s_waitcnt vmcnt(17)
	v_mfma_f32_16x16x32_f16 v[52:55], v[168:171], v[176:179], v[52:55]
	v_mfma_f32_16x16x32_f16 v[40:43], v[172:175], v[176:179], v[40:43]
	s_waitcnt vmcnt(16)
	v_mfma_f32_16x16x32_f16 v[48:51], v[168:171], v[180:183], v[48:51]
	v_mfma_f32_16x16x32_f16 v[44:47], v[172:175], v[180:183], v[44:47]
	s_waitcnt vmcnt(13)
	v_mfma_f32_16x16x32_f16 v[52:55], v[112:115], v[104:107], v[52:55]
	s_waitcnt vmcnt(11)
	v_mfma_f32_16x16x32_f16 v[40:43], v[120:123], v[104:107], v[40:43]
	v_mfma_f32_16x16x32_f16 v[48:51], v[112:115], v[108:111], v[48:51]
	v_mfma_f32_16x16x32_f16 v[44:47], v[120:123], v[108:111], v[44:47]
	s_waitcnt vmcnt(9)
	v_mfma_f32_16x16x32_f16 v[52:55], v[116:119], v[128:131], v[52:55]
	v_mfma_f32_16x16x32_f16 v[40:43], v[124:127], v[128:131], v[40:43]
	s_waitcnt vmcnt(8)
	v_mfma_f32_16x16x32_f16 v[48:51], v[116:119], v[132:135], v[48:51]
	v_mfma_f32_16x16x32_f16 v[44:47], v[124:127], v[132:135], v[44:47]
	s_waitcnt vmcnt(5)
	v_mfma_f32_16x16x32_f16 v[52:55], v[144:147], v[136:139], v[52:55]
	s_waitcnt vmcnt(3)
	v_mfma_f32_16x16x32_f16 v[40:43], v[152:155], v[136:139], v[40:43]
	v_mfma_f32_16x16x32_f16 v[48:51], v[144:147], v[140:143], v[48:51]
	v_mfma_f32_16x16x32_f16 v[44:47], v[152:155], v[140:143], v[44:47]
	s_waitcnt vmcnt(1)
	v_mfma_f32_16x16x32_f16 v[52:55], v[148:151], v[30:33], v[52:55]
	v_mfma_f32_16x16x32_f16 v[30:33], v[156:159], v[30:33], v[40:43]
	s_waitcnt vmcnt(0)
	v_mfma_f32_16x16x32_f16 v[40:43], v[148:151], v[160:163], v[48:51]
	v_mfma_f32_16x16x32_f16 v[44:47], v[156:159], v[160:163], v[44:47]
	s_nop 1
	v_lshlrev_b32_e32 v48, 12, v186
	v_add3_u32 v48, 0, v8, v48
	ds_write_b128 v48, v[52:55]
	ds_write_b128 v48, v[30:33] offset:1024
	s_nop 0
	ds_write_b128 v48, v[40:43] offset:2048
	ds_write_b128 v48, v[44:47] offset:3072
	v_lshrrev_b32_e32 v30, 4, v0
	v_and_b32_e32 v31, 60, v1
	v_mul_u32_u24_e32 v30, 0x110, v30
	v_lshlrev_b32_e32 v31, 2, v31
	s_movk_i32 s0, 0x50
	v_add3_u32 v30, 0, v30, v31
	v_cmp_gt_u32_e32 vcc, s0, v0
	ds_write_b128 v30, v[2:5] offset:32768
	s_and_saveexec_b64 s[0:1], vcc
	s_cbranch_execz .LBB23_14
	global_load_dwordx4 v[2:5], v[28:29], off
	v_lshl_add_u32 v0, v1, 2, 0
	s_waitcnt vmcnt(0)
	ds_write_b128 v0, v[2:5] offset:41472
.LBB23_14:
	s_or_b64 exec, exec, s[0:1]
	v_lshlrev_b32_e32 v0, 10, v39
	v_add3_u32 v8, 0, v0, v8
	s_waitcnt lgkmcnt(0)
	s_barrier
	ds_read_b128 v[0:3], v8
	ds_read_b128 v[28:31], v8 offset:4096
	ds_read_b128 v[40:43], v8 offset:8192
	v_cmp_eq_u32_e32 vcc, 0, v38
	v_lshl_add_u32 v84, v35, 4, 0
	s_waitcnt lgkmcnt(1)
	v_pk_add_f32 v[30:31], v[2:3], v[30:31]
	ds_read_b128 v[2:5], v8 offset:12288
	v_pk_add_f32 v[0:1], v[0:1], v[28:29]
	s_waitcnt lgkmcnt(1)
	v_pk_add_f32 v[32:33], v[30:31], v[42:43]
	ds_read_b128 v[28:31], v8 offset:16384
	v_pk_add_f32 v[0:1], v[0:1], v[40:41]
	s_waitcnt lgkmcnt(1)
	v_pk_add_f32 v[4:5], v[32:33], v[4:5]
	v_pk_add_f32 v[40:41], v[0:1], v[2:3]
	ds_read_b128 v[0:3], v8 offset:20480
	s_waitcnt lgkmcnt(1)
	v_pk_add_f32 v[4:5], v[4:5], v[30:31]
	ds_read_b128 v[30:33], v8 offset:24576
	v_pk_add_f32 v[28:29], v[40:41], v[28:29]
	ds_read_b128 v[40:43], v8 offset:28672
	v_lshl_add_u32 v8, v35, 2, 0
	s_waitcnt lgkmcnt(2)
	v_pk_add_f32 v[2:3], v[4:5], v[2:3]
	ds_read_b64 v[4:5], v8 offset:42624
	v_pk_add_f32 v[0:1], v[28:29], v[0:1]
	s_waitcnt lgkmcnt(2)
	v_pk_add_f32 v[2:3], v[2:3], v[32:33]
	v_pk_add_f32 v[0:1], v[0:1], v[30:31]
	s_waitcnt lgkmcnt(1)
	v_pk_add_f32 v[2:3], v[2:3], v[42:43]
	v_pk_add_f32 v[0:1], v[0:1], v[40:41]
	ds_read_b32 v29, v8 offset:42500
	v_cndmask_b32_e32 v1, v3, v1, vcc
	v_cndmask_b32_e32 v0, v2, v0, vcc
	s_waitcnt lgkmcnt(1)
	v_pk_add_f32 v[0:1], v[0:1], v[4:5]
	s_nop 0
	v_pk_add_f32 v[78:79], v[24:25], v[0:1]
	v_add_co_u32_e32 v0, vcc, s2, v26
	s_nop 1
	v_addc_co_u32_e32 v1, vcc, 0, v27, vcc
	global_store_dwordx2 v[0:1], v[78:79], off
	v_mad_u32_u24 v0, v35, 12, v8
	v_lshl_add_u32 v8, v35, 8, v0
	ds_read_b128 v[24:27], v0 offset:41472
	ds_read_b128 v[30:33], v8 offset:32896
	ds_read_b128 v[38:41], v8 offset:32912
	ds_read_b128 v[42:45], v8 offset:32928
	ds_read_b128 v[46:49], v8 offset:32944
	ds_read_b128 v[50:53], v8 offset:32960
	v_mad_i32_i24 v0, v35, -12, v84
	v_or_b32_e32 v1, 1, v35
	v_lshl_add_u32 v2, v1, 4, 0
	ds_read_b32 v28, v0 offset:42496
	ds_read_b128 v[54:57], v2 offset:41472
	v_lshl_add_u32 v85, v1, 8, v2
	ds_read_b128 v[58:61], v85 offset:32896
	ds_read_b128 v[62:65], v85 offset:32912
	ds_read_b128 v[66:69], v85 offset:32928
	ds_read_b128 v[70:73], v85 offset:32944
	ds_read_b128 v[74:77], v85 offset:32960
	s_waitcnt lgkmcnt(11)
	v_mov_b32_e32 v4, v30
	s_waitcnt lgkmcnt(4)
	v_mov_b32_e32 v5, v58
	v_mov_b32_e32 v80, v24
	v_mov_b32_e32 v81, v54
	v_pk_fma_f32 v[4:5], v[22:23], v[4:5], v[80:81]
	v_mov_b32_e32 v80, v38
	s_waitcnt lgkmcnt(3)
	v_mov_b32_e32 v81, v62
	v_pk_fma_f32 v[4:5], v[6:7], v[80:81], v[4:5]
	v_mov_b32_e32 v80, v42
	s_waitcnt lgkmcnt(2)
	v_mov_b32_e32 v81, v66
	v_pk_fma_f32 v[4:5], v[12:13], v[80:81], v[4:5]
	v_mov_b32_e32 v80, v46
	s_waitcnt lgkmcnt(1)
	v_mov_b32_e32 v81, v70
	v_mov_b32_e32 v58, v31
	v_mov_b32_e32 v54, v25
	v_pk_fma_f32 v[80:81], v[14:15], v[80:81], v[4:5]
	v_pk_fma_f32 v[4:5], v[22:23], v[58:59], v[54:55]
	v_mov_b32_e32 v62, v39
	v_pk_fma_f32 v[4:5], v[6:7], v[62:63], v[4:5]
	v_mov_b32_e32 v66, v43
	v_pk_fma_f32 v[4:5], v[12:13], v[66:67], v[4:5]
	v_mov_b32_e32 v70, v47
	v_pk_fma_f32 v[46:47], v[14:15], v[70:71], v[4:5]
	v_mov_b32_e32 v4, v32
	v_mov_b32_e32 v5, v60
	v_mov_b32_e32 v24, v26
	v_mov_b32_e32 v25, v56
	v_pk_fma_f32 v[4:5], v[22:23], v[4:5], v[24:25]
	v_mov_b32_e32 v24, v40
	v_mov_b32_e32 v25, v64
	v_pk_fma_f32 v[4:5], v[6:7], v[24:25], v[4:5]
	v_mov_b32_e32 v24, v44
	v_mov_b32_e32 v25, v68
	v_mov_b32_e32 v60, v33
	v_mov_b32_e32 v56, v27
	v_mov_b32_e32 v82, v50
	s_waitcnt lgkmcnt(0)
	v_mov_b32_e32 v83, v74
	v_mov_b32_e32 v74, v51
	v_pk_fma_f32 v[50:51], v[12:13], v[24:25], v[4:5]
	v_pk_fma_f32 v[4:5], v[22:23], v[60:61], v[56:57]
	v_mov_b32_e32 v64, v41
	ds_read_b128 v[0:3], v2 offset:41984
	v_pk_fma_f32 v[26:27], v[6:7], v[64:65], v[4:5]
	v_mov_b32_e32 v68, v45
	ds_read_b128 v[22:25], v8 offset:32976
	ds_read_b128 v[30:33], v8 offset:32992
	ds_read_b128 v[38:41], v8 offset:33008
	ds_read_b128 v[4:7], v84 offset:41984
	ds_read_b128 v[42:45], v85 offset:32976
	ds_read_b128 v[54:57], v85 offset:32992
	ds_read_b128 v[58:61], v85 offset:33008
	v_pk_fma_f32 v[64:65], v[18:19], v[82:83], v[80:81]
	s_waitcnt lgkmcnt(6)
	v_mov_b32_e32 v66, v22
	s_waitcnt lgkmcnt(2)
	v_mov_b32_e32 v67, v42
	v_pk_fma_f32 v[64:65], v[16:17], v[66:67], v[64:65]
	v_mov_b32_e32 v66, v30
	s_waitcnt lgkmcnt(1)
	v_mov_b32_e32 v67, v54
	v_pk_fma_f32 v[64:65], v[20:21], v[66:67], v[64:65]
	v_mov_b32_e32 v66, v38
	s_waitcnt lgkmcnt(0)
	v_mov_b32_e32 v67, v58
	v_pk_fma_f32 v[64:65], v[78:79], v[66:67], v[64:65]
	v_pk_fma_f32 v[46:47], v[18:19], v[74:75], v[46:47]
	v_mul_f32_e32 v8, 0x3d372713, v64
	v_mul_f32_e32 v8, v64, v8
	v_fma_f32 v8, v64, v8, v64
	v_mov_b32_e32 v42, v23
	v_mul_f32_e32 v8, 0x3f4c422a, v8
	v_pk_fma_f32 v[42:43], v[16:17], v[42:43], v[46:47]
	v_mov_b32_e32 v54, v31
	v_add_f32_e32 v8, v8, v8
	v_pk_fma_f32 v[30:31], v[20:21], v[54:55], v[42:43]
	v_mov_b32_e32 v58, v39
	v_mul_f32_e32 v8, 0x3fb8aa3b, v8
	v_pk_fma_f32 v[30:31], v[78:79], v[58:59], v[30:31]
	v_mov_b32_e32 v62, v48
	v_mov_b32_e32 v63, v72
	v_exp_f32_e32 v22, v8
	v_mul_f32_e32 v8, 0x3d372713, v30
	v_mul_f32_e32 v8, v30, v8
	v_pk_fma_f32 v[42:43], v[14:15], v[62:63], v[50:51]
	v_mov_b32_e32 v46, v52
	v_mov_b32_e32 v47, v76
	v_pk_fma_f32 v[12:13], v[12:13], v[68:69], v[26:27]
	v_mov_b32_e32 v72, v49
	v_fma_f32 v8, v30, v8, v30
	v_pk_fma_f32 v[42:43], v[18:19], v[46:47], v[42:43]
	v_mov_b32_e32 v46, v24
	v_mov_b32_e32 v47, v44
	v_pk_fma_f32 v[12:13], v[14:15], v[72:73], v[12:13]
	v_mul_f32_e32 v14, 0x3d372713, v65
	v_mul_f32_e32 v8, 0x3f4c422a, v8
	v_pk_fma_f32 v[42:43], v[16:17], v[46:47], v[42:43]
	v_mov_b32_e32 v46, v32
	v_mov_b32_e32 v47, v56
	v_mul_f32_e32 v14, v65, v14
	v_add_f32_e32 v8, v8, v8
	v_pk_fma_f32 v[42:43], v[20:21], v[46:47], v[42:43]
	v_mov_b32_e32 v46, v40
	v_mov_b32_e32 v47, v60
	v_fma_f32 v14, v65, v14, v65
	v_mul_f32_e32 v8, 0x3fb8aa3b, v8
	v_pk_fma_f32 v[42:43], v[78:79], v[46:47], v[42:43]
	v_mul_f32_e32 v14, 0x3f4c422a, v14
	v_exp_f32_e32 v38, v8
	v_mul_f32_e32 v8, 0x3d372713, v42
	v_add_f32_e32 v14, v14, v14
	v_mul_f32_e32 v8, v42, v8
	v_mov_b32_e32 v76, v53
	v_mul_f32_e32 v14, 0x3fb8aa3b, v14
	v_fma_f32 v8, v42, v8, v42
	v_pk_fma_f32 v[12:13], v[18:19], v[76:77], v[12:13]
	v_mov_b32_e32 v44, v25
	v_exp_f32_e32 v23, v14
	v_mul_f32_e32 v8, 0x3f4c422a, v8
	v_pk_fma_f32 v[12:13], v[16:17], v[44:45], v[12:13]
	v_mov_b32_e32 v56, v33
	v_add_f32_e32 v8, v8, v8
	v_pk_fma_f32 v[12:13], v[20:21], v[56:57], v[12:13]
	v_mov_b32_e32 v60, v41
	v_mul_f32_e32 v8, 0x3fb8aa3b, v8
	v_pk_fma_f32 v[12:13], v[78:79], v[60:61], v[12:13]
	v_exp_f32_e32 v24, v8
	v_mul_f32_e32 v8, 0x3d372713, v12
	v_pk_add_f32 v[14:15], v[22:23], 1.0 op_sel_hi:[1,0]
	v_mul_f32_e32 v8, v12, v8
	v_div_scale_f32 v17, s[0:1], v15, v15, 2.0
	v_fma_f32 v8, v12, v8, v12
	v_rcp_f32_e32 v18, v17
	v_mul_f32_e32 v8, 0x3f4c422a, v8
	v_add_f32_e32 v8, v8, v8
	v_mul_f32_e32 v8, 0x3fb8aa3b, v8
	v_exp_f32_e32 v16, v8
	v_fma_f32 v8, -v17, v18, 1.0
	v_fmac_f32_e32 v18, v8, v18
	v_div_scale_f32 v8, vcc, 2.0, v15, 2.0
	v_mul_f32_e32 v19, v8, v18
	v_fma_f32 v20, -v17, v19, v8
	v_fmac_f32_e32 v19, v20, v18
	v_fma_f32 v8, -v17, v19, v8
	v_div_scale_f32 v17, s[0:1], v14, v14, 2.0
	v_rcp_f32_e32 v20, v17
	v_div_fmas_f32 v8, v8, v18, v19
	v_div_fixup_f32 v15, v8, v15, 2.0
	v_fma_f32 v8, -v17, v20, 1.0
	v_fmac_f32_e32 v20, v8, v20
	v_div_scale_f32 v8, vcc, 2.0, v14, 2.0
	v_mul_f32_e32 v18, v8, v20
	v_fma_f32 v19, -v17, v18, v8
	v_fmac_f32_e32 v18, v19, v20
	v_fma_f32 v8, -v17, v18, v8
	v_div_fmas_f32 v8, v8, v20, v18
	v_div_fixup_f32 v14, v8, v14, 2.0
	v_mul_f32_e32 v8, 0x3d372713, v31
	v_mul_f32_e32 v8, v31, v8
	v_fma_f32 v8, v31, v8, v31
	v_mul_f32_e32 v8, 0x3f4c422a, v8
	v_add_f32_e32 v8, v8, v8
	v_mul_f32_e32 v8, 0x3fb8aa3b, v8
	v_exp_f32_e32 v39, v8
	v_pk_add_f32 v[14:15], v[14:15], 1.0 op_sel_hi:[1,0] neg_lo:[1,0] neg_hi:[1,0]
	v_pk_mul_f32 v[18:19], v[64:65], 0.5 op_sel_hi:[1,0]
	v_pk_add_f32 v[14:15], v[14:15], 1.0 op_sel_hi:[1,0]
	v_pk_add_f32 v[20:21], v[38:39], 1.0 op_sel_hi:[1,0]
	v_pk_mul_f32 v[14:15], v[18:19], v[14:15]
	v_div_scale_f32 v8, s[0:1], v21, v21, 2.0
	v_rcp_f32_e32 v17, v8
	v_mov_b32_e32 v19, v0
	v_mov_b32_e32 v18, v4
	v_fma_f32 v0, -v8, v17, 1.0
	v_fmac_f32_e32 v17, v0, v17
	v_div_scale_f32 v0, vcc, 2.0, v21, 2.0
	v_mul_f32_e32 v4, v0, v17
	v_fma_f32 v22, -v8, v4, v0
	v_fmac_f32_e32 v4, v22, v17
	v_fma_f32 v0, -v8, v4, v0
	v_div_scale_f32 v8, s[0:1], v20, v20, 2.0
	v_rcp_f32_e32 v22, v8
	v_div_fmas_f32 v0, v0, v17, v4
	v_div_fixup_f32 v21, v0, v21, 2.0
	v_fma_f32 v0, -v8, v22, 1.0
	v_fmac_f32_e32 v22, v0, v22
	v_div_scale_f32 v0, vcc, 2.0, v20, 2.0
	v_mul_f32_e32 v4, v0, v22
	v_fma_f32 v17, -v8, v4, v0
	v_fmac_f32_e32 v4, v17, v22
	v_fma_f32 v0, -v8, v4, v0
	v_div_fmas_f32 v0, v0, v22, v4
	v_div_fixup_f32 v20, v0, v20, 2.0
	v_mul_f32_e32 v0, 0x3d372713, v43
	v_mul_f32_e32 v0, v43, v0
	v_fma_f32 v0, v43, v0, v43
	v_mul_f32_e32 v0, 0x3f4c422a, v0
	v_add_f32_e32 v0, v0, v0
	v_mul_f32_e32 v0, 0x3fb8aa3b, v0
	v_exp_f32_e32 v25, v0
	v_pk_add_f32 v[20:21], v[20:21], 1.0 op_sel_hi:[1,0] neg_lo:[1,0] neg_hi:[1,0]
	v_pk_mul_f32 v[22:23], v[30:31], 0.5 op_sel_hi:[1,0]
	v_pk_add_f32 v[20:21], v[20:21], 1.0 op_sel_hi:[1,0]
	v_mov_b32_e32 v0, v5
	v_pk_mul_f32 v[20:21], v[22:23], v[20:21]
	v_pk_add_f32 v[22:23], v[24:25], 1.0 op_sel_hi:[1,0]
	v_pk_mul_f32 v[0:1], v[20:21], v[0:1]
	v_div_scale_f32 v4, s[0:1], v23, v23, 2.0
	v_rcp_f32_e32 v8, v4
	v_pk_fma_f32 v[0:1], v[14:15], v[18:19], v[0:1]
	v_fma_f32 v5, -v4, v8, 1.0
	v_fmac_f32_e32 v8, v5, v8
	v_div_scale_f32 v5, vcc, 2.0, v23, 2.0
	v_mul_f32_e32 v14, v5, v8
	v_fma_f32 v15, -v4, v14, v5
	v_fmac_f32_e32 v14, v15, v8
	v_div_scale_f32 v15, s[0:1], v22, v22, 2.0
	v_rcp_f32_e32 v17, v15
	v_fma_f32 v4, -v4, v14, v5
	v_div_fmas_f32 v4, v4, v8, v14
	v_div_fixup_f32 v5, v4, v23, 2.0
	v_fma_f32 v4, -v15, v17, 1.0
	v_fmac_f32_e32 v17, v4, v17
	v_div_scale_f32 v4, vcc, 2.0, v22, 2.0
	v_mul_f32_e32 v8, v4, v17
	v_fma_f32 v14, -v15, v8, v4
	v_fmac_f32_e32 v8, v14, v17
	v_fma_f32 v4, -v15, v8, v4
	v_div_fmas_f32 v4, v4, v17, v8
	v_mul_f32_e32 v8, 0x3d372713, v13
	v_mul_f32_e32 v8, v13, v8
	v_fma_f32 v8, v13, v8, v13
	v_mul_f32_e32 v8, 0x3f4c422a, v8
	v_add_f32_e32 v8, v8, v8
	v_mul_f32_e32 v8, 0x3fb8aa3b, v8
	v_exp_f32_e32 v17, v8
	v_div_fixup_f32 v4, v4, v22, 2.0
	v_pk_add_f32 v[4:5], v[4:5], 1.0 op_sel_hi:[1,0] neg_lo:[1,0] neg_hi:[1,0]
	v_pk_mul_f32 v[14:15], v[42:43], 0.5 op_sel_hi:[1,0]
	v_pk_add_f32 v[4:5], v[4:5], 1.0 op_sel_hi:[1,0]
	v_pk_mul_f32 v[12:13], v[12:13], 0.5 op_sel_hi:[1,0]
	v_pk_mul_f32 v[4:5], v[14:15], v[4:5]
	v_pk_add_f32 v[14:15], v[16:17], 1.0 op_sel_hi:[1,0]
	v_mov_b32_e32 v17, v2
	v_div_scale_f32 v8, s[0:1], v15, v15, 2.0
	v_rcp_f32_e32 v18, v8
	v_mov_b32_e32 v16, v6
	v_pk_fma_f32 v[0:1], v[4:5], v[16:17], v[0:1]
	v_div_scale_f32 v6, s[0:1], v14, v14, 2.0
	v_fma_f32 v2, -v8, v18, 1.0
	v_fmac_f32_e32 v18, v2, v18
	v_div_scale_f32 v2, vcc, 2.0, v15, 2.0
	v_mul_f32_e32 v4, v2, v18
	v_fma_f32 v5, -v8, v4, v2
	v_fmac_f32_e32 v4, v5, v18
	v_fma_f32 v2, -v8, v4, v2
	v_rcp_f32_e32 v8, v6
	v_div_fmas_f32 v2, v2, v18, v4
	v_div_fixup_f32 v5, v2, v15, 2.0
	s_mov_b32 s0, 0x800000
	v_fma_f32 v2, -v6, v8, 1.0
	v_fmac_f32_e32 v8, v2, v8
	v_div_scale_f32 v2, vcc, 2.0, v14, 2.0
	v_mul_f32_e32 v4, v2, v8
	v_fma_f32 v15, -v6, v4, v2
	v_fmac_f32_e32 v4, v15, v8
	v_fma_f32 v2, -v6, v4, v2
	v_div_fmas_f32 v2, v2, v8, v4
	v_div_fixup_f32 v4, v2, v14, 2.0
	v_pk_add_f32 v[4:5], v[4:5], 1.0 op_sel_hi:[1,0] neg_lo:[1,0] neg_hi:[1,0]
	v_mov_b32_e32 v2, v7
	v_pk_add_f32 v[4:5], v[4:5], 1.0 op_sel_hi:[1,0]
	s_nop 0
	v_pk_mul_f32 v[4:5], v[12:13], v[4:5]
	s_nop 0
	v_pk_fma_f32 v[0:1], v[4:5], v[2:3], v[0:1]
	v_add_co_u32_e32 v2, vcc, s0, v10
	s_lshl_b32 s0, s3, 3
	v_pk_add_f32 v[0:1], v[28:29], v[0:1]
	v_addc_co_u32_e32 v3, vcc, 0, v11, vcc
	s_addk_i32 s0, 0x100
	global_store_dwordx2 v[2:3], v[0:1], off
	v_add_u32_e32 v8, s0, v36
	v_lshlrev_b32_e32 v3, 1, v37
	v_cvt_pk_f16_f32 v2, v0, v1
	v_lshlrev_b64 v[0:1], 6, v[8:9]
	v_and_b32_e32 v3, 48, v3
	v_or3_b32 v0, v0, v3, v34
	v_and_b32_e32 v3, 6, v35
	v_lshl_add_u64 v[0:1], v[0:1], 4, s[12:13]
	v_lshlrev_b32_e32 v8, 1, v3
	v_lshl_add_u64 v[0:1], v[0:1], 0, v[8:9]
	global_store_dword v[0:1], v2, off
	s_endpgm
	s_nop 0
	s_nop 0
	s_nop 0
	s_nop 0
	s_nop 0
	s_nop 0
	s_nop 0
	s_nop 0
	s_nop 0
	s_nop 0
	s_nop 0
	s_nop 0
	s_nop 0
	s_nop 0
	s_nop 0
	s_nop 0
	s_nop 0
	s_nop 0
	s_nop 0
	s_nop 0
	s_nop 0
	s_nop 0
	s_nop 0
	s_nop 0
	s_nop 0
	s_nop 0
	s_nop 0
	s_nop 0
	s_nop 0
	s_nop 0
	s_nop 0
	s_nop 0
	s_nop 0
	s_nop 0
	s_nop 0
	s_nop 0
	s_nop 0
	s_nop 0
	s_nop 0
	s_nop 0
	s_nop 0
	s_nop 0
	s_nop 0
	s_nop 0
	s_nop 0
	s_nop 0
	s_nop 0
	s_nop 0
	s_nop 0
	s_nop 0
	s_nop 0
	s_nop 0
	s_nop 0
	s_nop 0
	s_nop 0
	s_nop 0
	s_nop 0
	s_nop 0
	s_nop 0
	s_nop 0
	s_nop 0
	s_endpgm

	.amdhsa_kernel _ZN12_GLOBAL__N_110gemm_fullkILi1ELi7EEEvPKDF16_S2_PKfPDF16_PfS6_S4_S4_S4_S4_S4_S5_
		.amdhsa_group_segment_fixed_size 0
		.amdhsa_private_segment_fixed_size 0
		.amdhsa_kernarg_size 96
		.amdhsa_user_sgpr_count 2
		.amdhsa_user_sgpr_dispatch_ptr 0
		.amdhsa_user_sgpr_queue_ptr 0
		.amdhsa_user_sgpr_kernarg_segment_ptr 1
		.amdhsa_user_sgpr_dispatch_id 0
		.amdhsa_user_sgpr_kernarg_preload_length 0
		.amdhsa_user_sgpr_kernarg_preload_offset 0
		.amdhsa_user_sgpr_private_segment_size 0
		.amdhsa_uses_dynamic_stack 0
		.amdhsa_enable_private_segment 0
		.amdhsa_system_sgpr_workgroup_id_x 1
		.amdhsa_system_sgpr_workgroup_id_y 0
		.amdhsa_system_sgpr_workgroup_id_z 0
		.amdhsa_system_sgpr_workgroup_info 0
		.amdhsa_system_vgpr_workitem_id 0
		.amdhsa_next_free_vgpr 187
		.amdhsa_next_free_sgpr 18
		.amdhsa_accum_offset 188
		.amdhsa_reserve_vcc 1
		.amdhsa_float_round_mode_32 0
		.amdhsa_float_round_mode_16_64 0
		.amdhsa_float_denorm_mode_32 3
		.amdhsa_float_denorm_mode_16_64 3
		.amdhsa_dx10_clamp 1
		.amdhsa_ieee_mode 1
		.amdhsa_fp16_overflow 0
		.amdhsa_tg_split 0
		.amdhsa_exception_fp_ieee_invalid_op 0
		.amdhsa_exception_fp_denorm_src 0
		.amdhsa_exception_fp_ieee_div_zero 0
		.amdhsa_exception_fp_ieee_overflow 0
		.amdhsa_exception_fp_ieee_underflow 0
		.amdhsa_exception_fp_ieee_inexact 0
		.amdhsa_exception_int_div_zero 0
	.end_amdhsa_kernel

amdhsa.kernels:
  - .agpr_count:     0
    .args:
      - .actual_access:  read_only
        .address_space:  global
        .offset:         0
        .size:           8
        .value_kind:     global_buffer
      - .actual_access:  read_only
        .address_space:  global
        .offset:         8
        .size:           8
        .value_kind:     global_buffer
      - .actual_access:  read_only
        .address_space:  global
        .offset:         16
        .size:           8
        .value_kind:     global_buffer
      - .actual_access:  read_only
        .address_space:  global
        .offset:         24
        .size:           8
        .value_kind:     global_buffer
      - .actual_access:  read_only
        .address_space:  global
        .offset:         32
        .size:           8
        .value_kind:     global_buffer
      - .actual_access:  write_only
        .address_space:  global
        .offset:         40
        .size:           8
        .value_kind:     global_buffer
      - .actual_access:  write_only
        .address_space:  global
        .offset:         48
        .size:           8
        .value_kind:     global_buffer
    .group_segment_fixed_size: 34816
    .kernarg_segment_align: 8
    .kernarg_segment_size: 56
    .language:       OpenCL C
    .language_version:
      - 2
      - 0
    .max_flat_workgroup_size: 512
    .name:           _ZN12_GLOBAL__N_16attn_qEPKDF16_S1_PK15HIP_vector_typeIfLj2EEPKhS7_PfS8_
    .private_segment_fixed_size: 0
    .sgpr_count:     30
    .sgpr_spill_count: 0
    .symbol:         _ZN12_GLOBAL__N_16attn_qEPKDF16_S1_PK15HIP_vector_typeIfLj2EEPKhS7_PfS8_.kd
    .uniform_work_group_size: 1
    .uses_dynamic_stack: false
    .vgpr_count:     172
    .vgpr_spill_count: 0
    .wavefront_size: 64
  - .agpr_count:     0
    .args:
      - .actual_access:  read_only
        .address_space:  global
        .offset:         0
        .size:           8
        .value_kind:     global_buffer
      - .actual_access:  read_only
        .address_space:  global
        .offset:         8
        .size:           8
        .value_kind:     global_buffer
      - .actual_access:  write_only
        .address_space:  global
        .offset:         16
        .size:           8
        .value_kind:     global_buffer
      - .actual_access:  read_only
        .address_space:  global
        .offset:         24
        .size:           8
        .value_kind:     global_buffer
      - .actual_access:  write_only
        .address_space:  global
        .offset:         32
        .size:           8
        .value_kind:     global_buffer
      - .actual_access:  read_only
        .address_space:  global
        .offset:         40
        .size:           8
        .value_kind:     global_buffer
      - .actual_access:  write_only
        .address_space:  global
        .offset:         48
        .size:           8
        .value_kind:     global_buffer
      - .actual_access:  read_only
        .address_space:  global
        .offset:         56
        .size:           8
        .value_kind:     global_buffer
      - .actual_access:  write_only
        .address_space:  global
        .offset:         64
        .size:           8
        .value_kind:     global_buffer
      - .actual_access:  read_only
        .address_space:  global
        .offset:         72
        .size:           8
        .value_kind:     global_buffer
      - .actual_access:  write_only
        .address_space:  global
        .offset:         80
        .size:           8
        .value_kind:     global_buffer
      - .actual_access:  read_only
        .address_space:  global
        .offset:         88
        .size:           8
        .value_kind:     global_buffer
      - .actual_access:  write_only
        .address_space:  global
        .offset:         96
        .size:           8
        .value_kind:     global_buffer
      - .actual_access:  write_only
        .address_space:  global
        .offset:         104
        .size:           8
        .value_kind:     global_buffer
      - .actual_access:  read_only
        .address_space:  global
        .offset:         112
        .size:           8
        .value_kind:     global_buffer
      - .actual_access:  write_only
        .address_space:  global
        .offset:         120
        .size:           8
        .value_kind:     global_buffer
      - .actual_access:  write_only
        .address_space:  global
        .offset:         128
        .size:           8
        .value_kind:     global_buffer
      - .actual_access:  read_only
        .address_space:  global
        .offset:         136
        .size:           8
        .value_kind:     global_buffer
      - .actual_access:  read_only
        .address_space:  global
        .offset:         144
        .size:           8
        .value_kind:     global_buffer
      - .actual_access:  write_only
        .address_space:  global
        .offset:         152
        .size:           8
        .value_kind:     global_buffer
      - .actual_access:  read_only
        .address_space:  global
        .offset:         160
        .size:           8
        .value_kind:     global_buffer
      - .actual_access:  read_only
        .address_space:  global
        .offset:         168
        .size:           8
        .value_kind:     global_buffer
      - .actual_access:  read_only
        .address_space:  global
        .offset:         176
        .size:           8
        .value_kind:     global_buffer
      - .actual_access:  write_only
        .address_space:  global
        .offset:         184
        .size:           8
        .value_kind:     global_buffer
      - .actual_access:  write_only
        .address_space:  global
        .offset:         192
        .size:           8
        .value_kind:     global_buffer
    .group_segment_fixed_size: 16640
    .kernarg_segment_align: 8
    .kernarg_segment_size: 200
    .language:       OpenCL C
    .language_version:
      - 2
      - 0
    .max_flat_workgroup_size: 256
    .name:           _ZN12_GLOBAL__N_18prep_allEPKiPKfPDF16_S3_S4_S3_S4_S3_S4_S3_S4_S3_S4_P15HIP_vector_typeIfLj2EES3_PfS4_S1_S1_S4_S3_S3_S3_S8_S8_
    .private_segment_fixed_size: 0
    .sgpr_count:     24
    .sgpr_spill_count: 0
    .symbol:         _ZN12_GLOBAL__N_18prep_allEPKiPKfPDF16_S3_S4_S3_S4_S3_S4_S3_S4_S3_S4_P15HIP_vector_typeIfLj2EES3_PfS4_S1_S1_S4_S3_S3_S3_S8_S8_.kd
    .uniform_work_group_size: 1
    .uses_dynamic_stack: false
    .vgpr_count:     35
    .vgpr_spill_count: 0
    .wavefront_size: 64
  - .agpr_count:     0
    .args:
      - .actual_access:  read_only
        .address_space:  global
        .offset:         0
        .size:           8
        .value_kind:     global_buffer
      - .actual_access:  read_only
        .address_space:  global
        .offset:         8
        .size:           8
        .value_kind:     global_buffer
      - .actual_access:  read_only
        .address_space:  global
        .offset:         16
        .size:           8
        .value_kind:     global_buffer
      - .actual_access:  write_only
        .address_space:  global
        .offset:         24
        .size:           8
        .value_kind:     global_buffer
      - .actual_access:  read_only
        .address_space:  global
        .offset:         32
        .size:           8
        .value_kind:     global_buffer
      - .actual_access:  write_only
        .address_space:  global
        .offset:         40
        .size:           8
        .value_kind:     global_buffer
      - .offset:         48
        .size:           4
        .value_kind:     by_value
    .group_segment_fixed_size: 32768
    .kernarg_segment_align: 8
    .kernarg_segment_size: 52
    .language:       OpenCL C
    .language_version:
      - 2
      - 0
    .max_flat_workgroup_size: 512
    .name:           _ZN12_GLOBAL__N_16o_gemmEPKfS1_PKDF16_PDF16_S1_S4_i
    .private_segment_fixed_size: 0
    .sgpr_count:     19
    .sgpr_spill_count: 0
    .symbol:         _ZN12_GLOBAL__N_16o_gemmEPKfS1_PKDF16_PDF16_S1_S4_i.kd
    .uniform_work_group_size: 1
    .uses_dynamic_stack: false
    .vgpr_count:     94
    .vgpr_spill_count: 0
    .wavefront_size: 64
  - .agpr_count:     0
    .args:
      - .actual_access:  read_only
        .address_space:  global
        .offset:         0
        .size:           8
        .value_kind:     global_buffer
      - .offset:         8
        .size:           4
        .value_kind:     by_value
      - .offset:         12
        .size:           4
        .value_kind:     by_value
      - .actual_access:  read_only
        .address_space:  global
        .offset:         16
        .size:           8
        .value_kind:     global_buffer
      - .actual_access:  read_only
        .address_space:  global
        .offset:         24
        .size:           8
        .value_kind:     global_buffer
      - .actual_access:  read_only
        .address_space:  global
        .offset:         32
        .size:           8
        .value_kind:     global_buffer
      - .actual_access:  write_only
        .address_space:  global
        .offset:         40
        .size:           8
        .value_kind:     global_buffer
      - .actual_access:  read_only
        .address_space:  global
        .offset:         48
        .size:           8
        .value_kind:     global_buffer
      - .actual_access:  write_only
        .address_space:  global
        .offset:         56
        .size:           8
        .value_kind:     global_buffer
      - .offset:         64
        .size:           4
        .value_kind:     by_value
    .group_segment_fixed_size: 0
    .kernarg_segment_align: 8
    .kernarg_segment_size: 68
    .language:       OpenCL C
    .language_version:
      - 2
      - 0
    .max_flat_workgroup_size: 1024
    .name:           _ZN12_GLOBAL__N_113sync_a_kernelEPKfiiPKiS3_S1_PDF16_S1_S4_i
    .private_segment_fixed_size: 0
    .sgpr_count:     33
    .sgpr_spill_count: 0
    .symbol:         _ZN12_GLOBAL__N_113sync_a_kernelEPKfiiPKiS3_S1_PDF16_S1_S4_i.kd
    .uniform_work_group_size: 1
    .uses_dynamic_stack: false
    .vgpr_count:     49
    .vgpr_spill_count: 0
    .wavefront_size: 64
  - .agpr_count:     0
    .args:
      - .actual_access:  read_only
        .address_space:  global
        .offset:         0
        .size:           8
        .value_kind:     global_buffer
      - .actual_access:  read_only
        .address_space:  global
        .offset:         8
        .size:           8
        .value_kind:     global_buffer
      - .actual_access:  write_only
        .address_space:  global
        .offset:         16
        .size:           8
        .value_kind:     global_buffer
      - .offset:         24
        .size:           4
        .value_kind:     by_value
      - .actual_access:  read_only
        .address_space:  global
        .offset:         32
        .size:           8
        .value_kind:     global_buffer
      - .actual_access:  read_only
        .address_space:  global
        .offset:         40
        .size:           8
        .value_kind:     global_buffer
      - .actual_access:  read_only
        .address_space:  global
        .offset:         48
        .size:           8
        .value_kind:     global_buffer
      - .actual_access:  write_only
        .address_space:  global
        .offset:         56
        .size:           8
        .value_kind:     global_buffer
    .group_segment_fixed_size: 8192
    .kernarg_segment_align: 8
    .kernarg_segment_size: 64
    .language:       OpenCL C
    .language_version:
      - 2
      - 0
    .max_flat_workgroup_size: 1024
    .name:           _ZN12_GLOBAL__N_110sync_a_incEPKfS1_PfiPKiS4_S1_PDF16_
    .private_segment_fixed_size: 0
    .sgpr_count:     24
    .sgpr_spill_count: 0
    .symbol:         _ZN12_GLOBAL__N_110sync_a_incEPKfS1_PfiPKiS4_S1_PDF16_.kd
    .uniform_work_group_size: 1
    .uses_dynamic_stack: false
    .vgpr_count:     14
    .vgpr_spill_count: 0
    .wavefront_size: 64
  - .agpr_count:     0
    .args:
      - .actual_access:  read_only
        .address_space:  global
        .offset:         0
        .size:           8
        .value_kind:     global_buffer
      - .actual_access:  read_only
        .address_space:  global
        .offset:         8
        .size:           8
        .value_kind:     global_buffer
      - .actual_access:  read_only
        .address_space:  global
        .offset:         16
        .size:           8
        .value_kind:     global_buffer
      - .actual_access:  read_only
        .address_space:  global
        .offset:         24
        .size:           8
        .value_kind:     global_buffer
      - .actual_access:  write_only
        .address_space:  global
        .offset:         32
        .size:           8
        .value_kind:     global_buffer
    .group_segment_fixed_size: 0
    .kernarg_segment_align: 8
    .kernarg_segment_size: 40
    .language:       OpenCL C
    .language_version:
      - 2
      - 0
    .max_flat_workgroup_size: 1024
    .name:           _ZN12_GLOBAL__N_110sync_o_allEPKfPKiS3_S1_PDF16_
    .private_segment_fixed_size: 0
    .sgpr_count:     18
    .sgpr_spill_count: 0
    .symbol:         _ZN12_GLOBAL__N_110sync_o_allEPKfPKiS3_S1_PDF16_.kd
    .uniform_work_group_size: 1
    .uses_dynamic_stack: false
    .vgpr_count:     33
    .vgpr_spill_count: 0
    .wavefront_size: 64
  - .agpr_count:     0
    .args:
      - .address_space:  global
        .offset:         0
        .size:           8
        .value_kind:     global_buffer
      - .address_space:  global
        .offset:         8
        .size:           8
        .value_kind:     global_buffer
      - .offset:         16
        .size:           4
        .value_kind:     by_value
      - .offset:         20
        .size:           4
        .value_kind:     by_value
      - .actual_access:  read_only
        .address_space:  global
        .offset:         24
        .size:           8
        .value_kind:     global_buffer
      - .actual_access:  write_only
        .address_space:  global
        .offset:         32
        .size:           8
        .value_kind:     global_buffer
      - .actual_access:  write_only
        .address_space:  global
        .offset:         40
        .size:           8
        .value_kind:     global_buffer
      - .actual_access:  read_only
        .address_space:  global
        .offset:         48
        .size:           8
        .value_kind:     global_buffer
      - .actual_access:  read_only
        .address_space:  global
        .offset:         56
        .size:           8
        .value_kind:     global_buffer
    .group_segment_fixed_size: 0
    .kernarg_segment_align: 8
    .kernarg_segment_size: 64
    .language:       OpenCL C
    .language_version:
      - 2
      - 0
    .max_flat_workgroup_size: 512
    .name:           _ZN12_GLOBAL__N_18big_gemmILi0EEEvPKDF16_S2_iiPK15HIP_vector_typeIfLj2EEPhS7_PKfPf
    .private_segment_fixed_size: 0
    .sgpr_count:     50
    .sgpr_spill_count: 0
    .symbol:         _ZN12_GLOBAL__N_18big_gemmILi0EEEvPKDF16_S2_iiPK15HIP_vector_typeIfLj2EEPhS7_PKfPf.kd
    .uniform_work_group_size: 1
    .uses_dynamic_stack: false
    .vgpr_count:     255
    .vgpr_spill_count: 0
    .wavefront_size: 64
  - .agpr_count:     0
    .args:
      - .address_space:  global
        .offset:         0
        .size:           8
        .value_kind:     global_buffer
      - .address_space:  global
        .offset:         8
        .size:           8
        .value_kind:     global_buffer
      - .offset:         16
        .size:           4
        .value_kind:     by_value
      - .offset:         20
        .size:           4
        .value_kind:     by_value
      - .actual_access:  read_only
        .address_space:  global
        .offset:         24
        .size:           8
        .value_kind:     global_buffer
      - .actual_access:  read_only
        .address_space:  global
        .offset:         32
        .size:           8
        .value_kind:     global_buffer
      - .actual_access:  read_only
        .address_space:  global
        .offset:         40
        .size:           8
        .value_kind:     global_buffer
      - .actual_access:  read_only
        .address_space:  global
        .offset:         48
        .size:           8
        .value_kind:     global_buffer
      - .actual_access:  write_only
        .address_space:  global
        .offset:         56
        .size:           8
        .value_kind:     global_buffer
    .group_segment_fixed_size: 0
    .kernarg_segment_align: 8
    .kernarg_segment_size: 64
    .language:       OpenCL C
    .language_version:
      - 2
      - 0
    .max_flat_workgroup_size: 512
    .name:           _ZN12_GLOBAL__N_18big_gemmILi1EEEvPKDF16_S2_iiPK15HIP_vector_typeIfLj2EEPhS7_PKfPf
    .private_segment_fixed_size: 0
    .sgpr_count:     49
    .sgpr_spill_count: 0
    .symbol:         _ZN12_GLOBAL__N_18big_gemmILi1EEEvPKDF16_S2_iiPK15HIP_vector_typeIfLj2EEPhS7_PKfPf.kd
    .uniform_work_group_size: 1
    .uses_dynamic_stack: false
    .vgpr_count:     234
    .vgpr_spill_count: 0
    .wavefront_size: 64
  - .agpr_count:     0
    .args:
      - .actual_access:  read_only
        .address_space:  global
        .offset:         0
        .size:           8
        .value_kind:     global_buffer
      - .actual_access:  read_only
        .address_space:  global
        .offset:         8
        .size:           8
        .value_kind:     global_buffer
      - .actual_access:  read_only
        .address_space:  global
        .offset:         16
        .size:           8
        .value_kind:     global_buffer
      - .actual_access:  write_only
        .address_space:  global
        .offset:         24
        .size:           8
        .value_kind:     global_buffer
      - .actual_access:  read_only
        .address_space:  global
        .offset:         32
        .size:           8
        .value_kind:     global_buffer
      - .actual_access:  read_only
        .address_space:  global
        .offset:         40
        .size:           8
        .value_kind:     global_buffer
      - .actual_access:  read_only
        .address_space:  global
        .offset:         48
        .size:           8
        .value_kind:     global_buffer
      - .actual_access:  read_only
        .address_space:  global
        .offset:         56
        .size:           8
        .value_kind:     global_buffer
      - .actual_access:  read_only
        .address_space:  global
        .offset:         64
        .size:           8
        .value_kind:     global_buffer
      - .actual_access:  read_only
        .address_space:  global
        .offset:         72
        .size:           8
        .value_kind:     global_buffer
      - .actual_access:  read_only
        .address_space:  global
        .offset:         80
        .size:           8
        .value_kind:     global_buffer
      - .actual_access:  read_only
        .address_space:  global
        .offset:         88
        .size:           8
        .value_kind:     global_buffer
    .group_segment_fixed_size: 0
    .kernarg_segment_align: 8
    .kernarg_segment_size: 96
    .language:       OpenCL C
    .language_version:
      - 2
      - 0
    .max_flat_workgroup_size: 512
    .name:           _ZN12_GLOBAL__N_110gemm_fullkILi0ELi0EEEvPKDF16_S2_PKfPDF16_PfS6_S4_S4_S4_S4_S4_S5_
    .private_segment_fixed_size: 0
    .sgpr_count:     20
    .sgpr_spill_count: 0
    .symbol:         _ZN12_GLOBAL__N_110gemm_fullkILi0ELi0EEEvPKDF16_S2_PKfPDF16_PfS6_S4_S4_S4_S4_S4_S5_.kd
    .uniform_work_group_size: 1
    .uses_dynamic_stack: false
    .vgpr_count:     231
    .vgpr_spill_count: 0
    .wavefront_size: 64
  - .agpr_count:     0
    .args:
      - .actual_access:  read_only
        .address_space:  global
        .offset:         0
        .size:           8
        .value_kind:     global_buffer
      - .actual_access:  read_only
        .address_space:  global
        .offset:         8
        .size:           8
        .value_kind:     global_buffer
      - .actual_access:  read_only
        .address_space:  global
        .offset:         16
        .size:           8
        .value_kind:     global_buffer
      - .actual_access:  read_only
        .address_space:  global
        .offset:         24
        .size:           8
        .value_kind:     global_buffer
      - .address_space:  global
        .offset:         32
        .size:           8
        .value_kind:     global_buffer
      - .actual_access:  write_only
        .address_space:  global
        .offset:         40
        .size:           8
        .value_kind:     global_buffer
      - .actual_access:  read_only
        .address_space:  global
        .offset:         48
        .size:           8
        .value_kind:     global_buffer
      - .actual_access:  read_only
        .address_space:  global
        .offset:         56
        .size:           8
        .value_kind:     global_buffer
      - .actual_access:  read_only
        .address_space:  global
        .offset:         64
        .size:           8
        .value_kind:     global_buffer
      - .actual_access:  read_only
        .address_space:  global
        .offset:         72
        .size:           8
        .value_kind:     global_buffer
      - .actual_access:  read_only
        .address_space:  global
        .offset:         80
        .size:           8
        .value_kind:     global_buffer
      - .actual_access:  write_only
        .address_space:  global
        .offset:         88
        .size:           8
        .value_kind:     global_buffer
    .group_segment_fixed_size: 0
    .kernarg_segment_align: 8
    .kernarg_segment_size: 96
    .language:       OpenCL C
    .language_version:
      - 2
      - 0
    .max_flat_workgroup_size: 512
    .name:           _ZN12_GLOBAL__N_110gemm_fullkILi1ELi0EEEvPKDF16_S2_PKfPDF16_PfS6_S4_S4_S4_S4_S4_S5_
    .private_segment_fixed_size: 0
    .sgpr_count:     24
    .sgpr_spill_count: 0
    .symbol:         _ZN12_GLOBAL__N_110gemm_fullkILi1ELi0EEEvPKDF16_S2_PKfPDF16_PfS6_S4_S4_S4_S4_S4_S5_.kd
    .uniform_work_group_size: 1
    .uses_dynamic_stack: false
    .vgpr_count:     175
    .vgpr_spill_count: 0
    .wavefront_size: 64
  - .agpr_count:     0
    .args:
      - .actual_access:  read_only
        .address_space:  global
        .offset:         0
        .size:           8
        .value_kind:     global_buffer
      - .actual_access:  read_only
        .address_space:  global
        .offset:         8
        .size:           8
        .value_kind:     global_buffer
      - .actual_access:  read_only
        .address_space:  global
        .offset:         16
        .size:           8
        .value_kind:     global_buffer
      - .actual_access:  write_only
        .address_space:  global
        .offset:         24
        .size:           8
        .value_kind:     global_buffer
      - .actual_access:  read_only
        .address_space:  global
        .offset:         32
        .size:           8
        .value_kind:     global_buffer
      - .actual_access:  read_only
        .address_space:  global
        .offset:         40
        .size:           8
        .value_kind:     global_buffer
      - .actual_access:  read_only
        .address_space:  global
        .offset:         48
        .size:           8
        .value_kind:     global_buffer
      - .actual_access:  read_only
        .address_space:  global
        .offset:         56
        .size:           8
        .value_kind:     global_buffer
      - .actual_access:  read_only
        .address_space:  global
        .offset:         64
        .size:           8
        .value_kind:     global_buffer
      - .actual_access:  read_only
        .address_space:  global
        .offset:         72
        .size:           8
        .value_kind:     global_buffer
      - .actual_access:  read_only
        .address_space:  global
        .offset:         80
        .size:           8
        .value_kind:     global_buffer
      - .actual_access:  read_only
        .address_space:  global
        .offset:         88
        .size:           8
        .value_kind:     global_buffer
    .group_segment_fixed_size: 0
    .kernarg_segment_align: 8
    .kernarg_segment_size: 96
    .language:       OpenCL C
    .language_version:
      - 2
      - 0
    .max_flat_workgroup_size: 512
    .name:           _ZN12_GLOBAL__N_110gemm_fullkILi0ELi1EEEvPKDF16_S2_PKfPDF16_PfS6_S4_S4_S4_S4_S4_S5_
    .private_segment_fixed_size: 0
    .sgpr_count:     20
    .sgpr_spill_count: 0
    .symbol:         _ZN12_GLOBAL__N_110gemm_fullkILi0ELi1EEEvPKDF16_S2_PKfPDF16_PfS6_S4_S4_S4_S4_S4_S5_.kd
    .uniform_work_group_size: 1
    .uses_dynamic_stack: false
    .vgpr_count:     231
    .vgpr_spill_count: 0
    .wavefront_size: 64
  - .agpr_count:     0
    .args:
      - .actual_access:  read_only
        .address_space:  global
        .offset:         0
        .size:           8
        .value_kind:     global_buffer
      - .actual_access:  read_only
        .address_space:  global
        .offset:         8
        .size:           8
        .value_kind:     global_buffer
      - .actual_access:  read_only
        .address_space:  global
        .offset:         16
        .size:           8
        .value_kind:     global_buffer
      - .actual_access:  read_only
        .address_space:  global
        .offset:         24
        .size:           8
        .value_kind:     global_buffer
      - .address_space:  global
        .offset:         32
        .size:           8
        .value_kind:     global_buffer
      - .address_space:  global
        .offset:         40
        .size:           8
        .value_kind:     global_buffer
      - .actual_access:  read_only
        .address_space:  global
        .offset:         48
        .size:           8
        .value_kind:     global_buffer
      - .actual_access:  read_only
        .address_space:  global
        .offset:         56
        .size:           8
        .value_kind:     global_buffer
      - .actual_access:  read_only
        .address_space:  global
        .offset:         64
        .size:           8
        .value_kind:     global_buffer
      - .actual_access:  read_only
        .address_space:  global
        .offset:         72
        .size:           8
        .value_kind:     global_buffer
      - .actual_access:  read_only
        .address_space:  global
        .offset:         80
        .size:           8
        .value_kind:     global_buffer
      - .actual_access:  write_only
        .address_space:  global
        .offset:         88
        .size:           8
        .value_kind:     global_buffer
    .group_segment_fixed_size: 0
    .kernarg_segment_align: 8
    .kernarg_segment_size: 96
    .language:       OpenCL C
    .language_version:
      - 2
      - 0
    .max_flat_workgroup_size: 512
    .name:           _ZN12_GLOBAL__N_110gemm_fullkILi1ELi1EEEvPKDF16_S2_PKfPDF16_PfS6_S4_S4_S4_S4_S4_S5_
    .private_segment_fixed_size: 0
    .sgpr_count:     24
    .sgpr_spill_count: 0
    .symbol:         _ZN12_GLOBAL__N_110gemm_fullkILi1ELi1EEEvPKDF16_S2_PKfPDF16_PfS6_S4_S4_S4_S4_S4_S5_.kd
    .uniform_work_group_size: 1
    .uses_dynamic_stack: false
    .vgpr_count:     177
    .vgpr_spill_count: 0
    .wavefront_size: 64
  - .agpr_count:     0
    .args:
      - .actual_access:  read_only
        .address_space:  global
        .offset:         0
        .size:           8
        .value_kind:     global_buffer
      - .actual_access:  read_only
        .address_space:  global
        .offset:         8
        .size:           8
        .value_kind:     global_buffer
      - .actual_access:  read_only
        .address_space:  global
        .offset:         16
        .size:           8
        .value_kind:     global_buffer
      - .actual_access:  write_only
        .address_space:  global
        .offset:         24
        .size:           8
        .value_kind:     global_buffer
      - .actual_access:  read_only
        .address_space:  global
        .offset:         32
        .size:           8
        .value_kind:     global_buffer
      - .actual_access:  read_only
        .address_space:  global
        .offset:         40
        .size:           8
        .value_kind:     global_buffer
      - .actual_access:  read_only
        .address_space:  global
        .offset:         48
        .size:           8
        .value_kind:     global_buffer
      - .actual_access:  read_only
        .address_space:  global
        .offset:         56
        .size:           8
        .value_kind:     global_buffer
      - .actual_access:  read_only
        .address_space:  global
        .offset:         64
        .size:           8
        .value_kind:     global_buffer
      - .actual_access:  read_only
        .address_space:  global
        .offset:         72
        .size:           8
        .value_kind:     global_buffer
      - .actual_access:  read_only
        .address_space:  global
        .offset:         80
        .size:           8
        .value_kind:     global_buffer
      - .actual_access:  read_only
        .address_space:  global
        .offset:         88
        .size:           8
        .value_kind:     global_buffer
    .group_segment_fixed_size: 0
    .kernarg_segment_align: 8
    .kernarg_segment_size: 96
    .language:       OpenCL C
    .language_version:
      - 2
      - 0
    .max_flat_workgroup_size: 512
    .name:           _ZN12_GLOBAL__N_110gemm_fullkILi0ELi2EEEvPKDF16_S2_PKfPDF16_PfS6_S4_S4_S4_S4_S4_S5_
    .private_segment_fixed_size: 0
    .sgpr_count:     20
    .sgpr_spill_count: 0
    .symbol:         _ZN12_GLOBAL__N_110gemm_fullkILi0ELi2EEEvPKDF16_S2_PKfPDF16_PfS6_S4_S4_S4_S4_S4_S5_.kd
    .uniform_work_group_size: 1
    .uses_dynamic_stack: false
    .vgpr_count:     231
    .vgpr_spill_count: 0
    .wavefront_size: 64
  - .agpr_count:     0
    .args:
      - .actual_access:  read_only
        .address_space:  global
        .offset:         0
        .size:           8
        .value_kind:     global_buffer
      - .actual_access:  read_only
        .address_space:  global
        .offset:         8
        .size:           8
        .value_kind:     global_buffer
      - .actual_access:  read_only
        .address_space:  global
        .offset:         16
        .size:           8
        .value_kind:     global_buffer
      - .actual_access:  read_only
        .address_space:  global
        .offset:         24
        .size:           8
        .value_kind:     global_buffer
      - .address_space:  global
        .offset:         32
        .size:           8
        .value_kind:     global_buffer
      - .address_space:  global
        .offset:         40
        .size:           8
        .value_kind:     global_buffer
      - .actual_access:  read_only
        .address_space:  global
        .offset:         48
        .size:           8
        .value_kind:     global_buffer
      - .actual_access:  read_only
        .address_space:  global
        .offset:         56
        .size:           8
        .value_kind:     global_buffer
      - .actual_access:  read_only
        .address_space:  global
        .offset:         64
        .size:           8
        .value_kind:     global_buffer
      - .actual_access:  read_only
        .address_space:  global
        .offset:         72
        .size:           8
        .value_kind:     global_buffer
      - .actual_access:  read_only
        .address_space:  global
        .offset:         80
        .size:           8
        .value_kind:     global_buffer
      - .actual_access:  write_only
        .address_space:  global
        .offset:         88
        .size:           8
        .value_kind:     global_buffer
    .group_segment_fixed_size: 0
    .kernarg_segment_align: 8
    .kernarg_segment_size: 96
    .language:       OpenCL C
    .language_version:
      - 2
      - 0
    .max_flat_workgroup_size: 512
    .name:           _ZN12_GLOBAL__N_110gemm_fullkILi1ELi2EEEvPKDF16_S2_PKfPDF16_PfS6_S4_S4_S4_S4_S4_S5_
    .private_segment_fixed_size: 0
    .sgpr_count:     24
    .sgpr_spill_count: 0
    .symbol:         _ZN12_GLOBAL__N_110gemm_fullkILi1ELi2EEEvPKDF16_S2_PKfPDF16_PfS6_S4_S4_S4_S4_S4_S5_.kd
    .uniform_work_group_size: 1
    .uses_dynamic_stack: false
    .vgpr_count:     177
    .vgpr_spill_count: 0
    .wavefront_size: 64
  - .agpr_count:     0
    .args:
      - .actual_access:  read_only
        .address_space:  global
        .offset:         0
        .size:           8
        .value_kind:     global_buffer
      - .actual_access:  read_only
        .address_space:  global
        .offset:         8
        .size:           8
        .value_kind:     global_buffer
      - .actual_access:  read_only
        .address_space:  global
        .offset:         16
        .size:           8
        .value_kind:     global_buffer
      - .actual_access:  write_only
        .address_space:  global
        .offset:         24
        .size:           8
        .value_kind:     global_buffer
      - .actual_access:  read_only
        .address_space:  global
        .offset:         32
        .size:           8
        .value_kind:     global_buffer
      - .actual_access:  read_only
        .address_space:  global
        .offset:         40
        .size:           8
        .value_kind:     global_buffer
      - .actual_access:  read_only
        .address_space:  global
        .offset:         48
        .size:           8
        .value_kind:     global_buffer
      - .actual_access:  read_only
        .address_space:  global
        .offset:         56
        .size:           8
        .value_kind:     global_buffer
      - .actual_access:  read_only
        .address_space:  global
        .offset:         64
        .size:           8
        .value_kind:     global_buffer
      - .actual_access:  read_only
        .address_space:  global
        .offset:         72
        .size:           8
        .value_kind:     global_buffer
      - .actual_access:  read_only
        .address_space:  global
        .offset:         80
        .size:           8
        .value_kind:     global_buffer
      - .actual_access:  read_only
        .address_space:  global
        .offset:         88
        .size:           8
        .value_kind:     global_buffer
    .group_segment_fixed_size: 0
    .kernarg_segment_align: 8
    .kernarg_segment_size: 96
    .language:       OpenCL C
    .language_version:
      - 2
      - 0
    .max_flat_workgroup_size: 512
    .name:           _ZN12_GLOBAL__N_110gemm_fullkILi0ELi3EEEvPKDF16_S2_PKfPDF16_PfS6_S4_S4_S4_S4_S4_S5_
    .private_segment_fixed_size: 0
    .sgpr_count:     20
    .sgpr_spill_count: 0
    .symbol:         _ZN12_GLOBAL__N_110gemm_fullkILi0ELi3EEEvPKDF16_S2_PKfPDF16_PfS6_S4_S4_S4_S4_S4_S5_.kd
    .uniform_work_group_size: 1
    .uses_dynamic_stack: false
    .vgpr_count:     231
    .vgpr_spill_count: 0
    .wavefront_size: 64
  - .agpr_count:     0
    .args:
      - .actual_access:  read_only
        .address_space:  global
        .offset:         0
        .size:           8
        .value_kind:     global_buffer
      - .actual_access:  read_only
        .address_space:  global
        .offset:         8
        .size:           8
        .value_kind:     global_buffer
      - .actual_access:  read_only
        .address_space:  global
        .offset:         16
        .size:           8
        .value_kind:     global_buffer
      - .actual_access:  read_only
        .address_space:  global
        .offset:         24
        .size:           8
        .value_kind:     global_buffer
      - .address_space:  global
        .offset:         32
        .size:           8
        .value_kind:     global_buffer
      - .address_space:  global
        .offset:         40
        .size:           8
        .value_kind:     global_buffer
      - .actual_access:  read_only
        .address_space:  global
        .offset:         48
        .size:           8
        .value_kind:     global_buffer
      - .actual_access:  read_only
        .address_space:  global
        .offset:         56
        .size:           8
        .value_kind:     global_buffer
      - .actual_access:  read_only
        .address_space:  global
        .offset:         64
        .size:           8
        .value_kind:     global_buffer
      - .actual_access:  read_only
        .address_space:  global
        .offset:         72
        .size:           8
        .value_kind:     global_buffer
      - .actual_access:  read_only
        .address_space:  global
        .offset:         80
        .size:           8
        .value_kind:     global_buffer
      - .actual_access:  write_only
        .address_space:  global
        .offset:         88
        .size:           8
        .value_kind:     global_buffer
    .group_segment_fixed_size: 0
    .kernarg_segment_align: 8
    .kernarg_segment_size: 96
    .language:       OpenCL C
    .language_version:
      - 2
      - 0
    .max_flat_workgroup_size: 512
    .name:           _ZN12_GLOBAL__N_110gemm_fullkILi1ELi3EEEvPKDF16_S2_PKfPDF16_PfS6_S4_S4_S4_S4_S4_S5_
    .private_segment_fixed_size: 0
    .sgpr_count:     24
    .sgpr_spill_count: 0
    .symbol:         _ZN12_GLOBAL__N_110gemm_fullkILi1ELi3EEEvPKDF16_S2_PKfPDF16_PfS6_S4_S4_S4_S4_S4_S5_.kd
    .uniform_work_group_size: 1
    .uses_dynamic_stack: false
    .vgpr_count:     179
    .vgpr_spill_count: 0
    .wavefront_size: 64
  - .agpr_count:     0
    .args:
      - .actual_access:  read_only
        .address_space:  global
        .offset:         0
        .size:           8
        .value_kind:     global_buffer
      - .actual_access:  read_only
        .address_space:  global
        .offset:         8
        .size:           8
        .value_kind:     global_buffer
      - .actual_access:  read_only
        .address_space:  global
        .offset:         16
        .size:           8
        .value_kind:     global_buffer
      - .actual_access:  write_only
        .address_space:  global
        .offset:         24
        .size:           8
        .value_kind:     global_buffer
      - .actual_access:  read_only
        .address_space:  global
        .offset:         32
        .size:           8
        .value_kind:     global_buffer
      - .actual_access:  read_only
        .address_space:  global
        .offset:         40
        .size:           8
        .value_kind:     global_buffer
      - .actual_access:  read_only
        .address_space:  global
        .offset:         48
        .size:           8
        .value_kind:     global_buffer
      - .actual_access:  read_only
        .address_space:  global
        .offset:         56
        .size:           8
        .value_kind:     global_buffer
      - .actual_access:  read_only
        .address_space:  global
        .offset:         64
        .size:           8
        .value_kind:     global_buffer
      - .actual_access:  read_only
        .address_space:  global
        .offset:         72
        .size:           8
        .value_kind:     global_buffer
      - .actual_access:  read_only
        .address_space:  global
        .offset:         80
        .size:           8
        .value_kind:     global_buffer
      - .actual_access:  read_only
        .address_space:  global
        .offset:         88
        .size:           8
        .value_kind:     global_buffer
    .group_segment_fixed_size: 0
    .kernarg_segment_align: 8
    .kernarg_segment_size: 96
    .language:       OpenCL C
    .language_version:
      - 2
      - 0
    .max_flat_workgroup_size: 512
    .name:           _ZN12_GLOBAL__N_110gemm_fullkILi0ELi4EEEvPKDF16_S2_PKfPDF16_PfS6_S4_S4_S4_S4_S4_S5_
    .private_segment_fixed_size: 0
    .sgpr_count:     20
    .sgpr_spill_count: 0
    .symbol:         _ZN12_GLOBAL__N_110gemm_fullkILi0ELi4EEEvPKDF16_S2_PKfPDF16_PfS6_S4_S4_S4_S4_S4_S5_.kd
    .uniform_work_group_size: 1
    .uses_dynamic_stack: false
    .vgpr_count:     231
    .vgpr_spill_count: 0
    .wavefront_size: 64
  - .agpr_count:     0
    .args:
      - .actual_access:  read_only
        .address_space:  global
        .offset:         0
        .size:           8
        .value_kind:     global_buffer
      - .actual_access:  read_only
        .address_space:  global
        .offset:         8
        .size:           8
        .value_kind:     global_buffer
      - .actual_access:  read_only
        .address_space:  global
        .offset:         16
        .size:           8
        .value_kind:     global_buffer
      - .actual_access:  read_only
        .address_space:  global
        .offset:         24
        .size:           8
        .value_kind:     global_buffer
      - .address_space:  global
        .offset:         32
        .size:           8
        .value_kind:     global_buffer
      - .address_space:  global
        .offset:         40
        .size:           8
        .value_kind:     global_buffer
      - .actual_access:  read_only
        .address_space:  global
        .offset:         48
        .size:           8
        .value_kind:     global_buffer
      - .actual_access:  read_only
        .address_space:  global
        .offset:         56
        .size:           8
        .value_kind:     global_buffer
      - .actual_access:  read_only
        .address_space:  global
        .offset:         64
        .size:           8
        .value_kind:     global_buffer
      - .actual_access:  read_only
        .address_space:  global
        .offset:         72
        .size:           8
        .value_kind:     global_buffer
      - .actual_access:  read_only
        .address_space:  global
        .offset:         80
        .size:           8
        .value_kind:     global_buffer
      - .actual_access:  write_only
        .address_space:  global
        .offset:         88
        .size:           8
        .value_kind:     global_buffer
    .group_segment_fixed_size: 0
    .kernarg_segment_align: 8
    .kernarg_segment_size: 96
    .language:       OpenCL C
    .language_version:
      - 2
      - 0
    .max_flat_workgroup_size: 512
    .name:           _ZN12_GLOBAL__N_110gemm_fullkILi1ELi4EEEvPKDF16_S2_PKfPDF16_PfS6_S4_S4_S4_S4_S4_S5_
    .private_segment_fixed_size: 0
    .sgpr_count:     24
    .sgpr_spill_count: 0
    .symbol:         _ZN12_GLOBAL__N_110gemm_fullkILi1ELi4EEEvPKDF16_S2_PKfPDF16_PfS6_S4_S4_S4_S4_S4_S5_.kd
    .uniform_work_group_size: 1
    .uses_dynamic_stack: false
    .vgpr_count:     181
    .vgpr_spill_count: 0
    .wavefront_size: 64
  - .agpr_count:     0
    .args:
      - .actual_access:  read_only
        .address_space:  global
        .offset:         0
        .size:           8
        .value_kind:     global_buffer
      - .actual_access:  read_only
        .address_space:  global
        .offset:         8
        .size:           8
        .value_kind:     global_buffer
      - .actual_access:  read_only
        .address_space:  global
        .offset:         16
        .size:           8
        .value_kind:     global_buffer
      - .actual_access:  write_only
        .address_space:  global
        .offset:         24
        .size:           8
        .value_kind:     global_buffer
      - .actual_access:  read_only
        .address_space:  global
        .offset:         32
        .size:           8
        .value_kind:     global_buffer
      - .actual_access:  read_only
        .address_space:  global
        .offset:         40
        .size:           8
        .value_kind:     global_buffer
      - .actual_access:  read_only
        .address_space:  global
        .offset:         48
        .size:           8
        .value_kind:     global_buffer
      - .actual_access:  read_only
        .address_space:  global
        .offset:         56
        .size:           8
        .value_kind:     global_buffer
      - .actual_access:  read_only
        .address_space:  global
        .offset:         64
        .size:           8
        .value_kind:     global_buffer
      - .actual_access:  read_only
        .address_space:  global
        .offset:         72
        .size:           8
        .value_kind:     global_buffer
      - .actual_access:  read_only
        .address_space:  global
        .offset:         80
        .size:           8
        .value_kind:     global_buffer
      - .actual_access:  read_only
        .address_space:  global
        .offset:         88
        .size:           8
        .value_kind:     global_buffer
    .group_segment_fixed_size: 0
    .kernarg_segment_align: 8
    .kernarg_segment_size: 96
    .language:       OpenCL C
    .language_version:
      - 2
      - 0
    .max_flat_workgroup_size: 512
    .name:           _ZN12_GLOBAL__N_110gemm_fullkILi0ELi5EEEvPKDF16_S2_PKfPDF16_PfS6_S4_S4_S4_S4_S4_S5_
    .private_segment_fixed_size: 0
    .sgpr_count:     20
    .sgpr_spill_count: 0
    .symbol:         _ZN12_GLOBAL__N_110gemm_fullkILi0ELi5EEEvPKDF16_S2_PKfPDF16_PfS6_S4_S4_S4_S4_S4_S5_.kd
    .uniform_work_group_size: 1
    .uses_dynamic_stack: false
    .vgpr_count:     231
    .vgpr_spill_count: 0
    .wavefront_size: 64
  - .agpr_count:     0
    .args:
      - .actual_access:  read_only
        .address_space:  global
        .offset:         0
        .size:           8
        .value_kind:     global_buffer
      - .actual_access:  read_only
        .address_space:  global
        .offset:         8
        .size:           8
        .value_kind:     global_buffer
      - .actual_access:  read_only
        .address_space:  global
        .offset:         16
        .size:           8
        .value_kind:     global_buffer
      - .actual_access:  read_only
        .address_space:  global
        .offset:         24
        .size:           8
        .value_kind:     global_buffer
      - .address_space:  global
        .offset:         32
        .size:           8
        .value_kind:     global_buffer
      - .address_space:  global
        .offset:         40
        .size:           8
        .value_kind:     global_buffer
      - .actual_access:  read_only
        .address_space:  global
        .offset:         48
        .size:           8
        .value_kind:     global_buffer
      - .actual_access:  read_only
        .address_space:  global
        .offset:         56
        .size:           8
        .value_kind:     global_buffer
      - .actual_access:  read_only
        .address_space:  global
        .offset:         64
        .size:           8
        .value_kind:     global_buffer
      - .actual_access:  read_only
        .address_space:  global
        .offset:         72
        .size:           8
        .value_kind:     global_buffer
      - .actual_access:  read_only
        .address_space:  global
        .offset:         80
        .size:           8
        .value_kind:     global_buffer
      - .actual_access:  write_only
        .address_space:  global
        .offset:         88
        .size:           8
        .value_kind:     global_buffer
    .group_segment_fixed_size: 0
    .kernarg_segment_align: 8
    .kernarg_segment_size: 96
    .language:       OpenCL C
    .language_version:
      - 2
      - 0
    .max_flat_workgroup_size: 512
    .name:           _ZN12_GLOBAL__N_110gemm_fullkILi1ELi5EEEvPKDF16_S2_PKfPDF16_PfS6_S4_S4_S4_S4_S4_S5_
    .private_segment_fixed_size: 0
    .sgpr_count:     24
    .sgpr_spill_count: 0
    .symbol:         _ZN12_GLOBAL__N_110gemm_fullkILi1ELi5EEEvPKDF16_S2_PKfPDF16_PfS6_S4_S4_S4_S4_S4_S5_.kd
    .uniform_work_group_size: 1
    .uses_dynamic_stack: false
    .vgpr_count:     183
    .vgpr_spill_count: 0
    .wavefront_size: 64
  - .agpr_count:     0
    .args:
      - .actual_access:  read_only
        .address_space:  global
        .offset:         0
        .size:           8
        .value_kind:     global_buffer
      - .actual_access:  read_only
        .address_space:  global
        .offset:         8
        .size:           8
        .value_kind:     global_buffer
      - .actual_access:  read_only
        .address_space:  global
        .offset:         16
        .size:           8
        .value_kind:     global_buffer
      - .actual_access:  write_only
        .address_space:  global
        .offset:         24
        .size:           8
        .value_kind:     global_buffer
      - .actual_access:  read_only
        .address_space:  global
        .offset:         32
        .size:           8
        .value_kind:     global_buffer
      - .actual_access:  read_only
        .address_space:  global
        .offset:         40
        .size:           8
        .value_kind:     global_buffer
      - .actual_access:  read_only
        .address_space:  global
        .offset:         48
        .size:           8
        .value_kind:     global_buffer
      - .actual_access:  read_only
        .address_space:  global
        .offset:         56
        .size:           8
        .value_kind:     global_buffer
      - .actual_access:  read_only
        .address_space:  global
        .offset:         64
        .size:           8
        .value_kind:     global_buffer
      - .actual_access:  read_only
        .address_space:  global
        .offset:         72
        .size:           8
        .value_kind:     global_buffer
      - .actual_access:  read_only
        .address_space:  global
        .offset:         80
        .size:           8
        .value_kind:     global_buffer
      - .actual_access:  read_only
        .address_space:  global
        .offset:         88
        .size:           8
        .value_kind:     global_buffer
    .group_segment_fixed_size: 0
    .kernarg_segment_align: 8
    .kernarg_segment_size: 96
    .language:       OpenCL C
    .language_version:
      - 2
      - 0
    .max_flat_workgroup_size: 512
    .name:           _ZN12_GLOBAL__N_110gemm_fullkILi0ELi6EEEvPKDF16_S2_PKfPDF16_PfS6_S4_S4_S4_S4_S4_S5_
    .private_segment_fixed_size: 0
    .sgpr_count:     20
    .sgpr_spill_count: 0
    .symbol:         _ZN12_GLOBAL__N_110gemm_fullkILi0ELi6EEEvPKDF16_S2_PKfPDF16_PfS6_S4_S4_S4_S4_S4_S5_.kd
    .uniform_work_group_size: 1
    .uses_dynamic_stack: false
    .vgpr_count:     231
    .vgpr_spill_count: 0
    .wavefront_size: 64
  - .agpr_count:     0
    .args:
      - .actual_access:  read_only
        .address_space:  global
        .offset:         0
        .size:           8
        .value_kind:     global_buffer
      - .actual_access:  read_only
        .address_space:  global
        .offset:         8
        .size:           8
        .value_kind:     global_buffer
      - .actual_access:  read_only
        .address_space:  global
        .offset:         16
        .size:           8
        .value_kind:     global_buffer
      - .actual_access:  read_only
        .address_space:  global
        .offset:         24
        .size:           8
        .value_kind:     global_buffer
      - .address_space:  global
        .offset:         32
        .size:           8
        .value_kind:     global_buffer
      - .address_space:  global
        .offset:         40
        .size:           8
        .value_kind:     global_buffer
      - .actual_access:  read_only
        .address_space:  global
        .offset:         48
        .size:           8
        .value_kind:     global_buffer
      - .actual_access:  read_only
        .address_space:  global
        .offset:         56
        .size:           8
        .value_kind:     global_buffer
      - .actual_access:  read_only
        .address_space:  global
        .offset:         64
        .size:           8
        .value_kind:     global_buffer
      - .actual_access:  read_only
        .address_space:  global
        .offset:         72
        .size:           8
        .value_kind:     global_buffer
      - .actual_access:  read_only
        .address_space:  global
        .offset:         80
        .size:           8
        .value_kind:     global_buffer
      - .actual_access:  write_only
        .address_space:  global
        .offset:         88
        .size:           8
        .value_kind:     global_buffer
    .group_segment_fixed_size: 0
    .kernarg_segment_align: 8
    .kernarg_segment_size: 96
    .language:       OpenCL C
    .language_version:
      - 2
      - 0
    .max_flat_workgroup_size: 512
    .name:           _ZN12_GLOBAL__N_110gemm_fullkILi1ELi6EEEvPKDF16_S2_PKfPDF16_PfS6_S4_S4_S4_S4_S4_S5_
    .private_segment_fixed_size: 0
    .sgpr_count:     24
    .sgpr_spill_count: 0
    .symbol:         _ZN12_GLOBAL__N_110gemm_fullkILi1ELi6EEEvPKDF16_S2_PKfPDF16_PfS6_S4_S4_S4_S4_S4_S5_.kd
    .uniform_work_group_size: 1
    .uses_dynamic_stack: false
    .vgpr_count:     185
    .vgpr_spill_count: 0
    .wavefront_size: 64
  - .agpr_count:     0
    .args:
      - .actual_access:  read_only
        .address_space:  global
        .offset:         0
        .size:           8
        .value_kind:     global_buffer
      - .actual_access:  read_only
        .address_space:  global
        .offset:         8
        .size:           8
        .value_kind:     global_buffer
      - .actual_access:  read_only
        .address_space:  global
        .offset:         16
        .size:           8
        .value_kind:     global_buffer
      - .actual_access:  write_only
        .address_space:  global
        .offset:         24
        .size:           8
        .value_kind:     global_buffer
      - .actual_access:  read_only
        .address_space:  global
        .offset:         32
        .size:           8
        .value_kind:     global_buffer
      - .actual_access:  read_only
        .address_space:  global
        .offset:         40
        .size:           8
        .value_kind:     global_buffer
      - .actual_access:  read_only
        .address_space:  global
        .offset:         48
        .size:           8
        .value_kind:     global_buffer
      - .actual_access:  read_only
        .address_space:  global
        .offset:         56
        .size:           8
        .value_kind:     global_buffer
      - .actual_access:  read_only
        .address_space:  global
        .offset:         64
        .size:           8
        .value_kind:     global_buffer
      - .actual_access:  read_only
        .address_space:  global
        .offset:         72
        .size:           8
        .value_kind:     global_buffer
      - .actual_access:  read_only
        .address_space:  global
        .offset:         80
        .size:           8
        .value_kind:     global_buffer
      - .actual_access:  read_only
        .address_space:  global
        .offset:         88
        .size:           8
        .value_kind:     global_buffer
    .group_segment_fixed_size: 0
    .kernarg_segment_align: 8
    .kernarg_segment_size: 96
    .language:       OpenCL C
    .language_version:
      - 2
      - 0
    .max_flat_workgroup_size: 512
    .name:           _ZN12_GLOBAL__N_110gemm_fullkILi0ELi7EEEvPKDF16_S2_PKfPDF16_PfS6_S4_S4_S4_S4_S4_S5_
    .private_segment_fixed_size: 0
    .sgpr_count:     20
    .sgpr_spill_count: 0
    .symbol:         _ZN12_GLOBAL__N_110gemm_fullkILi0ELi7EEEvPKDF16_S2_PKfPDF16_PfS6_S4_S4_S4_S4_S4_S5_.kd
    .uniform_work_group_size: 1
    .uses_dynamic_stack: false
    .vgpr_count:     231
    .vgpr_spill_count: 0
    .wavefront_size: 64
  - .agpr_count:     0
    .args:
      - .actual_access:  read_only
        .address_space:  global
        .offset:         0
        .size:           8
        .value_kind:     global_buffer
      - .actual_access:  read_only
        .address_space:  global
        .offset:         8
        .size:           8
        .value_kind:     global_buffer
      - .actual_access:  read_only
        .address_space:  global
        .offset:         16
        .size:           8
        .value_kind:     global_buffer
      - .actual_access:  read_only
        .address_space:  global
        .offset:         24
        .size:           8
        .value_kind:     global_buffer
      - .address_space:  global
        .offset:         32
        .size:           8
        .value_kind:     global_buffer
      - .address_space:  global
        .offset:         40
        .size:           8
        .value_kind:     global_buffer
      - .actual_access:  read_only
        .address_space:  global
        .offset:         48
        .size:           8
        .value_kind:     global_buffer
      - .actual_access:  read_only
        .address_space:  global
        .offset:         56
        .size:           8
        .value_kind:     global_buffer
      - .actual_access:  read_only
        .address_space:  global
        .offset:         64
        .size:           8
        .value_kind:     global_buffer
      - .actual_access:  read_only
        .address_space:  global
        .offset:         72
        .size:           8
        .value_kind:     global_buffer
      - .actual_access:  read_only
        .address_space:  global
        .offset:         80
        .size:           8
        .value_kind:     global_buffer
      - .actual_access:  write_only
        .address_space:  global
        .offset:         88
        .size:           8
        .value_kind:     global_buffer
    .group_segment_fixed_size: 0
    .kernarg_segment_align: 8
    .kernarg_segment_size: 96
    .language:       OpenCL C
    .language_version:
      - 2
      - 0
    .max_flat_workgroup_size: 512
    .name:           _ZN12_GLOBAL__N_110gemm_fullkILi1ELi7EEEvPKDF16_S2_PKfPDF16_PfS6_S4_S4_S4_S4_S4_S5_
    .private_segment_fixed_size: 0
    .sgpr_count:     24
    .sgpr_spill_count: 0
    .symbol:         _ZN12_GLOBAL__N_110gemm_fullkILi1ELi7EEEvPKDF16_S2_PKfPDF16_PfS6_S4_S4_S4_S4_S4_S5_.kd
    .uniform_work_group_size: 1
    .uses_dynamic_stack: false
    .vgpr_count:     187
    .vgpr_spill_count: 0
    .wavefront_size: 64
